# GEMM K-loops: drop s_setprio to 0 four MFMAs before the end of each 32-MFMA compute segment (priority handed to the loading partner wave earlier); no other change
# speedup vs baseline: 1.0026x; 1.0026x over previous
; #define PG8_STAGE(bufoff, gbase, voff) do { _Pragma("unroll") for (int _i = 0; _i < 2; ++_i) \
;         __builtin_amdgcn_global_load_lds((const unsigned*)((const char*)(gbase) + (voff)[_i]), (PG8_LAS unsigned*)(lds + (bufoff) + ldsw + _i * 8192), 16, 0, 0); } while (0)
; #define PG8_WAIT_V(n) asm volatile("s_waitcnt vmcnt(" #n ")" ::: "memory")
; #define PG8_WAIT_L(n) asm volatile("s_waitcnt lgkmcnt(" #n ")" ::: "memory")
; #define PG8_BAR __builtin_amdgcn_s_barrier()
; #define PG8_SCHED __builtin_amdgcn_sched_barrier(0)
; template <class Epi, class Sched, bool ALIGN_EPI, bool F8 = false>
; __device__ __forceinline__ void gemm_phase(PG8_LAS unsigned char* lds, const Gemm g, const Sched& S, const Epi& E, int tid) {
;     ...
;         for (int t = 0; t < nt; t += 2) {
;             const bool last = (t == nt - 2);
;             const char* a1 = cA + (size_t)(t + 1) * kstep;
;             const char* a2 = last ? nA : cA + (size_t)(t + 2) * kstep; const char* b2 = last ? nB : cB + (size_t)(t + 2) * kstep;
;             const char* a3 = a2 + kstep; const char* b3 = b2 + kstep;
;             if (last && has_next) S.a_ready(nxt);
;             PG8_LDB(B0, 0, 0); PG8_LDB(B1, 0, 1); PG8_SCHED; PG8_LDA(At, 0, 0); PG8_STAGE(PG8_SA(1, 1), a1 + hstepA, voffA);
;             PG8_WAIT_V(8); PG8_WAIT_L(0); PG8_BAR; PG8_MMA(0, 0, At, B0); PG8_MMA(0, 1, At, B1); PG8_BAR; PG8_SCHED;
;             PG8_LDA(At, 0, 1); PG8_STAGE(PG8_SB(0, 0), b2, voffB); PG8_STAGE(PG8_SB(0, 1), b2 + hstepB, voffB); PG8_STAGE(PG8_SA(0, 0), a2, voffA);
.LBB0_592:
	s_add_u32 s14, s10, 0xfff80080
	s_addc_u32 s15, s11, -1
	s_add_i32 s89, 0, 0x10000
	s_cmp_eq_u32 s88, 28
	s_cselect_b32 s39, s7, s15
	s_cselect_b32 s38, s9, s14
	s_cselect_b32 s15, s29, s87
	s_cselect_b32 s14, s31, s86
	s_add_i32 s16, 0, 0x14000
	v_add_u32_e32 v46, s89, v173
	v_add_u32_e32 v170, s16, v173
	ds_read_b128 v[34:37], v46
	ds_read_b128 v[38:41], v46 offset:1024
	ds_read_b128 v[42:45], v46 offset:2048
	ds_read_b128 v[46:49], v46 offset:3072
	ds_read_b128 v[162:165], v170
	ds_read_b128 v[166:169], v170 offset:1024
	ds_read_b128 v[190:193], v170 offset:2048
	ds_read_b128 v[198:201], v170 offset:3072
	v_lshl_add_u64 v[170:171], s[10:11], 0, v[158:159]
	s_add_i32 m0, s5, 0xc000
	ds_read_b128 v[202:205], v174
	ds_read_b128 v[206:209], v174 offset:1024
	ds_read_b128 v[210:213], v174 offset:2048
	ds_read_b128 v[214:217], v174 offset:3072
	ds_read_b128 v[236:239], v174 offset:4096
	ds_read_b128 v[240:243], v174 offset:5120
	ds_read_b128 v[244:247], v174 offset:6144
	ds_read_b128 v[248:251], v174 offset:7168
	global_load_lds_dwordx4 v[170:171], off
	v_lshl_add_u64 v[170:171], s[10:11], 0, v[160:161]
	s_add_i32 m0, s5, 0xe000
	s_nop 0
	global_load_lds_dwordx4 v[170:171], off
	s_waitcnt vmcnt(8)
	s_waitcnt lgkmcnt(0)
	s_barrier
	s_setprio 1
	s_waitcnt lgkmcnt(0)
	v_mfma_f32_16x16x32_bf16 v[142:145], v[34:37], v[202:205], v[142:145]
	v_mfma_f32_16x16x32_bf16 v[138:141], v[42:45], v[202:205], v[138:141]
	v_mfma_f32_16x16x32_bf16 v[126:129], v[34:37], v[210:213], v[126:129]
	v_mfma_f32_16x16x32_bf16 v[122:125], v[42:45], v[210:213], v[122:125]
	v_mfma_f32_16x16x32_bf16 v[110:113], v[34:37], v[236:239], v[110:113]
	v_mfma_f32_16x16x32_bf16 v[106:109], v[42:45], v[236:239], v[106:109]
	v_mfma_f32_16x16x32_bf16 v[94:97], v[34:37], v[244:247], v[94:97]
	v_mfma_f32_16x16x32_bf16 v[90:93], v[42:45], v[244:247], v[90:93]
	v_mfma_f32_16x16x32_bf16 v[142:145], v[38:41], v[206:209], v[142:145]
	v_mfma_f32_16x16x32_bf16 v[138:141], v[46:49], v[206:209], v[138:141]
	v_mfma_f32_16x16x32_bf16 v[126:129], v[38:41], v[214:217], v[126:129]
	v_mfma_f32_16x16x32_bf16 v[122:125], v[46:49], v[214:217], v[122:125]
	v_mfma_f32_16x16x32_bf16 v[110:113], v[38:41], v[240:243], v[110:113]
	v_mfma_f32_16x16x32_bf16 v[106:109], v[46:49], v[240:243], v[106:109]
	v_mfma_f32_16x16x32_bf16 v[94:97], v[38:41], v[248:251], v[94:97]
	v_mfma_f32_16x16x32_bf16 v[90:93], v[46:49], v[248:251], v[90:93]
	s_setprio 0
	s_setprio 1
	v_mfma_f32_16x16x32_bf16 v[134:137], v[162:165], v[202:205], v[134:137]
	v_mfma_f32_16x16x32_bf16 v[130:133], v[190:193], v[202:205], v[130:133]
	v_mfma_f32_16x16x32_bf16 v[118:121], v[162:165], v[210:213], v[118:121]
	v_mfma_f32_16x16x32_bf16 v[114:117], v[190:193], v[210:213], v[114:117]
	v_mfma_f32_16x16x32_bf16 v[102:105], v[162:165], v[236:239], v[102:105]
	v_mfma_f32_16x16x32_bf16 v[98:101], v[190:193], v[236:239], v[98:101]
	v_mfma_f32_16x16x32_bf16 v[86:89], v[162:165], v[244:247], v[86:89]
	v_mfma_f32_16x16x32_bf16 v[82:85], v[190:193], v[244:247], v[82:85]
	v_mfma_f32_16x16x32_bf16 v[134:137], v[166:169], v[206:209], v[134:137]
	v_mfma_f32_16x16x32_bf16 v[130:133], v[198:201], v[206:209], v[130:133]
	v_mfma_f32_16x16x32_bf16 v[118:121], v[166:169], v[214:217], v[118:121]
	v_mfma_f32_16x16x32_bf16 v[114:117], v[198:201], v[214:217], v[114:117]
	s_setprio 0
	v_mfma_f32_16x16x32_bf16 v[102:105], v[166:169], v[240:243], v[102:105]
	v_mfma_f32_16x16x32_bf16 v[98:101], v[198:201], v[240:243], v[98:101]
	v_mfma_f32_16x16x32_bf16 v[86:89], v[166:169], v[248:251], v[86:89]
	v_mfma_f32_16x16x32_bf16 v[82:85], v[198:201], v[248:251], v[82:85]
	s_barrier
	s_add_i32 s89, s89, s4
	v_lshl_add_u64 v[170:171], s[14:15], 0, v[148:149]
	s_mov_b32 m0, s89
	ds_read_b128 v[202:205], v174 offset:16384
	ds_read_b128 v[206:209], v174 offset:17408
	ds_read_b128 v[210:213], v174 offset:18432
	ds_read_b128 v[214:217], v174 offset:19456
	ds_read_b128 v[236:239], v174 offset:20480
	ds_read_b128 v[240:243], v174 offset:21504
	ds_read_b128 v[244:247], v174 offset:22528
	ds_read_b128 v[248:251], v174 offset:23552
	global_load_lds_dwordx4 v[170:171], off
	s_add_i32 m0, s89, 0x2000
	s_add_u32 vcc_lo, s14, 0x80000
	v_lshl_add_u64 v[176:177], s[14:15], 0, v[152:153]
	s_addc_u32 vcc_hi, s15, 0
	s_add_i32 s16, s16, s4
	global_load_lds_dwordx4 v[176:177], off
	v_lshl_add_u64 v[178:179], vcc, 0, v[148:149]
	s_mov_b32 m0, s16
	v_lshl_add_u64 v[180:181], s[38:39], 0, v[150:151]
	global_load_lds_dwordx4 v[178:179], off
	v_lshl_add_u64 v[178:179], vcc, 0, v[152:153]
	s_add_i32 m0, s16, 0x2000
	s_nop 0
	global_load_lds_dwordx4 v[178:179], off
	v_lshl_add_u64 v[178:179], s[38:39], 0, v[146:147]
	s_mov_b32 m0, s5
	s_nop 0
	global_load_lds_dwordx4 v[178:179], off
	s_mov_b32 m0, s22
	s_nop 0
	global_load_lds_dwordx4 v[180:181], off
	s_waitcnt vmcnt(8)
	s_waitcnt lgkmcnt(0)
	s_barrier
; #define PG8_STAGE(bufoff, gbase, voff) do { _Pragma("unroll") for (int _i = 0; _i < 2; ++_i) \
;         __builtin_amdgcn_global_load_lds((const unsigned*)((const char*)(gbase) + (voff)[_i]), (PG8_LAS unsigned*)(lds + (bufoff) + ldsw + _i * 8192), 16, 0, 0); } while (0)
; #define PG8_WAIT_V(n) asm volatile("s_waitcnt vmcnt(" #n ")" ::: "memory")
; #define PG8_WAIT_L(n) asm volatile("s_waitcnt lgkmcnt(" #n ")" ::: "memory")
; #define PG8_BAR __builtin_amdgcn_s_barrier()
; #define PG8_SCHED __builtin_amdgcn_sched_barrier(0)
; template <class Epi, class Sched, bool ALIGN_EPI, bool F8 = false>
; __device__ __forceinline__ void gemm_phase(PG8_LAS unsigned char* lds, const Gemm g, const Sched& S, const Epi& E, int tid) {
;     ...
;             PG8_WAIT_V(8); PG8_WAIT_L(0); PG8_BAR; PG8_MMA(1, 0, At, B0); PG8_MMA(1, 1, At, B1); PG8_BAR; PG8_SCHED;
;             PG8_LDB(B0, 1, 0); PG8_LDB(B1, 1, 1); PG8_SCHED; PG8_LDA(At, 1, 0); PG8_STAGE(PG8_SA(0, 1), a2 + hstepA, voffA);
;             PG8_WAIT_V(8); PG8_WAIT_L(0); PG8_BAR; PG8_MMA(0, 0, At, B0); PG8_MMA(0, 1, At, B1); PG8_BAR; PG8_SCHED;
	s_setprio 1
	s_waitcnt lgkmcnt(0)
	v_mfma_f32_16x16x32_bf16 v[78:81], v[34:37], v[202:205], v[78:81]
	v_mfma_f32_16x16x32_bf16 v[74:77], v[42:45], v[202:205], v[74:77]
	v_mfma_f32_16x16x32_bf16 v[62:65], v[34:37], v[210:213], v[62:65]
	v_mfma_f32_16x16x32_bf16 v[58:61], v[42:45], v[210:213], v[58:61]
	v_mfma_f32_16x16x32_bf16 v[30:33], v[34:37], v[236:239], v[30:33]
	v_mfma_f32_16x16x32_bf16 v[26:29], v[42:45], v[236:239], v[26:29]
	v_mfma_f32_16x16x32_bf16 v[14:17], v[34:37], v[244:247], v[14:17]
	v_mfma_f32_16x16x32_bf16 v[10:13], v[42:45], v[244:247], v[10:13]
	v_mfma_f32_16x16x32_bf16 v[78:81], v[38:41], v[206:209], v[78:81]
	v_mfma_f32_16x16x32_bf16 v[74:77], v[46:49], v[206:209], v[74:77]
	v_mfma_f32_16x16x32_bf16 v[62:65], v[38:41], v[214:217], v[62:65]
	v_mfma_f32_16x16x32_bf16 v[58:61], v[46:49], v[214:217], v[58:61]
	v_mfma_f32_16x16x32_bf16 v[30:33], v[38:41], v[240:243], v[30:33]
	v_mfma_f32_16x16x32_bf16 v[26:29], v[46:49], v[240:243], v[26:29]
	v_mfma_f32_16x16x32_bf16 v[14:17], v[38:41], v[248:251], v[14:17]
	v_mfma_f32_16x16x32_bf16 v[10:13], v[46:49], v[248:251], v[10:13]
	s_setprio 0
	s_setprio 1
	v_mfma_f32_16x16x32_bf16 v[22:25], v[162:165], v[236:239], v[22:25]
	v_mfma_f32_16x16x32_bf16 v[18:21], v[190:193], v[236:239], v[18:21]
	v_mfma_f32_16x16x32_bf16 v[6:9], v[162:165], v[244:247], v[6:9]
	v_mfma_f32_16x16x32_bf16 v[2:5], v[190:193], v[244:247], v[2:5]
	v_mfma_f32_16x16x32_bf16 v[34:37], v[162:165], v[202:205], v[70:73]
	v_mfma_f32_16x16x32_bf16 v[38:41], v[190:193], v[202:205], v[66:69]
	v_mfma_f32_16x16x32_bf16 v[42:45], v[162:165], v[210:213], v[54:57]
	v_mfma_f32_16x16x32_bf16 v[46:49], v[190:193], v[210:213], v[50:53]
	v_mfma_f32_16x16x32_bf16 v[22:25], v[166:169], v[240:243], v[22:25]
	v_mfma_f32_16x16x32_bf16 v[18:21], v[198:201], v[240:243], v[18:21]
	v_mfma_f32_16x16x32_bf16 v[6:9], v[166:169], v[248:251], v[6:9]
	v_mfma_f32_16x16x32_bf16 v[2:5], v[198:201], v[248:251], v[2:5]
	s_setprio 0
	v_mfma_f32_16x16x32_bf16 v[34:37], v[166:169], v[206:209], v[34:37]
	v_mfma_f32_16x16x32_bf16 v[38:41], v[198:201], v[206:209], v[38:41]
	v_mfma_f32_16x16x32_bf16 v[42:45], v[166:169], v[214:217], v[42:45]
	v_mfma_f32_16x16x32_bf16 v[46:49], v[198:201], v[214:217], v[46:49]
	s_barrier
	s_add_i32 s16, 0, 0x18000
	s_add_i32 s89, 0, 0x1c000
	v_add_u32_e32 v70, s16, v173
	v_add_u32_e32 v175, s89, v173
	ds_read_b128 v[50:53], v70
	ds_read_b128 v[54:57], v70 offset:1024
	ds_read_b128 v[66:69], v70 offset:2048
	ds_read_b128 v[70:73], v70 offset:3072
	ds_read_b128 v[162:165], v175
	ds_read_b128 v[166:169], v175 offset:1024
	ds_read_b128 v[190:193], v175 offset:2048
	ds_read_b128 v[198:201], v175 offset:3072
	s_add_u32 s38, s38, 0x80000
	s_addc_u32 s39, s39, 0
	s_mov_b32 m0, s23
	v_lshl_add_u64 v[182:183], s[38:39], 0, v[146:147]
	ds_read_b128 v[202:205], v174 offset:32768
	ds_read_b128 v[206:209], v174 offset:33792
	ds_read_b128 v[210:213], v174 offset:34816
	ds_read_b128 v[214:217], v174 offset:35840
	ds_read_b128 v[236:239], v174 offset:36864
	ds_read_b128 v[240:243], v174 offset:37888
	ds_read_b128 v[244:247], v174 offset:38912
	ds_read_b128 v[248:251], v174 offset:39936
	global_load_lds_dwordx4 v[182:183], off
	v_lshl_add_u64 v[182:183], s[38:39], 0, v[150:151]
	s_mov_b32 m0, s24
	s_nop 0
	global_load_lds_dwordx4 v[182:183], off
	s_waitcnt vmcnt(8)
	s_waitcnt lgkmcnt(0)
	s_barrier
	s_setprio 1
	s_waitcnt lgkmcnt(0)
	v_mfma_f32_16x16x32_bf16 v[142:145], v[50:53], v[202:205], v[142:145]
	v_mfma_f32_16x16x32_bf16 v[138:141], v[66:69], v[202:205], v[138:141]
	v_mfma_f32_16x16x32_bf16 v[126:129], v[50:53], v[210:213], v[126:129]
	v_mfma_f32_16x16x32_bf16 v[122:125], v[66:69], v[210:213], v[122:125]
	v_mfma_f32_16x16x32_bf16 v[110:113], v[50:53], v[236:239], v[110:113]
	v_mfma_f32_16x16x32_bf16 v[106:109], v[66:69], v[236:239], v[106:109]
	v_mfma_f32_16x16x32_bf16 v[94:97], v[50:53], v[244:247], v[94:97]
	v_mfma_f32_16x16x32_bf16 v[90:93], v[66:69], v[244:247], v[90:93]
	v_mfma_f32_16x16x32_bf16 v[142:145], v[54:57], v[206:209], v[142:145]
	v_mfma_f32_16x16x32_bf16 v[138:141], v[70:73], v[206:209], v[138:141]
	v_mfma_f32_16x16x32_bf16 v[126:129], v[54:57], v[214:217], v[126:129]
	v_mfma_f32_16x16x32_bf16 v[122:125], v[70:73], v[214:217], v[122:125]
	v_mfma_f32_16x16x32_bf16 v[110:113], v[54:57], v[240:243], v[110:113]
	v_mfma_f32_16x16x32_bf16 v[106:109], v[70:73], v[240:243], v[106:109]
	v_mfma_f32_16x16x32_bf16 v[94:97], v[54:57], v[248:251], v[94:97]
	v_mfma_f32_16x16x32_bf16 v[90:93], v[70:73], v[248:251], v[90:93]
	s_setprio 0
	s_setprio 1
	v_mfma_f32_16x16x32_bf16 v[134:137], v[162:165], v[202:205], v[134:137]
	v_mfma_f32_16x16x32_bf16 v[130:133], v[190:193], v[202:205], v[130:133]
	v_mfma_f32_16x16x32_bf16 v[118:121], v[162:165], v[210:213], v[118:121]
	v_mfma_f32_16x16x32_bf16 v[114:117], v[190:193], v[210:213], v[114:117]
	v_mfma_f32_16x16x32_bf16 v[102:105], v[162:165], v[236:239], v[102:105]
	v_mfma_f32_16x16x32_bf16 v[98:101], v[190:193], v[236:239], v[98:101]
	v_mfma_f32_16x16x32_bf16 v[86:89], v[162:165], v[244:247], v[86:89]
	v_mfma_f32_16x16x32_bf16 v[82:85], v[190:193], v[244:247], v[82:85]
	v_mfma_f32_16x16x32_bf16 v[134:137], v[166:169], v[206:209], v[134:137]
	v_mfma_f32_16x16x32_bf16 v[130:133], v[198:201], v[206:209], v[130:133]
	v_mfma_f32_16x16x32_bf16 v[118:121], v[166:169], v[214:217], v[118:121]
	v_mfma_f32_16x16x32_bf16 v[114:117], v[198:201], v[214:217], v[114:117]
	s_setprio 0
	v_mfma_f32_16x16x32_bf16 v[102:105], v[166:169], v[240:243], v[102:105]
	v_mfma_f32_16x16x32_bf16 v[98:101], v[198:201], v[240:243], v[98:101]
	v_mfma_f32_16x16x32_bf16 v[86:89], v[166:169], v[248:251], v[86:89]
	v_mfma_f32_16x16x32_bf16 v[82:85], v[198:201], v[248:251], v[82:85]
	s_barrier
; #define PG8_STAGE(bufoff, gbase, voff) do { _Pragma("unroll") for (int _i = 0; _i < 2; ++_i) \
;         __builtin_amdgcn_global_load_lds((const unsigned*)((const char*)(gbase) + (voff)[_i]), (PG8_LAS unsigned*)(lds + (bufoff) + ldsw + _i * 8192), 16, 0, 0); } while (0)
; #define PG8_WAIT_V(n) asm volatile("s_waitcnt vmcnt(" #n ")" ::: "memory")
; #define PG8_WAIT_L(n) asm volatile("s_waitcnt lgkmcnt(" #n ")" ::: "memory")
; #define PG8_BAR __builtin_amdgcn_s_barrier()
; #define PG8_SCHED __builtin_amdgcn_sched_barrier(0)
; template <class Epi, class Sched, bool ALIGN_EPI, bool F8 = false>
; __device__ __forceinline__ void gemm_phase(PG8_LAS unsigned char* lds, const Gemm g, const Sched& S, const Epi& E, int tid) {
;     ...
;             PG8_LDA(At, 1, 1); PG8_STAGE(PG8_SB(1, 0), b3, voffB); PG8_STAGE(PG8_SB(1, 1), b3 + hstepB, voffB); PG8_STAGE(PG8_SA(1, 0), a3, voffA);
;             PG8_WAIT_V(8); PG8_WAIT_L(0); PG8_BAR; PG8_MMA(1, 0, At, B0); PG8_MMA(1, 1, At, B1); PG8_BAR; PG8_SCHED;
;         }
;         if constexpr (ALIGN_EPI) { if (wr == 0) PG8_BAR; }
	s_add_i32 s16, s16, s4
	v_lshl_add_u64 v[170:171], v[170:171], 0, s[60:61]
	s_mov_b32 m0, s16
	ds_read_b128 v[202:205], v174 offset:49152
	ds_read_b128 v[206:209], v174 offset:50176
	ds_read_b128 v[210:213], v174 offset:51200
	ds_read_b128 v[214:217], v174 offset:52224
	ds_read_b128 v[236:239], v174 offset:53248
	ds_read_b128 v[240:243], v174 offset:54272
	ds_read_b128 v[244:247], v174 offset:55296
	ds_read_b128 v[248:251], v174 offset:56320
	global_load_lds_dwordx4 v[170:171], off
	s_add_i32 m0, s16, 0x2000
	s_add_u32 s14, s14, 0x80080
	v_lshl_add_u64 v[170:171], v[176:177], 0, s[60:61]
	s_addc_u32 s15, s15, 0
	s_add_i32 s16, s89, s4
	global_load_lds_dwordx4 v[170:171], off
	v_lshl_add_u64 v[170:171], s[14:15], 0, v[148:149]
	s_mov_b32 m0, s16
	s_nop 0
	global_load_lds_dwordx4 v[170:171], off
	v_lshl_add_u64 v[170:171], s[14:15], 0, v[152:153]
	s_add_i32 m0, s16, 0x2000
	s_nop 0
	global_load_lds_dwordx4 v[170:171], off
	v_lshl_add_u64 v[170:171], v[178:179], 0, s[60:61]
	s_mov_b32 m0, s25
	s_nop 0
	global_load_lds_dwordx4 v[170:171], off
	v_lshl_add_u64 v[170:171], v[180:181], 0, s[60:61]
	s_mov_b32 m0, s0
	s_nop 0
	global_load_lds_dwordx4 v[170:171], off
	s_waitcnt vmcnt(8)
	s_waitcnt lgkmcnt(0)
	s_barrier
	s_setprio 1
	s_waitcnt lgkmcnt(0)
	v_mfma_f32_16x16x32_bf16 v[78:81], v[50:53], v[202:205], v[78:81]
	v_mfma_f32_16x16x32_bf16 v[74:77], v[66:69], v[202:205], v[74:77]
	v_mfma_f32_16x16x32_bf16 v[62:65], v[50:53], v[210:213], v[62:65]
	v_mfma_f32_16x16x32_bf16 v[58:61], v[66:69], v[210:213], v[58:61]
	v_mfma_f32_16x16x32_bf16 v[30:33], v[50:53], v[236:239], v[30:33]
	v_mfma_f32_16x16x32_bf16 v[26:29], v[66:69], v[236:239], v[26:29]
	v_mfma_f32_16x16x32_bf16 v[14:17], v[50:53], v[244:247], v[14:17]
	v_mfma_f32_16x16x32_bf16 v[10:13], v[66:69], v[244:247], v[10:13]
	v_mfma_f32_16x16x32_bf16 v[78:81], v[54:57], v[206:209], v[78:81]
	v_mfma_f32_16x16x32_bf16 v[74:77], v[70:73], v[206:209], v[74:77]
	v_mfma_f32_16x16x32_bf16 v[62:65], v[54:57], v[214:217], v[62:65]
	v_mfma_f32_16x16x32_bf16 v[58:61], v[70:73], v[214:217], v[58:61]
	v_mfma_f32_16x16x32_bf16 v[30:33], v[54:57], v[240:243], v[30:33]
	v_mfma_f32_16x16x32_bf16 v[26:29], v[70:73], v[240:243], v[26:29]
	v_mfma_f32_16x16x32_bf16 v[14:17], v[54:57], v[248:251], v[14:17]
	v_mfma_f32_16x16x32_bf16 v[10:13], v[70:73], v[248:251], v[10:13]
	s_setprio 0
	s_setprio 1
	v_mfma_f32_16x16x32_bf16 v[34:37], v[162:165], v[202:205], v[34:37]
	v_mfma_f32_16x16x32_bf16 v[70:73], v[166:169], v[206:209], v[34:37]
	v_mfma_f32_16x16x32_bf16 v[34:37], v[190:193], v[202:205], v[38:41]
	v_mfma_f32_16x16x32_bf16 v[66:69], v[198:201], v[206:209], v[34:37]
	v_mfma_f32_16x16x32_bf16 v[34:37], v[162:165], v[210:213], v[42:45]
	v_mfma_f32_16x16x32_bf16 v[54:57], v[166:169], v[214:217], v[34:37]
	v_mfma_f32_16x16x32_bf16 v[34:37], v[190:193], v[210:213], v[46:49]
	v_mfma_f32_16x16x32_bf16 v[22:25], v[162:165], v[236:239], v[22:25]
	v_mfma_f32_16x16x32_bf16 v[18:21], v[190:193], v[236:239], v[18:21]
	v_mfma_f32_16x16x32_bf16 v[6:9], v[162:165], v[244:247], v[6:9]
	v_mfma_f32_16x16x32_bf16 v[2:5], v[190:193], v[244:247], v[2:5]
	v_mfma_f32_16x16x32_bf16 v[50:53], v[198:201], v[214:217], v[34:37]
	s_setprio 0
	v_mfma_f32_16x16x32_bf16 v[22:25], v[166:169], v[240:243], v[22:25]
	v_mfma_f32_16x16x32_bf16 v[18:21], v[198:201], v[240:243], v[18:21]
	v_mfma_f32_16x16x32_bf16 v[6:9], v[166:169], v[248:251], v[6:9]
	v_mfma_f32_16x16x32_bf16 v[2:5], v[198:201], v[248:251], v[2:5]
	s_barrier
	s_add_i32 s88, s88, 2
	s_add_u32 s10, s10, 0x100
	s_addc_u32 s11, s11, 0
	s_add_u32 s86, s86, 0x100
	s_addc_u32 s87, s87, 0
	s_cmp_gt_u32 s88, 29
	s_cbranch_scc0 .LBB0_592
	s_and_b64 vcc, exec, s[26:27]
	s_cbranch_vccz .LBB0_595
	s_barrier

; #define PG8_STAGE(bufoff, gbase, voff) do { _Pragma("unroll") for (int _i = 0; _i < 2; ++_i) \
;         __builtin_amdgcn_global_load_lds((const unsigned*)((const char*)(gbase) + (voff)[_i]), (PG8_LAS unsigned*)(lds + (bufoff) + ldsw + _i * 8192), 16, 0, 0); } while (0)
; #define PG8_WAIT_V(n) asm volatile("s_waitcnt vmcnt(" #n ")" ::: "memory")
; #define PG8_WAIT_L(n) asm volatile("s_waitcnt lgkmcnt(" #n ")" ::: "memory")
; #define PG8_BAR __builtin_amdgcn_s_barrier()
; #define PG8_SCHED __builtin_amdgcn_sched_barrier(0)
; template <class Epi, class Sched, bool ALIGN_EPI, bool F8 = false>
; __device__ __forceinline__ void gemm_phase(PG8_LAS unsigned char* lds, const Gemm g, const Sched& S, const Epi& E, int tid) {
;     ...
;         for (int t = 0; t < nt; t += 2) {
;             const bool last = (t == nt - 2);
;             const char* a1 = cA + (size_t)(t + 1) * kstep;
;             const char* a2 = last ? nA : cA + (size_t)(t + 2) * kstep; const char* b2 = last ? nB : cB + (size_t)(t + 2) * kstep;
;             const char* a3 = a2 + kstep; const char* b3 = b2 + kstep;
;             if (last && has_next) S.a_ready(nxt);
;             PG8_LDB(B0, 0, 0); PG8_LDB(B1, 0, 1); PG8_SCHED; PG8_LDA(At, 0, 0); PG8_STAGE(PG8_SA(1, 1), a1 + hstepA, voffA);
;             PG8_WAIT_V(8); PG8_WAIT_L(0); PG8_BAR; PG8_MMA(0, 0, At, B0); PG8_MMA(0, 1, At, B1); PG8_BAR; PG8_SCHED;
;             PG8_LDA(At, 0, 1); PG8_STAGE(PG8_SB(0, 0), b2, voffB); PG8_STAGE(PG8_SB(0, 1), b2 + hstepB, voffB); PG8_STAGE(PG8_SA(0, 0), a2, voffA);
;             PG8_WAIT_V(8); PG8_WAIT_L(0); PG8_BAR; PG8_MMA(1, 0, At, B0); PG8_MMA(1, 1, At, B1); PG8_BAR; PG8_SCHED;
.LBB0_713:
	s_add_u32 s14, s6, 0xfffc0080
	s_addc_u32 s15, s7, -1
	s_add_i32 s85, 0, 0x10000
	s_cmp_eq_u32 s84, 12
	s_cselect_b32 s35, s4, s15
	s_cselect_b32 s34, s5, s14
	s_cselect_b32 s15, s23, s45
	s_cselect_b32 s14, s25, s44
	s_add_i32 s86, 0, 0x14000
	v_add_u32_e32 v2, s85, v198
	v_add_u32_e32 v14, s86, v198
	ds_read_b128 v[18:21], v2
	ds_read_b128 v[22:25], v2 offset:1024
	ds_read_b128 v[26:29], v2 offset:2048
	ds_read_b128 v[30:33], v2 offset:3072
	ds_read_b128 v[2:5], v14
	ds_read_b128 v[6:9], v14 offset:1024
	ds_read_b128 v[10:13], v14 offset:2048
	ds_read_b128 v[14:17], v14 offset:3072
	v_lshl_add_u64 v[176:177], s[6:7], 0, v[172:173]
	s_add_i32 m0, s39, 0xc000
	ds_read_b128 v[200:203], v199
	ds_read_b128 v[204:207], v199 offset:1024
	ds_read_b128 v[208:211], v199 offset:2048
	ds_read_b128 v[212:215], v199 offset:3072
	ds_read_b128 v[236:239], v199 offset:4096
	ds_read_b128 v[240:243], v199 offset:5120
	ds_read_b128 v[244:247], v199 offset:6144
	ds_read_b128 v[248:251], v199 offset:7168
	global_load_lds_dwordx4 v[176:177], off
	v_lshl_add_u64 v[176:177], s[6:7], 0, v[174:175]
	s_add_i32 m0, s39, 0xe000
	s_nop 0
	global_load_lds_dwordx4 v[176:177], off
	s_waitcnt vmcnt(8)
	s_waitcnt lgkmcnt(0)
	s_barrier
	s_setprio 1
	s_waitcnt lgkmcnt(0)
	v_mfma_f32_16x16x128_f8f6f4 v[158:161], v[18:25], v[200:207], v[158:161]
	v_mfma_f32_16x16x128_f8f6f4 v[154:157], v[26:33], v[200:207], v[154:157]
	v_mfma_f32_16x16x128_f8f6f4 v[142:145], v[18:25], v[208:215], v[142:145]
	v_mfma_f32_16x16x128_f8f6f4 v[138:141], v[26:33], v[208:215], v[138:141]
	v_mfma_f32_16x16x128_f8f6f4 v[126:129], v[18:25], v[236:243], v[126:129]
	v_mfma_f32_16x16x128_f8f6f4 v[122:125], v[26:33], v[236:243], v[122:125]
	v_mfma_f32_16x16x128_f8f6f4 v[110:113], v[18:25], v[244:251], v[110:113]
	v_mfma_f32_16x16x128_f8f6f4 v[106:109], v[26:33], v[244:251], v[106:109]
	s_setprio 0
	s_setprio 1
	v_mfma_f32_16x16x128_f8f6f4 v[150:153], v[2:9], v[200:207], v[150:153]
	v_mfma_f32_16x16x128_f8f6f4 v[146:149], v[10:17], v[200:207], v[146:149]
	v_mfma_f32_16x16x128_f8f6f4 v[134:137], v[2:9], v[208:215], v[134:137]
	v_mfma_f32_16x16x128_f8f6f4 v[130:133], v[10:17], v[208:215], v[130:133]
	v_mfma_f32_16x16x128_f8f6f4 v[118:121], v[2:9], v[236:243], v[118:121]
	v_mfma_f32_16x16x128_f8f6f4 v[114:117], v[10:17], v[236:243], v[114:117]
	s_setprio 0
	v_mfma_f32_16x16x128_f8f6f4 v[102:105], v[2:9], v[244:251], v[102:105]
	v_mfma_f32_16x16x128_f8f6f4 v[98:101], v[10:17], v[244:251], v[98:101]
	s_barrier
	s_add_i32 s16, s85, s38
	v_lshl_add_u64 v[176:177], s[14:15], 0, v[0:1]
	s_mov_b32 m0, s16
	ds_read_b128 v[200:203], v199 offset:16384
	ds_read_b128 v[204:207], v199 offset:17408
	ds_read_b128 v[208:211], v199 offset:18432
	ds_read_b128 v[212:215], v199 offset:19456
	ds_read_b128 v[236:239], v199 offset:20480
	ds_read_b128 v[240:243], v199 offset:21504
	ds_read_b128 v[244:247], v199 offset:22528
	ds_read_b128 v[248:251], v199 offset:23552
	global_load_lds_dwordx4 v[176:177], off
	s_add_i32 m0, s16, 0x2000
	s_add_u32 s88, s14, 0x40000
	v_lshl_add_u64 v[190:191], s[14:15], 0, v[162:163]
	s_addc_u32 s89, s15, 0
	s_add_i32 s16, s86, s38
	global_load_lds_dwordx4 v[190:191], off
	v_lshl_add_u64 v[178:179], s[88:89], 0, v[0:1]
	s_mov_b32 m0, s16
	v_lshl_add_u64 v[192:193], s[34:35], 0, v[166:167]
	global_load_lds_dwordx4 v[178:179], off
	v_lshl_add_u64 v[178:179], s[88:89], 0, v[162:163]
	s_add_i32 m0, s16, 0x2000
	v_lshl_add_u64 v[194:195], s[34:35], 0, v[164:165]
	global_load_lds_dwordx4 v[178:179], off
	s_mov_b32 m0, s39
	s_nop 0
	global_load_lds_dwordx4 v[192:193], off
	s_mov_b32 m0, s50
	s_nop 0
	global_load_lds_dwordx4 v[194:195], off
	s_waitcnt vmcnt(8)
	s_waitcnt lgkmcnt(0)
	s_barrier
	s_setprio 1
	s_waitcnt lgkmcnt(0)
	v_mfma_f32_16x16x128_f8f6f4 v[94:97], v[18:25], v[200:207], v[94:97]
	v_mfma_f32_16x16x128_f8f6f4 v[90:93], v[26:33], v[200:207], v[90:93]
	v_mfma_f32_16x16x128_f8f6f4 v[78:81], v[18:25], v[208:215], v[78:81]
	v_mfma_f32_16x16x128_f8f6f4 v[74:77], v[26:33], v[208:215], v[74:77]
	v_mfma_f32_16x16x128_f8f6f4 v[62:65], v[18:25], v[236:243], v[62:65]
	v_mfma_f32_16x16x128_f8f6f4 v[58:61], v[26:33], v[236:243], v[58:61]
	v_mfma_f32_16x16x128_f8f6f4 v[46:49], v[18:25], v[244:251], v[46:49]
	v_mfma_f32_16x16x128_f8f6f4 v[42:45], v[26:33], v[244:251], v[42:45]
	s_setprio 0
	s_setprio 1
	v_mfma_f32_16x16x128_f8f6f4 v[86:89], v[2:9], v[200:207], v[86:89]
	v_mfma_f32_16x16x128_f8f6f4 v[82:85], v[10:17], v[200:207], v[82:85]
	v_mfma_f32_16x16x128_f8f6f4 v[70:73], v[2:9], v[208:215], v[70:73]
	v_mfma_f32_16x16x128_f8f6f4 v[66:69], v[10:17], v[208:215], v[66:69]
	v_mfma_f32_16x16x128_f8f6f4 v[54:57], v[2:9], v[236:243], v[54:57]
	v_mfma_f32_16x16x128_f8f6f4 v[50:53], v[10:17], v[236:243], v[50:53]
	s_setprio 0
	v_mfma_f32_16x16x128_f8f6f4 v[38:41], v[2:9], v[244:251], v[38:41]
	v_mfma_f32_16x16x128_f8f6f4 v[34:37], v[10:17], v[244:251], v[34:37]
	s_barrier
; #define PG8_STAGE(bufoff, gbase, voff) do { _Pragma("unroll") for (int _i = 0; _i < 2; ++_i) \
;         __builtin_amdgcn_global_load_lds((const unsigned*)((const char*)(gbase) + (voff)[_i]), (PG8_LAS unsigned*)(lds + (bufoff) + ldsw + _i * 8192), 16, 0, 0); } while (0)
; #define PG8_WAIT_V(n) asm volatile("s_waitcnt vmcnt(" #n ")" ::: "memory")
; #define PG8_WAIT_L(n) asm volatile("s_waitcnt lgkmcnt(" #n ")" ::: "memory")
; #define PG8_BAR __builtin_amdgcn_s_barrier()
; #define PG8_SCHED __builtin_amdgcn_sched_barrier(0)
; template <class Epi, class Sched, bool ALIGN_EPI, bool F8 = false>
; __device__ __forceinline__ void gemm_phase(PG8_LAS unsigned char* lds, const Gemm g, const Sched& S, const Epi& E, int tid) {
;     ...
;             PG8_LDB(B0, 1, 0); PG8_LDB(B1, 1, 1); PG8_SCHED; PG8_LDA(At, 1, 0); PG8_STAGE(PG8_SA(0, 1), a2 + hstepA, voffA);
;             PG8_WAIT_V(8); PG8_WAIT_L(0); PG8_BAR; PG8_MMA(0, 0, At, B0); PG8_MMA(0, 1, At, B1); PG8_BAR; PG8_SCHED;
;             PG8_LDA(At, 1, 1); PG8_STAGE(PG8_SB(1, 0), b3, voffB); PG8_STAGE(PG8_SB(1, 1), b3 + hstepB, voffB); PG8_STAGE(PG8_SA(1, 0), a3, voffA);
;             PG8_WAIT_V(8); PG8_WAIT_L(0); PG8_BAR; PG8_MMA(1, 0, At, B0); PG8_MMA(1, 1, At, B1); PG8_BAR; PG8_SCHED;
;         }
;         if constexpr (ALIGN_EPI) { if (wr == 0) PG8_BAR; }
	s_add_i32 s16, 0, 0x18000
	s_add_i32 s85, 0, 0x1c000
	v_add_u32_e32 v14, s16, v198
	v_add_u32_e32 v30, s85, v198
	ds_read_b128 v[2:5], v14
	ds_read_b128 v[6:9], v14 offset:1024
	ds_read_b128 v[10:13], v14 offset:2048
	ds_read_b128 v[14:17], v14 offset:3072
	ds_read_b128 v[18:21], v30
	ds_read_b128 v[22:25], v30 offset:1024
	ds_read_b128 v[26:29], v30 offset:2048
	ds_read_b128 v[30:33], v30 offset:3072
	s_add_u32 s34, s34, 0x40000
	s_addc_u32 s35, s35, 0
	s_mov_b32 m0, s51
	v_lshl_add_u64 v[178:179], s[34:35], 0, v[166:167]
	ds_read_b128 v[200:203], v199 offset:32768
	ds_read_b128 v[204:207], v199 offset:33792
	ds_read_b128 v[208:211], v199 offset:34816
	ds_read_b128 v[212:215], v199 offset:35840
	ds_read_b128 v[236:239], v199 offset:36864
	ds_read_b128 v[240:243], v199 offset:37888
	ds_read_b128 v[244:247], v199 offset:38912
	ds_read_b128 v[248:251], v199 offset:39936
	global_load_lds_dwordx4 v[178:179], off
	v_lshl_add_u64 v[178:179], s[34:35], 0, v[164:165]
	s_mov_b32 m0, s68
	s_nop 0
	global_load_lds_dwordx4 v[178:179], off
	s_waitcnt vmcnt(8)
	s_waitcnt lgkmcnt(0)
	s_barrier
	s_setprio 1
	s_waitcnt lgkmcnt(0)
	v_mfma_f32_16x16x128_f8f6f4 v[158:161], v[2:9], v[200:207], v[158:161]
	v_mfma_f32_16x16x128_f8f6f4 v[154:157], v[10:17], v[200:207], v[154:157]
	v_mfma_f32_16x16x128_f8f6f4 v[142:145], v[2:9], v[208:215], v[142:145]
	v_mfma_f32_16x16x128_f8f6f4 v[138:141], v[10:17], v[208:215], v[138:141]
	v_mfma_f32_16x16x128_f8f6f4 v[126:129], v[2:9], v[236:243], v[126:129]
	v_mfma_f32_16x16x128_f8f6f4 v[122:125], v[10:17], v[236:243], v[122:125]
	v_mfma_f32_16x16x128_f8f6f4 v[110:113], v[2:9], v[244:251], v[110:113]
	v_mfma_f32_16x16x128_f8f6f4 v[106:109], v[10:17], v[244:251], v[106:109]
	s_setprio 0
	s_setprio 1
	v_mfma_f32_16x16x128_f8f6f4 v[150:153], v[18:25], v[200:207], v[150:153]
	v_mfma_f32_16x16x128_f8f6f4 v[146:149], v[26:33], v[200:207], v[146:149]
	v_mfma_f32_16x16x128_f8f6f4 v[134:137], v[18:25], v[208:215], v[134:137]
	v_mfma_f32_16x16x128_f8f6f4 v[130:133], v[26:33], v[208:215], v[130:133]
	v_mfma_f32_16x16x128_f8f6f4 v[118:121], v[18:25], v[236:243], v[118:121]
	v_mfma_f32_16x16x128_f8f6f4 v[114:117], v[26:33], v[236:243], v[114:117]
	s_setprio 0
	v_mfma_f32_16x16x128_f8f6f4 v[102:105], v[18:25], v[244:251], v[102:105]
	v_mfma_f32_16x16x128_f8f6f4 v[98:101], v[26:33], v[244:251], v[98:101]
	s_barrier
	s_add_i32 s16, s16, s38
	v_lshl_add_u64 v[176:177], v[176:177], 0, s[60:61]
	s_mov_b32 m0, s16
	ds_read_b128 v[200:203], v199 offset:49152
	ds_read_b128 v[204:207], v199 offset:50176
	ds_read_b128 v[208:211], v199 offset:51200
	ds_read_b128 v[212:215], v199 offset:52224
	ds_read_b128 v[236:239], v199 offset:53248
	ds_read_b128 v[240:243], v199 offset:54272
	ds_read_b128 v[244:247], v199 offset:55296
	ds_read_b128 v[248:251], v199 offset:56320
	global_load_lds_dwordx4 v[176:177], off
	s_add_i32 m0, s16, 0x2000
	s_add_u32 s14, s14, 0x40080
	v_lshl_add_u64 v[176:177], v[190:191], 0, s[60:61]
	s_addc_u32 s15, s15, 0
	s_add_i32 s16, s85, s38
	global_load_lds_dwordx4 v[176:177], off
	v_lshl_add_u64 v[176:177], s[14:15], 0, v[0:1]
	s_mov_b32 m0, s16
	s_nop 0
	global_load_lds_dwordx4 v[176:177], off
	v_lshl_add_u64 v[176:177], s[14:15], 0, v[162:163]
	s_add_i32 m0, s16, 0x2000
	s_nop 0
	global_load_lds_dwordx4 v[176:177], off
	v_lshl_add_u64 v[176:177], v[192:193], 0, s[60:61]
	s_mov_b32 m0, s69
	s_nop 0
	global_load_lds_dwordx4 v[176:177], off
	v_lshl_add_u64 v[176:177], v[194:195], 0, s[60:61]
	s_mov_b32 m0, s82
	s_nop 0
	global_load_lds_dwordx4 v[176:177], off
	s_waitcnt vmcnt(8)
	s_waitcnt lgkmcnt(0)
	s_barrier
	s_setprio 1
	s_waitcnt lgkmcnt(0)
	v_mfma_f32_16x16x128_f8f6f4 v[94:97], v[2:9], v[200:207], v[94:97]
	v_mfma_f32_16x16x128_f8f6f4 v[90:93], v[10:17], v[200:207], v[90:93]
	v_mfma_f32_16x16x128_f8f6f4 v[78:81], v[2:9], v[208:215], v[78:81]
	v_mfma_f32_16x16x128_f8f6f4 v[74:77], v[10:17], v[208:215], v[74:77]
	v_mfma_f32_16x16x128_f8f6f4 v[62:65], v[2:9], v[236:243], v[62:65]
	v_mfma_f32_16x16x128_f8f6f4 v[58:61], v[10:17], v[236:243], v[58:61]
	v_mfma_f32_16x16x128_f8f6f4 v[46:49], v[2:9], v[244:251], v[46:49]
	v_mfma_f32_16x16x128_f8f6f4 v[42:45], v[10:17], v[244:251], v[42:45]
	s_setprio 0
	s_setprio 1
	v_mfma_f32_16x16x128_f8f6f4 v[86:89], v[18:25], v[200:207], v[86:89]
	v_mfma_f32_16x16x128_f8f6f4 v[82:85], v[26:33], v[200:207], v[82:85]
	v_mfma_f32_16x16x128_f8f6f4 v[70:73], v[18:25], v[208:215], v[70:73]
	v_mfma_f32_16x16x128_f8f6f4 v[66:69], v[26:33], v[208:215], v[66:69]
	v_mfma_f32_16x16x128_f8f6f4 v[54:57], v[18:25], v[236:243], v[54:57]
	v_mfma_f32_16x16x128_f8f6f4 v[50:53], v[26:33], v[236:243], v[50:53]
	s_setprio 0
	v_mfma_f32_16x16x128_f8f6f4 v[38:41], v[18:25], v[244:251], v[38:41]
	v_mfma_f32_16x16x128_f8f6f4 v[34:37], v[26:33], v[244:251], v[34:37]
	s_barrier
	s_add_i32 s84, s84, 2
	s_add_u32 s6, s6, 0x100
	s_addc_u32 s7, s7, 0
	s_add_u32 s44, s44, 0x100
	s_addc_u32 s45, s45, 0
	s_cmp_gt_u32 s84, 13
	s_cbranch_scc0 .LBB0_713
	s_and_b64 vcc, exec, s[10:11]
	s_movk_i32 s84, 0x2000
	s_cbranch_vccz .LBB0_716
	s_barrier

; #define PG8_STAGE(bufoff, gbase, voff) do { _Pragma("unroll") for (int _i = 0; _i < 2; ++_i) \
;         __builtin_amdgcn_global_load_lds((const unsigned*)((const char*)(gbase) + (voff)[_i]), (PG8_LAS unsigned*)(lds + (bufoff) + ldsw + _i * 8192), 16, 0, 0); } while (0)
; #define PG8_WAIT_V(n) asm volatile("s_waitcnt vmcnt(" #n ")" ::: "memory")
; #define PG8_WAIT_L(n) asm volatile("s_waitcnt lgkmcnt(" #n ")" ::: "memory")
; #define PG8_BAR __builtin_amdgcn_s_barrier()
; #define PG8_SCHED __builtin_amdgcn_sched_barrier(0)
; template <class Epi, class Sched, bool ALIGN_EPI, bool F8 = false>
; __device__ __forceinline__ void gemm_phase(PG8_LAS unsigned char* lds, const Gemm g, const Sched& S, const Epi& E, int tid) {
;     ...
;         for (int t = 0; t < nt; t += 2) {
;             const bool last = (t == nt - 2);
;             const char* a1 = cA + (size_t)(t + 1) * kstep;
;             const char* a2 = last ? nA : cA + (size_t)(t + 2) * kstep; const char* b2 = last ? nB : cB + (size_t)(t + 2) * kstep;
;             const char* a3 = a2 + kstep; const char* b3 = b2 + kstep;
;             if (last && has_next) S.a_ready(nxt);
;             PG8_LDB(B0, 0, 0); PG8_LDB(B1, 0, 1); PG8_SCHED; PG8_LDA(At, 0, 0); PG8_STAGE(PG8_SA(1, 1), a1 + hstepA, voffA);
;             PG8_WAIT_V(8); PG8_WAIT_L(0); PG8_BAR; PG8_MMA(0, 0, At, B0); PG8_MMA(0, 1, At, B1); PG8_BAR; PG8_SCHED;
;             PG8_LDA(At, 0, 1); PG8_STAGE(PG8_SB(0, 0), b2, voffB); PG8_STAGE(PG8_SB(0, 1), b2 + hstepB, voffB); PG8_STAGE(PG8_SA(0, 0), a2, voffA);
.LBB0_739:
	s_add_u32 s14, s50, 0xfff80080
	s_addc_u32 s15, s51, -1
	s_add_i32 s84, 0, 0x10000
	s_cmp_eq_u32 s83, 28
	s_cselect_b32 s69, s5, s15
	s_cselect_b32 s68, s7, s14
	v_add_u32_e32 v0, s84, v173
	s_cselect_b32 s15, s23, s82
	s_cselect_b32 s14, s25, s45
	s_add_i32 vcc_lo, 0, 0x14000
	ds_read_b128 v[54:57], v0
	ds_read_b128 v[62:65], v0 offset:1024
	ds_read_b128 v[66:69], v0 offset:2048
	ds_read_b128 v[70:73], v0 offset:3072
	v_add_u32_e32 v0, vcc_lo, v173
	ds_read_b128 v[162:165], v0
	ds_read_b128 v[166:169], v0 offset:1024
	ds_read_b128 v[190:193], v0 offset:2048
	ds_read_b128 v[198:201], v0 offset:3072
	v_lshl_add_u64 v[170:171], s[50:51], 0, v[158:159]
	s_add_i32 m0, s1, 0xc000
	ds_read_b128 v[202:205], v175
	ds_read_b128 v[206:209], v175 offset:1024
	ds_read_b128 v[210:213], v175 offset:2048
	ds_read_b128 v[214:217], v175 offset:3072
	ds_read_b128 v[236:239], v175 offset:4096
	ds_read_b128 v[240:243], v175 offset:5120
	ds_read_b128 v[244:247], v175 offset:6144
	ds_read_b128 v[248:251], v175 offset:7168
	global_load_lds_dwordx4 v[170:171], off
	v_lshl_add_u64 v[170:171], s[50:51], 0, v[160:161]
	s_add_i32 m0, s1, 0xe000
	s_nop 0
	global_load_lds_dwordx4 v[170:171], off
	s_waitcnt vmcnt(8)
	s_waitcnt lgkmcnt(0)
	s_barrier
	s_setprio 1
	s_waitcnt lgkmcnt(0)
	v_mfma_f32_16x16x32_bf16 v[142:145], v[54:57], v[202:205], v[142:145]
	v_mfma_f32_16x16x32_bf16 v[138:141], v[66:69], v[202:205], v[138:141]
	v_mfma_f32_16x16x32_bf16 v[126:129], v[54:57], v[210:213], v[126:129]
	v_mfma_f32_16x16x32_bf16 v[122:125], v[66:69], v[210:213], v[122:125]
	v_mfma_f32_16x16x32_bf16 v[110:113], v[54:57], v[236:239], v[110:113]
	v_mfma_f32_16x16x32_bf16 v[106:109], v[66:69], v[236:239], v[106:109]
	v_mfma_f32_16x16x32_bf16 v[94:97], v[54:57], v[244:247], v[94:97]
	v_mfma_f32_16x16x32_bf16 v[90:93], v[66:69], v[244:247], v[90:93]
	v_mfma_f32_16x16x32_bf16 v[142:145], v[62:65], v[206:209], v[142:145]
	v_mfma_f32_16x16x32_bf16 v[138:141], v[70:73], v[206:209], v[138:141]
	v_mfma_f32_16x16x32_bf16 v[126:129], v[62:65], v[214:217], v[126:129]
	v_mfma_f32_16x16x32_bf16 v[122:125], v[70:73], v[214:217], v[122:125]
	v_mfma_f32_16x16x32_bf16 v[110:113], v[62:65], v[240:243], v[110:113]
	v_mfma_f32_16x16x32_bf16 v[106:109], v[70:73], v[240:243], v[106:109]
	v_mfma_f32_16x16x32_bf16 v[94:97], v[62:65], v[248:251], v[94:97]
	v_mfma_f32_16x16x32_bf16 v[90:93], v[70:73], v[248:251], v[90:93]
	s_setprio 0
	s_setprio 1
	v_mfma_f32_16x16x32_bf16 v[134:137], v[162:165], v[202:205], v[134:137]
	v_mfma_f32_16x16x32_bf16 v[130:133], v[190:193], v[202:205], v[130:133]
	v_mfma_f32_16x16x32_bf16 v[118:121], v[162:165], v[210:213], v[118:121]
	v_mfma_f32_16x16x32_bf16 v[114:117], v[190:193], v[210:213], v[114:117]
	v_mfma_f32_16x16x32_bf16 v[102:105], v[162:165], v[236:239], v[102:105]
	v_mfma_f32_16x16x32_bf16 v[98:101], v[190:193], v[236:239], v[98:101]
	v_mfma_f32_16x16x32_bf16 v[86:89], v[162:165], v[244:247], v[86:89]
	v_mfma_f32_16x16x32_bf16 v[82:85], v[190:193], v[244:247], v[82:85]
	v_mfma_f32_16x16x32_bf16 v[134:137], v[166:169], v[206:209], v[134:137]
	v_mfma_f32_16x16x32_bf16 v[130:133], v[198:201], v[206:209], v[130:133]
	v_mfma_f32_16x16x32_bf16 v[118:121], v[166:169], v[214:217], v[118:121]
	v_mfma_f32_16x16x32_bf16 v[114:117], v[198:201], v[214:217], v[114:117]
	s_setprio 0
	v_mfma_f32_16x16x32_bf16 v[102:105], v[166:169], v[240:243], v[102:105]
	v_mfma_f32_16x16x32_bf16 v[98:101], v[198:201], v[240:243], v[98:101]
	v_mfma_f32_16x16x32_bf16 v[86:89], v[166:169], v[248:251], v[86:89]
	v_mfma_f32_16x16x32_bf16 v[82:85], v[198:201], v[248:251], v[82:85]
	s_barrier
	s_add_i32 s84, s84, s0
	v_lshl_add_u64 v[170:171], s[14:15], 0, v[148:149]
	s_mov_b32 m0, s84
	ds_read_b128 v[202:205], v175 offset:16384
	ds_read_b128 v[206:209], v175 offset:17408
	ds_read_b128 v[210:213], v175 offset:18432
	ds_read_b128 v[214:217], v175 offset:19456
	ds_read_b128 v[236:239], v175 offset:20480
	ds_read_b128 v[240:243], v175 offset:21504
	ds_read_b128 v[244:247], v175 offset:22528
	ds_read_b128 v[248:251], v175 offset:23552
	global_load_lds_dwordx4 v[170:171], off
	s_add_i32 m0, s84, 0x2000
	s_add_u32 s84, s14, 0x80000
	v_lshl_add_u64 v[176:177], s[14:15], 0, v[152:153]
	s_addc_u32 s85, s15, 0
	s_add_i32 vcc_lo, vcc_lo, s0
	global_load_lds_dwordx4 v[176:177], off
	v_lshl_add_u64 v[178:179], s[84:85], 0, v[148:149]
	s_mov_b32 m0, vcc_lo
	v_lshl_add_u64 v[180:181], s[68:69], 0, v[150:151]
	global_load_lds_dwordx4 v[178:179], off
	v_lshl_add_u64 v[178:179], s[84:85], 0, v[152:153]
	s_add_i32 m0, vcc_lo, 0x2000
	s_nop 0
	global_load_lds_dwordx4 v[178:179], off
	v_lshl_add_u64 v[178:179], s[68:69], 0, v[146:147]
	s_mov_b32 m0, s1
	s_nop 0
	global_load_lds_dwordx4 v[178:179], off
	s_mov_b32 m0, s44
	s_nop 0
	global_load_lds_dwordx4 v[180:181], off
	s_waitcnt vmcnt(8)
	s_waitcnt lgkmcnt(0)
	s_barrier
; #define PG8_STAGE(bufoff, gbase, voff) do { _Pragma("unroll") for (int _i = 0; _i < 2; ++_i) \
;         __builtin_amdgcn_global_load_lds((const unsigned*)((const char*)(gbase) + (voff)[_i]), (PG8_LAS unsigned*)(lds + (bufoff) + ldsw + _i * 8192), 16, 0, 0); } while (0)
; #define PG8_WAIT_V(n) asm volatile("s_waitcnt vmcnt(" #n ")" ::: "memory")
; #define PG8_WAIT_L(n) asm volatile("s_waitcnt lgkmcnt(" #n ")" ::: "memory")
; #define PG8_BAR __builtin_amdgcn_s_barrier()
; #define PG8_SCHED __builtin_amdgcn_sched_barrier(0)
; template <class Epi, class Sched, bool ALIGN_EPI, bool F8 = false>
; __device__ __forceinline__ void gemm_phase(PG8_LAS unsigned char* lds, const Gemm g, const Sched& S, const Epi& E, int tid) {
;     ...
;             PG8_WAIT_V(8); PG8_WAIT_L(0); PG8_BAR; PG8_MMA(1, 0, At, B0); PG8_MMA(1, 1, At, B1); PG8_BAR; PG8_SCHED;
;             PG8_LDB(B0, 1, 0); PG8_LDB(B1, 1, 1); PG8_SCHED; PG8_LDA(At, 1, 0); PG8_STAGE(PG8_SA(0, 1), a2 + hstepA, voffA);
;             PG8_WAIT_V(8); PG8_WAIT_L(0); PG8_BAR; PG8_MMA(0, 0, At, B0); PG8_MMA(0, 1, At, B1); PG8_BAR; PG8_SCHED;
	s_setprio 1
	s_waitcnt lgkmcnt(0)
	v_mfma_f32_16x16x32_bf16 v[78:81], v[54:57], v[202:205], v[78:81]
	v_mfma_f32_16x16x32_bf16 v[74:77], v[66:69], v[202:205], v[74:77]
	v_mfma_f32_16x16x32_bf16 v[46:49], v[54:57], v[210:213], v[46:49]
	v_mfma_f32_16x16x32_bf16 v[42:45], v[66:69], v[210:213], v[42:45]
	v_mfma_f32_16x16x32_bf16 v[30:33], v[54:57], v[236:239], v[30:33]
	v_mfma_f32_16x16x32_bf16 v[26:29], v[66:69], v[236:239], v[26:29]
	v_mfma_f32_16x16x32_bf16 v[14:17], v[54:57], v[244:247], v[14:17]
	v_mfma_f32_16x16x32_bf16 v[10:13], v[66:69], v[244:247], v[10:13]
	v_mfma_f32_16x16x32_bf16 v[78:81], v[62:65], v[206:209], v[78:81]
	v_mfma_f32_16x16x32_bf16 v[74:77], v[70:73], v[206:209], v[74:77]
	v_mfma_f32_16x16x32_bf16 v[46:49], v[62:65], v[214:217], v[46:49]
	v_mfma_f32_16x16x32_bf16 v[42:45], v[70:73], v[214:217], v[42:45]
	v_mfma_f32_16x16x32_bf16 v[30:33], v[62:65], v[240:243], v[30:33]
	v_mfma_f32_16x16x32_bf16 v[26:29], v[70:73], v[240:243], v[26:29]
	v_mfma_f32_16x16x32_bf16 v[14:17], v[62:65], v[248:251], v[14:17]
	v_mfma_f32_16x16x32_bf16 v[10:13], v[70:73], v[248:251], v[10:13]
	s_setprio 0
	s_setprio 1
	v_mfma_f32_16x16x32_bf16 v[50:53], v[190:193], v[202:205], v[50:53]
	v_mfma_f32_16x16x32_bf16 v[38:41], v[162:165], v[210:213], v[38:41]
	v_mfma_f32_16x16x32_bf16 v[34:37], v[190:193], v[210:213], v[34:37]
	v_mfma_f32_16x16x32_bf16 v[22:25], v[162:165], v[236:239], v[22:25]
	v_mfma_f32_16x16x32_bf16 v[18:21], v[190:193], v[236:239], v[18:21]
	v_mfma_f32_16x16x32_bf16 v[6:9], v[162:165], v[244:247], v[6:9]
	v_mfma_f32_16x16x32_bf16 v[2:5], v[190:193], v[244:247], v[2:5]
	v_mfma_f32_16x16x32_bf16 v[54:57], v[162:165], v[202:205], v[58:61]
	v_mfma_f32_16x16x32_bf16 v[50:53], v[198:201], v[206:209], v[50:53]
	v_mfma_f32_16x16x32_bf16 v[38:41], v[166:169], v[214:217], v[38:41]
	v_mfma_f32_16x16x32_bf16 v[34:37], v[198:201], v[214:217], v[34:37]
	v_mfma_f32_16x16x32_bf16 v[22:25], v[166:169], v[240:243], v[22:25]
	s_setprio 0
	v_mfma_f32_16x16x32_bf16 v[18:21], v[198:201], v[240:243], v[18:21]
	v_mfma_f32_16x16x32_bf16 v[6:9], v[166:169], v[248:251], v[6:9]
	v_mfma_f32_16x16x32_bf16 v[2:5], v[198:201], v[248:251], v[2:5]
	v_mfma_f32_16x16x32_bf16 v[54:57], v[166:169], v[206:209], v[54:57]
	s_barrier
	s_add_i32 s84, 0, 0x18000
	v_add_u32_e32 v0, s84, v173
	s_add_i32 s85, 0, 0x1c000
	ds_read_b128 v[58:61], v0
	ds_read_b128 v[62:65], v0 offset:1024
	ds_read_b128 v[66:69], v0 offset:2048
	ds_read_b128 v[70:73], v0 offset:3072
	v_add_u32_e32 v0, s85, v173
	ds_read_b128 v[162:165], v0
	ds_read_b128 v[166:169], v0 offset:1024
	ds_read_b128 v[190:193], v0 offset:2048
	ds_read_b128 v[198:201], v0 offset:3072
	s_add_u32 s68, s68, 0x80000
	s_addc_u32 s69, s69, 0
	s_mov_b32 m0, s86
	v_lshl_add_u64 v[182:183], s[68:69], 0, v[146:147]
	ds_read_b128 v[202:205], v175 offset:32768
	ds_read_b128 v[206:209], v175 offset:33792
	ds_read_b128 v[210:213], v175 offset:34816
	ds_read_b128 v[214:217], v175 offset:35840
	ds_read_b128 v[236:239], v175 offset:36864
	ds_read_b128 v[240:243], v175 offset:37888
	ds_read_b128 v[244:247], v175 offset:38912
	ds_read_b128 v[248:251], v175 offset:39936
	global_load_lds_dwordx4 v[182:183], off
	v_lshl_add_u64 v[182:183], s[68:69], 0, v[150:151]
	s_mov_b32 m0, s87
	s_nop 0
	global_load_lds_dwordx4 v[182:183], off
	s_waitcnt vmcnt(8)
	s_waitcnt lgkmcnt(0)
	s_barrier
	s_setprio 1
	s_waitcnt lgkmcnt(0)
	v_mfma_f32_16x16x32_bf16 v[142:145], v[58:61], v[202:205], v[142:145]
	v_mfma_f32_16x16x32_bf16 v[138:141], v[66:69], v[202:205], v[138:141]
	v_mfma_f32_16x16x32_bf16 v[126:129], v[58:61], v[210:213], v[126:129]
	v_mfma_f32_16x16x32_bf16 v[122:125], v[66:69], v[210:213], v[122:125]
	v_mfma_f32_16x16x32_bf16 v[110:113], v[58:61], v[236:239], v[110:113]
	v_mfma_f32_16x16x32_bf16 v[106:109], v[66:69], v[236:239], v[106:109]
	v_mfma_f32_16x16x32_bf16 v[94:97], v[58:61], v[244:247], v[94:97]
	v_mfma_f32_16x16x32_bf16 v[90:93], v[66:69], v[244:247], v[90:93]
	v_mfma_f32_16x16x32_bf16 v[142:145], v[62:65], v[206:209], v[142:145]
	v_mfma_f32_16x16x32_bf16 v[138:141], v[70:73], v[206:209], v[138:141]
	v_mfma_f32_16x16x32_bf16 v[126:129], v[62:65], v[214:217], v[126:129]
	v_mfma_f32_16x16x32_bf16 v[122:125], v[70:73], v[214:217], v[122:125]
	v_mfma_f32_16x16x32_bf16 v[110:113], v[62:65], v[240:243], v[110:113]
	v_mfma_f32_16x16x32_bf16 v[106:109], v[70:73], v[240:243], v[106:109]
	v_mfma_f32_16x16x32_bf16 v[94:97], v[62:65], v[248:251], v[94:97]
	v_mfma_f32_16x16x32_bf16 v[90:93], v[70:73], v[248:251], v[90:93]
	s_setprio 0
	s_setprio 1
	v_mfma_f32_16x16x32_bf16 v[134:137], v[162:165], v[202:205], v[134:137]
	v_mfma_f32_16x16x32_bf16 v[130:133], v[190:193], v[202:205], v[130:133]
	v_mfma_f32_16x16x32_bf16 v[118:121], v[162:165], v[210:213], v[118:121]
	v_mfma_f32_16x16x32_bf16 v[114:117], v[190:193], v[210:213], v[114:117]
	v_mfma_f32_16x16x32_bf16 v[102:105], v[162:165], v[236:239], v[102:105]
	v_mfma_f32_16x16x32_bf16 v[98:101], v[190:193], v[236:239], v[98:101]
	v_mfma_f32_16x16x32_bf16 v[86:89], v[162:165], v[244:247], v[86:89]
	v_mfma_f32_16x16x32_bf16 v[82:85], v[190:193], v[244:247], v[82:85]
	v_mfma_f32_16x16x32_bf16 v[134:137], v[166:169], v[206:209], v[134:137]
	v_mfma_f32_16x16x32_bf16 v[130:133], v[198:201], v[206:209], v[130:133]
	v_mfma_f32_16x16x32_bf16 v[118:121], v[166:169], v[214:217], v[118:121]
	v_mfma_f32_16x16x32_bf16 v[114:117], v[198:201], v[214:217], v[114:117]
	s_setprio 0
	v_mfma_f32_16x16x32_bf16 v[102:105], v[166:169], v[240:243], v[102:105]
	v_mfma_f32_16x16x32_bf16 v[98:101], v[198:201], v[240:243], v[98:101]
	v_mfma_f32_16x16x32_bf16 v[86:89], v[166:169], v[248:251], v[86:89]
	v_mfma_f32_16x16x32_bf16 v[82:85], v[198:201], v[248:251], v[82:85]
	s_barrier
; #define PG8_STAGE(bufoff, gbase, voff) do { _Pragma("unroll") for (int _i = 0; _i < 2; ++_i) \
;         __builtin_amdgcn_global_load_lds((const unsigned*)((const char*)(gbase) + (voff)[_i]), (PG8_LAS unsigned*)(lds + (bufoff) + ldsw + _i * 8192), 16, 0, 0); } while (0)
; #define PG8_WAIT_V(n) asm volatile("s_waitcnt vmcnt(" #n ")" ::: "memory")
; #define PG8_WAIT_L(n) asm volatile("s_waitcnt lgkmcnt(" #n ")" ::: "memory")
; #define PG8_BAR __builtin_amdgcn_s_barrier()
; #define PG8_SCHED __builtin_amdgcn_sched_barrier(0)
; template <class Epi, class Sched, bool ALIGN_EPI, bool F8 = false>
; __device__ __forceinline__ void gemm_phase(PG8_LAS unsigned char* lds, const Gemm g, const Sched& S, const Epi& E, int tid) {
;     ...
;             PG8_LDA(At, 1, 1); PG8_STAGE(PG8_SB(1, 0), b3, voffB); PG8_STAGE(PG8_SB(1, 1), b3 + hstepB, voffB); PG8_STAGE(PG8_SA(1, 0), a3, voffA);
;             PG8_WAIT_V(8); PG8_WAIT_L(0); PG8_BAR; PG8_MMA(1, 0, At, B0); PG8_MMA(1, 1, At, B1); PG8_BAR; PG8_SCHED;
;         }
;         if constexpr (ALIGN_EPI) { if (wr == 0) PG8_BAR; }
	s_add_i32 s68, s84, s0
	v_lshl_add_u64 v[170:171], v[170:171], 0, s[60:61]
	s_mov_b32 m0, s68
	ds_read_b128 v[202:205], v175 offset:49152
	ds_read_b128 v[206:209], v175 offset:50176
	ds_read_b128 v[210:213], v175 offset:51200
	ds_read_b128 v[214:217], v175 offset:52224
	ds_read_b128 v[236:239], v175 offset:53248
	ds_read_b128 v[240:243], v175 offset:54272
	ds_read_b128 v[244:247], v175 offset:55296
	ds_read_b128 v[248:251], v175 offset:56320
	global_load_lds_dwordx4 v[170:171], off
	s_add_i32 m0, s68, 0x2000
	s_add_u32 s14, s14, 0x80080
	v_lshl_add_u64 v[170:171], v[176:177], 0, s[60:61]
	s_addc_u32 s15, s15, 0
	s_add_i32 s68, s85, s0
	global_load_lds_dwordx4 v[170:171], off
	v_lshl_add_u64 v[170:171], s[14:15], 0, v[148:149]
	s_mov_b32 m0, s68
	s_nop 0
	global_load_lds_dwordx4 v[170:171], off
	v_lshl_add_u64 v[170:171], s[14:15], 0, v[152:153]
	s_add_i32 m0, s68, 0x2000
	s_nop 0
	global_load_lds_dwordx4 v[170:171], off
	v_lshl_add_u64 v[170:171], v[178:179], 0, s[60:61]
	s_mov_b32 m0, s88
	s_nop 0
	global_load_lds_dwordx4 v[170:171], off
	v_lshl_add_u64 v[170:171], v[180:181], 0, s[60:61]
	s_mov_b32 m0, s89
	s_nop 0
	global_load_lds_dwordx4 v[170:171], off
	s_waitcnt vmcnt(8)
	s_waitcnt lgkmcnt(0)
	s_barrier
	s_setprio 1
	s_waitcnt lgkmcnt(0)
	v_mfma_f32_16x16x32_bf16 v[78:81], v[58:61], v[202:205], v[78:81]
	v_mfma_f32_16x16x32_bf16 v[74:77], v[66:69], v[202:205], v[74:77]
	v_mfma_f32_16x16x32_bf16 v[46:49], v[58:61], v[210:213], v[46:49]
	v_mfma_f32_16x16x32_bf16 v[42:45], v[66:69], v[210:213], v[42:45]
	v_mfma_f32_16x16x32_bf16 v[30:33], v[58:61], v[236:239], v[30:33]
	v_mfma_f32_16x16x32_bf16 v[26:29], v[66:69], v[236:239], v[26:29]
	v_mfma_f32_16x16x32_bf16 v[14:17], v[58:61], v[244:247], v[14:17]
	v_mfma_f32_16x16x32_bf16 v[10:13], v[66:69], v[244:247], v[10:13]
	v_mfma_f32_16x16x32_bf16 v[78:81], v[62:65], v[206:209], v[78:81]
	v_mfma_f32_16x16x32_bf16 v[74:77], v[70:73], v[206:209], v[74:77]
	v_mfma_f32_16x16x32_bf16 v[46:49], v[62:65], v[214:217], v[46:49]
	v_mfma_f32_16x16x32_bf16 v[42:45], v[70:73], v[214:217], v[42:45]
	v_mfma_f32_16x16x32_bf16 v[30:33], v[62:65], v[240:243], v[30:33]
	v_mfma_f32_16x16x32_bf16 v[26:29], v[70:73], v[240:243], v[26:29]
	v_mfma_f32_16x16x32_bf16 v[14:17], v[62:65], v[248:251], v[14:17]
	v_mfma_f32_16x16x32_bf16 v[10:13], v[70:73], v[248:251], v[10:13]
	s_setprio 0
	s_setprio 1
	v_mfma_f32_16x16x32_bf16 v[54:57], v[162:165], v[202:205], v[54:57]
	v_mfma_f32_16x16x32_bf16 v[50:53], v[190:193], v[202:205], v[50:53]
	v_mfma_f32_16x16x32_bf16 v[38:41], v[162:165], v[210:213], v[38:41]
	v_mfma_f32_16x16x32_bf16 v[34:37], v[190:193], v[210:213], v[34:37]
	v_mfma_f32_16x16x32_bf16 v[22:25], v[162:165], v[236:239], v[22:25]
	v_mfma_f32_16x16x32_bf16 v[18:21], v[190:193], v[236:239], v[18:21]
	v_mfma_f32_16x16x32_bf16 v[6:9], v[162:165], v[244:247], v[6:9]
	v_mfma_f32_16x16x32_bf16 v[2:5], v[190:193], v[244:247], v[2:5]
	v_mfma_f32_16x16x32_bf16 v[58:61], v[166:169], v[206:209], v[54:57]
	v_mfma_f32_16x16x32_bf16 v[50:53], v[198:201], v[206:209], v[50:53]
	v_mfma_f32_16x16x32_bf16 v[38:41], v[166:169], v[214:217], v[38:41]
	v_mfma_f32_16x16x32_bf16 v[34:37], v[198:201], v[214:217], v[34:37]
	s_setprio 0
	v_mfma_f32_16x16x32_bf16 v[22:25], v[166:169], v[240:243], v[22:25]
	v_mfma_f32_16x16x32_bf16 v[18:21], v[198:201], v[240:243], v[18:21]
	v_mfma_f32_16x16x32_bf16 v[6:9], v[166:169], v[248:251], v[6:9]
	v_mfma_f32_16x16x32_bf16 v[2:5], v[198:201], v[248:251], v[2:5]
	s_barrier
	s_add_i32 s83, s83, 2
	s_add_u32 s50, s50, 0x100
	s_addc_u32 s51, s51, 0
	s_add_u32 s45, s45, 0x100
	s_addc_u32 s82, s82, 0
	s_cmp_gt_u32 s83, 29
	s_cbranch_scc0 .LBB0_739
	s_and_b64 vcc, exec, s[20:21]
	s_cbranch_vccz .LBB0_742
	s_barrier

; #define PG8_STAGE(bufoff, gbase, voff) do { _Pragma("unroll") for (int _i = 0; _i < 2; ++_i) \
;         __builtin_amdgcn_global_load_lds((const unsigned*)((const char*)(gbase) + (voff)[_i]), (PG8_LAS unsigned*)(lds + (bufoff) + ldsw + _i * 8192), 16, 0, 0); } while (0)
; #define PG8_WAIT_V(n) asm volatile("s_waitcnt vmcnt(" #n ")" ::: "memory")
; #define PG8_WAIT_L(n) asm volatile("s_waitcnt lgkmcnt(" #n ")" ::: "memory")
; #define PG8_BAR __builtin_amdgcn_s_barrier()
; #define PG8_SCHED __builtin_amdgcn_sched_barrier(0)
; template <class Epi, class Sched, bool ALIGN_EPI, bool F8 = false>
; __device__ __forceinline__ void gemm_phase(PG8_LAS unsigned char* lds, const Gemm g, const Sched& S, const Epi& E, int tid) {
;     ...
;         for (int t = 0; t < nt; t += 2) {
;             const bool last = (t == nt - 2);
;             const char* a1 = cA + (size_t)(t + 1) * kstep;
;             const char* a2 = last ? nA : cA + (size_t)(t + 2) * kstep; const char* b2 = last ? nB : cB + (size_t)(t + 2) * kstep;
;             const char* a3 = a2 + kstep; const char* b3 = b2 + kstep;
;             if (last && has_next) S.a_ready(nxt);
;             PG8_LDB(B0, 0, 0); PG8_LDB(B1, 0, 1); PG8_SCHED; PG8_LDA(At, 0, 0); PG8_STAGE(PG8_SA(1, 1), a1 + hstepA, voffA);
;             PG8_WAIT_V(8); PG8_WAIT_L(0); PG8_BAR; PG8_MMA(0, 0, At, B0); PG8_MMA(0, 1, At, B1); PG8_BAR; PG8_SCHED;
;             PG8_LDA(At, 0, 1); PG8_STAGE(PG8_SB(0, 0), b2, voffB); PG8_STAGE(PG8_SB(0, 1), b2 + hstepB, voffB); PG8_STAGE(PG8_SA(0, 0), a2, voffA);
;             PG8_WAIT_V(8); PG8_WAIT_L(0); PG8_BAR; PG8_MMA(1, 0, At, B0); PG8_MMA(1, 1, At, B1); PG8_BAR; PG8_SCHED;
.LBB0_860:
	s_add_u32 s22, s20, 0xfffc0080
	s_addc_u32 s23, s21, -1
	s_add_i32 s51, 0, 0x10000
	s_cmp_eq_u32 s50, 12
	s_cselect_b32 s25, s11, s23
	s_cselect_b32 s24, s38, s22
	s_cselect_b32 s23, s9, s45
	s_cselect_b32 s22, s39, s44
	s_add_i32 s68, 0, 0x14000
	v_add_u32_e32 v2, s51, v196
	v_add_u32_e32 v14, s68, v196
	ds_read_b128 v[18:21], v2
	ds_read_b128 v[22:25], v2 offset:1024
	ds_read_b128 v[26:29], v2 offset:2048
	ds_read_b128 v[30:33], v2 offset:3072
	ds_read_b128 v[2:5], v14
	ds_read_b128 v[6:9], v14 offset:1024
	ds_read_b128 v[10:13], v14 offset:2048
	ds_read_b128 v[14:17], v14 offset:3072
	v_lshl_add_u64 v[176:177], s[20:21], 0, v[172:173]
	s_add_i32 m0, s1, 0xc000
	ds_read_b128 v[200:203], v199
	ds_read_b128 v[204:207], v199 offset:1024
	ds_read_b128 v[208:211], v199 offset:2048
	ds_read_b128 v[212:215], v199 offset:3072
	ds_read_b128 v[236:239], v199 offset:4096
	ds_read_b128 v[240:243], v199 offset:5120
	ds_read_b128 v[244:247], v199 offset:6144
	ds_read_b128 v[248:251], v199 offset:7168
	global_load_lds_dwordx4 v[176:177], off
	v_lshl_add_u64 v[176:177], s[20:21], 0, v[174:175]
	s_add_i32 m0, s1, 0xe000
	s_nop 0
	global_load_lds_dwordx4 v[176:177], off
	s_waitcnt vmcnt(8)
	s_waitcnt lgkmcnt(0)
	s_barrier
	s_setprio 1
	s_waitcnt lgkmcnt(0)
	v_mfma_f32_16x16x128_f8f6f4 v[158:161], v[18:25], v[200:207], v[158:161]
	v_mfma_f32_16x16x128_f8f6f4 v[154:157], v[26:33], v[200:207], v[154:157]
	v_mfma_f32_16x16x128_f8f6f4 v[142:145], v[18:25], v[208:215], v[142:145]
	v_mfma_f32_16x16x128_f8f6f4 v[138:141], v[26:33], v[208:215], v[138:141]
	v_mfma_f32_16x16x128_f8f6f4 v[126:129], v[18:25], v[236:243], v[126:129]
	v_mfma_f32_16x16x128_f8f6f4 v[122:125], v[26:33], v[236:243], v[122:125]
	v_mfma_f32_16x16x128_f8f6f4 v[110:113], v[18:25], v[244:251], v[110:113]
	v_mfma_f32_16x16x128_f8f6f4 v[106:109], v[26:33], v[244:251], v[106:109]
	s_setprio 0
	s_setprio 1
	v_mfma_f32_16x16x128_f8f6f4 v[150:153], v[2:9], v[200:207], v[150:153]
	v_mfma_f32_16x16x128_f8f6f4 v[146:149], v[10:17], v[200:207], v[146:149]
	v_mfma_f32_16x16x128_f8f6f4 v[134:137], v[2:9], v[208:215], v[134:137]
	v_mfma_f32_16x16x128_f8f6f4 v[130:133], v[10:17], v[208:215], v[130:133]
	v_mfma_f32_16x16x128_f8f6f4 v[118:121], v[2:9], v[236:243], v[118:121]
	v_mfma_f32_16x16x128_f8f6f4 v[114:117], v[10:17], v[236:243], v[114:117]
	s_setprio 0
	v_mfma_f32_16x16x128_f8f6f4 v[102:105], v[2:9], v[244:251], v[102:105]
	v_mfma_f32_16x16x128_f8f6f4 v[98:101], v[10:17], v[244:251], v[98:101]
	s_barrier
	s_add_i32 s51, s51, s0
	v_lshl_add_u64 v[176:177], s[22:23], 0, v[0:1]
	s_mov_b32 m0, s51
	ds_read_b128 v[200:203], v199 offset:16384
	ds_read_b128 v[204:207], v199 offset:17408
	ds_read_b128 v[208:211], v199 offset:18432
	ds_read_b128 v[212:215], v199 offset:19456
	ds_read_b128 v[236:239], v199 offset:20480
	ds_read_b128 v[240:243], v199 offset:21504
	ds_read_b128 v[244:247], v199 offset:22528
	ds_read_b128 v[248:251], v199 offset:23552
	global_load_lds_dwordx4 v[176:177], off
	s_add_i32 m0, s51, 0x2000
	s_add_u32 s82, s22, 0x40000
	v_lshl_add_u64 v[190:191], s[22:23], 0, v[162:163]
	s_addc_u32 s83, s23, 0
	s_add_i32 s51, s68, s0
	global_load_lds_dwordx4 v[190:191], off
	v_lshl_add_u64 v[178:179], s[82:83], 0, v[0:1]
	s_mov_b32 m0, s51
	v_lshl_add_u64 v[192:193], s[24:25], 0, v[166:167]
	global_load_lds_dwordx4 v[178:179], off
	v_lshl_add_u64 v[178:179], s[82:83], 0, v[162:163]
	s_add_i32 m0, s51, 0x2000
	v_lshl_add_u64 v[194:195], s[24:25], 0, v[164:165]
	global_load_lds_dwordx4 v[178:179], off
	s_mov_b32 m0, s1
	s_nop 0
	global_load_lds_dwordx4 v[192:193], off
	s_mov_b32 m0, s26
	s_nop 0
	global_load_lds_dwordx4 v[194:195], off
	s_waitcnt vmcnt(8)
	s_waitcnt lgkmcnt(0)
	s_barrier
	s_setprio 1
	s_waitcnt lgkmcnt(0)
	v_mfma_f32_16x16x128_f8f6f4 v[94:97], v[18:25], v[200:207], v[94:97]
	v_mfma_f32_16x16x128_f8f6f4 v[90:93], v[26:33], v[200:207], v[90:93]
	v_mfma_f32_16x16x128_f8f6f4 v[78:81], v[18:25], v[208:215], v[78:81]
	v_mfma_f32_16x16x128_f8f6f4 v[74:77], v[26:33], v[208:215], v[74:77]
	v_mfma_f32_16x16x128_f8f6f4 v[62:65], v[18:25], v[236:243], v[62:65]
	v_mfma_f32_16x16x128_f8f6f4 v[58:61], v[26:33], v[236:243], v[58:61]
	v_mfma_f32_16x16x128_f8f6f4 v[46:49], v[18:25], v[244:251], v[46:49]
	v_mfma_f32_16x16x128_f8f6f4 v[42:45], v[26:33], v[244:251], v[42:45]
	s_setprio 0
	s_setprio 1
	v_mfma_f32_16x16x128_f8f6f4 v[86:89], v[2:9], v[200:207], v[86:89]
	v_mfma_f32_16x16x128_f8f6f4 v[82:85], v[10:17], v[200:207], v[82:85]
	v_mfma_f32_16x16x128_f8f6f4 v[70:73], v[2:9], v[208:215], v[70:73]
	v_mfma_f32_16x16x128_f8f6f4 v[66:69], v[10:17], v[208:215], v[66:69]
	v_mfma_f32_16x16x128_f8f6f4 v[54:57], v[2:9], v[236:243], v[54:57]
	v_mfma_f32_16x16x128_f8f6f4 v[50:53], v[10:17], v[236:243], v[50:53]
	s_setprio 0
	v_mfma_f32_16x16x128_f8f6f4 v[38:41], v[2:9], v[244:251], v[38:41]
	v_mfma_f32_16x16x128_f8f6f4 v[34:37], v[10:17], v[244:251], v[34:37]
	s_barrier
; #define PG8_STAGE(bufoff, gbase, voff) do { _Pragma("unroll") for (int _i = 0; _i < 2; ++_i) \
;         __builtin_amdgcn_global_load_lds((const unsigned*)((const char*)(gbase) + (voff)[_i]), (PG8_LAS unsigned*)(lds + (bufoff) + ldsw + _i * 8192), 16, 0, 0); } while (0)
; #define PG8_WAIT_V(n) asm volatile("s_waitcnt vmcnt(" #n ")" ::: "memory")
; #define PG8_WAIT_L(n) asm volatile("s_waitcnt lgkmcnt(" #n ")" ::: "memory")
; #define PG8_BAR __builtin_amdgcn_s_barrier()
; #define PG8_SCHED __builtin_amdgcn_sched_barrier(0)
; template <class Epi, class Sched, bool ALIGN_EPI, bool F8 = false>
; __device__ __forceinline__ void gemm_phase(PG8_LAS unsigned char* lds, const Gemm g, const Sched& S, const Epi& E, int tid) {
;     ...
;             PG8_LDB(B0, 1, 0); PG8_LDB(B1, 1, 1); PG8_SCHED; PG8_LDA(At, 1, 0); PG8_STAGE(PG8_SA(0, 1), a2 + hstepA, voffA);
;             PG8_WAIT_V(8); PG8_WAIT_L(0); PG8_BAR; PG8_MMA(0, 0, At, B0); PG8_MMA(0, 1, At, B1); PG8_BAR; PG8_SCHED;
;             PG8_LDA(At, 1, 1); PG8_STAGE(PG8_SB(1, 0), b3, voffB); PG8_STAGE(PG8_SB(1, 1), b3 + hstepB, voffB); PG8_STAGE(PG8_SA(1, 0), a3, voffA);
;             PG8_WAIT_V(8); PG8_WAIT_L(0); PG8_BAR; PG8_MMA(1, 0, At, B0); PG8_MMA(1, 1, At, B1); PG8_BAR; PG8_SCHED;
;         }
;         if constexpr (ALIGN_EPI) { if (wr == 0) PG8_BAR; }
	s_add_i32 s51, 0, 0x18000
	s_add_i32 s68, 0, 0x1c000
	v_add_u32_e32 v14, s51, v196
	v_add_u32_e32 v30, s68, v196
	ds_read_b128 v[2:5], v14
	ds_read_b128 v[6:9], v14 offset:1024
	ds_read_b128 v[10:13], v14 offset:2048
	ds_read_b128 v[14:17], v14 offset:3072
	ds_read_b128 v[18:21], v30
	ds_read_b128 v[22:25], v30 offset:1024
	ds_read_b128 v[26:29], v30 offset:2048
	ds_read_b128 v[30:33], v30 offset:3072
	s_add_u32 s24, s24, 0x40000
	s_addc_u32 s25, s25, 0
	s_mov_b32 m0, s27
	v_lshl_add_u64 v[178:179], s[24:25], 0, v[166:167]
	ds_read_b128 v[200:203], v199 offset:32768
	ds_read_b128 v[204:207], v199 offset:33792
	ds_read_b128 v[208:211], v199 offset:34816
	ds_read_b128 v[212:215], v199 offset:35840
	ds_read_b128 v[236:239], v199 offset:36864
	ds_read_b128 v[240:243], v199 offset:37888
	ds_read_b128 v[244:247], v199 offset:38912
	ds_read_b128 v[248:251], v199 offset:39936
	global_load_lds_dwordx4 v[178:179], off
	v_lshl_add_u64 v[178:179], s[24:25], 0, v[164:165]
	s_mov_b32 m0, s28
	s_nop 0
	global_load_lds_dwordx4 v[178:179], off
	s_waitcnt vmcnt(8)
	s_waitcnt lgkmcnt(0)
	s_barrier
	s_setprio 1
	s_waitcnt lgkmcnt(0)
	v_mfma_f32_16x16x128_f8f6f4 v[158:161], v[2:9], v[200:207], v[158:161]
	v_mfma_f32_16x16x128_f8f6f4 v[154:157], v[10:17], v[200:207], v[154:157]
	v_mfma_f32_16x16x128_f8f6f4 v[142:145], v[2:9], v[208:215], v[142:145]
	v_mfma_f32_16x16x128_f8f6f4 v[138:141], v[10:17], v[208:215], v[138:141]
	v_mfma_f32_16x16x128_f8f6f4 v[126:129], v[2:9], v[236:243], v[126:129]
	v_mfma_f32_16x16x128_f8f6f4 v[122:125], v[10:17], v[236:243], v[122:125]
	v_mfma_f32_16x16x128_f8f6f4 v[110:113], v[2:9], v[244:251], v[110:113]
	v_mfma_f32_16x16x128_f8f6f4 v[106:109], v[10:17], v[244:251], v[106:109]
	s_setprio 0
	s_setprio 1
	v_mfma_f32_16x16x128_f8f6f4 v[150:153], v[18:25], v[200:207], v[150:153]
	v_mfma_f32_16x16x128_f8f6f4 v[146:149], v[26:33], v[200:207], v[146:149]
	v_mfma_f32_16x16x128_f8f6f4 v[134:137], v[18:25], v[208:215], v[134:137]
	v_mfma_f32_16x16x128_f8f6f4 v[130:133], v[26:33], v[208:215], v[130:133]
	v_mfma_f32_16x16x128_f8f6f4 v[118:121], v[18:25], v[236:243], v[118:121]
	v_mfma_f32_16x16x128_f8f6f4 v[114:117], v[26:33], v[236:243], v[114:117]
	s_setprio 0
	v_mfma_f32_16x16x128_f8f6f4 v[102:105], v[18:25], v[244:251], v[102:105]
	v_mfma_f32_16x16x128_f8f6f4 v[98:101], v[26:33], v[244:251], v[98:101]
	s_barrier
	s_add_i32 s24, s51, s0
	v_lshl_add_u64 v[176:177], v[176:177], 0, s[60:61]
	s_mov_b32 m0, s24
	ds_read_b128 v[200:203], v199 offset:49152
	ds_read_b128 v[204:207], v199 offset:50176
	ds_read_b128 v[208:211], v199 offset:51200
	ds_read_b128 v[212:215], v199 offset:52224
	ds_read_b128 v[236:239], v199 offset:53248
	ds_read_b128 v[240:243], v199 offset:54272
	ds_read_b128 v[244:247], v199 offset:55296
	ds_read_b128 v[248:251], v199 offset:56320
	global_load_lds_dwordx4 v[176:177], off
	s_add_i32 m0, s24, 0x2000
	s_add_u32 s22, s22, 0x40080
	v_lshl_add_u64 v[176:177], v[190:191], 0, s[60:61]
	s_addc_u32 s23, s23, 0
	s_add_i32 s24, s68, s0
	global_load_lds_dwordx4 v[176:177], off
	v_lshl_add_u64 v[176:177], s[22:23], 0, v[0:1]
	s_mov_b32 m0, s24
	s_nop 0
	global_load_lds_dwordx4 v[176:177], off
	v_lshl_add_u64 v[176:177], s[22:23], 0, v[162:163]
	s_add_i32 m0, s24, 0x2000
	s_nop 0
	global_load_lds_dwordx4 v[176:177], off
	v_lshl_add_u64 v[176:177], v[192:193], 0, s[60:61]
	s_mov_b32 m0, s29
	s_nop 0
	global_load_lds_dwordx4 v[176:177], off
	v_lshl_add_u64 v[176:177], v[194:195], 0, s[60:61]
	s_mov_b32 m0, s30
	s_nop 0
	global_load_lds_dwordx4 v[176:177], off
	s_waitcnt vmcnt(8)
	s_waitcnt lgkmcnt(0)
	s_barrier
	s_setprio 1
	s_waitcnt lgkmcnt(0)
	v_mfma_f32_16x16x128_f8f6f4 v[94:97], v[2:9], v[200:207], v[94:97]
	v_mfma_f32_16x16x128_f8f6f4 v[90:93], v[10:17], v[200:207], v[90:93]
	v_mfma_f32_16x16x128_f8f6f4 v[78:81], v[2:9], v[208:215], v[78:81]
	v_mfma_f32_16x16x128_f8f6f4 v[74:77], v[10:17], v[208:215], v[74:77]
	v_mfma_f32_16x16x128_f8f6f4 v[62:65], v[2:9], v[236:243], v[62:65]
	v_mfma_f32_16x16x128_f8f6f4 v[58:61], v[10:17], v[236:243], v[58:61]
	v_mfma_f32_16x16x128_f8f6f4 v[46:49], v[2:9], v[244:251], v[46:49]
	v_mfma_f32_16x16x128_f8f6f4 v[42:45], v[10:17], v[244:251], v[42:45]
	s_setprio 0
	s_setprio 1
	v_mfma_f32_16x16x128_f8f6f4 v[86:89], v[18:25], v[200:207], v[86:89]
	v_mfma_f32_16x16x128_f8f6f4 v[82:85], v[26:33], v[200:207], v[82:85]
	v_mfma_f32_16x16x128_f8f6f4 v[70:73], v[18:25], v[208:215], v[70:73]
	v_mfma_f32_16x16x128_f8f6f4 v[66:69], v[26:33], v[208:215], v[66:69]
	v_mfma_f32_16x16x128_f8f6f4 v[54:57], v[18:25], v[236:243], v[54:57]
	v_mfma_f32_16x16x128_f8f6f4 v[50:53], v[26:33], v[236:243], v[50:53]
	s_setprio 0
	v_mfma_f32_16x16x128_f8f6f4 v[38:41], v[18:25], v[244:251], v[38:41]
	v_mfma_f32_16x16x128_f8f6f4 v[34:37], v[26:33], v[244:251], v[34:37]
	s_barrier
	s_add_i32 s50, s50, 2
	s_add_u32 s20, s20, 0x100
	s_addc_u32 s21, s21, 0
	s_add_u32 s44, s44, 0x100
	s_addc_u32 s45, s45, 0
	s_cmp_gt_u32 s50, 13
	s_cbranch_scc0 .LBB0_860
	s_and_b64 vcc, exec, s[6:7]
	s_cbranch_vccz .LBB0_863
	s_barrier

; #define PG8_STAGE(bufoff, gbase, voff) do { _Pragma("unroll") for (int _i = 0; _i < 2; ++_i) \
;         __builtin_amdgcn_global_load_lds((const unsigned*)((const char*)(gbase) + (voff)[_i]), (PG8_LAS unsigned*)(lds + (bufoff) + ldsw + _i * 8192), 16, 0, 0); } while (0)
; #define PG8_WAIT_V(n) asm volatile("s_waitcnt vmcnt(" #n ")" ::: "memory")
; #define PG8_WAIT_L(n) asm volatile("s_waitcnt lgkmcnt(" #n ")" ::: "memory")
; #define PG8_BAR __builtin_amdgcn_s_barrier()
; #define PG8_SCHED __builtin_amdgcn_sched_barrier(0)
; template <class Epi, class Sched, bool ALIGN_EPI, bool F8 = false>
; __device__ __forceinline__ void gemm_phase(PG8_LAS unsigned char* lds, const Gemm g, const Sched& S, const Epi& E, int tid) {
;     ...
;         for (int t = 0; t < nt; t += 2) {
;             const bool last = (t == nt - 2);
;             const char* a1 = cA + (size_t)(t + 1) * kstep;
;             const char* a2 = last ? nA : cA + (size_t)(t + 2) * kstep; const char* b2 = last ? nB : cB + (size_t)(t + 2) * kstep;
;             const char* a3 = a2 + kstep; const char* b3 = b2 + kstep;
;             if (last && has_next) S.a_ready(nxt);
;             PG8_LDB(B0, 0, 0); PG8_LDB(B1, 0, 1); PG8_SCHED; PG8_LDA(At, 0, 0); PG8_STAGE(PG8_SA(1, 1), a1 + hstepA, voffA);
;             PG8_WAIT_V(8); PG8_WAIT_L(0); PG8_BAR; PG8_MMA(0, 0, At, B0); PG8_MMA(0, 1, At, B1); PG8_BAR; PG8_SCHED;
;             PG8_LDA(At, 0, 1); PG8_STAGE(PG8_SB(0, 0), b2, voffB); PG8_STAGE(PG8_SB(0, 1), b2 + hstepB, voffB); PG8_STAGE(PG8_SA(0, 0), a2, voffA);
.LBB0_1057:
	s_add_u32 s24, s22, 0x100
	s_addc_u32 s25, s23, 0
	s_add_i32 s50, 0, 0x10000
	s_cmp_eq_u32 vcc_hi, 4
	s_cselect_b32 s29, s19, s25
	s_cselect_b32 s28, s18, s24
	v_add_u32_e32 v140, s50, v144
	s_cselect_b32 s27, s13, vcc_lo
	s_cselect_b32 s26, s84, s85
	s_add_i32 s51, 0, 0x14000
	ds_read_b128 v[148:151], v140
	ds_read_b128 v[152:155], v140 offset:1024
	ds_read_b128 v[156:159], v140 offset:2048
	ds_read_b128 v[160:163], v140 offset:3072
	v_add_u32_e32 v140, s51, v144
	ds_read_b128 v[164:167], v140
	ds_read_b128 v[168:171], v140 offset:1024
	ds_read_b128 v[172:175], v140 offset:2048
	ds_read_b128 v[190:193], v140 offset:3072
	v_lshl_add_u64 v[142:143], s[22:23], 0, v[136:137]
	s_add_i32 m0, s17, 0xc000
	ds_read_b128 v[194:197], v146
	ds_read_b128 v[198:201], v146 offset:1024
	ds_read_b128 v[202:205], v146 offset:2048
	ds_read_b128 v[206:209], v146 offset:3072
	ds_read_b128 v[210:213], v146 offset:4096
	ds_read_b128 v[214:217], v146 offset:5120
	ds_read_b128 v[236:239], v146 offset:6144
	ds_read_b128 v[240:243], v146 offset:7168
	global_load_lds_dwordx4 v[142:143], off
	v_lshl_add_u64 v[142:143], s[22:23], 0, v[138:139]
	s_add_i32 m0, s17, 0xe000
	s_nop 0
	global_load_lds_dwordx4 v[142:143], off
	s_waitcnt vmcnt(8)
	s_waitcnt lgkmcnt(0)
	s_barrier
	s_setprio 1
	s_waitcnt lgkmcnt(0)
	v_mfma_f32_16x16x32_bf16 v[126:129], v[148:151], v[194:197], v[126:129]
	v_mfma_f32_16x16x32_bf16 v[122:125], v[156:159], v[194:197], v[122:125]
	v_mfma_f32_16x16x32_bf16 v[114:117], v[148:151], v[202:205], v[114:117]
	v_mfma_f32_16x16x32_bf16 v[106:109], v[156:159], v[202:205], v[106:109]
	v_mfma_f32_16x16x32_bf16 v[98:101], v[148:151], v[210:213], v[98:101]
	v_mfma_f32_16x16x32_bf16 v[90:93], v[156:159], v[210:213], v[90:93]
	v_mfma_f32_16x16x32_bf16 v[82:85], v[148:151], v[236:239], v[82:85]
	v_mfma_f32_16x16x32_bf16 v[74:77], v[156:159], v[236:239], v[74:77]
	v_mfma_f32_16x16x32_bf16 v[126:129], v[152:155], v[198:201], v[126:129]
	v_mfma_f32_16x16x32_bf16 v[122:125], v[160:163], v[198:201], v[122:125]
	v_mfma_f32_16x16x32_bf16 v[114:117], v[152:155], v[206:209], v[114:117]
	v_mfma_f32_16x16x32_bf16 v[106:109], v[160:163], v[206:209], v[106:109]
	v_mfma_f32_16x16x32_bf16 v[98:101], v[152:155], v[214:217], v[98:101]
	v_mfma_f32_16x16x32_bf16 v[90:93], v[160:163], v[214:217], v[90:93]
	v_mfma_f32_16x16x32_bf16 v[82:85], v[152:155], v[240:243], v[82:85]
	v_mfma_f32_16x16x32_bf16 v[74:77], v[160:163], v[240:243], v[74:77]
	s_setprio 0
	s_setprio 1
	v_mfma_f32_16x16x32_bf16 v[118:121], v[164:167], v[194:197], v[118:121]
	v_mfma_f32_16x16x32_bf16 v[110:113], v[172:175], v[194:197], v[110:113]
	v_mfma_f32_16x16x32_bf16 v[102:105], v[164:167], v[202:205], v[102:105]
	v_mfma_f32_16x16x32_bf16 v[94:97], v[172:175], v[202:205], v[94:97]
	v_mfma_f32_16x16x32_bf16 v[86:89], v[164:167], v[210:213], v[86:89]
	v_mfma_f32_16x16x32_bf16 v[78:81], v[172:175], v[210:213], v[78:81]
	v_mfma_f32_16x16x32_bf16 v[70:73], v[164:167], v[236:239], v[70:73]
	v_mfma_f32_16x16x32_bf16 v[66:69], v[172:175], v[236:239], v[66:69]
	v_mfma_f32_16x16x32_bf16 v[118:121], v[168:171], v[198:201], v[118:121]
	v_mfma_f32_16x16x32_bf16 v[110:113], v[190:193], v[198:201], v[110:113]
	v_mfma_f32_16x16x32_bf16 v[102:105], v[168:171], v[206:209], v[102:105]
	v_mfma_f32_16x16x32_bf16 v[94:97], v[190:193], v[206:209], v[94:97]
	s_setprio 0
	v_mfma_f32_16x16x32_bf16 v[86:89], v[168:171], v[214:217], v[86:89]
	v_mfma_f32_16x16x32_bf16 v[78:81], v[190:193], v[214:217], v[78:81]
	v_mfma_f32_16x16x32_bf16 v[70:73], v[168:171], v[240:243], v[70:73]
	v_mfma_f32_16x16x32_bf16 v[66:69], v[190:193], v[240:243], v[66:69]
	s_barrier
	s_add_i32 s22, s50, s34
	v_lshl_add_u64 v[142:143], s[26:27], 0, v[0:1]
	s_mov_b32 m0, s22
	ds_read_b128 v[194:197], v146 offset:16384
	ds_read_b128 v[198:201], v146 offset:17408
	ds_read_b128 v[202:205], v146 offset:18432
	ds_read_b128 v[206:209], v146 offset:19456
	ds_read_b128 v[210:213], v146 offset:20480
	ds_read_b128 v[214:217], v146 offset:21504
	ds_read_b128 v[236:239], v146 offset:22528
	ds_read_b128 v[240:243], v146 offset:23552
	global_load_lds_dwordx4 v[142:143], off
	s_add_i32 m0, s22, 0x2000
	s_add_u32 s22, s26, 0x20000
	v_lshl_add_u64 v[176:177], s[26:27], 0, v[134:135]
	s_addc_u32 s23, s27, 0
	s_add_i32 s50, s51, s34
	global_load_lds_dwordx4 v[176:177], off
	v_lshl_add_u64 v[178:179], s[22:23], 0, v[0:1]
	s_mov_b32 m0, s50
	v_lshl_add_u64 v[180:181], s[28:29], 0, v[132:133]
	global_load_lds_dwordx4 v[178:179], off
	v_lshl_add_u64 v[178:179], s[22:23], 0, v[134:135]
	s_add_i32 m0, s50, 0x2000
	s_nop 0
	global_load_lds_dwordx4 v[178:179], off
	v_lshl_add_u64 v[178:179], s[28:29], 0, v[130:131]
	s_mov_b32 m0, s17
	s_nop 0
	global_load_lds_dwordx4 v[178:179], off
	s_mov_b32 m0, s35
	s_nop 0
	global_load_lds_dwordx4 v[180:181], off
	s_waitcnt vmcnt(8)
	s_waitcnt lgkmcnt(0)
	s_barrier
; #define PG8_STAGE(bufoff, gbase, voff) do { _Pragma("unroll") for (int _i = 0; _i < 2; ++_i) \
;         __builtin_amdgcn_global_load_lds((const unsigned*)((const char*)(gbase) + (voff)[_i]), (PG8_LAS unsigned*)(lds + (bufoff) + ldsw + _i * 8192), 16, 0, 0); } while (0)
; #define PG8_WAIT_V(n) asm volatile("s_waitcnt vmcnt(" #n ")" ::: "memory")
; #define PG8_WAIT_L(n) asm volatile("s_waitcnt lgkmcnt(" #n ")" ::: "memory")
; #define PG8_BAR __builtin_amdgcn_s_barrier()
; #define PG8_SCHED __builtin_amdgcn_sched_barrier(0)
; template <class Epi, class Sched, bool ALIGN_EPI, bool F8 = false>
; __device__ __forceinline__ void gemm_phase(PG8_LAS unsigned char* lds, const Gemm g, const Sched& S, const Epi& E, int tid) {
;     ...
;             PG8_WAIT_V(8); PG8_WAIT_L(0); PG8_BAR; PG8_MMA(1, 0, At, B0); PG8_MMA(1, 1, At, B1); PG8_BAR; PG8_SCHED;
;             PG8_LDB(B0, 1, 0); PG8_LDB(B1, 1, 1); PG8_SCHED; PG8_LDA(At, 1, 0); PG8_STAGE(PG8_SA(0, 1), a2 + hstepA, voffA);
;             PG8_WAIT_V(8); PG8_WAIT_L(0); PG8_BAR; PG8_MMA(0, 0, At, B0); PG8_MMA(0, 1, At, B1); PG8_BAR; PG8_SCHED;
	s_setprio 1
	s_waitcnt lgkmcnt(0)
	v_mfma_f32_16x16x32_bf16 v[62:65], v[148:151], v[194:197], v[62:65]
	v_mfma_f32_16x16x32_bf16 v[58:61], v[156:159], v[194:197], v[58:61]
	v_mfma_f32_16x16x32_bf16 v[50:53], v[148:151], v[202:205], v[50:53]
	v_mfma_f32_16x16x32_bf16 v[42:45], v[156:159], v[202:205], v[42:45]
	v_mfma_f32_16x16x32_bf16 v[34:37], v[148:151], v[210:213], v[34:37]
	v_mfma_f32_16x16x32_bf16 v[26:29], v[156:159], v[210:213], v[26:29]
	v_mfma_f32_16x16x32_bf16 v[18:21], v[148:151], v[236:239], v[18:21]
	v_mfma_f32_16x16x32_bf16 v[10:13], v[156:159], v[236:239], v[10:13]
	v_mfma_f32_16x16x32_bf16 v[62:65], v[152:155], v[198:201], v[62:65]
	v_mfma_f32_16x16x32_bf16 v[58:61], v[160:163], v[198:201], v[58:61]
	v_mfma_f32_16x16x32_bf16 v[50:53], v[152:155], v[206:209], v[50:53]
	v_mfma_f32_16x16x32_bf16 v[42:45], v[160:163], v[206:209], v[42:45]
	v_mfma_f32_16x16x32_bf16 v[34:37], v[152:155], v[214:217], v[34:37]
	v_mfma_f32_16x16x32_bf16 v[26:29], v[160:163], v[214:217], v[26:29]
	v_mfma_f32_16x16x32_bf16 v[18:21], v[152:155], v[240:243], v[18:21]
	v_mfma_f32_16x16x32_bf16 v[10:13], v[160:163], v[240:243], v[10:13]
	s_setprio 0
	s_setprio 1
	v_mfma_f32_16x16x32_bf16 v[54:57], v[164:167], v[194:197], v[54:57]
	v_mfma_f32_16x16x32_bf16 v[46:49], v[172:175], v[194:197], v[46:49]
	v_mfma_f32_16x16x32_bf16 v[38:41], v[164:167], v[202:205], v[38:41]
	v_mfma_f32_16x16x32_bf16 v[30:33], v[172:175], v[202:205], v[30:33]
	v_mfma_f32_16x16x32_bf16 v[22:25], v[164:167], v[210:213], v[22:25]
	v_mfma_f32_16x16x32_bf16 v[14:17], v[172:175], v[210:213], v[14:17]
	v_mfma_f32_16x16x32_bf16 v[6:9], v[164:167], v[236:239], v[6:9]
	v_mfma_f32_16x16x32_bf16 v[2:5], v[172:175], v[236:239], v[2:5]
	v_mfma_f32_16x16x32_bf16 v[54:57], v[168:171], v[198:201], v[54:57]
	v_mfma_f32_16x16x32_bf16 v[46:49], v[190:193], v[198:201], v[46:49]
	v_mfma_f32_16x16x32_bf16 v[38:41], v[168:171], v[206:209], v[38:41]
	v_mfma_f32_16x16x32_bf16 v[30:33], v[190:193], v[206:209], v[30:33]
	s_setprio 0
	v_mfma_f32_16x16x32_bf16 v[22:25], v[168:171], v[214:217], v[22:25]
	v_mfma_f32_16x16x32_bf16 v[14:17], v[190:193], v[214:217], v[14:17]
	v_mfma_f32_16x16x32_bf16 v[6:9], v[168:171], v[240:243], v[6:9]
	v_mfma_f32_16x16x32_bf16 v[2:5], v[190:193], v[240:243], v[2:5]
	s_barrier
	s_add_i32 s50, 0, 0x18000
	v_add_u32_e32 v140, s50, v144
	s_add_i32 s51, 0, 0x1c000
	ds_read_b128 v[148:151], v140
	ds_read_b128 v[152:155], v140 offset:1024
	ds_read_b128 v[156:159], v140 offset:2048
	ds_read_b128 v[160:163], v140 offset:3072
	v_add_u32_e32 v140, s51, v144
	ds_read_b128 v[164:167], v140
	ds_read_b128 v[168:171], v140 offset:1024
	ds_read_b128 v[172:175], v140 offset:2048
	ds_read_b128 v[190:193], v140 offset:3072
	s_add_u32 s22, s28, 0x110000
	s_addc_u32 s23, s29, 0
	s_mov_b32 m0, s38
	v_lshl_add_u64 v[182:183], s[22:23], 0, v[130:131]
	ds_read_b128 v[194:197], v146 offset:32768
	ds_read_b128 v[198:201], v146 offset:33792
	ds_read_b128 v[202:205], v146 offset:34816
	ds_read_b128 v[206:209], v146 offset:35840
	ds_read_b128 v[210:213], v146 offset:36864
	ds_read_b128 v[214:217], v146 offset:37888
	ds_read_b128 v[236:239], v146 offset:38912
	ds_read_b128 v[240:243], v146 offset:39936
	global_load_lds_dwordx4 v[182:183], off
	v_lshl_add_u64 v[182:183], s[22:23], 0, v[132:133]
	s_mov_b32 m0, s39
	s_nop 0
	global_load_lds_dwordx4 v[182:183], off
	s_waitcnt vmcnt(8)
	s_waitcnt lgkmcnt(0)
	s_barrier
	s_setprio 1
	s_waitcnt lgkmcnt(0)
	v_mfma_f32_16x16x32_bf16 v[126:129], v[148:151], v[194:197], v[126:129]
	v_mfma_f32_16x16x32_bf16 v[122:125], v[156:159], v[194:197], v[122:125]
	v_mfma_f32_16x16x32_bf16 v[114:117], v[148:151], v[202:205], v[114:117]
	v_mfma_f32_16x16x32_bf16 v[106:109], v[156:159], v[202:205], v[106:109]
	v_mfma_f32_16x16x32_bf16 v[98:101], v[148:151], v[210:213], v[98:101]
	v_mfma_f32_16x16x32_bf16 v[90:93], v[156:159], v[210:213], v[90:93]
	v_mfma_f32_16x16x32_bf16 v[82:85], v[148:151], v[236:239], v[82:85]
	v_mfma_f32_16x16x32_bf16 v[74:77], v[156:159], v[236:239], v[74:77]
	v_mfma_f32_16x16x32_bf16 v[126:129], v[152:155], v[198:201], v[126:129]
	v_mfma_f32_16x16x32_bf16 v[122:125], v[160:163], v[198:201], v[122:125]
	v_mfma_f32_16x16x32_bf16 v[114:117], v[152:155], v[206:209], v[114:117]
	v_mfma_f32_16x16x32_bf16 v[106:109], v[160:163], v[206:209], v[106:109]
	v_mfma_f32_16x16x32_bf16 v[98:101], v[152:155], v[214:217], v[98:101]
	v_mfma_f32_16x16x32_bf16 v[90:93], v[160:163], v[214:217], v[90:93]
	v_mfma_f32_16x16x32_bf16 v[82:85], v[152:155], v[240:243], v[82:85]
	v_mfma_f32_16x16x32_bf16 v[74:77], v[160:163], v[240:243], v[74:77]
	s_setprio 0
	s_setprio 1
	v_mfma_f32_16x16x32_bf16 v[118:121], v[164:167], v[194:197], v[118:121]
	v_mfma_f32_16x16x32_bf16 v[110:113], v[172:175], v[194:197], v[110:113]
	v_mfma_f32_16x16x32_bf16 v[102:105], v[164:167], v[202:205], v[102:105]
	v_mfma_f32_16x16x32_bf16 v[94:97], v[172:175], v[202:205], v[94:97]
	v_mfma_f32_16x16x32_bf16 v[86:89], v[164:167], v[210:213], v[86:89]
	v_mfma_f32_16x16x32_bf16 v[78:81], v[172:175], v[210:213], v[78:81]
	v_mfma_f32_16x16x32_bf16 v[70:73], v[164:167], v[236:239], v[70:73]
	v_mfma_f32_16x16x32_bf16 v[66:69], v[172:175], v[236:239], v[66:69]
	v_mfma_f32_16x16x32_bf16 v[118:121], v[168:171], v[198:201], v[118:121]
	v_mfma_f32_16x16x32_bf16 v[110:113], v[190:193], v[198:201], v[110:113]
	v_mfma_f32_16x16x32_bf16 v[102:105], v[168:171], v[206:209], v[102:105]
	v_mfma_f32_16x16x32_bf16 v[94:97], v[190:193], v[206:209], v[94:97]
	s_setprio 0
	v_mfma_f32_16x16x32_bf16 v[86:89], v[168:171], v[214:217], v[86:89]
	v_mfma_f32_16x16x32_bf16 v[78:81], v[190:193], v[214:217], v[78:81]
	v_mfma_f32_16x16x32_bf16 v[70:73], v[168:171], v[240:243], v[70:73]
	v_mfma_f32_16x16x32_bf16 v[66:69], v[190:193], v[240:243], v[66:69]
	s_barrier
; #define PG8_STAGE(bufoff, gbase, voff) do { _Pragma("unroll") for (int _i = 0; _i < 2; ++_i) \
;         __builtin_amdgcn_global_load_lds((const unsigned*)((const char*)(gbase) + (voff)[_i]), (PG8_LAS unsigned*)(lds + (bufoff) + ldsw + _i * 8192), 16, 0, 0); } while (0)
; #define PG8_WAIT_V(n) asm volatile("s_waitcnt vmcnt(" #n ")" ::: "memory")
; #define PG8_WAIT_L(n) asm volatile("s_waitcnt lgkmcnt(" #n ")" ::: "memory")
; #define PG8_BAR __builtin_amdgcn_s_barrier()
; #define PG8_SCHED __builtin_amdgcn_sched_barrier(0)
; template <class Epi, class Sched, bool ALIGN_EPI, bool F8 = false>
; __device__ __forceinline__ void gemm_phase(PG8_LAS unsigned char* lds, const Gemm g, const Sched& S, const Epi& E, int tid) {
;     ...
;             PG8_LDA(At, 1, 1); PG8_STAGE(PG8_SB(1, 0), b3, voffB); PG8_STAGE(PG8_SB(1, 1), b3 + hstepB, voffB); PG8_STAGE(PG8_SA(1, 0), a3, voffA);
;             PG8_WAIT_V(8); PG8_WAIT_L(0); PG8_BAR; PG8_MMA(1, 0, At, B0); PG8_MMA(1, 1, At, B1); PG8_BAR; PG8_SCHED;
;         }
;         if constexpr (ALIGN_EPI) { if (wr == 0) PG8_BAR; }
	s_add_i32 s22, s50, s34
	v_lshl_add_u64 v[142:143], v[142:143], 0, s[60:61]
	s_mov_b32 m0, s22
	ds_read_b128 v[194:197], v146 offset:49152
	ds_read_b128 v[198:201], v146 offset:50176
	ds_read_b128 v[202:205], v146 offset:51200
	ds_read_b128 v[206:209], v146 offset:52224
	ds_read_b128 v[210:213], v146 offset:53248
	ds_read_b128 v[214:217], v146 offset:54272
	ds_read_b128 v[236:239], v146 offset:55296
	ds_read_b128 v[240:243], v146 offset:56320
	global_load_lds_dwordx4 v[142:143], off
	s_add_i32 m0, s22, 0x2000
	s_add_u32 s22, s26, 0x20080
	v_lshl_add_u64 v[142:143], v[176:177], 0, s[60:61]
	s_addc_u32 s23, s27, 0
	s_add_i32 s26, s51, s34
	global_load_lds_dwordx4 v[142:143], off
	v_lshl_add_u64 v[142:143], s[22:23], 0, v[0:1]
	s_mov_b32 m0, s26
	s_nop 0
	global_load_lds_dwordx4 v[142:143], off
	v_lshl_add_u64 v[142:143], s[22:23], 0, v[134:135]
	s_add_i32 m0, s26, 0x2000
	s_nop 0
	global_load_lds_dwordx4 v[142:143], off
	v_lshl_add_u64 v[142:143], v[178:179], 0, s[60:61]
	s_mov_b32 m0, s82
	s_nop 0
	global_load_lds_dwordx4 v[142:143], off
	v_lshl_add_u64 v[142:143], v[180:181], 0, s[60:61]
	s_mov_b32 m0, s83
	s_nop 0
	global_load_lds_dwordx4 v[142:143], off
	s_waitcnt vmcnt(8)
	s_waitcnt lgkmcnt(0)
	s_barrier
	s_setprio 1
	s_waitcnt lgkmcnt(0)
	v_mfma_f32_16x16x32_bf16 v[62:65], v[148:151], v[194:197], v[62:65]
	v_mfma_f32_16x16x32_bf16 v[58:61], v[156:159], v[194:197], v[58:61]
	v_mfma_f32_16x16x32_bf16 v[50:53], v[148:151], v[202:205], v[50:53]
	v_mfma_f32_16x16x32_bf16 v[42:45], v[156:159], v[202:205], v[42:45]
	v_mfma_f32_16x16x32_bf16 v[34:37], v[148:151], v[210:213], v[34:37]
	v_mfma_f32_16x16x32_bf16 v[26:29], v[156:159], v[210:213], v[26:29]
	v_mfma_f32_16x16x32_bf16 v[18:21], v[148:151], v[236:239], v[18:21]
	v_mfma_f32_16x16x32_bf16 v[10:13], v[156:159], v[236:239], v[10:13]
	v_mfma_f32_16x16x32_bf16 v[62:65], v[152:155], v[198:201], v[62:65]
	v_mfma_f32_16x16x32_bf16 v[58:61], v[160:163], v[198:201], v[58:61]
	v_mfma_f32_16x16x32_bf16 v[50:53], v[152:155], v[206:209], v[50:53]
	v_mfma_f32_16x16x32_bf16 v[42:45], v[160:163], v[206:209], v[42:45]
	v_mfma_f32_16x16x32_bf16 v[34:37], v[152:155], v[214:217], v[34:37]
	v_mfma_f32_16x16x32_bf16 v[26:29], v[160:163], v[214:217], v[26:29]
	v_mfma_f32_16x16x32_bf16 v[18:21], v[152:155], v[240:243], v[18:21]
	v_mfma_f32_16x16x32_bf16 v[10:13], v[160:163], v[240:243], v[10:13]
	s_setprio 0
	s_setprio 1
	v_mfma_f32_16x16x32_bf16 v[54:57], v[164:167], v[194:197], v[54:57]
	v_mfma_f32_16x16x32_bf16 v[46:49], v[172:175], v[194:197], v[46:49]
	v_mfma_f32_16x16x32_bf16 v[38:41], v[164:167], v[202:205], v[38:41]
	v_mfma_f32_16x16x32_bf16 v[30:33], v[172:175], v[202:205], v[30:33]
	v_mfma_f32_16x16x32_bf16 v[22:25], v[164:167], v[210:213], v[22:25]
	v_mfma_f32_16x16x32_bf16 v[14:17], v[172:175], v[210:213], v[14:17]
	v_mfma_f32_16x16x32_bf16 v[6:9], v[164:167], v[236:239], v[6:9]
	v_mfma_f32_16x16x32_bf16 v[2:5], v[172:175], v[236:239], v[2:5]
	v_mfma_f32_16x16x32_bf16 v[54:57], v[168:171], v[198:201], v[54:57]
	v_mfma_f32_16x16x32_bf16 v[46:49], v[190:193], v[198:201], v[46:49]
	v_mfma_f32_16x16x32_bf16 v[38:41], v[168:171], v[206:209], v[38:41]
	v_mfma_f32_16x16x32_bf16 v[30:33], v[190:193], v[206:209], v[30:33]
	s_setprio 0
	v_mfma_f32_16x16x32_bf16 v[22:25], v[168:171], v[214:217], v[22:25]
	v_mfma_f32_16x16x32_bf16 v[14:17], v[190:193], v[214:217], v[14:17]
	v_mfma_f32_16x16x32_bf16 v[6:9], v[168:171], v[240:243], v[6:9]
	v_mfma_f32_16x16x32_bf16 v[2:5], v[190:193], v[240:243], v[2:5]
	s_barrier
	s_add_i32 vcc_hi, vcc_hi, 2
	s_add_u32 s85, s85, 0x100
	s_addc_u32 vcc_lo, vcc_lo, 0
	s_cmp_gt_u32 vcc_hi, 5
	s_mov_b64 s[22:23], s[24:25]
	s_cbranch_scc0 .LBB0_1057
	s_and_b64 vcc, exec, s[8:9]
	s_cbranch_vccz .LBB0_1060
	s_barrier

; #define PG8_STAGE(bufoff, gbase, voff) do { _Pragma("unroll") for (int _i = 0; _i < 2; ++_i) \
;         __builtin_amdgcn_global_load_lds((const unsigned*)((const char*)(gbase) + (voff)[_i]), (PG8_LAS unsigned*)(lds + (bufoff) + ldsw + _i * 8192), 16, 0, 0); } while (0)
; #define PG8_WAIT_V(n) asm volatile("s_waitcnt vmcnt(" #n ")" ::: "memory")
; #define PG8_WAIT_L(n) asm volatile("s_waitcnt lgkmcnt(" #n ")" ::: "memory")
; #define PG8_BAR __builtin_amdgcn_s_barrier()
; #define PG8_SCHED __builtin_amdgcn_sched_barrier(0)
; template <class Epi, class Sched, bool ALIGN_EPI, bool F8 = false>
; __device__ __forceinline__ void gemm_phase(PG8_LAS unsigned char* lds, const Gemm g, const Sched& S, const Epi& E, int tid) {
;     ...
;         for (int t = 0; t < nt; t += 2) {
;             const bool last = (t == nt - 2);
;             const char* a1 = cA + (size_t)(t + 1) * kstep;
;             const char* a2 = last ? nA : cA + (size_t)(t + 2) * kstep; const char* b2 = last ? nB : cB + (size_t)(t + 2) * kstep;
;             const char* a3 = a2 + kstep; const char* b3 = b2 + kstep;
;             if (last && has_next) S.a_ready(nxt);
;             PG8_LDB(B0, 0, 0); PG8_LDB(B1, 0, 1); PG8_SCHED; PG8_LDA(At, 0, 0); PG8_STAGE(PG8_SA(1, 1), a1 + hstepA, voffA);
;             PG8_WAIT_V(8); PG8_WAIT_L(0); PG8_BAR; PG8_MMA(0, 0, At, B0); PG8_MMA(0, 1, At, B1); PG8_BAR; PG8_SCHED;
;             PG8_LDA(At, 0, 1); PG8_STAGE(PG8_SB(0, 0), b2, voffB); PG8_STAGE(PG8_SB(0, 1), b2 + hstepB, voffB); PG8_STAGE(PG8_SA(0, 0), a2, voffA);
.LBB0_1147:
	s_add_u32 s24, s22, 0xfff00080
	s_addc_u32 s25, s23, -1
	s_add_i32 s88, 0, 0x10000
	s_cmp_eq_u32 s87, 4
	s_cselect_b32 s27, s83, s25
	s_cselect_b32 s26, s84, s24
	v_add_u32_e32 v144, s88, v145
	s_cselect_b32 s25, s11, s86
	s_cselect_b32 s24, s13, s85
	s_add_i32 s94, 0, 0x14000
	ds_read_b128 v[150:153], v144
	ds_read_b128 v[154:157], v144 offset:1024
	ds_read_b128 v[158:161], v144 offset:2048
	ds_read_b128 v[162:165], v144 offset:3072
	v_add_u32_e32 v144, s94, v145
	ds_read_b128 v[166:169], v144
	ds_read_b128 v[170:173], v144 offset:1024
	ds_read_b128 v[174:177], v144 offset:2048
	ds_read_b128 v[178:181], v144 offset:3072
	v_lshl_add_u64 v[146:147], s[22:23], 0, v[140:141]
	s_add_i32 m0, s31, 0xc000
	ds_read_b128 v[182:185], v148
	ds_read_b128 v[186:189], v148 offset:1024
	ds_read_b128 v[190:193], v148 offset:2048
	ds_read_b128 v[194:197], v148 offset:3072
	ds_read_b128 v[198:201], v148 offset:4096
	ds_read_b128 v[202:205], v148 offset:5120
	ds_read_b128 v[206:209], v148 offset:6144
	ds_read_b128 v[210:213], v148 offset:7168
	global_load_lds_dwordx4 v[146:147], off
	v_lshl_add_u64 v[146:147], s[22:23], 0, v[142:143]
	s_add_i32 m0, s31, 0xe000
	s_nop 0
	global_load_lds_dwordx4 v[146:147], off
	s_waitcnt vmcnt(8)
	s_waitcnt lgkmcnt(0)
	s_barrier
	s_setprio 1
	s_waitcnt lgkmcnt(0)
	v_mfma_f32_16x16x32_bf16 v[126:129], v[150:153], v[182:185], v[126:129]
	v_mfma_f32_16x16x32_bf16 v[122:125], v[158:161], v[182:185], v[122:125]
	v_mfma_f32_16x16x32_bf16 v[114:117], v[150:153], v[190:193], v[114:117]
	v_mfma_f32_16x16x32_bf16 v[106:109], v[158:161], v[190:193], v[106:109]
	v_mfma_f32_16x16x32_bf16 v[98:101], v[150:153], v[198:201], v[98:101]
	v_mfma_f32_16x16x32_bf16 v[90:93], v[158:161], v[198:201], v[90:93]
	v_mfma_f32_16x16x32_bf16 v[82:85], v[150:153], v[206:209], v[82:85]
	v_mfma_f32_16x16x32_bf16 v[74:77], v[158:161], v[206:209], v[74:77]
	v_mfma_f32_16x16x32_bf16 v[126:129], v[154:157], v[186:189], v[126:129]
	v_mfma_f32_16x16x32_bf16 v[122:125], v[162:165], v[186:189], v[122:125]
	v_mfma_f32_16x16x32_bf16 v[114:117], v[154:157], v[194:197], v[114:117]
	v_mfma_f32_16x16x32_bf16 v[106:109], v[162:165], v[194:197], v[106:109]
	v_mfma_f32_16x16x32_bf16 v[98:101], v[154:157], v[202:205], v[98:101]
	v_mfma_f32_16x16x32_bf16 v[90:93], v[162:165], v[202:205], v[90:93]
	v_mfma_f32_16x16x32_bf16 v[82:85], v[154:157], v[210:213], v[82:85]
	v_mfma_f32_16x16x32_bf16 v[74:77], v[162:165], v[210:213], v[74:77]
	s_setprio 0
	s_setprio 1
	v_mfma_f32_16x16x32_bf16 v[118:121], v[166:169], v[182:185], v[118:121]
	v_mfma_f32_16x16x32_bf16 v[110:113], v[174:177], v[182:185], v[110:113]
	v_mfma_f32_16x16x32_bf16 v[102:105], v[166:169], v[190:193], v[102:105]
	v_mfma_f32_16x16x32_bf16 v[94:97], v[174:177], v[190:193], v[94:97]
	v_mfma_f32_16x16x32_bf16 v[86:89], v[166:169], v[198:201], v[86:89]
	v_mfma_f32_16x16x32_bf16 v[78:81], v[174:177], v[198:201], v[78:81]
	v_mfma_f32_16x16x32_bf16 v[70:73], v[166:169], v[206:209], v[70:73]
	v_mfma_f32_16x16x32_bf16 v[66:69], v[174:177], v[206:209], v[66:69]
	v_mfma_f32_16x16x32_bf16 v[118:121], v[170:173], v[186:189], v[118:121]
	v_mfma_f32_16x16x32_bf16 v[110:113], v[178:181], v[186:189], v[110:113]
	v_mfma_f32_16x16x32_bf16 v[102:105], v[170:173], v[194:197], v[102:105]
	v_mfma_f32_16x16x32_bf16 v[94:97], v[178:181], v[194:197], v[94:97]
	s_setprio 0
	v_mfma_f32_16x16x32_bf16 v[86:89], v[170:173], v[202:205], v[86:89]
	v_mfma_f32_16x16x32_bf16 v[78:81], v[178:181], v[202:205], v[78:81]
	v_mfma_f32_16x16x32_bf16 v[70:73], v[170:173], v[210:213], v[70:73]
	v_mfma_f32_16x16x32_bf16 v[66:69], v[178:181], v[210:213], v[66:69]
	s_barrier
	s_add_i32 s88, s88, s30
	v_lshl_add_u64 v[146:147], s[24:25], 0, v[134:135]
	s_mov_b32 m0, s88
	ds_read_b128 v[182:185], v148 offset:16384
	ds_read_b128 v[186:189], v148 offset:17408
	ds_read_b128 v[190:193], v148 offset:18432
	ds_read_b128 v[194:197], v148 offset:19456
	ds_read_b128 v[198:201], v148 offset:20480
	ds_read_b128 v[202:205], v148 offset:21504
	ds_read_b128 v[206:209], v148 offset:22528
	ds_read_b128 v[210:213], v148 offset:23552
	global_load_lds_dwordx4 v[146:147], off
	s_add_i32 m0, s88, 0x2000
	s_add_u32 s88, s24, 0x80000
	v_lshl_add_u64 v[214:215], s[24:25], 0, v[130:131]
	s_addc_u32 s89, s25, 0
	s_add_i32 s94, s94, s30
	global_load_lds_dwordx4 v[214:215], off
	v_lshl_add_u64 v[216:217], s[88:89], 0, v[134:135]
	s_mov_b32 m0, s94
	v_lshl_add_u64 v[218:219], s[26:27], 0, v[132:133]
	global_load_lds_dwordx4 v[216:217], off
	v_lshl_add_u64 v[216:217], s[88:89], 0, v[130:131]
	s_add_i32 m0, s94, 0x2000
	s_nop 0
	global_load_lds_dwordx4 v[216:217], off
	v_lshl_add_u64 v[216:217], s[26:27], 0, v[136:137]
	s_mov_b32 m0, s31
	s_nop 0
	global_load_lds_dwordx4 v[216:217], off
	s_mov_b32 m0, s34
	s_nop 0
	global_load_lds_dwordx4 v[218:219], off
	s_waitcnt vmcnt(8)
	s_waitcnt lgkmcnt(0)
	s_barrier
; #define PG8_STAGE(bufoff, gbase, voff) do { _Pragma("unroll") for (int _i = 0; _i < 2; ++_i) \
;         __builtin_amdgcn_global_load_lds((const unsigned*)((const char*)(gbase) + (voff)[_i]), (PG8_LAS unsigned*)(lds + (bufoff) + ldsw + _i * 8192), 16, 0, 0); } while (0)
; #define PG8_WAIT_V(n) asm volatile("s_waitcnt vmcnt(" #n ")" ::: "memory")
; #define PG8_WAIT_L(n) asm volatile("s_waitcnt lgkmcnt(" #n ")" ::: "memory")
; #define PG8_BAR __builtin_amdgcn_s_barrier()
; #define PG8_SCHED __builtin_amdgcn_sched_barrier(0)
; template <class Epi, class Sched, bool ALIGN_EPI, bool F8 = false>
; __device__ __forceinline__ void gemm_phase(PG8_LAS unsigned char* lds, const Gemm g, const Sched& S, const Epi& E, int tid) {
;     ...
;             PG8_WAIT_V(8); PG8_WAIT_L(0); PG8_BAR; PG8_MMA(1, 0, At, B0); PG8_MMA(1, 1, At, B1); PG8_BAR; PG8_SCHED;
;             PG8_LDB(B0, 1, 0); PG8_LDB(B1, 1, 1); PG8_SCHED; PG8_LDA(At, 1, 0); PG8_STAGE(PG8_SA(0, 1), a2 + hstepA, voffA);
;             PG8_WAIT_V(8); PG8_WAIT_L(0); PG8_BAR; PG8_MMA(0, 0, At, B0); PG8_MMA(0, 1, At, B1); PG8_BAR; PG8_SCHED;
	s_setprio 1
	s_waitcnt lgkmcnt(0)
	v_mfma_f32_16x16x32_bf16 v[62:65], v[150:153], v[182:185], v[62:65]
	v_mfma_f32_16x16x32_bf16 v[58:61], v[158:161], v[182:185], v[58:61]
	v_mfma_f32_16x16x32_bf16 v[50:53], v[150:153], v[190:193], v[50:53]
	v_mfma_f32_16x16x32_bf16 v[42:45], v[158:161], v[190:193], v[42:45]
	v_mfma_f32_16x16x32_bf16 v[34:37], v[150:153], v[198:201], v[34:37]
	v_mfma_f32_16x16x32_bf16 v[26:29], v[158:161], v[198:201], v[26:29]
	v_mfma_f32_16x16x32_bf16 v[18:21], v[150:153], v[206:209], v[18:21]
	v_mfma_f32_16x16x32_bf16 v[10:13], v[158:161], v[206:209], v[10:13]
	v_mfma_f32_16x16x32_bf16 v[62:65], v[154:157], v[186:189], v[62:65]
	v_mfma_f32_16x16x32_bf16 v[58:61], v[162:165], v[186:189], v[58:61]
	v_mfma_f32_16x16x32_bf16 v[50:53], v[154:157], v[194:197], v[50:53]
	v_mfma_f32_16x16x32_bf16 v[42:45], v[162:165], v[194:197], v[42:45]
	v_mfma_f32_16x16x32_bf16 v[34:37], v[154:157], v[202:205], v[34:37]
	v_mfma_f32_16x16x32_bf16 v[26:29], v[162:165], v[202:205], v[26:29]
	v_mfma_f32_16x16x32_bf16 v[18:21], v[154:157], v[210:213], v[18:21]
	v_mfma_f32_16x16x32_bf16 v[10:13], v[162:165], v[210:213], v[10:13]
	s_setprio 0
	s_setprio 1
	v_mfma_f32_16x16x32_bf16 v[54:57], v[166:169], v[182:185], v[54:57]
	v_mfma_f32_16x16x32_bf16 v[46:49], v[174:177], v[182:185], v[46:49]
	v_mfma_f32_16x16x32_bf16 v[38:41], v[166:169], v[190:193], v[38:41]
	v_mfma_f32_16x16x32_bf16 v[30:33], v[174:177], v[190:193], v[30:33]
	v_mfma_f32_16x16x32_bf16 v[22:25], v[166:169], v[198:201], v[22:25]
	v_mfma_f32_16x16x32_bf16 v[14:17], v[174:177], v[198:201], v[14:17]
	v_mfma_f32_16x16x32_bf16 v[6:9], v[166:169], v[206:209], v[6:9]
	v_mfma_f32_16x16x32_bf16 v[2:5], v[174:177], v[206:209], v[2:5]
	v_mfma_f32_16x16x32_bf16 v[54:57], v[170:173], v[186:189], v[54:57]
	v_mfma_f32_16x16x32_bf16 v[46:49], v[178:181], v[186:189], v[46:49]
	v_mfma_f32_16x16x32_bf16 v[38:41], v[170:173], v[194:197], v[38:41]
	v_mfma_f32_16x16x32_bf16 v[30:33], v[178:181], v[194:197], v[30:33]
	s_setprio 0
	v_mfma_f32_16x16x32_bf16 v[22:25], v[170:173], v[202:205], v[22:25]
	v_mfma_f32_16x16x32_bf16 v[14:17], v[178:181], v[202:205], v[14:17]
	v_mfma_f32_16x16x32_bf16 v[6:9], v[170:173], v[210:213], v[6:9]
	v_mfma_f32_16x16x32_bf16 v[2:5], v[178:181], v[210:213], v[2:5]
	s_barrier
	s_add_i32 s88, 0, 0x18000
	v_add_u32_e32 v144, s88, v145
	s_add_i32 s89, 0, 0x1c000
	ds_read_b128 v[150:153], v144
	ds_read_b128 v[154:157], v144 offset:1024
	ds_read_b128 v[158:161], v144 offset:2048
	ds_read_b128 v[162:165], v144 offset:3072
	v_add_u32_e32 v144, s89, v145
	ds_read_b128 v[166:169], v144
	ds_read_b128 v[170:173], v144 offset:1024
	ds_read_b128 v[174:177], v144 offset:2048
	ds_read_b128 v[178:181], v144 offset:3072
	s_add_u32 s26, s26, 0x100000
	s_addc_u32 s27, s27, 0
	s_mov_b32 m0, s35
	v_lshl_add_u64 v[220:221], s[26:27], 0, v[136:137]
	ds_read_b128 v[182:185], v148 offset:32768
	ds_read_b128 v[186:189], v148 offset:33792
	ds_read_b128 v[190:193], v148 offset:34816
	ds_read_b128 v[194:197], v148 offset:35840
	ds_read_b128 v[198:201], v148 offset:36864
	ds_read_b128 v[202:205], v148 offset:37888
	ds_read_b128 v[206:209], v148 offset:38912
	ds_read_b128 v[210:213], v148 offset:39936
	global_load_lds_dwordx4 v[220:221], off
	v_lshl_add_u64 v[220:221], s[26:27], 0, v[132:133]
	s_mov_b32 m0, s38
	s_nop 0
	global_load_lds_dwordx4 v[220:221], off
	s_waitcnt vmcnt(8)
	s_waitcnt lgkmcnt(0)
	s_barrier
	s_setprio 1
	s_waitcnt lgkmcnt(0)
	v_mfma_f32_16x16x32_bf16 v[126:129], v[150:153], v[182:185], v[126:129]
	v_mfma_f32_16x16x32_bf16 v[122:125], v[158:161], v[182:185], v[122:125]
	v_mfma_f32_16x16x32_bf16 v[114:117], v[150:153], v[190:193], v[114:117]
	v_mfma_f32_16x16x32_bf16 v[106:109], v[158:161], v[190:193], v[106:109]
	v_mfma_f32_16x16x32_bf16 v[98:101], v[150:153], v[198:201], v[98:101]
	v_mfma_f32_16x16x32_bf16 v[90:93], v[158:161], v[198:201], v[90:93]
	v_mfma_f32_16x16x32_bf16 v[82:85], v[150:153], v[206:209], v[82:85]
	v_mfma_f32_16x16x32_bf16 v[74:77], v[158:161], v[206:209], v[74:77]
	v_mfma_f32_16x16x32_bf16 v[126:129], v[154:157], v[186:189], v[126:129]
	v_mfma_f32_16x16x32_bf16 v[122:125], v[162:165], v[186:189], v[122:125]
	v_mfma_f32_16x16x32_bf16 v[114:117], v[154:157], v[194:197], v[114:117]
	v_mfma_f32_16x16x32_bf16 v[106:109], v[162:165], v[194:197], v[106:109]
	v_mfma_f32_16x16x32_bf16 v[98:101], v[154:157], v[202:205], v[98:101]
	v_mfma_f32_16x16x32_bf16 v[90:93], v[162:165], v[202:205], v[90:93]
	v_mfma_f32_16x16x32_bf16 v[82:85], v[154:157], v[210:213], v[82:85]
	v_mfma_f32_16x16x32_bf16 v[74:77], v[162:165], v[210:213], v[74:77]
	s_setprio 0
	s_setprio 1
	v_mfma_f32_16x16x32_bf16 v[118:121], v[166:169], v[182:185], v[118:121]
	v_mfma_f32_16x16x32_bf16 v[110:113], v[174:177], v[182:185], v[110:113]
	v_mfma_f32_16x16x32_bf16 v[102:105], v[166:169], v[190:193], v[102:105]
	v_mfma_f32_16x16x32_bf16 v[94:97], v[174:177], v[190:193], v[94:97]
	v_mfma_f32_16x16x32_bf16 v[86:89], v[166:169], v[198:201], v[86:89]
	v_mfma_f32_16x16x32_bf16 v[78:81], v[174:177], v[198:201], v[78:81]
	v_mfma_f32_16x16x32_bf16 v[70:73], v[166:169], v[206:209], v[70:73]
	v_mfma_f32_16x16x32_bf16 v[66:69], v[174:177], v[206:209], v[66:69]
	v_mfma_f32_16x16x32_bf16 v[118:121], v[170:173], v[186:189], v[118:121]
	v_mfma_f32_16x16x32_bf16 v[110:113], v[178:181], v[186:189], v[110:113]
	v_mfma_f32_16x16x32_bf16 v[102:105], v[170:173], v[194:197], v[102:105]
	v_mfma_f32_16x16x32_bf16 v[94:97], v[178:181], v[194:197], v[94:97]
	s_setprio 0
	v_mfma_f32_16x16x32_bf16 v[86:89], v[170:173], v[202:205], v[86:89]
	v_mfma_f32_16x16x32_bf16 v[78:81], v[178:181], v[202:205], v[78:81]
	v_mfma_f32_16x16x32_bf16 v[70:73], v[170:173], v[210:213], v[70:73]
	v_mfma_f32_16x16x32_bf16 v[66:69], v[178:181], v[210:213], v[66:69]
	s_barrier
; #define PG8_STAGE(bufoff, gbase, voff) do { _Pragma("unroll") for (int _i = 0; _i < 2; ++_i) \
;         __builtin_amdgcn_global_load_lds((const unsigned*)((const char*)(gbase) + (voff)[_i]), (PG8_LAS unsigned*)(lds + (bufoff) + ldsw + _i * 8192), 16, 0, 0); } while (0)
; #define PG8_WAIT_V(n) asm volatile("s_waitcnt vmcnt(" #n ")" ::: "memory")
; #define PG8_WAIT_L(n) asm volatile("s_waitcnt lgkmcnt(" #n ")" ::: "memory")
; #define PG8_BAR __builtin_amdgcn_s_barrier()
; #define PG8_SCHED __builtin_amdgcn_sched_barrier(0)
; template <class Epi, class Sched, bool ALIGN_EPI, bool F8 = false>
; __device__ __forceinline__ void gemm_phase(PG8_LAS unsigned char* lds, const Gemm g, const Sched& S, const Epi& E, int tid) {
;     ...
;             PG8_LDA(At, 1, 1); PG8_STAGE(PG8_SB(1, 0), b3, voffB); PG8_STAGE(PG8_SB(1, 1), b3 + hstepB, voffB); PG8_STAGE(PG8_SA(1, 0), a3, voffA);
;             PG8_WAIT_V(8); PG8_WAIT_L(0); PG8_BAR; PG8_MMA(1, 0, At, B0); PG8_MMA(1, 1, At, B1); PG8_BAR; PG8_SCHED;
;         }
;         if constexpr (ALIGN_EPI) { if (wr == 0) PG8_BAR; }
	s_add_i32 s26, s88, s30
	v_lshl_add_u64 v[146:147], v[146:147], 0, s[60:61]
	s_mov_b32 m0, s26
	ds_read_b128 v[182:185], v148 offset:49152
	ds_read_b128 v[186:189], v148 offset:50176
	ds_read_b128 v[190:193], v148 offset:51200
	ds_read_b128 v[194:197], v148 offset:52224
	ds_read_b128 v[198:201], v148 offset:53248
	ds_read_b128 v[202:205], v148 offset:54272
	ds_read_b128 v[206:209], v148 offset:55296
	ds_read_b128 v[210:213], v148 offset:56320
	global_load_lds_dwordx4 v[146:147], off
	s_add_i32 m0, s26, 0x2000
	s_add_u32 s24, s24, 0x80080
	v_lshl_add_u64 v[146:147], v[214:215], 0, s[60:61]
	s_addc_u32 s25, s25, 0
	s_add_i32 s26, s89, s30
	global_load_lds_dwordx4 v[146:147], off
	v_lshl_add_u64 v[146:147], s[24:25], 0, v[134:135]
	s_mov_b32 m0, s26
	s_nop 0
	global_load_lds_dwordx4 v[146:147], off
	v_lshl_add_u64 v[146:147], s[24:25], 0, v[130:131]
	s_add_i32 m0, s26, 0x2000
	s_nop 0
	global_load_lds_dwordx4 v[146:147], off
	v_lshl_add_u64 v[146:147], v[216:217], 0, s[60:61]
	s_mov_b32 m0, s45
	s_nop 0
	global_load_lds_dwordx4 v[146:147], off
	v_lshl_add_u64 v[146:147], v[218:219], 0, s[60:61]
	s_mov_b32 m0, s50
	s_nop 0
	global_load_lds_dwordx4 v[146:147], off
	s_waitcnt vmcnt(8)
	s_waitcnt lgkmcnt(0)
	s_barrier
	s_setprio 1
	s_waitcnt lgkmcnt(0)
	v_mfma_f32_16x16x32_bf16 v[62:65], v[150:153], v[182:185], v[62:65]
	v_mfma_f32_16x16x32_bf16 v[58:61], v[158:161], v[182:185], v[58:61]
	v_mfma_f32_16x16x32_bf16 v[50:53], v[150:153], v[190:193], v[50:53]
	v_mfma_f32_16x16x32_bf16 v[42:45], v[158:161], v[190:193], v[42:45]
	v_mfma_f32_16x16x32_bf16 v[34:37], v[150:153], v[198:201], v[34:37]
	v_mfma_f32_16x16x32_bf16 v[26:29], v[158:161], v[198:201], v[26:29]
	v_mfma_f32_16x16x32_bf16 v[18:21], v[150:153], v[206:209], v[18:21]
	v_mfma_f32_16x16x32_bf16 v[10:13], v[158:161], v[206:209], v[10:13]
	v_mfma_f32_16x16x32_bf16 v[62:65], v[154:157], v[186:189], v[62:65]
	v_mfma_f32_16x16x32_bf16 v[58:61], v[162:165], v[186:189], v[58:61]
	v_mfma_f32_16x16x32_bf16 v[50:53], v[154:157], v[194:197], v[50:53]
	v_mfma_f32_16x16x32_bf16 v[42:45], v[162:165], v[194:197], v[42:45]
	v_mfma_f32_16x16x32_bf16 v[34:37], v[154:157], v[202:205], v[34:37]
	v_mfma_f32_16x16x32_bf16 v[26:29], v[162:165], v[202:205], v[26:29]
	v_mfma_f32_16x16x32_bf16 v[18:21], v[154:157], v[210:213], v[18:21]
	v_mfma_f32_16x16x32_bf16 v[10:13], v[162:165], v[210:213], v[10:13]
	s_setprio 0
	s_setprio 1
	v_mfma_f32_16x16x32_bf16 v[54:57], v[166:169], v[182:185], v[54:57]
	v_mfma_f32_16x16x32_bf16 v[46:49], v[174:177], v[182:185], v[46:49]
	v_mfma_f32_16x16x32_bf16 v[38:41], v[166:169], v[190:193], v[38:41]
	v_mfma_f32_16x16x32_bf16 v[30:33], v[174:177], v[190:193], v[30:33]
	v_mfma_f32_16x16x32_bf16 v[22:25], v[166:169], v[198:201], v[22:25]
	v_mfma_f32_16x16x32_bf16 v[14:17], v[174:177], v[198:201], v[14:17]
	v_mfma_f32_16x16x32_bf16 v[6:9], v[166:169], v[206:209], v[6:9]
	v_mfma_f32_16x16x32_bf16 v[2:5], v[174:177], v[206:209], v[2:5]
	v_mfma_f32_16x16x32_bf16 v[54:57], v[170:173], v[186:189], v[54:57]
	v_mfma_f32_16x16x32_bf16 v[46:49], v[178:181], v[186:189], v[46:49]
	v_mfma_f32_16x16x32_bf16 v[38:41], v[170:173], v[194:197], v[38:41]
	v_mfma_f32_16x16x32_bf16 v[30:33], v[178:181], v[194:197], v[30:33]
	s_setprio 0
	v_mfma_f32_16x16x32_bf16 v[22:25], v[170:173], v[202:205], v[22:25]
	v_mfma_f32_16x16x32_bf16 v[14:17], v[178:181], v[202:205], v[14:17]
	v_mfma_f32_16x16x32_bf16 v[6:9], v[170:173], v[210:213], v[6:9]
	v_mfma_f32_16x16x32_bf16 v[2:5], v[178:181], v[210:213], v[2:5]
	s_barrier
	s_add_i32 s87, s87, 2
	s_add_u32 s22, s22, 0x100
	s_addc_u32 s23, s23, 0
	s_add_u32 s85, s85, 0x100
	s_addc_u32 s86, s86, 0
	s_cmp_gt_u32 s87, 5
	s_cbranch_scc0 .LBB0_1147
	s_and_b64 vcc, exec, s[6:7]
	s_cbranch_vccz .LBB0_1150
	s_barrier

; #define PG8_STAGE(bufoff, gbase, voff) do { _Pragma("unroll") for (int _i = 0; _i < 2; ++_i) \
;         __builtin_amdgcn_global_load_lds((const unsigned*)((const char*)(gbase) + (voff)[_i]), (PG8_LAS unsigned*)(lds + (bufoff) + ldsw + _i * 8192), 16, 0, 0); } while (0)
; #define PG8_WAIT_V(n) asm volatile("s_waitcnt vmcnt(" #n ")" ::: "memory")
; #define PG8_WAIT_L(n) asm volatile("s_waitcnt lgkmcnt(" #n ")" ::: "memory")
; #define PG8_BAR __builtin_amdgcn_s_barrier()
; #define PG8_SCHED __builtin_amdgcn_sched_barrier(0)
; template <class Epi, class Sched, bool ALIGN_EPI, bool F8 = false>
; __device__ __forceinline__ void gemm_phase(PG8_LAS unsigned char* lds, const Gemm g, const Sched& S, const Epi& E, int tid) {
;     ...
;         for (int t = 0; t < nt; t += 2) {
;             const bool last = (t == nt - 2);
;             const char* a1 = cA + (size_t)(t + 1) * kstep;
;             const char* a2 = last ? nA : cA + (size_t)(t + 2) * kstep; const char* b2 = last ? nB : cB + (size_t)(t + 2) * kstep;
;             const char* a3 = a2 + kstep; const char* b3 = b2 + kstep;
;             if (last && has_next) S.a_ready(nxt);
;             PG8_LDB(B0, 0, 0); PG8_LDB(B1, 0, 1); PG8_SCHED; PG8_LDA(At, 0, 0); PG8_STAGE(PG8_SA(1, 1), a1 + hstepA, voffA);
;             PG8_WAIT_V(8); PG8_WAIT_L(0); PG8_BAR; PG8_MMA(0, 0, At, B0); PG8_MMA(0, 1, At, B1); PG8_BAR; PG8_SCHED;
;             PG8_LDA(At, 0, 1); PG8_STAGE(PG8_SB(0, 0), b2, voffB); PG8_STAGE(PG8_SB(0, 1), b2 + hstepB, voffB); PG8_STAGE(PG8_SA(0, 0), a2, voffA);
.LBB0_1163:
	s_add_u32 s24, s22, 0xfff80080
	s_addc_u32 s25, s23, -1
	s_add_i32 s87, 0, 0x10000
	s_cmp_eq_u32 s86, 4
	s_cselect_b32 s27, s9, s25
	s_cselect_b32 s26, s11, s24
	v_add_u32_e32 v144, s87, v145
	s_cselect_b32 s25, s13, s85
	s_cselect_b32 s24, s83, s84
	s_add_i32 s94, 0, 0x14000
	ds_read_b128 v[150:153], v144
	ds_read_b128 v[154:157], v144 offset:1024
	ds_read_b128 v[158:161], v144 offset:2048
	ds_read_b128 v[162:165], v144 offset:3072
	v_add_u32_e32 v144, s94, v145
	ds_read_b128 v[166:169], v144
	ds_read_b128 v[170:173], v144 offset:1024
	ds_read_b128 v[174:177], v144 offset:2048
	ds_read_b128 v[178:181], v144 offset:3072
	v_lshl_add_u64 v[146:147], s[22:23], 0, v[140:141]
	s_add_i32 m0, s31, 0xc000
	ds_read_b128 v[182:185], v148
	ds_read_b128 v[186:189], v148 offset:1024
	ds_read_b128 v[190:193], v148 offset:2048
	ds_read_b128 v[194:197], v148 offset:3072
	ds_read_b128 v[198:201], v148 offset:4096
	ds_read_b128 v[202:205], v148 offset:5120
	ds_read_b128 v[206:209], v148 offset:6144
	ds_read_b128 v[210:213], v148 offset:7168
	global_load_lds_dwordx4 v[146:147], off
	v_lshl_add_u64 v[146:147], s[22:23], 0, v[142:143]
	s_add_i32 m0, s31, 0xe000
	s_nop 0
	global_load_lds_dwordx4 v[146:147], off
	s_waitcnt vmcnt(8)
	s_waitcnt lgkmcnt(0)
	s_barrier
	s_setprio 1
	s_waitcnt lgkmcnt(0)
	v_mfma_f32_16x16x32_bf16 v[126:129], v[150:153], v[182:185], v[126:129]
	v_mfma_f32_16x16x32_bf16 v[122:125], v[158:161], v[182:185], v[122:125]
	v_mfma_f32_16x16x32_bf16 v[114:117], v[150:153], v[190:193], v[114:117]
	v_mfma_f32_16x16x32_bf16 v[106:109], v[158:161], v[190:193], v[106:109]
	v_mfma_f32_16x16x32_bf16 v[98:101], v[150:153], v[198:201], v[98:101]
	v_mfma_f32_16x16x32_bf16 v[90:93], v[158:161], v[198:201], v[90:93]
	v_mfma_f32_16x16x32_bf16 v[82:85], v[150:153], v[206:209], v[82:85]
	v_mfma_f32_16x16x32_bf16 v[74:77], v[158:161], v[206:209], v[74:77]
	v_mfma_f32_16x16x32_bf16 v[126:129], v[154:157], v[186:189], v[126:129]
	v_mfma_f32_16x16x32_bf16 v[122:125], v[162:165], v[186:189], v[122:125]
	v_mfma_f32_16x16x32_bf16 v[114:117], v[154:157], v[194:197], v[114:117]
	v_mfma_f32_16x16x32_bf16 v[106:109], v[162:165], v[194:197], v[106:109]
	v_mfma_f32_16x16x32_bf16 v[98:101], v[154:157], v[202:205], v[98:101]
	v_mfma_f32_16x16x32_bf16 v[90:93], v[162:165], v[202:205], v[90:93]
	v_mfma_f32_16x16x32_bf16 v[82:85], v[154:157], v[210:213], v[82:85]
	v_mfma_f32_16x16x32_bf16 v[74:77], v[162:165], v[210:213], v[74:77]
	s_setprio 0
	s_setprio 1
	v_mfma_f32_16x16x32_bf16 v[118:121], v[166:169], v[182:185], v[118:121]
	v_mfma_f32_16x16x32_bf16 v[110:113], v[174:177], v[182:185], v[110:113]
	v_mfma_f32_16x16x32_bf16 v[102:105], v[166:169], v[190:193], v[102:105]
	v_mfma_f32_16x16x32_bf16 v[94:97], v[174:177], v[190:193], v[94:97]
	v_mfma_f32_16x16x32_bf16 v[86:89], v[166:169], v[198:201], v[86:89]
	v_mfma_f32_16x16x32_bf16 v[78:81], v[174:177], v[198:201], v[78:81]
	v_mfma_f32_16x16x32_bf16 v[70:73], v[166:169], v[206:209], v[70:73]
	v_mfma_f32_16x16x32_bf16 v[66:69], v[174:177], v[206:209], v[66:69]
	v_mfma_f32_16x16x32_bf16 v[118:121], v[170:173], v[186:189], v[118:121]
	v_mfma_f32_16x16x32_bf16 v[110:113], v[178:181], v[186:189], v[110:113]
	v_mfma_f32_16x16x32_bf16 v[102:105], v[170:173], v[194:197], v[102:105]
	v_mfma_f32_16x16x32_bf16 v[94:97], v[178:181], v[194:197], v[94:97]
	s_setprio 0
	v_mfma_f32_16x16x32_bf16 v[86:89], v[170:173], v[202:205], v[86:89]
	v_mfma_f32_16x16x32_bf16 v[78:81], v[178:181], v[202:205], v[78:81]
	v_mfma_f32_16x16x32_bf16 v[70:73], v[170:173], v[210:213], v[70:73]
	v_mfma_f32_16x16x32_bf16 v[66:69], v[178:181], v[210:213], v[66:69]
	s_barrier
	s_add_i32 s87, s87, s30
	v_lshl_add_u64 v[146:147], s[24:25], 0, v[134:135]
	s_mov_b32 m0, s87
	ds_read_b128 v[182:185], v148 offset:16384
	ds_read_b128 v[186:189], v148 offset:17408
	ds_read_b128 v[190:193], v148 offset:18432
	ds_read_b128 v[194:197], v148 offset:19456
	ds_read_b128 v[198:201], v148 offset:20480
	ds_read_b128 v[202:205], v148 offset:21504
	ds_read_b128 v[206:209], v148 offset:22528
	ds_read_b128 v[210:213], v148 offset:23552
	global_load_lds_dwordx4 v[146:147], off
	s_add_i32 m0, s87, 0x2000
	s_add_u32 s88, s24, 0x100000
	v_lshl_add_u64 v[214:215], s[24:25], 0, v[130:131]
	s_addc_u32 s89, s25, 0
	s_add_i32 s87, s94, s30
	global_load_lds_dwordx4 v[214:215], off
	v_lshl_add_u64 v[216:217], s[88:89], 0, v[134:135]
	s_mov_b32 m0, s87
	v_lshl_add_u64 v[218:219], s[26:27], 0, v[132:133]
	global_load_lds_dwordx4 v[216:217], off
	v_lshl_add_u64 v[216:217], s[88:89], 0, v[130:131]
	s_add_i32 m0, s87, 0x2000
	s_nop 0
	global_load_lds_dwordx4 v[216:217], off
	v_lshl_add_u64 v[216:217], s[26:27], 0, v[136:137]
	s_mov_b32 m0, s31
	s_nop 0
	global_load_lds_dwordx4 v[216:217], off
	s_mov_b32 m0, s34
	s_nop 0
	global_load_lds_dwordx4 v[218:219], off
	s_waitcnt vmcnt(8)
	s_waitcnt lgkmcnt(0)
	s_barrier
; #define PG8_STAGE(bufoff, gbase, voff) do { _Pragma("unroll") for (int _i = 0; _i < 2; ++_i) \
;         __builtin_amdgcn_global_load_lds((const unsigned*)((const char*)(gbase) + (voff)[_i]), (PG8_LAS unsigned*)(lds + (bufoff) + ldsw + _i * 8192), 16, 0, 0); } while (0)
; #define PG8_WAIT_V(n) asm volatile("s_waitcnt vmcnt(" #n ")" ::: "memory")
; #define PG8_WAIT_L(n) asm volatile("s_waitcnt lgkmcnt(" #n ")" ::: "memory")
; #define PG8_BAR __builtin_amdgcn_s_barrier()
; #define PG8_SCHED __builtin_amdgcn_sched_barrier(0)
; template <class Epi, class Sched, bool ALIGN_EPI, bool F8 = false>
; __device__ __forceinline__ void gemm_phase(PG8_LAS unsigned char* lds, const Gemm g, const Sched& S, const Epi& E, int tid) {
;     ...
;             PG8_WAIT_V(8); PG8_WAIT_L(0); PG8_BAR; PG8_MMA(1, 0, At, B0); PG8_MMA(1, 1, At, B1); PG8_BAR; PG8_SCHED;
;             PG8_LDB(B0, 1, 0); PG8_LDB(B1, 1, 1); PG8_SCHED; PG8_LDA(At, 1, 0); PG8_STAGE(PG8_SA(0, 1), a2 + hstepA, voffA);
;             PG8_WAIT_V(8); PG8_WAIT_L(0); PG8_BAR; PG8_MMA(0, 0, At, B0); PG8_MMA(0, 1, At, B1); PG8_BAR; PG8_SCHED;
	s_setprio 1
	s_waitcnt lgkmcnt(0)
	v_mfma_f32_16x16x32_bf16 v[62:65], v[150:153], v[182:185], v[62:65]
	v_mfma_f32_16x16x32_bf16 v[58:61], v[158:161], v[182:185], v[58:61]
	v_mfma_f32_16x16x32_bf16 v[50:53], v[150:153], v[190:193], v[50:53]
	v_mfma_f32_16x16x32_bf16 v[42:45], v[158:161], v[190:193], v[42:45]
	v_mfma_f32_16x16x32_bf16 v[34:37], v[150:153], v[198:201], v[34:37]
	v_mfma_f32_16x16x32_bf16 v[26:29], v[158:161], v[198:201], v[26:29]
	v_mfma_f32_16x16x32_bf16 v[18:21], v[150:153], v[206:209], v[18:21]
	v_mfma_f32_16x16x32_bf16 v[10:13], v[158:161], v[206:209], v[10:13]
	v_mfma_f32_16x16x32_bf16 v[62:65], v[154:157], v[186:189], v[62:65]
	v_mfma_f32_16x16x32_bf16 v[58:61], v[162:165], v[186:189], v[58:61]
	v_mfma_f32_16x16x32_bf16 v[50:53], v[154:157], v[194:197], v[50:53]
	v_mfma_f32_16x16x32_bf16 v[42:45], v[162:165], v[194:197], v[42:45]
	v_mfma_f32_16x16x32_bf16 v[34:37], v[154:157], v[202:205], v[34:37]
	v_mfma_f32_16x16x32_bf16 v[26:29], v[162:165], v[202:205], v[26:29]
	v_mfma_f32_16x16x32_bf16 v[18:21], v[154:157], v[210:213], v[18:21]
	v_mfma_f32_16x16x32_bf16 v[10:13], v[162:165], v[210:213], v[10:13]
	s_setprio 0
	s_setprio 1
	v_mfma_f32_16x16x32_bf16 v[54:57], v[166:169], v[182:185], v[54:57]
	v_mfma_f32_16x16x32_bf16 v[46:49], v[174:177], v[182:185], v[46:49]
	v_mfma_f32_16x16x32_bf16 v[38:41], v[166:169], v[190:193], v[38:41]
	v_mfma_f32_16x16x32_bf16 v[30:33], v[174:177], v[190:193], v[30:33]
	v_mfma_f32_16x16x32_bf16 v[22:25], v[166:169], v[198:201], v[22:25]
	v_mfma_f32_16x16x32_bf16 v[14:17], v[174:177], v[198:201], v[14:17]
	v_mfma_f32_16x16x32_bf16 v[6:9], v[166:169], v[206:209], v[6:9]
	v_mfma_f32_16x16x32_bf16 v[2:5], v[174:177], v[206:209], v[2:5]
	v_mfma_f32_16x16x32_bf16 v[54:57], v[170:173], v[186:189], v[54:57]
	v_mfma_f32_16x16x32_bf16 v[46:49], v[178:181], v[186:189], v[46:49]
	v_mfma_f32_16x16x32_bf16 v[38:41], v[170:173], v[194:197], v[38:41]
	v_mfma_f32_16x16x32_bf16 v[30:33], v[178:181], v[194:197], v[30:33]
	s_setprio 0
	v_mfma_f32_16x16x32_bf16 v[22:25], v[170:173], v[202:205], v[22:25]
	v_mfma_f32_16x16x32_bf16 v[14:17], v[178:181], v[202:205], v[14:17]
	v_mfma_f32_16x16x32_bf16 v[6:9], v[170:173], v[210:213], v[6:9]
	v_mfma_f32_16x16x32_bf16 v[2:5], v[178:181], v[210:213], v[2:5]
	s_barrier
	s_add_i32 s87, 0, 0x18000
	v_add_u32_e32 v144, s87, v145
	s_add_i32 s88, 0, 0x1c000
	ds_read_b128 v[150:153], v144
	ds_read_b128 v[154:157], v144 offset:1024
	ds_read_b128 v[158:161], v144 offset:2048
	ds_read_b128 v[162:165], v144 offset:3072
	v_add_u32_e32 v144, s88, v145
	ds_read_b128 v[166:169], v144
	ds_read_b128 v[170:173], v144 offset:1024
	ds_read_b128 v[174:177], v144 offset:2048
	ds_read_b128 v[178:181], v144 offset:3072
	s_add_u32 s26, s26, 0x80000
	s_addc_u32 s27, s27, 0
	s_mov_b32 m0, s35
	v_lshl_add_u64 v[220:221], s[26:27], 0, v[136:137]
	ds_read_b128 v[182:185], v148 offset:32768
	ds_read_b128 v[186:189], v148 offset:33792
	ds_read_b128 v[190:193], v148 offset:34816
	ds_read_b128 v[194:197], v148 offset:35840
	ds_read_b128 v[198:201], v148 offset:36864
	ds_read_b128 v[202:205], v148 offset:37888
	ds_read_b128 v[206:209], v148 offset:38912
	ds_read_b128 v[210:213], v148 offset:39936
	global_load_lds_dwordx4 v[220:221], off
	v_lshl_add_u64 v[220:221], s[26:27], 0, v[132:133]
	s_mov_b32 m0, s38
	s_nop 0
	global_load_lds_dwordx4 v[220:221], off
	s_waitcnt vmcnt(8)
	s_waitcnt lgkmcnt(0)
	s_barrier
	s_setprio 1
	s_waitcnt lgkmcnt(0)
	v_mfma_f32_16x16x32_bf16 v[126:129], v[150:153], v[182:185], v[126:129]
	v_mfma_f32_16x16x32_bf16 v[122:125], v[158:161], v[182:185], v[122:125]
	v_mfma_f32_16x16x32_bf16 v[114:117], v[150:153], v[190:193], v[114:117]
	v_mfma_f32_16x16x32_bf16 v[106:109], v[158:161], v[190:193], v[106:109]
	v_mfma_f32_16x16x32_bf16 v[98:101], v[150:153], v[198:201], v[98:101]
	v_mfma_f32_16x16x32_bf16 v[90:93], v[158:161], v[198:201], v[90:93]
	v_mfma_f32_16x16x32_bf16 v[82:85], v[150:153], v[206:209], v[82:85]
	v_mfma_f32_16x16x32_bf16 v[74:77], v[158:161], v[206:209], v[74:77]
	v_mfma_f32_16x16x32_bf16 v[126:129], v[154:157], v[186:189], v[126:129]
	v_mfma_f32_16x16x32_bf16 v[122:125], v[162:165], v[186:189], v[122:125]
	v_mfma_f32_16x16x32_bf16 v[114:117], v[154:157], v[194:197], v[114:117]
	v_mfma_f32_16x16x32_bf16 v[106:109], v[162:165], v[194:197], v[106:109]
	v_mfma_f32_16x16x32_bf16 v[98:101], v[154:157], v[202:205], v[98:101]
	v_mfma_f32_16x16x32_bf16 v[90:93], v[162:165], v[202:205], v[90:93]
	v_mfma_f32_16x16x32_bf16 v[82:85], v[154:157], v[210:213], v[82:85]
	v_mfma_f32_16x16x32_bf16 v[74:77], v[162:165], v[210:213], v[74:77]
	s_setprio 0
	s_setprio 1
	v_mfma_f32_16x16x32_bf16 v[118:121], v[166:169], v[182:185], v[118:121]
	v_mfma_f32_16x16x32_bf16 v[110:113], v[174:177], v[182:185], v[110:113]
	v_mfma_f32_16x16x32_bf16 v[102:105], v[166:169], v[190:193], v[102:105]
	v_mfma_f32_16x16x32_bf16 v[94:97], v[174:177], v[190:193], v[94:97]
	v_mfma_f32_16x16x32_bf16 v[86:89], v[166:169], v[198:201], v[86:89]
	v_mfma_f32_16x16x32_bf16 v[78:81], v[174:177], v[198:201], v[78:81]
	v_mfma_f32_16x16x32_bf16 v[70:73], v[166:169], v[206:209], v[70:73]
	v_mfma_f32_16x16x32_bf16 v[66:69], v[174:177], v[206:209], v[66:69]
	v_mfma_f32_16x16x32_bf16 v[118:121], v[170:173], v[186:189], v[118:121]
	v_mfma_f32_16x16x32_bf16 v[110:113], v[178:181], v[186:189], v[110:113]
	v_mfma_f32_16x16x32_bf16 v[102:105], v[170:173], v[194:197], v[102:105]
	v_mfma_f32_16x16x32_bf16 v[94:97], v[178:181], v[194:197], v[94:97]
	s_setprio 0
	v_mfma_f32_16x16x32_bf16 v[86:89], v[170:173], v[202:205], v[86:89]
	v_mfma_f32_16x16x32_bf16 v[78:81], v[178:181], v[202:205], v[78:81]
	v_mfma_f32_16x16x32_bf16 v[70:73], v[170:173], v[210:213], v[70:73]
	v_mfma_f32_16x16x32_bf16 v[66:69], v[178:181], v[210:213], v[66:69]
	s_barrier
; #define PG8_STAGE(bufoff, gbase, voff) do { _Pragma("unroll") for (int _i = 0; _i < 2; ++_i) \
;         __builtin_amdgcn_global_load_lds((const unsigned*)((const char*)(gbase) + (voff)[_i]), (PG8_LAS unsigned*)(lds + (bufoff) + ldsw + _i * 8192), 16, 0, 0); } while (0)
; #define PG8_WAIT_V(n) asm volatile("s_waitcnt vmcnt(" #n ")" ::: "memory")
; #define PG8_WAIT_L(n) asm volatile("s_waitcnt lgkmcnt(" #n ")" ::: "memory")
; #define PG8_BAR __builtin_amdgcn_s_barrier()
; #define PG8_SCHED __builtin_amdgcn_sched_barrier(0)
; template <class Epi, class Sched, bool ALIGN_EPI, bool F8 = false>
; __device__ __forceinline__ void gemm_phase(PG8_LAS unsigned char* lds, const Gemm g, const Sched& S, const Epi& E, int tid) {
;     ...
;             PG8_LDA(At, 1, 1); PG8_STAGE(PG8_SB(1, 0), b3, voffB); PG8_STAGE(PG8_SB(1, 1), b3 + hstepB, voffB); PG8_STAGE(PG8_SA(1, 0), a3, voffA);
;             PG8_WAIT_V(8); PG8_WAIT_L(0); PG8_BAR; PG8_MMA(1, 0, At, B0); PG8_MMA(1, 1, At, B1); PG8_BAR; PG8_SCHED;
;         }
;         if constexpr (ALIGN_EPI) { if (wr == 0) PG8_BAR; }
	s_add_i32 s26, s87, s30
	v_lshl_add_u64 v[146:147], v[146:147], 0, s[60:61]
	s_mov_b32 m0, s26
	ds_read_b128 v[182:185], v148 offset:49152
	ds_read_b128 v[186:189], v148 offset:50176
	ds_read_b128 v[190:193], v148 offset:51200
	ds_read_b128 v[194:197], v148 offset:52224
	ds_read_b128 v[198:201], v148 offset:53248
	ds_read_b128 v[202:205], v148 offset:54272
	ds_read_b128 v[206:209], v148 offset:55296
	ds_read_b128 v[210:213], v148 offset:56320
	global_load_lds_dwordx4 v[146:147], off
	s_add_i32 m0, s26, 0x2000
	s_add_u32 s24, s24, 0x100080
	v_lshl_add_u64 v[146:147], v[214:215], 0, s[60:61]
	s_addc_u32 s25, s25, 0
	s_add_i32 s26, s88, s30
	global_load_lds_dwordx4 v[146:147], off
	v_lshl_add_u64 v[146:147], s[24:25], 0, v[134:135]
	s_mov_b32 m0, s26
	s_nop 0
	global_load_lds_dwordx4 v[146:147], off
	v_lshl_add_u64 v[146:147], s[24:25], 0, v[130:131]
	s_add_i32 m0, s26, 0x2000
	s_nop 0
	global_load_lds_dwordx4 v[146:147], off
	v_lshl_add_u64 v[146:147], v[216:217], 0, s[60:61]
	s_mov_b32 m0, s45
	s_nop 0
	global_load_lds_dwordx4 v[146:147], off
	v_lshl_add_u64 v[146:147], v[218:219], 0, s[60:61]
	s_mov_b32 m0, s50
	s_nop 0
	global_load_lds_dwordx4 v[146:147], off
	s_waitcnt vmcnt(8)
	s_waitcnt lgkmcnt(0)
	s_barrier
	s_setprio 1
	s_waitcnt lgkmcnt(0)
	v_mfma_f32_16x16x32_bf16 v[62:65], v[150:153], v[182:185], v[62:65]
	v_mfma_f32_16x16x32_bf16 v[58:61], v[158:161], v[182:185], v[58:61]
	v_mfma_f32_16x16x32_bf16 v[50:53], v[150:153], v[190:193], v[50:53]
	v_mfma_f32_16x16x32_bf16 v[42:45], v[158:161], v[190:193], v[42:45]
	v_mfma_f32_16x16x32_bf16 v[34:37], v[150:153], v[198:201], v[34:37]
	v_mfma_f32_16x16x32_bf16 v[26:29], v[158:161], v[198:201], v[26:29]
	v_mfma_f32_16x16x32_bf16 v[18:21], v[150:153], v[206:209], v[18:21]
	v_mfma_f32_16x16x32_bf16 v[10:13], v[158:161], v[206:209], v[10:13]
	v_mfma_f32_16x16x32_bf16 v[62:65], v[154:157], v[186:189], v[62:65]
	v_mfma_f32_16x16x32_bf16 v[58:61], v[162:165], v[186:189], v[58:61]
	v_mfma_f32_16x16x32_bf16 v[50:53], v[154:157], v[194:197], v[50:53]
	v_mfma_f32_16x16x32_bf16 v[42:45], v[162:165], v[194:197], v[42:45]
	v_mfma_f32_16x16x32_bf16 v[34:37], v[154:157], v[202:205], v[34:37]
	v_mfma_f32_16x16x32_bf16 v[26:29], v[162:165], v[202:205], v[26:29]
	v_mfma_f32_16x16x32_bf16 v[18:21], v[154:157], v[210:213], v[18:21]
	v_mfma_f32_16x16x32_bf16 v[10:13], v[162:165], v[210:213], v[10:13]
	s_setprio 0
	s_setprio 1
	v_mfma_f32_16x16x32_bf16 v[54:57], v[166:169], v[182:185], v[54:57]
	v_mfma_f32_16x16x32_bf16 v[46:49], v[174:177], v[182:185], v[46:49]
	v_mfma_f32_16x16x32_bf16 v[38:41], v[166:169], v[190:193], v[38:41]
	v_mfma_f32_16x16x32_bf16 v[30:33], v[174:177], v[190:193], v[30:33]
	v_mfma_f32_16x16x32_bf16 v[22:25], v[166:169], v[198:201], v[22:25]
	v_mfma_f32_16x16x32_bf16 v[14:17], v[174:177], v[198:201], v[14:17]
	v_mfma_f32_16x16x32_bf16 v[6:9], v[166:169], v[206:209], v[6:9]
	v_mfma_f32_16x16x32_bf16 v[2:5], v[174:177], v[206:209], v[2:5]
	v_mfma_f32_16x16x32_bf16 v[54:57], v[170:173], v[186:189], v[54:57]
	v_mfma_f32_16x16x32_bf16 v[46:49], v[178:181], v[186:189], v[46:49]
	v_mfma_f32_16x16x32_bf16 v[38:41], v[170:173], v[194:197], v[38:41]
	v_mfma_f32_16x16x32_bf16 v[30:33], v[178:181], v[194:197], v[30:33]
	s_setprio 0
	v_mfma_f32_16x16x32_bf16 v[22:25], v[170:173], v[202:205], v[22:25]
	v_mfma_f32_16x16x32_bf16 v[14:17], v[178:181], v[202:205], v[14:17]
	v_mfma_f32_16x16x32_bf16 v[6:9], v[170:173], v[210:213], v[6:9]
	v_mfma_f32_16x16x32_bf16 v[2:5], v[178:181], v[210:213], v[2:5]
	s_barrier
	s_add_i32 s86, s86, 2
	s_add_u32 s22, s22, 0x100
	s_addc_u32 s23, s23, 0
	s_add_u32 s84, s84, 0x100
	s_addc_u32 s85, s85, 0
	s_cmp_gt_u32 s86, 5
	s_cbranch_scc0 .LBB0_1163
	s_and_b64 vcc, exec, s[6:7]
	s_cbranch_vccz .LBB0_1166
	s_barrier

; #define PG8_STAGE(bufoff, gbase, voff) do { _Pragma("unroll") for (int _i = 0; _i < 2; ++_i) \
;         __builtin_amdgcn_global_load_lds((const unsigned*)((const char*)(gbase) + (voff)[_i]), (PG8_LAS unsigned*)(lds + (bufoff) + ldsw + _i * 8192), 16, 0, 0); } while (0)
; #define PG8_WAIT_V(n) asm volatile("s_waitcnt vmcnt(" #n ")" ::: "memory")
; #define PG8_WAIT_L(n) asm volatile("s_waitcnt lgkmcnt(" #n ")" ::: "memory")
; #define PG8_BAR __builtin_amdgcn_s_barrier()
; #define PG8_SCHED __builtin_amdgcn_sched_barrier(0)
; template <class Epi, class Sched, bool ALIGN_EPI, bool F8 = false>
; __device__ __forceinline__ void gemm_phase(PG8_LAS unsigned char* lds, const Gemm g, const Sched& S, const Epi& E, int tid) {
;     ...
;         for (int t = 0; t < nt; t += 2) {
;             const bool last = (t == nt - 2);
;             const char* a1 = cA + (size_t)(t + 1) * kstep;
;             const char* a2 = last ? nA : cA + (size_t)(t + 2) * kstep; const char* b2 = last ? nB : cB + (size_t)(t + 2) * kstep;
;             const char* a3 = a2 + kstep; const char* b3 = b2 + kstep;
;             if (last && has_next) S.a_ready(nxt);
;             PG8_LDB(B0, 0, 0); PG8_LDB(B1, 0, 1); PG8_SCHED; PG8_LDA(At, 0, 0); PG8_STAGE(PG8_SA(1, 1), a1 + hstepA, voffA);
;             PG8_WAIT_V(8); PG8_WAIT_L(0); PG8_BAR; PG8_MMA(0, 0, At, B0); PG8_MMA(0, 1, At, B1); PG8_BAR; PG8_SCHED;
;             PG8_LDA(At, 0, 1); PG8_STAGE(PG8_SB(0, 0), b2, voffB); PG8_STAGE(PG8_SB(0, 1), b2 + hstepB, voffB); PG8_STAGE(PG8_SA(0, 0), a2, voffA);
.LBB0_1239:
	s_add_u32 s10, s12, 0x100
	s_addc_u32 s11, s13, 0
	s_add_i32 s88, 0, 0x10000
	s_cmp_eq_u32 s25, 12
	s_cselect_b32 s31, s27, s11
	s_cselect_b32 s30, s26, s10
	s_cselect_b32 s15, s29, s7
	s_cselect_b32 s14, s28, s6
	s_add_i32 s89, 0, 0x14000
	v_add_u32_e32 v152, s88, v236
	v_add_u32_e32 v168, s89, v236
	ds_read_b128 v[140:143], v152
	ds_read_b128 v[144:147], v152 offset:1024
	ds_read_b128 v[148:151], v152 offset:2048
	ds_read_b128 v[152:155], v152 offset:3072
	ds_read_b128 v[156:159], v168
	ds_read_b128 v[160:163], v168 offset:1024
	ds_read_b128 v[164:167], v168 offset:2048
	ds_read_b128 v[168:171], v168 offset:3072
	v_lshl_add_u64 v[204:205], s[12:13], 0, v[136:137]
	s_add_i32 m0, s45, 0xc000
	ds_read_b128 v[172:175], v238
	ds_read_b128 v[176:179], v238 offset:1024
	ds_read_b128 v[180:183], v238 offset:2048
	ds_read_b128 v[184:187], v238 offset:3072
	ds_read_b128 v[188:191], v238 offset:4096
	ds_read_b128 v[192:195], v238 offset:5120
	ds_read_b128 v[196:199], v238 offset:6144
	ds_read_b128 v[200:203], v238 offset:7168
	global_load_lds_dwordx4 v[204:205], off
	v_lshl_add_u64 v[204:205], s[12:13], 0, v[138:139]
	s_add_i32 m0, s45, 0xe000
	s_nop 0
	global_load_lds_dwordx4 v[204:205], off
	s_waitcnt vmcnt(8)
	s_waitcnt lgkmcnt(0)
	s_barrier
	s_setprio 1
	s_waitcnt lgkmcnt(0)
	v_mfma_f32_16x16x32_bf16 v[126:129], v[140:143], v[172:175], v[126:129]
	v_mfma_f32_16x16x32_bf16 v[122:125], v[148:151], v[172:175], v[122:125]
	v_mfma_f32_16x16x32_bf16 v[118:121], v[140:143], v[180:183], v[118:121]
	v_mfma_f32_16x16x32_bf16 v[114:117], v[148:151], v[180:183], v[114:117]
	v_mfma_f32_16x16x32_bf16 v[110:113], v[140:143], v[188:191], v[110:113]
	v_mfma_f32_16x16x32_bf16 v[106:109], v[148:151], v[188:191], v[106:109]
	v_mfma_f32_16x16x32_bf16 v[102:105], v[140:143], v[196:199], v[102:105]
	v_mfma_f32_16x16x32_bf16 v[98:101], v[148:151], v[196:199], v[98:101]
	v_mfma_f32_16x16x32_bf16 v[126:129], v[144:147], v[176:179], v[126:129]
	v_mfma_f32_16x16x32_bf16 v[122:125], v[152:155], v[176:179], v[122:125]
	v_mfma_f32_16x16x32_bf16 v[118:121], v[144:147], v[184:187], v[118:121]
	v_mfma_f32_16x16x32_bf16 v[114:117], v[152:155], v[184:187], v[114:117]
	v_mfma_f32_16x16x32_bf16 v[110:113], v[144:147], v[192:195], v[110:113]
	v_mfma_f32_16x16x32_bf16 v[106:109], v[152:155], v[192:195], v[106:109]
	v_mfma_f32_16x16x32_bf16 v[102:105], v[144:147], v[200:203], v[102:105]
	v_mfma_f32_16x16x32_bf16 v[98:101], v[152:155], v[200:203], v[98:101]
	s_setprio 0
	s_setprio 1
	v_mfma_f32_16x16x32_bf16 v[94:97], v[156:159], v[172:175], v[94:97]
	v_mfma_f32_16x16x32_bf16 v[90:93], v[164:167], v[172:175], v[90:93]
	v_mfma_f32_16x16x32_bf16 v[86:89], v[156:159], v[180:183], v[86:89]
	v_mfma_f32_16x16x32_bf16 v[82:85], v[164:167], v[180:183], v[82:85]
	v_mfma_f32_16x16x32_bf16 v[78:81], v[156:159], v[188:191], v[78:81]
	v_mfma_f32_16x16x32_bf16 v[74:77], v[164:167], v[188:191], v[74:77]
	v_mfma_f32_16x16x32_bf16 v[70:73], v[156:159], v[196:199], v[70:73]
	v_mfma_f32_16x16x32_bf16 v[66:69], v[164:167], v[196:199], v[66:69]
	v_mfma_f32_16x16x32_bf16 v[94:97], v[160:163], v[176:179], v[94:97]
	v_mfma_f32_16x16x32_bf16 v[90:93], v[168:171], v[176:179], v[90:93]
	v_mfma_f32_16x16x32_bf16 v[86:89], v[160:163], v[184:187], v[86:89]
	v_mfma_f32_16x16x32_bf16 v[82:85], v[168:171], v[184:187], v[82:85]
	s_setprio 0
	v_mfma_f32_16x16x32_bf16 v[78:81], v[160:163], v[192:195], v[78:81]
	v_mfma_f32_16x16x32_bf16 v[74:77], v[168:171], v[192:195], v[74:77]
	v_mfma_f32_16x16x32_bf16 v[70:73], v[160:163], v[200:203], v[70:73]
	v_mfma_f32_16x16x32_bf16 v[66:69], v[168:171], v[200:203], v[66:69]
	s_barrier
	s_add_i32 s12, s88, s44
	v_lshl_add_u64 v[204:205], s[14:15], 0, v[0:1]
	s_mov_b32 m0, s12
	ds_read_b128 v[172:175], v238 offset:16384
	ds_read_b128 v[176:179], v238 offset:17408
	ds_read_b128 v[180:183], v238 offset:18432
	ds_read_b128 v[184:187], v238 offset:19456
	ds_read_b128 v[188:191], v238 offset:20480
	ds_read_b128 v[192:195], v238 offset:21504
	ds_read_b128 v[196:199], v238 offset:22528
	ds_read_b128 v[200:203], v238 offset:23552
	global_load_lds_dwordx4 v[204:205], off
	s_add_i32 m0, s12, 0x2000
	s_add_u32 s12, s14, 0xc0000
	v_lshl_add_u64 v[206:207], s[14:15], 0, v[130:131]
	s_addc_u32 s13, s15, 0
	s_add_i32 s88, s89, s44
	global_load_lds_dwordx4 v[206:207], off
	v_lshl_add_u64 v[208:209], s[12:13], 0, v[0:1]
	s_mov_b32 m0, s88
	v_lshl_add_u64 v[210:211], s[30:31], 0, v[132:133]
	global_load_lds_dwordx4 v[208:209], off
	v_lshl_add_u64 v[208:209], s[12:13], 0, v[130:131]
	s_add_i32 m0, s88, 0x2000
	s_nop 0
	global_load_lds_dwordx4 v[208:209], off
	v_lshl_add_u64 v[208:209], s[30:31], 0, v[134:135]
	s_mov_b32 m0, s45
	s_nop 0
	global_load_lds_dwordx4 v[208:209], off
	s_mov_b32 m0, s50
	s_nop 0
	global_load_lds_dwordx4 v[210:211], off
	s_waitcnt vmcnt(8)
	s_waitcnt lgkmcnt(0)
	s_barrier
; #define PG8_STAGE(bufoff, gbase, voff) do { _Pragma("unroll") for (int _i = 0; _i < 2; ++_i) \
;         __builtin_amdgcn_global_load_lds((const unsigned*)((const char*)(gbase) + (voff)[_i]), (PG8_LAS unsigned*)(lds + (bufoff) + ldsw + _i * 8192), 16, 0, 0); } while (0)
; #define PG8_WAIT_V(n) asm volatile("s_waitcnt vmcnt(" #n ")" ::: "memory")
; #define PG8_WAIT_L(n) asm volatile("s_waitcnt lgkmcnt(" #n ")" ::: "memory")
; #define PG8_BAR __builtin_amdgcn_s_barrier()
; #define PG8_SCHED __builtin_amdgcn_sched_barrier(0)
; template <class Epi, class Sched, bool ALIGN_EPI, bool F8 = false>
; __device__ __forceinline__ void gemm_phase(PG8_LAS unsigned char* lds, const Gemm g, const Sched& S, const Epi& E, int tid) {
;     ...
;             PG8_WAIT_V(8); PG8_WAIT_L(0); PG8_BAR; PG8_MMA(1, 0, At, B0); PG8_MMA(1, 1, At, B1); PG8_BAR; PG8_SCHED;
;             PG8_LDB(B0, 1, 0); PG8_LDB(B1, 1, 1); PG8_SCHED; PG8_LDA(At, 1, 0); PG8_STAGE(PG8_SA(0, 1), a2 + hstepA, voffA);
;             PG8_WAIT_V(8); PG8_WAIT_L(0); PG8_BAR; PG8_MMA(0, 0, At, B0); PG8_MMA(0, 1, At, B1); PG8_BAR; PG8_SCHED;
	s_setprio 1
	s_waitcnt lgkmcnt(0)
	v_mfma_f32_16x16x32_bf16 v[62:65], v[140:143], v[172:175], v[62:65]
	v_mfma_f32_16x16x32_bf16 v[58:61], v[148:151], v[172:175], v[58:61]
	v_mfma_f32_16x16x32_bf16 v[54:57], v[140:143], v[180:183], v[54:57]
	v_mfma_f32_16x16x32_bf16 v[50:53], v[148:151], v[180:183], v[50:53]
	v_mfma_f32_16x16x32_bf16 v[46:49], v[140:143], v[188:191], v[46:49]
	v_mfma_f32_16x16x32_bf16 v[42:45], v[148:151], v[188:191], v[42:45]
	v_mfma_f32_16x16x32_bf16 v[38:41], v[140:143], v[196:199], v[38:41]
	v_mfma_f32_16x16x32_bf16 v[34:37], v[148:151], v[196:199], v[34:37]
	v_mfma_f32_16x16x32_bf16 v[62:65], v[144:147], v[176:179], v[62:65]
	v_mfma_f32_16x16x32_bf16 v[58:61], v[152:155], v[176:179], v[58:61]
	v_mfma_f32_16x16x32_bf16 v[54:57], v[144:147], v[184:187], v[54:57]
	v_mfma_f32_16x16x32_bf16 v[50:53], v[152:155], v[184:187], v[50:53]
	v_mfma_f32_16x16x32_bf16 v[46:49], v[144:147], v[192:195], v[46:49]
	v_mfma_f32_16x16x32_bf16 v[42:45], v[152:155], v[192:195], v[42:45]
	v_mfma_f32_16x16x32_bf16 v[38:41], v[144:147], v[200:203], v[38:41]
	v_mfma_f32_16x16x32_bf16 v[34:37], v[152:155], v[200:203], v[34:37]
	s_setprio 0
	s_setprio 1
	v_mfma_f32_16x16x32_bf16 v[30:33], v[156:159], v[172:175], v[30:33]
	v_mfma_f32_16x16x32_bf16 v[26:29], v[164:167], v[172:175], v[26:29]
	v_mfma_f32_16x16x32_bf16 v[22:25], v[156:159], v[180:183], v[22:25]
	v_mfma_f32_16x16x32_bf16 v[18:21], v[164:167], v[180:183], v[18:21]
	v_mfma_f32_16x16x32_bf16 v[14:17], v[156:159], v[188:191], v[14:17]
	v_mfma_f32_16x16x32_bf16 v[10:13], v[164:167], v[188:191], v[10:13]
	v_mfma_f32_16x16x32_bf16 v[6:9], v[156:159], v[196:199], v[6:9]
	v_mfma_f32_16x16x32_bf16 v[2:5], v[164:167], v[196:199], v[2:5]
	v_mfma_f32_16x16x32_bf16 v[30:33], v[160:163], v[176:179], v[30:33]
	v_mfma_f32_16x16x32_bf16 v[26:29], v[168:171], v[176:179], v[26:29]
	v_mfma_f32_16x16x32_bf16 v[22:25], v[160:163], v[184:187], v[22:25]
	v_mfma_f32_16x16x32_bf16 v[18:21], v[168:171], v[184:187], v[18:21]
	s_setprio 0
	v_mfma_f32_16x16x32_bf16 v[14:17], v[160:163], v[192:195], v[14:17]
	v_mfma_f32_16x16x32_bf16 v[10:13], v[168:171], v[192:195], v[10:13]
	v_mfma_f32_16x16x32_bf16 v[6:9], v[160:163], v[200:203], v[6:9]
	v_mfma_f32_16x16x32_bf16 v[2:5], v[168:171], v[200:203], v[2:5]
	s_barrier
	s_add_i32 s88, 0, 0x18000
	s_add_i32 s89, 0, 0x1c000
	v_add_u32_e32 v152, s88, v236
	v_add_u32_e32 v168, s89, v236
	ds_read_b128 v[140:143], v152
	ds_read_b128 v[144:147], v152 offset:1024
	ds_read_b128 v[148:151], v152 offset:2048
	ds_read_b128 v[152:155], v152 offset:3072
	ds_read_b128 v[156:159], v168
	ds_read_b128 v[160:163], v168 offset:1024
	ds_read_b128 v[164:167], v168 offset:2048
	ds_read_b128 v[168:171], v168 offset:3072
	s_add_u32 s12, s30, 0xc0000
	s_addc_u32 s13, s31, 0
	s_mov_b32 m0, s51
	v_lshl_add_u64 v[212:213], s[12:13], 0, v[134:135]
	ds_read_b128 v[172:175], v238 offset:32768
	ds_read_b128 v[176:179], v238 offset:33792
	ds_read_b128 v[180:183], v238 offset:34816
	ds_read_b128 v[184:187], v238 offset:35840
	ds_read_b128 v[188:191], v238 offset:36864
	ds_read_b128 v[192:195], v238 offset:37888
	ds_read_b128 v[196:199], v238 offset:38912
	ds_read_b128 v[200:203], v238 offset:39936
	global_load_lds_dwordx4 v[212:213], off
	v_lshl_add_u64 v[212:213], s[12:13], 0, v[132:133]
	s_mov_b32 m0, s68
	s_nop 0
	global_load_lds_dwordx4 v[212:213], off
	s_waitcnt vmcnt(8)
	s_waitcnt lgkmcnt(0)
	s_barrier
	s_setprio 1
	s_waitcnt lgkmcnt(0)
	v_mfma_f32_16x16x32_bf16 v[126:129], v[140:143], v[172:175], v[126:129]
	v_mfma_f32_16x16x32_bf16 v[122:125], v[148:151], v[172:175], v[122:125]
	v_mfma_f32_16x16x32_bf16 v[118:121], v[140:143], v[180:183], v[118:121]
	v_mfma_f32_16x16x32_bf16 v[114:117], v[148:151], v[180:183], v[114:117]
	v_mfma_f32_16x16x32_bf16 v[110:113], v[140:143], v[188:191], v[110:113]
	v_mfma_f32_16x16x32_bf16 v[106:109], v[148:151], v[188:191], v[106:109]
	v_mfma_f32_16x16x32_bf16 v[102:105], v[140:143], v[196:199], v[102:105]
	v_mfma_f32_16x16x32_bf16 v[98:101], v[148:151], v[196:199], v[98:101]
	v_mfma_f32_16x16x32_bf16 v[126:129], v[144:147], v[176:179], v[126:129]
	v_mfma_f32_16x16x32_bf16 v[122:125], v[152:155], v[176:179], v[122:125]
	v_mfma_f32_16x16x32_bf16 v[118:121], v[144:147], v[184:187], v[118:121]
	v_mfma_f32_16x16x32_bf16 v[114:117], v[152:155], v[184:187], v[114:117]
	v_mfma_f32_16x16x32_bf16 v[110:113], v[144:147], v[192:195], v[110:113]
	v_mfma_f32_16x16x32_bf16 v[106:109], v[152:155], v[192:195], v[106:109]
	v_mfma_f32_16x16x32_bf16 v[102:105], v[144:147], v[200:203], v[102:105]
	v_mfma_f32_16x16x32_bf16 v[98:101], v[152:155], v[200:203], v[98:101]
	s_setprio 0
	s_setprio 1
	v_mfma_f32_16x16x32_bf16 v[94:97], v[156:159], v[172:175], v[94:97]
	v_mfma_f32_16x16x32_bf16 v[90:93], v[164:167], v[172:175], v[90:93]
	v_mfma_f32_16x16x32_bf16 v[86:89], v[156:159], v[180:183], v[86:89]
	v_mfma_f32_16x16x32_bf16 v[82:85], v[164:167], v[180:183], v[82:85]
	v_mfma_f32_16x16x32_bf16 v[78:81], v[156:159], v[188:191], v[78:81]
	v_mfma_f32_16x16x32_bf16 v[74:77], v[164:167], v[188:191], v[74:77]
	v_mfma_f32_16x16x32_bf16 v[70:73], v[156:159], v[196:199], v[70:73]
	v_mfma_f32_16x16x32_bf16 v[66:69], v[164:167], v[196:199], v[66:69]
	v_mfma_f32_16x16x32_bf16 v[94:97], v[160:163], v[176:179], v[94:97]
	v_mfma_f32_16x16x32_bf16 v[90:93], v[168:171], v[176:179], v[90:93]
	v_mfma_f32_16x16x32_bf16 v[86:89], v[160:163], v[184:187], v[86:89]
	v_mfma_f32_16x16x32_bf16 v[82:85], v[168:171], v[184:187], v[82:85]
	s_setprio 0
	v_mfma_f32_16x16x32_bf16 v[78:81], v[160:163], v[192:195], v[78:81]
	v_mfma_f32_16x16x32_bf16 v[74:77], v[168:171], v[192:195], v[74:77]
	v_mfma_f32_16x16x32_bf16 v[70:73], v[160:163], v[200:203], v[70:73]
	v_mfma_f32_16x16x32_bf16 v[66:69], v[168:171], v[200:203], v[66:69]
	s_barrier
; #define PG8_STAGE(bufoff, gbase, voff) do { _Pragma("unroll") for (int _i = 0; _i < 2; ++_i) \
;         __builtin_amdgcn_global_load_lds((const unsigned*)((const char*)(gbase) + (voff)[_i]), (PG8_LAS unsigned*)(lds + (bufoff) + ldsw + _i * 8192), 16, 0, 0); } while (0)
; #define PG8_WAIT_V(n) asm volatile("s_waitcnt vmcnt(" #n ")" ::: "memory")
; #define PG8_WAIT_L(n) asm volatile("s_waitcnt lgkmcnt(" #n ")" ::: "memory")
; #define PG8_BAR __builtin_amdgcn_s_barrier()
; #define PG8_SCHED __builtin_amdgcn_sched_barrier(0)
; template <class Epi, class Sched, bool ALIGN_EPI, bool F8 = false>
; __device__ __forceinline__ void gemm_phase(PG8_LAS unsigned char* lds, const Gemm g, const Sched& S, const Epi& E, int tid) {
;     ...
;             PG8_LDA(At, 1, 1); PG8_STAGE(PG8_SB(1, 0), b3, voffB); PG8_STAGE(PG8_SB(1, 1), b3 + hstepB, voffB); PG8_STAGE(PG8_SA(1, 0), a3, voffA);
;             PG8_WAIT_V(8); PG8_WAIT_L(0); PG8_BAR; PG8_MMA(1, 0, At, B0); PG8_MMA(1, 1, At, B1); PG8_BAR; PG8_SCHED;
;         }
;         if constexpr (ALIGN_EPI) { if (wr == 0) PG8_BAR; }
	s_add_i32 s12, s88, s44
	v_lshl_add_u64 v[204:205], v[204:205], 0, s[60:61]
	s_mov_b32 m0, s12
	ds_read_b128 v[172:175], v238 offset:49152
	ds_read_b128 v[176:179], v238 offset:50176
	ds_read_b128 v[180:183], v238 offset:51200
	ds_read_b128 v[184:187], v238 offset:52224
	ds_read_b128 v[188:191], v238 offset:53248
	ds_read_b128 v[192:195], v238 offset:54272
	ds_read_b128 v[196:199], v238 offset:55296
	ds_read_b128 v[200:203], v238 offset:56320
	global_load_lds_dwordx4 v[204:205], off
	s_add_i32 m0, s12, 0x2000
	s_add_u32 s12, s14, 0xc0080
	v_lshl_add_u64 v[204:205], v[206:207], 0, s[60:61]
	s_addc_u32 s13, s15, 0
	s_add_i32 s14, s89, s44
	global_load_lds_dwordx4 v[204:205], off
	v_lshl_add_u64 v[204:205], s[12:13], 0, v[0:1]
	s_mov_b32 m0, s14
	s_nop 0
	global_load_lds_dwordx4 v[204:205], off
	v_lshl_add_u64 v[204:205], s[12:13], 0, v[130:131]
	s_add_i32 m0, s14, 0x2000
	s_nop 0
	global_load_lds_dwordx4 v[204:205], off
	v_lshl_add_u64 v[204:205], v[208:209], 0, s[60:61]
	s_mov_b32 m0, s69
	s_nop 0
	global_load_lds_dwordx4 v[204:205], off
	v_lshl_add_u64 v[204:205], v[210:211], 0, s[60:61]
	s_mov_b32 m0, s82
	s_nop 0
	global_load_lds_dwordx4 v[204:205], off
	s_waitcnt vmcnt(8)
	s_waitcnt lgkmcnt(0)
	s_barrier
	s_setprio 1
	s_waitcnt lgkmcnt(0)
	v_mfma_f32_16x16x32_bf16 v[62:65], v[140:143], v[172:175], v[62:65]
	v_mfma_f32_16x16x32_bf16 v[58:61], v[148:151], v[172:175], v[58:61]
	v_mfma_f32_16x16x32_bf16 v[54:57], v[140:143], v[180:183], v[54:57]
	v_mfma_f32_16x16x32_bf16 v[50:53], v[148:151], v[180:183], v[50:53]
	v_mfma_f32_16x16x32_bf16 v[46:49], v[140:143], v[188:191], v[46:49]
	v_mfma_f32_16x16x32_bf16 v[42:45], v[148:151], v[188:191], v[42:45]
	v_mfma_f32_16x16x32_bf16 v[38:41], v[140:143], v[196:199], v[38:41]
	v_mfma_f32_16x16x32_bf16 v[34:37], v[148:151], v[196:199], v[34:37]
	v_mfma_f32_16x16x32_bf16 v[62:65], v[144:147], v[176:179], v[62:65]
	v_mfma_f32_16x16x32_bf16 v[58:61], v[152:155], v[176:179], v[58:61]
	v_mfma_f32_16x16x32_bf16 v[54:57], v[144:147], v[184:187], v[54:57]
	v_mfma_f32_16x16x32_bf16 v[50:53], v[152:155], v[184:187], v[50:53]
	v_mfma_f32_16x16x32_bf16 v[46:49], v[144:147], v[192:195], v[46:49]
	v_mfma_f32_16x16x32_bf16 v[42:45], v[152:155], v[192:195], v[42:45]
	v_mfma_f32_16x16x32_bf16 v[38:41], v[144:147], v[200:203], v[38:41]
	v_mfma_f32_16x16x32_bf16 v[34:37], v[152:155], v[200:203], v[34:37]
	s_setprio 0
	s_setprio 1
	v_mfma_f32_16x16x32_bf16 v[30:33], v[156:159], v[172:175], v[30:33]
	v_mfma_f32_16x16x32_bf16 v[26:29], v[164:167], v[172:175], v[26:29]
	v_mfma_f32_16x16x32_bf16 v[22:25], v[156:159], v[180:183], v[22:25]
	v_mfma_f32_16x16x32_bf16 v[18:21], v[164:167], v[180:183], v[18:21]
	v_mfma_f32_16x16x32_bf16 v[14:17], v[156:159], v[188:191], v[14:17]
	v_mfma_f32_16x16x32_bf16 v[10:13], v[164:167], v[188:191], v[10:13]
	v_mfma_f32_16x16x32_bf16 v[6:9], v[156:159], v[196:199], v[6:9]
	v_mfma_f32_16x16x32_bf16 v[2:5], v[164:167], v[196:199], v[2:5]
	v_mfma_f32_16x16x32_bf16 v[30:33], v[160:163], v[176:179], v[30:33]
	v_mfma_f32_16x16x32_bf16 v[26:29], v[168:171], v[176:179], v[26:29]
	v_mfma_f32_16x16x32_bf16 v[22:25], v[160:163], v[184:187], v[22:25]
	v_mfma_f32_16x16x32_bf16 v[18:21], v[168:171], v[184:187], v[18:21]
	s_setprio 0
	v_mfma_f32_16x16x32_bf16 v[14:17], v[160:163], v[192:195], v[14:17]
	v_mfma_f32_16x16x32_bf16 v[10:13], v[168:171], v[192:195], v[10:13]
	v_mfma_f32_16x16x32_bf16 v[6:9], v[160:163], v[200:203], v[6:9]
	v_mfma_f32_16x16x32_bf16 v[2:5], v[168:171], v[200:203], v[2:5]
	s_barrier
	s_add_i32 s25, s25, 2
	s_add_u32 s6, s6, 0x100
	s_addc_u32 s7, s7, 0
	s_cmp_gt_u32 s25, 13
	s_mov_b64 s[12:13], s[10:11]
	s_cbranch_scc0 .LBB0_1239
	s_and_b64 vcc, exec, s[22:23]
	s_cbranch_vccz .LBB0_1242
	s_barrier

; #define PG8_STAGE(bufoff, gbase, voff) do { _Pragma("unroll") for (int _i = 0; _i < 2; ++_i) \
;         __builtin_amdgcn_global_load_lds((const unsigned*)((const char*)(gbase) + (voff)[_i]), (PG8_LAS unsigned*)(lds + (bufoff) + ldsw + _i * 8192), 16, 0, 0); } while (0)
; #define PG8_WAIT_V(n) asm volatile("s_waitcnt vmcnt(" #n ")" ::: "memory")
; #define PG8_WAIT_L(n) asm volatile("s_waitcnt lgkmcnt(" #n ")" ::: "memory")
; #define PG8_BAR __builtin_amdgcn_s_barrier()
; #define PG8_SCHED __builtin_amdgcn_sched_barrier(0)
; template <class Epi, class Sched, bool ALIGN_EPI, bool F8 = false>
; __device__ __forceinline__ void gemm_phase(PG8_LAS unsigned char* lds, const Gemm g, const Sched& S, const Epi& E, int tid) {
;     ...
;         for (int t = 0; t < nt; t += 2) {
;             const bool last = (t == nt - 2);
;             const char* a1 = cA + (size_t)(t + 1) * kstep;
;             const char* a2 = last ? nA : cA + (size_t)(t + 2) * kstep; const char* b2 = last ? nB : cB + (size_t)(t + 2) * kstep;
;             const char* a3 = a2 + kstep; const char* b3 = b2 + kstep;
;             if (last && has_next) S.a_ready(nxt);
;             PG8_LDB(B0, 0, 0); PG8_LDB(B1, 0, 1); PG8_SCHED; PG8_LDA(At, 0, 0); PG8_STAGE(PG8_SA(1, 1), a1 + hstepA, voffA);
;             PG8_WAIT_V(8); PG8_WAIT_L(0); PG8_BAR; PG8_MMA(0, 0, At, B0); PG8_MMA(0, 1, At, B1); PG8_BAR; PG8_SCHED;
;             PG8_LDA(At, 0, 1); PG8_STAGE(PG8_SB(0, 0), b2, voffB); PG8_STAGE(PG8_SB(0, 1), b2 + hstepB, voffB); PG8_STAGE(PG8_SA(0, 0), a2, voffA);
.LBB0_1397:
	s_add_u32 s7, s24, 0xfff80080
	s_addc_u32 s26, s25, -1
	s_add_i32 s50, 0, 0x10000
	s_cmp_eq_u32 s6, 28
	s_cselect_b32 s29, s21, s26
	s_cselect_b32 s28, s20, s7
	s_cselect_b32 s27, s23, s19
	s_cselect_b32 s26, s22, s17
	s_add_i32 s7, 0, 0x14000
	v_add_u32_e32 v142, s50, v201
	v_add_u32_e32 v168, s7, v201
	ds_read_b128 v[130:133], v142
	ds_read_b128 v[134:137], v142 offset:1024
	ds_read_b128 v[138:141], v142 offset:2048
	ds_read_b128 v[142:145], v142 offset:3072
	ds_read_b128 v[146:149], v168
	ds_read_b128 v[150:153], v168 offset:1024
	ds_read_b128 v[154:157], v168 offset:2048
	ds_read_b128 v[168:171], v168 offset:3072
	v_lshl_add_u64 v[208:209], s[24:25], 0, v[164:165]
	s_add_i32 m0, s38, 0xc000
	ds_read_b128 v[172:175], v203
	ds_read_b128 v[176:179], v203 offset:1024
	ds_read_b128 v[180:183], v203 offset:2048
	ds_read_b128 v[184:187], v203 offset:3072
	ds_read_b128 v[188:191], v203 offset:4096
	ds_read_b128 v[192:195], v203 offset:5120
	ds_read_b128 v[196:199], v203 offset:6144
	ds_read_b128 v[204:207], v203 offset:7168
	global_load_lds_dwordx4 v[208:209], off
	v_lshl_add_u64 v[208:209], s[24:25], 0, v[166:167]
	s_add_i32 m0, s38, 0xe000
	s_nop 0
	global_load_lds_dwordx4 v[208:209], off
	s_waitcnt vmcnt(8)
	s_waitcnt lgkmcnt(0)
	s_barrier
	s_setprio 1
	s_waitcnt lgkmcnt(0)
	v_mfma_f32_16x16x32_bf16 v[126:129], v[130:133], v[172:175], v[126:129]
	v_mfma_f32_16x16x32_bf16 v[122:125], v[138:141], v[172:175], v[122:125]
	v_mfma_f32_16x16x32_bf16 v[110:113], v[130:133], v[180:183], v[110:113]
	v_mfma_f32_16x16x32_bf16 v[106:109], v[138:141], v[180:183], v[106:109]
	v_mfma_f32_16x16x32_bf16 v[94:97], v[130:133], v[188:191], v[94:97]
	v_mfma_f32_16x16x32_bf16 v[90:93], v[138:141], v[188:191], v[90:93]
	v_mfma_f32_16x16x32_bf16 v[78:81], v[130:133], v[196:199], v[78:81]
	v_mfma_f32_16x16x32_bf16 v[74:77], v[138:141], v[196:199], v[74:77]
	v_mfma_f32_16x16x32_bf16 v[126:129], v[134:137], v[176:179], v[126:129]
	v_mfma_f32_16x16x32_bf16 v[122:125], v[142:145], v[176:179], v[122:125]
	v_mfma_f32_16x16x32_bf16 v[110:113], v[134:137], v[184:187], v[110:113]
	v_mfma_f32_16x16x32_bf16 v[106:109], v[142:145], v[184:187], v[106:109]
	v_mfma_f32_16x16x32_bf16 v[94:97], v[134:137], v[192:195], v[94:97]
	v_mfma_f32_16x16x32_bf16 v[90:93], v[142:145], v[192:195], v[90:93]
	v_mfma_f32_16x16x32_bf16 v[78:81], v[134:137], v[204:207], v[78:81]
	v_mfma_f32_16x16x32_bf16 v[74:77], v[142:145], v[204:207], v[74:77]
	s_setprio 0
	s_setprio 1
	v_mfma_f32_16x16x32_bf16 v[118:121], v[146:149], v[172:175], v[118:121]
	v_mfma_f32_16x16x32_bf16 v[114:117], v[154:157], v[172:175], v[114:117]
	v_mfma_f32_16x16x32_bf16 v[102:105], v[146:149], v[180:183], v[102:105]
	v_mfma_f32_16x16x32_bf16 v[98:101], v[154:157], v[180:183], v[98:101]
	v_mfma_f32_16x16x32_bf16 v[86:89], v[146:149], v[188:191], v[86:89]
	v_mfma_f32_16x16x32_bf16 v[82:85], v[154:157], v[188:191], v[82:85]
	v_mfma_f32_16x16x32_bf16 v[70:73], v[146:149], v[196:199], v[70:73]
	v_mfma_f32_16x16x32_bf16 v[66:69], v[154:157], v[196:199], v[66:69]
	v_mfma_f32_16x16x32_bf16 v[118:121], v[150:153], v[176:179], v[118:121]
	v_mfma_f32_16x16x32_bf16 v[114:117], v[168:171], v[176:179], v[114:117]
	v_mfma_f32_16x16x32_bf16 v[102:105], v[150:153], v[184:187], v[102:105]
	v_mfma_f32_16x16x32_bf16 v[98:101], v[168:171], v[184:187], v[98:101]
	s_setprio 0
	v_mfma_f32_16x16x32_bf16 v[86:89], v[150:153], v[192:195], v[86:89]
	v_mfma_f32_16x16x32_bf16 v[82:85], v[168:171], v[192:195], v[82:85]
	v_mfma_f32_16x16x32_bf16 v[70:73], v[150:153], v[204:207], v[70:73]
	v_mfma_f32_16x16x32_bf16 v[66:69], v[168:171], v[204:207], v[66:69]
	s_barrier
	s_add_i32 s50, s50, s35
	v_lshl_add_u64 v[208:209], s[26:27], 0, v[0:1]
	s_mov_b32 m0, s50
	ds_read_b128 v[172:175], v203 offset:16384
	ds_read_b128 v[176:179], v203 offset:17408
	ds_read_b128 v[180:183], v203 offset:18432
	ds_read_b128 v[184:187], v203 offset:19456
	ds_read_b128 v[188:191], v203 offset:20480
	ds_read_b128 v[192:195], v203 offset:21504
	ds_read_b128 v[196:199], v203 offset:22528
	ds_read_b128 v[204:207], v203 offset:23552
	global_load_lds_dwordx4 v[208:209], off
	s_add_i32 m0, s50, 0x2000
	s_add_u32 s86, s26, 0x80000
	v_lshl_add_u64 v[210:211], s[26:27], 0, v[158:159]
	s_addc_u32 s87, s27, 0
	s_add_i32 s7, s7, s35
	global_load_lds_dwordx4 v[210:211], off
	v_lshl_add_u64 v[212:213], s[86:87], 0, v[0:1]
	s_mov_b32 m0, s7
	v_lshl_add_u64 v[214:215], s[28:29], 0, v[160:161]
	global_load_lds_dwordx4 v[212:213], off
	v_lshl_add_u64 v[212:213], s[86:87], 0, v[158:159]
	s_add_i32 m0, s7, 0x2000
	s_nop 0
	global_load_lds_dwordx4 v[212:213], off
	v_lshl_add_u64 v[212:213], s[28:29], 0, v[162:163]
	s_mov_b32 m0, s38
	s_nop 0
	global_load_lds_dwordx4 v[212:213], off
	s_mov_b32 m0, s39
	s_nop 0
	global_load_lds_dwordx4 v[214:215], off
	s_waitcnt vmcnt(8)
	s_waitcnt lgkmcnt(0)
	s_barrier
; #define PG8_STAGE(bufoff, gbase, voff) do { _Pragma("unroll") for (int _i = 0; _i < 2; ++_i) \
;         __builtin_amdgcn_global_load_lds((const unsigned*)((const char*)(gbase) + (voff)[_i]), (PG8_LAS unsigned*)(lds + (bufoff) + ldsw + _i * 8192), 16, 0, 0); } while (0)
; #define PG8_WAIT_V(n) asm volatile("s_waitcnt vmcnt(" #n ")" ::: "memory")
; #define PG8_WAIT_L(n) asm volatile("s_waitcnt lgkmcnt(" #n ")" ::: "memory")
; #define PG8_BAR __builtin_amdgcn_s_barrier()
; #define PG8_SCHED __builtin_amdgcn_sched_barrier(0)
; template <class Epi, class Sched, bool ALIGN_EPI, bool F8 = false>
; __device__ __forceinline__ void gemm_phase(PG8_LAS unsigned char* lds, const Gemm g, const Sched& S, const Epi& E, int tid) {
;     ...
;             PG8_WAIT_V(8); PG8_WAIT_L(0); PG8_BAR; PG8_MMA(1, 0, At, B0); PG8_MMA(1, 1, At, B1); PG8_BAR; PG8_SCHED;
;             PG8_LDB(B0, 1, 0); PG8_LDB(B1, 1, 1); PG8_SCHED; PG8_LDA(At, 1, 0); PG8_STAGE(PG8_SA(0, 1), a2 + hstepA, voffA);
;             PG8_WAIT_V(8); PG8_WAIT_L(0); PG8_BAR; PG8_MMA(0, 0, At, B0); PG8_MMA(0, 1, At, B1); PG8_BAR; PG8_SCHED;
	s_setprio 1
	s_waitcnt lgkmcnt(0)
	v_mfma_f32_16x16x32_bf16 v[62:65], v[130:133], v[172:175], v[62:65]
	v_mfma_f32_16x16x32_bf16 v[58:61], v[138:141], v[172:175], v[58:61]
	v_mfma_f32_16x16x32_bf16 v[46:49], v[130:133], v[180:183], v[46:49]
	v_mfma_f32_16x16x32_bf16 v[42:45], v[138:141], v[180:183], v[42:45]
	v_mfma_f32_16x16x32_bf16 v[30:33], v[130:133], v[188:191], v[30:33]
	v_mfma_f32_16x16x32_bf16 v[26:29], v[138:141], v[188:191], v[26:29]
	v_mfma_f32_16x16x32_bf16 v[14:17], v[130:133], v[196:199], v[14:17]
	v_mfma_f32_16x16x32_bf16 v[10:13], v[138:141], v[196:199], v[10:13]
	v_mfma_f32_16x16x32_bf16 v[62:65], v[134:137], v[176:179], v[62:65]
	v_mfma_f32_16x16x32_bf16 v[58:61], v[142:145], v[176:179], v[58:61]
	v_mfma_f32_16x16x32_bf16 v[46:49], v[134:137], v[184:187], v[46:49]
	v_mfma_f32_16x16x32_bf16 v[42:45], v[142:145], v[184:187], v[42:45]
	v_mfma_f32_16x16x32_bf16 v[30:33], v[134:137], v[192:195], v[30:33]
	v_mfma_f32_16x16x32_bf16 v[26:29], v[142:145], v[192:195], v[26:29]
	v_mfma_f32_16x16x32_bf16 v[14:17], v[134:137], v[204:207], v[14:17]
	v_mfma_f32_16x16x32_bf16 v[10:13], v[142:145], v[204:207], v[10:13]
	s_setprio 0
	s_setprio 1
	v_mfma_f32_16x16x32_bf16 v[54:57], v[146:149], v[172:175], v[54:57]
	v_mfma_f32_16x16x32_bf16 v[50:53], v[154:157], v[172:175], v[50:53]
	v_mfma_f32_16x16x32_bf16 v[38:41], v[146:149], v[180:183], v[38:41]
	v_mfma_f32_16x16x32_bf16 v[34:37], v[154:157], v[180:183], v[34:37]
	v_mfma_f32_16x16x32_bf16 v[22:25], v[146:149], v[188:191], v[22:25]
	v_mfma_f32_16x16x32_bf16 v[18:21], v[154:157], v[188:191], v[18:21]
	v_mfma_f32_16x16x32_bf16 v[6:9], v[146:149], v[196:199], v[6:9]
	v_mfma_f32_16x16x32_bf16 v[2:5], v[154:157], v[196:199], v[2:5]
	v_mfma_f32_16x16x32_bf16 v[54:57], v[150:153], v[176:179], v[54:57]
	v_mfma_f32_16x16x32_bf16 v[50:53], v[168:171], v[176:179], v[50:53]
	v_mfma_f32_16x16x32_bf16 v[38:41], v[150:153], v[184:187], v[38:41]
	v_mfma_f32_16x16x32_bf16 v[34:37], v[168:171], v[184:187], v[34:37]
	s_setprio 0
	v_mfma_f32_16x16x32_bf16 v[22:25], v[150:153], v[192:195], v[22:25]
	v_mfma_f32_16x16x32_bf16 v[18:21], v[168:171], v[192:195], v[18:21]
	v_mfma_f32_16x16x32_bf16 v[6:9], v[150:153], v[204:207], v[6:9]
	v_mfma_f32_16x16x32_bf16 v[2:5], v[168:171], v[204:207], v[2:5]
	s_barrier
	s_add_i32 s7, 0, 0x18000
	s_add_i32 s50, 0, 0x1c000
	v_add_u32_e32 v142, s7, v201
	v_add_u32_e32 v168, s50, v201
	ds_read_b128 v[130:133], v142
	ds_read_b128 v[134:137], v142 offset:1024
	ds_read_b128 v[138:141], v142 offset:2048
	ds_read_b128 v[142:145], v142 offset:3072
	ds_read_b128 v[146:149], v168
	ds_read_b128 v[150:153], v168 offset:1024
	ds_read_b128 v[154:157], v168 offset:2048
	ds_read_b128 v[168:171], v168 offset:3072
	s_add_u32 s28, s28, 0x80000
	s_addc_u32 s29, s29, 0
	s_mov_b32 m0, s44
	v_lshl_add_u64 v[216:217], s[28:29], 0, v[162:163]
	ds_read_b128 v[172:175], v203 offset:32768
	ds_read_b128 v[176:179], v203 offset:33792
	ds_read_b128 v[180:183], v203 offset:34816
	ds_read_b128 v[184:187], v203 offset:35840
	ds_read_b128 v[188:191], v203 offset:36864
	ds_read_b128 v[192:195], v203 offset:37888
	ds_read_b128 v[196:199], v203 offset:38912
	ds_read_b128 v[204:207], v203 offset:39936
	global_load_lds_dwordx4 v[216:217], off
	v_lshl_add_u64 v[216:217], s[28:29], 0, v[160:161]
	s_mov_b32 m0, s45
	s_nop 0
	global_load_lds_dwordx4 v[216:217], off
	s_waitcnt vmcnt(8)
	s_waitcnt lgkmcnt(0)
	s_barrier
	s_setprio 1
	s_waitcnt lgkmcnt(0)
	v_mfma_f32_16x16x32_bf16 v[126:129], v[130:133], v[172:175], v[126:129]
	v_mfma_f32_16x16x32_bf16 v[122:125], v[138:141], v[172:175], v[122:125]
	v_mfma_f32_16x16x32_bf16 v[110:113], v[130:133], v[180:183], v[110:113]
	v_mfma_f32_16x16x32_bf16 v[106:109], v[138:141], v[180:183], v[106:109]
	v_mfma_f32_16x16x32_bf16 v[94:97], v[130:133], v[188:191], v[94:97]
	v_mfma_f32_16x16x32_bf16 v[90:93], v[138:141], v[188:191], v[90:93]
	v_mfma_f32_16x16x32_bf16 v[78:81], v[130:133], v[196:199], v[78:81]
	v_mfma_f32_16x16x32_bf16 v[74:77], v[138:141], v[196:199], v[74:77]
	v_mfma_f32_16x16x32_bf16 v[126:129], v[134:137], v[176:179], v[126:129]
	v_mfma_f32_16x16x32_bf16 v[122:125], v[142:145], v[176:179], v[122:125]
	v_mfma_f32_16x16x32_bf16 v[110:113], v[134:137], v[184:187], v[110:113]
	v_mfma_f32_16x16x32_bf16 v[106:109], v[142:145], v[184:187], v[106:109]
	v_mfma_f32_16x16x32_bf16 v[94:97], v[134:137], v[192:195], v[94:97]
	v_mfma_f32_16x16x32_bf16 v[90:93], v[142:145], v[192:195], v[90:93]
	v_mfma_f32_16x16x32_bf16 v[78:81], v[134:137], v[204:207], v[78:81]
	v_mfma_f32_16x16x32_bf16 v[74:77], v[142:145], v[204:207], v[74:77]
	s_setprio 0
	s_setprio 1
	v_mfma_f32_16x16x32_bf16 v[118:121], v[146:149], v[172:175], v[118:121]
	v_mfma_f32_16x16x32_bf16 v[114:117], v[154:157], v[172:175], v[114:117]
	v_mfma_f32_16x16x32_bf16 v[102:105], v[146:149], v[180:183], v[102:105]
	v_mfma_f32_16x16x32_bf16 v[98:101], v[154:157], v[180:183], v[98:101]
	v_mfma_f32_16x16x32_bf16 v[86:89], v[146:149], v[188:191], v[86:89]
	v_mfma_f32_16x16x32_bf16 v[82:85], v[154:157], v[188:191], v[82:85]
	v_mfma_f32_16x16x32_bf16 v[70:73], v[146:149], v[196:199], v[70:73]
	v_mfma_f32_16x16x32_bf16 v[66:69], v[154:157], v[196:199], v[66:69]
	v_mfma_f32_16x16x32_bf16 v[118:121], v[150:153], v[176:179], v[118:121]
	v_mfma_f32_16x16x32_bf16 v[114:117], v[168:171], v[176:179], v[114:117]
	v_mfma_f32_16x16x32_bf16 v[102:105], v[150:153], v[184:187], v[102:105]
	v_mfma_f32_16x16x32_bf16 v[98:101], v[168:171], v[184:187], v[98:101]
	s_setprio 0
	v_mfma_f32_16x16x32_bf16 v[86:89], v[150:153], v[192:195], v[86:89]
	v_mfma_f32_16x16x32_bf16 v[82:85], v[168:171], v[192:195], v[82:85]
	v_mfma_f32_16x16x32_bf16 v[70:73], v[150:153], v[204:207], v[70:73]
	v_mfma_f32_16x16x32_bf16 v[66:69], v[168:171], v[204:207], v[66:69]
	s_barrier
; #define PG8_STAGE(bufoff, gbase, voff) do { _Pragma("unroll") for (int _i = 0; _i < 2; ++_i) \
;         __builtin_amdgcn_global_load_lds((const unsigned*)((const char*)(gbase) + (voff)[_i]), (PG8_LAS unsigned*)(lds + (bufoff) + ldsw + _i * 8192), 16, 0, 0); } while (0)
; #define PG8_WAIT_V(n) asm volatile("s_waitcnt vmcnt(" #n ")" ::: "memory")
; #define PG8_WAIT_L(n) asm volatile("s_waitcnt lgkmcnt(" #n ")" ::: "memory")
; #define PG8_BAR __builtin_amdgcn_s_barrier()
; #define PG8_SCHED __builtin_amdgcn_sched_barrier(0)
; template <class Epi, class Sched, bool ALIGN_EPI, bool F8 = false>
; __device__ __forceinline__ void gemm_phase(PG8_LAS unsigned char* lds, const Gemm g, const Sched& S, const Epi& E, int tid) {
;     ...
;             PG8_LDA(At, 1, 1); PG8_STAGE(PG8_SB(1, 0), b3, voffB); PG8_STAGE(PG8_SB(1, 1), b3 + hstepB, voffB); PG8_STAGE(PG8_SA(1, 0), a3, voffA);
;             PG8_WAIT_V(8); PG8_WAIT_L(0); PG8_BAR; PG8_MMA(1, 0, At, B0); PG8_MMA(1, 1, At, B1); PG8_BAR; PG8_SCHED;
;         }
	s_add_i32 s7, s7, s35
	v_lshl_add_u64 v[208:209], v[208:209], 0, s[60:61]
	s_mov_b32 m0, s7
	ds_read_b128 v[172:175], v203 offset:49152
	ds_read_b128 v[176:179], v203 offset:50176
	ds_read_b128 v[180:183], v203 offset:51200
	ds_read_b128 v[184:187], v203 offset:52224
	ds_read_b128 v[188:191], v203 offset:53248
	ds_read_b128 v[192:195], v203 offset:54272
	ds_read_b128 v[196:199], v203 offset:55296
	ds_read_b128 v[204:207], v203 offset:56320
	global_load_lds_dwordx4 v[208:209], off
	s_add_i32 m0, s7, 0x2000
	s_add_u32 s26, s26, 0x80080
	v_lshl_add_u64 v[208:209], v[210:211], 0, s[60:61]
	s_addc_u32 s27, s27, 0
	s_add_i32 s7, s50, s35
	global_load_lds_dwordx4 v[208:209], off
	v_lshl_add_u64 v[208:209], s[26:27], 0, v[0:1]
	s_mov_b32 m0, s7
	s_nop 0
	global_load_lds_dwordx4 v[208:209], off
	v_lshl_add_u64 v[208:209], s[26:27], 0, v[158:159]
	s_add_i32 m0, s7, 0x2000
	s_nop 0
	global_load_lds_dwordx4 v[208:209], off
	v_lshl_add_u64 v[208:209], v[212:213], 0, s[60:61]
	s_mov_b32 m0, s68
	s_nop 0
	global_load_lds_dwordx4 v[208:209], off
	v_lshl_add_u64 v[208:209], v[214:215], 0, s[60:61]
	s_mov_b32 m0, s69
	s_nop 0
	global_load_lds_dwordx4 v[208:209], off
	s_waitcnt vmcnt(8)
	s_waitcnt lgkmcnt(0)
	s_barrier
	s_setprio 1
	s_waitcnt lgkmcnt(0)
	v_mfma_f32_16x16x32_bf16 v[62:65], v[130:133], v[172:175], v[62:65]
	v_mfma_f32_16x16x32_bf16 v[58:61], v[138:141], v[172:175], v[58:61]
	v_mfma_f32_16x16x32_bf16 v[46:49], v[130:133], v[180:183], v[46:49]
	v_mfma_f32_16x16x32_bf16 v[42:45], v[138:141], v[180:183], v[42:45]
	v_mfma_f32_16x16x32_bf16 v[30:33], v[130:133], v[188:191], v[30:33]
	v_mfma_f32_16x16x32_bf16 v[26:29], v[138:141], v[188:191], v[26:29]
	v_mfma_f32_16x16x32_bf16 v[14:17], v[130:133], v[196:199], v[14:17]
	v_mfma_f32_16x16x32_bf16 v[10:13], v[138:141], v[196:199], v[10:13]
	v_mfma_f32_16x16x32_bf16 v[62:65], v[134:137], v[176:179], v[62:65]
	v_mfma_f32_16x16x32_bf16 v[58:61], v[142:145], v[176:179], v[58:61]
	v_mfma_f32_16x16x32_bf16 v[46:49], v[134:137], v[184:187], v[46:49]
	v_mfma_f32_16x16x32_bf16 v[42:45], v[142:145], v[184:187], v[42:45]
	v_mfma_f32_16x16x32_bf16 v[30:33], v[134:137], v[192:195], v[30:33]
	v_mfma_f32_16x16x32_bf16 v[26:29], v[142:145], v[192:195], v[26:29]
	v_mfma_f32_16x16x32_bf16 v[14:17], v[134:137], v[204:207], v[14:17]
	v_mfma_f32_16x16x32_bf16 v[10:13], v[142:145], v[204:207], v[10:13]
	s_setprio 0
	s_setprio 1
	v_mfma_f32_16x16x32_bf16 v[54:57], v[146:149], v[172:175], v[54:57]
	v_mfma_f32_16x16x32_bf16 v[50:53], v[154:157], v[172:175], v[50:53]
	v_mfma_f32_16x16x32_bf16 v[38:41], v[146:149], v[180:183], v[38:41]
	v_mfma_f32_16x16x32_bf16 v[34:37], v[154:157], v[180:183], v[34:37]
	v_mfma_f32_16x16x32_bf16 v[22:25], v[146:149], v[188:191], v[22:25]
	v_mfma_f32_16x16x32_bf16 v[18:21], v[154:157], v[188:191], v[18:21]
	v_mfma_f32_16x16x32_bf16 v[6:9], v[146:149], v[196:199], v[6:9]
	v_mfma_f32_16x16x32_bf16 v[2:5], v[154:157], v[196:199], v[2:5]
	v_mfma_f32_16x16x32_bf16 v[54:57], v[150:153], v[176:179], v[54:57]
	v_mfma_f32_16x16x32_bf16 v[50:53], v[168:171], v[176:179], v[50:53]
	v_mfma_f32_16x16x32_bf16 v[38:41], v[150:153], v[184:187], v[38:41]
	v_mfma_f32_16x16x32_bf16 v[34:37], v[168:171], v[184:187], v[34:37]
	s_setprio 0
	v_mfma_f32_16x16x32_bf16 v[22:25], v[150:153], v[192:195], v[22:25]
	v_mfma_f32_16x16x32_bf16 v[18:21], v[168:171], v[192:195], v[18:21]
	v_mfma_f32_16x16x32_bf16 v[6:9], v[150:153], v[204:207], v[6:9]
	v_mfma_f32_16x16x32_bf16 v[2:5], v[168:171], v[204:207], v[2:5]
	s_barrier
	s_add_i32 s6, s6, 2
	s_add_u32 s24, s24, 0x100
	s_addc_u32 s25, s25, 0
	s_add_u32 s17, s17, 0x100
	s_addc_u32 s19, s19, 0
	s_cmp_gt_u32 s6, 29
	s_cbranch_scc0 .LBB0_1397
; __device__ __forceinline__ float sum_xor16(float v) { auto r = __builtin_amdgcn_permlane16_swap(__float_as_uint(v), __float_as_uint(v), false, false); return __uint_as_float(r[0]) + __uint_as_float(r[1]); }
; __device__ __forceinline__ float sum_xor32(float v) { auto r = __builtin_amdgcn_permlane32_swap(__float_as_uint(v), __float_as_uint(v), false, false); return __uint_as_float(r[0]) + __uint_as_float(r[1]); }
; __device__ __forceinline__ float bf_lo(unsigned w) { return __uint_as_float(w << 16); }
;     __device__ __forceinline__ void operator()(const f32x4 (&acc)[2][2][4][2], const Unit& u, int wr, int wc, int fr, int fq) const {
;         const int row0 = u.pm * BM + wr * 64 + fr, col0 = u.pn * BM + wc * 32 + 8 * fq;
; #pragma unroll
;         for (int ai = 0; ai < 2; ++ai) {
;             u32x4 old[4][2];
; #pragma unroll
;             for (int m = 0; m < 4; ++m)
; #pragma unroll
;                 for (int bj = 0; bj < 2; ++bj) old[m][bj] = *(const u32x4*)(xb + (size_t)(row0 + ai * HALF + m * 16) * 2048 + col0 + bj * HALF);
; #pragma unroll
;             for (int m = 0; m < 4; ++m) { const size_t row = (size_t)(row0 + ai * HALF + m * 16); bf16_t* rowp = xb + row * 2048 + col0; float ss = 0.f;
; #pragma unroll
;                 for (int bj = 0; bj < 2; ++bj) { const u32x4 oo = old[m][bj]; const f32x4 a0 = acc[ai][bj][m][0], a1 = acc[ai][bj][m][1];
;                     const float x0 = a0[0] + bf_lo(oo.x), x1 = a0[1] + bf_hi(oo.x), x2 = a0[2] + bf_lo(oo.y), x3 = a0[3] + bf_hi(oo.y), x4 = a1[0] + bf_lo(oo.z), x5 = a1[1] + bf_hi(oo.z), x6 = a1[2] + bf_lo(oo.w), x7 = a1[3] + bf_hi(oo.w);
;                     ss += (x0 * x0 + x1 * x1) + (x2 * x2 + x3 * x3) + (x4 * x4 + x5 * x5) + (x6 * x6 + x7 * x7);
;                     u32x4 w; w.x = cvt_pk_bf16(x0, x1); w.y = cvt_pk_bf16(x2, x3); w.z = cvt_pk_bf16(x4, x5); w.w = cvt_pk_bf16(x6, x7);
;                     *(u32x4*)(rowp + bj * HALF) = w;
;                     if (h8) { u32x2 q; q.x = pk4_fp8_(x0 * F8_SA_, x1 * F8_SA_, x2 * F8_SA_, x3 * F8_SA_); q.y = pk4_fp8_(x4 * F8_SA_, x5 * F8_SA_, x6 * F8_SA_, x7 * F8_SA_);
;                         *(u32x2*)(h8 + row * 2048 + col0 + bj * HALF) = q; } }
;                 ss = sum_xor32(sum_xor16(ss));
;                 if (fq == 0) SS[row * 32 + u.pn * 4 + wc] = ss; }
;             asm volatile("" ::: "memory"); }
	v_lshl_or_b32 v168, s83, 8, v202
	v_lshl_add_u32 v172, s84, 8, v200
	v_ashrrev_i32_e32 v169, 31, v168
	v_lshlrev_b64 v[182:183], 1, v[168:169]
	v_ashrrev_i32_e32 v173, 31, v172
	v_lshl_add_u64 v[170:171], s[12:13], 0, v[182:183]
	v_lshlrev_b64 v[184:185], 12, v[172:173]
	v_lshl_add_u64 v[130:131], v[170:171], 0, v[184:185]
	global_load_dwordx4 v[178:181], v[130:131], off
	global_load_dwordx4 v[154:157], v[130:131], off offset:256
	v_or_b32_e32 v192, 16, v172
	v_ashrrev_i32_e32 v193, 31, v192
	v_or_b32_e32 v176, 32, v172
	v_lshlrev_b64 v[196:197], 12, v[192:193]
	v_ashrrev_i32_e32 v177, 31, v176
	v_or_b32_e32 v174, 48, v172
	v_lshl_add_u64 v[130:131], v[170:171], 0, v[196:197]
	v_lshlrev_b64 v[194:195], 12, v[176:177]
	v_ashrrev_i32_e32 v175, 31, v174
	global_load_dwordx4 v[150:153], v[130:131], off
	global_load_dwordx4 v[146:149], v[130:131], off offset:256
	v_lshl_add_u64 v[130:131], v[170:171], 0, v[194:195]
	v_lshlrev_b64 v[190:191], 12, v[174:175]
	global_load_dwordx4 v[142:145], v[130:131], off
	global_load_dwordx4 v[138:141], v[130:131], off offset:256
	v_lshl_add_u64 v[130:131], v[170:171], 0, v[190:191]
	global_load_dwordx4 v[134:137], v[130:131], off
	s_nop 0
	global_load_dwordx4 v[130:133], v[130:131], off offset:256
	v_lshl_add_u64 v[184:185], s[12:13], 0, v[184:185]
	v_lshl_add_u64 v[198:199], v[184:185], 0, v[182:183]
	s_waitcnt vmcnt(0)
	v_lshlrev_b32_e32 v182, 16, v178
	v_and_b32_e32 v178, 0xffff0000, v178
	v_add_f32_e32 v127, v127, v178
	v_lshlrev_b32_e32 v178, 16, v179
	v_add_f32_e32 v128, v128, v178
	v_and_b32_e32 v178, 0xffff0000, v179
	v_add_f32_e32 v129, v129, v178
	v_lshlrev_b32_e32 v178, 16, v180
	v_add_f32_e32 v178, v122, v178
	v_and_b32_e32 v122, 0xffff0000, v180
	v_add_f32_e32 v179, v123, v122
	v_lshlrev_b32_e32 v122, 16, v181
	v_add_f32_e32 v180, v124, v122
	v_and_b32_e32 v122, 0xffff0000, v181
	v_add_f32_e32 v126, v126, v182
	v_add_f32_e32 v125, v125, v122
	v_mul_f32_e32 v122, v127, v127
	v_mul_f32_e32 v123, v129, v129
	v_fmac_f32_e32 v122, v126, v126
	v_fmac_f32_e32 v123, v128, v128
	v_add_f32_e32 v122, v122, v123
	v_mul_f32_e32 v123, v179, v179
	v_fmac_f32_e32 v123, v178, v178
	v_add_f32_e32 v122, v123, v122
	v_mul_f32_e32 v123, v125, v125
	v_fmac_f32_e32 v123, v180, v180
	v_add_f32_e32 v181, v123, v122
	v_cvt_pk_bf16_f32 v122, v126, v127
	v_cvt_pk_bf16_f32 v123, v128, v129
	v_cvt_pk_bf16_f32 v124, v178, v179
	v_cvt_pk_bf16_f32 v125, v180, v125
	global_store_dwordx4 v[198:199], v[122:125], off
	s_nop 1
	v_lshlrev_b32_e32 v122, 16, v154
	v_add_f32_e32 v118, v118, v122
	v_and_b32_e32 v122, 0xffff0000, v154
	v_add_f32_e32 v119, v119, v122
	v_lshlrev_b32_e32 v122, 16, v155
	v_add_f32_e32 v120, v120, v122
	v_and_b32_e32 v122, 0xffff0000, v155
	v_add_f32_e32 v121, v121, v122
	v_lshlrev_b32_e32 v122, 16, v156
	v_add_f32_e32 v122, v114, v122
	v_and_b32_e32 v114, 0xffff0000, v156
	v_add_f32_e32 v123, v115, v114
	v_lshlrev_b32_e32 v114, 16, v157
	v_add_f32_e32 v124, v116, v114
	v_and_b32_e32 v114, 0xffff0000, v157
	v_add_f32_e32 v117, v117, v114
	v_mul_f32_e32 v114, v119, v119
	v_mul_f32_e32 v115, v121, v121
	v_fmac_f32_e32 v114, v118, v118
	v_fmac_f32_e32 v115, v120, v120
	v_add_f32_e32 v114, v114, v115
	v_mul_f32_e32 v115, v123, v123
	v_fmac_f32_e32 v115, v122, v122
	v_add_f32_e32 v114, v115, v114
	v_mul_f32_e32 v115, v117, v117
	v_fmac_f32_e32 v115, v124, v124
	v_add_f32_e32 v114, v115, v114
	v_add_f32_e32 v125, v181, v114
	v_cvt_pk_bf16_f32 v114, v118, v119
	v_cvt_pk_bf16_f32 v115, v120, v121
	v_cvt_pk_bf16_f32 v116, v122, v123
	v_cvt_pk_bf16_f32 v117, v124, v117
	global_store_dwordx4 v[198:199], v[114:117], off offset:256
	s_nop 1
	v_mov_b32_e32 v114, v125
	s_nop 1
	v_permlane16_swap_b32_e32 v125, v114
	v_add_f32_e32 v114, v125, v114
	v_mov_b32_e32 v115, v114
	s_nop 1
	v_permlane32_swap_b32_e32 v114, v115
	s_and_saveexec_b64 s[24:25], s[8:9]
	s_cbranch_execz .LBB0_1400
	v_add_f32_e32 v116, v114, v115
	s_lshl_b32 s6, s83, 2
	v_lshlrev_b64 v[114:115], 7, v[172:173]
	s_ashr_i32 s7, s6, 31
	v_lshl_add_u64 v[114:115], s[14:15], 0, v[114:115]
	v_lshl_add_u64 v[114:115], s[6:7], 2, v[114:115]
	s_lshl_b32 s94, s51, 2
	v_lshl_add_u64 v[114:115], v[114:115], 0, s[94:95]
	global_store_dword v[114:115], v116, off

; #define PG8_STAGE(bufoff, gbase, voff) do { _Pragma("unroll") for (int _i = 0; _i < 2; ++_i) \
;         __builtin_amdgcn_global_load_lds((const unsigned*)((const char*)(gbase) + (voff)[_i]), (PG8_LAS unsigned*)(lds + (bufoff) + ldsw + _i * 8192), 16, 0, 0); } while (0)
; #define PG8_WAIT_V(n) asm volatile("s_waitcnt vmcnt(" #n ")" ::: "memory")
; #define PG8_WAIT_L(n) asm volatile("s_waitcnt lgkmcnt(" #n ")" ::: "memory")
; #define PG8_BAR __builtin_amdgcn_s_barrier()
; #define PG8_SCHED __builtin_amdgcn_sched_barrier(0)
; template <class Epi, class Sched, bool ALIGN_EPI, bool F8 = false>
; __device__ __forceinline__ void gemm_phase(PG8_LAS unsigned char* lds, const Gemm g, const Sched& S, const Epi& E, int tid) {
;     ...
;             PG8_LDB(B0, 0, 0); PG8_LDB(B1, 0, 1); PG8_SCHED; PG8_LDA(At, 0, 0); PG8_STAGE(PG8_SA(1, 1), a1 + hstepA, voffA);
;             PG8_WAIT_V(8); PG8_WAIT_L(0); PG8_BAR; PG8_MMA(0, 0, At, B0); PG8_MMA(0, 1, At, B1); PG8_BAR; PG8_SCHED;
;             PG8_LDA(At, 0, 1); PG8_STAGE(PG8_SB(0, 0), b2, voffB); PG8_STAGE(PG8_SB(0, 1), b2 + hstepB, voffB); PG8_STAGE(PG8_SA(0, 0), a2, voffA);
;             PG8_WAIT_V(8); PG8_WAIT_L(0); PG8_BAR; PG8_MMA(1, 0, At, B0); PG8_MMA(1, 1, At, B1); PG8_BAR; PG8_SCHED;
.LBB0_1454:
	s_add_u32 s8, s14, 0xfff80080
	s_addc_u32 s9, s15, -1
	s_add_i32 s18, 0, 0x10000
	s_cmp_eq_u32 s7, 28
	s_cselect_b32 s45, s27, s9
	s_cselect_b32 s44, vcc_lo, s8
	s_cselect_b32 s39, s25, s6
	s_cselect_b32 s38, vcc_hi, s50
	s_add_i32 s19, 0, 0x14000
	v_add_u32_e32 v152, s18, v160
	v_add_u32_e32 v156, s19, v160
	ds_read_b128 v[140:143], v152
	ds_read_b128 v[144:147], v152 offset:1024
	ds_read_b128 v[148:151], v152 offset:2048
	ds_read_b128 v[152:155], v152 offset:3072
	ds_read_b128 v[174:177], v156
	ds_read_b128 v[178:181], v156 offset:1024
	ds_read_b128 v[182:185], v156 offset:2048
	ds_read_b128 v[186:189], v156 offset:3072
	v_lshl_add_u64 v[156:157], s[14:15], 0, v[136:137]
	s_add_i32 m0, s82, 0xc000
	ds_read_b128 v[190:193], v173
	ds_read_b128 v[194:197], v173 offset:1024
	ds_read_b128 v[198:201], v173 offset:2048
	ds_read_b128 v[202:205], v173 offset:3072
	ds_read_b128 v[206:209], v173 offset:4096
	ds_read_b128 v[210:213], v173 offset:5120
	ds_read_b128 v[214:217], v173 offset:6144
	ds_read_b128 v[218:221], v173 offset:7168
	global_load_lds_dwordx4 v[156:157], off
	v_lshl_add_u64 v[156:157], s[14:15], 0, v[138:139]
	s_add_i32 m0, s82, 0xe000
	s_nop 0
	global_load_lds_dwordx4 v[156:157], off
	s_waitcnt vmcnt(8)
	s_waitcnt lgkmcnt(0)
	s_barrier
	s_setprio 1
	s_waitcnt lgkmcnt(0)
	v_mfma_f32_16x16x32_bf16 v[126:129], v[140:143], v[190:193], v[126:129]
	v_mfma_f32_16x16x32_bf16 v[122:125], v[148:151], v[190:193], v[122:125]
	v_mfma_f32_16x16x32_bf16 v[110:113], v[140:143], v[198:201], v[110:113]
	v_mfma_f32_16x16x32_bf16 v[106:109], v[148:151], v[198:201], v[106:109]
	v_mfma_f32_16x16x32_bf16 v[94:97], v[140:143], v[206:209], v[94:97]
	v_mfma_f32_16x16x32_bf16 v[90:93], v[148:151], v[206:209], v[90:93]
	v_mfma_f32_16x16x32_bf16 v[78:81], v[140:143], v[214:217], v[78:81]
	v_mfma_f32_16x16x32_bf16 v[74:77], v[148:151], v[214:217], v[74:77]
	v_mfma_f32_16x16x32_bf16 v[126:129], v[144:147], v[194:197], v[126:129]
	v_mfma_f32_16x16x32_bf16 v[122:125], v[152:155], v[194:197], v[122:125]
	v_mfma_f32_16x16x32_bf16 v[110:113], v[144:147], v[202:205], v[110:113]
	v_mfma_f32_16x16x32_bf16 v[106:109], v[152:155], v[202:205], v[106:109]
	v_mfma_f32_16x16x32_bf16 v[94:97], v[144:147], v[210:213], v[94:97]
	v_mfma_f32_16x16x32_bf16 v[90:93], v[152:155], v[210:213], v[90:93]
	v_mfma_f32_16x16x32_bf16 v[78:81], v[144:147], v[218:221], v[78:81]
	v_mfma_f32_16x16x32_bf16 v[74:77], v[152:155], v[218:221], v[74:77]
	s_setprio 0
	s_setprio 1
	v_mfma_f32_16x16x32_bf16 v[118:121], v[174:177], v[190:193], v[118:121]
	v_mfma_f32_16x16x32_bf16 v[114:117], v[182:185], v[190:193], v[114:117]
	v_mfma_f32_16x16x32_bf16 v[102:105], v[174:177], v[198:201], v[102:105]
	v_mfma_f32_16x16x32_bf16 v[98:101], v[182:185], v[198:201], v[98:101]
	v_mfma_f32_16x16x32_bf16 v[86:89], v[174:177], v[206:209], v[86:89]
	v_mfma_f32_16x16x32_bf16 v[82:85], v[182:185], v[206:209], v[82:85]
	v_mfma_f32_16x16x32_bf16 v[70:73], v[174:177], v[214:217], v[70:73]
	v_mfma_f32_16x16x32_bf16 v[66:69], v[182:185], v[214:217], v[66:69]
	v_mfma_f32_16x16x32_bf16 v[118:121], v[178:181], v[194:197], v[118:121]
	v_mfma_f32_16x16x32_bf16 v[114:117], v[186:189], v[194:197], v[114:117]
	v_mfma_f32_16x16x32_bf16 v[102:105], v[178:181], v[202:205], v[102:105]
	v_mfma_f32_16x16x32_bf16 v[98:101], v[186:189], v[202:205], v[98:101]
	s_setprio 0
	v_mfma_f32_16x16x32_bf16 v[86:89], v[178:181], v[210:213], v[86:89]
	v_mfma_f32_16x16x32_bf16 v[82:85], v[186:189], v[210:213], v[82:85]
	v_mfma_f32_16x16x32_bf16 v[70:73], v[178:181], v[218:221], v[70:73]
	v_mfma_f32_16x16x32_bf16 v[66:69], v[186:189], v[218:221], v[66:69]
	s_barrier
	s_add_i32 s8, s18, s69
	v_lshl_add_u64 v[156:157], s[38:39], 0, v[0:1]
	s_mov_b32 m0, s8
	ds_read_b128 v[190:193], v173 offset:16384
	ds_read_b128 v[194:197], v173 offset:17408
	ds_read_b128 v[198:201], v173 offset:18432
	ds_read_b128 v[202:205], v173 offset:19456
	ds_read_b128 v[206:209], v173 offset:20480
	ds_read_b128 v[210:213], v173 offset:21504
	ds_read_b128 v[214:217], v173 offset:22528
	ds_read_b128 v[218:221], v173 offset:23552
	global_load_lds_dwordx4 v[156:157], off
	s_add_i32 m0, s8, 0x2000
	s_add_u32 s8, s38, 0x80000
	v_lshl_add_u64 v[226:227], s[38:39], 0, v[130:131]
	s_addc_u32 s9, s39, 0
	s_add_i32 s18, s19, s69
	global_load_lds_dwordx4 v[226:227], off
	v_lshl_add_u64 v[228:229], s[8:9], 0, v[0:1]
	s_mov_b32 m0, s18
	v_lshl_add_u64 v[236:237], s[44:45], 0, v[132:133]
	global_load_lds_dwordx4 v[228:229], off
	v_lshl_add_u64 v[228:229], s[8:9], 0, v[130:131]
	s_add_i32 m0, s18, 0x2000
	s_nop 0
	global_load_lds_dwordx4 v[228:229], off
	v_lshl_add_u64 v[228:229], s[44:45], 0, v[134:135]
	s_mov_b32 m0, s82
	s_nop 0
	global_load_lds_dwordx4 v[228:229], off
	s_mov_b32 m0, s83
	s_nop 0
	global_load_lds_dwordx4 v[236:237], off
	s_waitcnt vmcnt(8)
	s_waitcnt lgkmcnt(0)
	s_barrier
; #define PG8_STAGE(bufoff, gbase, voff) do { _Pragma("unroll") for (int _i = 0; _i < 2; ++_i) \
;         __builtin_amdgcn_global_load_lds((const unsigned*)((const char*)(gbase) + (voff)[_i]), (PG8_LAS unsigned*)(lds + (bufoff) + ldsw + _i * 8192), 16, 0, 0); } while (0)
; #define PG8_WAIT_V(n) asm volatile("s_waitcnt vmcnt(" #n ")" ::: "memory")
; #define PG8_WAIT_L(n) asm volatile("s_waitcnt lgkmcnt(" #n ")" ::: "memory")
; #define PG8_BAR __builtin_amdgcn_s_barrier()
; #define PG8_SCHED __builtin_amdgcn_sched_barrier(0)
; template <class Epi, class Sched, bool ALIGN_EPI, bool F8 = false>
; __device__ __forceinline__ void gemm_phase(PG8_LAS unsigned char* lds, const Gemm g, const Sched& S, const Epi& E, int tid) {
;     ...
;             PG8_WAIT_V(8); PG8_WAIT_L(0); PG8_BAR; PG8_MMA(1, 0, At, B0); PG8_MMA(1, 1, At, B1); PG8_BAR; PG8_SCHED;
;             PG8_LDB(B0, 1, 0); PG8_LDB(B1, 1, 1); PG8_SCHED; PG8_LDA(At, 1, 0); PG8_STAGE(PG8_SA(0, 1), a2 + hstepA, voffA);
;             PG8_WAIT_V(8); PG8_WAIT_L(0); PG8_BAR; PG8_MMA(0, 0, At, B0); PG8_MMA(0, 1, At, B1); PG8_BAR; PG8_SCHED;
;             PG8_LDA(At, 1, 1); PG8_STAGE(PG8_SB(1, 0), b3, voffB); PG8_STAGE(PG8_SB(1, 1), b3 + hstepB, voffB); PG8_STAGE(PG8_SA(1, 0), a3, voffA);
	s_setprio 1
	s_waitcnt lgkmcnt(0)
	v_mfma_f32_16x16x32_bf16 v[62:65], v[140:143], v[190:193], v[62:65]
	v_mfma_f32_16x16x32_bf16 v[58:61], v[148:151], v[190:193], v[58:61]
	v_mfma_f32_16x16x32_bf16 v[46:49], v[140:143], v[198:201], v[46:49]
	v_mfma_f32_16x16x32_bf16 v[42:45], v[148:151], v[198:201], v[42:45]
	v_mfma_f32_16x16x32_bf16 v[30:33], v[140:143], v[206:209], v[30:33]
	v_mfma_f32_16x16x32_bf16 v[26:29], v[148:151], v[206:209], v[26:29]
	v_mfma_f32_16x16x32_bf16 v[14:17], v[140:143], v[214:217], v[14:17]
	v_mfma_f32_16x16x32_bf16 v[10:13], v[148:151], v[214:217], v[10:13]
	v_mfma_f32_16x16x32_bf16 v[62:65], v[144:147], v[194:197], v[62:65]
	v_mfma_f32_16x16x32_bf16 v[58:61], v[152:155], v[194:197], v[58:61]
	v_mfma_f32_16x16x32_bf16 v[46:49], v[144:147], v[202:205], v[46:49]
	v_mfma_f32_16x16x32_bf16 v[42:45], v[152:155], v[202:205], v[42:45]
	v_mfma_f32_16x16x32_bf16 v[30:33], v[144:147], v[210:213], v[30:33]
	v_mfma_f32_16x16x32_bf16 v[26:29], v[152:155], v[210:213], v[26:29]
	v_mfma_f32_16x16x32_bf16 v[14:17], v[144:147], v[218:221], v[14:17]
	v_mfma_f32_16x16x32_bf16 v[10:13], v[152:155], v[218:221], v[10:13]
	s_setprio 0
	s_setprio 1
	v_mfma_f32_16x16x32_bf16 v[54:57], v[174:177], v[190:193], v[54:57]
	v_mfma_f32_16x16x32_bf16 v[50:53], v[182:185], v[190:193], v[50:53]
	v_mfma_f32_16x16x32_bf16 v[38:41], v[174:177], v[198:201], v[38:41]
	v_mfma_f32_16x16x32_bf16 v[34:37], v[182:185], v[198:201], v[34:37]
	v_mfma_f32_16x16x32_bf16 v[22:25], v[174:177], v[206:209], v[22:25]
	v_mfma_f32_16x16x32_bf16 v[18:21], v[182:185], v[206:209], v[18:21]
	v_mfma_f32_16x16x32_bf16 v[6:9], v[174:177], v[214:217], v[6:9]
	v_mfma_f32_16x16x32_bf16 v[2:5], v[182:185], v[214:217], v[2:5]
	v_mfma_f32_16x16x32_bf16 v[54:57], v[178:181], v[194:197], v[54:57]
	v_mfma_f32_16x16x32_bf16 v[50:53], v[186:189], v[194:197], v[50:53]
	v_mfma_f32_16x16x32_bf16 v[38:41], v[178:181], v[202:205], v[38:41]
	v_mfma_f32_16x16x32_bf16 v[34:37], v[186:189], v[202:205], v[34:37]
	s_setprio 0
	v_mfma_f32_16x16x32_bf16 v[22:25], v[178:181], v[210:213], v[22:25]
	v_mfma_f32_16x16x32_bf16 v[18:21], v[186:189], v[210:213], v[18:21]
	v_mfma_f32_16x16x32_bf16 v[6:9], v[178:181], v[218:221], v[6:9]
	v_mfma_f32_16x16x32_bf16 v[2:5], v[186:189], v[218:221], v[2:5]
	s_barrier
	s_add_i32 s18, 0, 0x18000
	s_add_i32 s19, 0, 0x1c000
	v_add_u32_e32 v152, s18, v160
	v_add_u32_e32 v186, s19, v160
	ds_read_b128 v[140:143], v152
	ds_read_b128 v[144:147], v152 offset:1024
	ds_read_b128 v[148:151], v152 offset:2048
	ds_read_b128 v[152:155], v152 offset:3072
	ds_read_b128 v[174:177], v186
	ds_read_b128 v[178:181], v186 offset:1024
	ds_read_b128 v[182:185], v186 offset:2048
	ds_read_b128 v[186:189], v186 offset:3072
	s_add_u32 s8, s44, 0x80000
	s_addc_u32 s9, s45, 0
	s_mov_b32 m0, s84
	v_lshl_add_u64 v[238:239], s[8:9], 0, v[134:135]
	ds_read_b128 v[190:193], v173 offset:32768
	ds_read_b128 v[194:197], v173 offset:33792
	ds_read_b128 v[198:201], v173 offset:34816
	ds_read_b128 v[202:205], v173 offset:35840
	ds_read_b128 v[206:209], v173 offset:36864
	ds_read_b128 v[210:213], v173 offset:37888
	ds_read_b128 v[214:217], v173 offset:38912
	ds_read_b128 v[218:221], v173 offset:39936
	global_load_lds_dwordx4 v[238:239], off
	v_lshl_add_u64 v[238:239], s[8:9], 0, v[132:133]
	s_mov_b32 m0, s85
	s_nop 0
	global_load_lds_dwordx4 v[238:239], off
	s_waitcnt vmcnt(8)
	s_waitcnt lgkmcnt(0)
	s_barrier
	s_setprio 1
	s_waitcnt lgkmcnt(0)
	v_mfma_f32_16x16x32_bf16 v[126:129], v[140:143], v[190:193], v[126:129]
	v_mfma_f32_16x16x32_bf16 v[122:125], v[148:151], v[190:193], v[122:125]
	v_mfma_f32_16x16x32_bf16 v[110:113], v[140:143], v[198:201], v[110:113]
	v_mfma_f32_16x16x32_bf16 v[106:109], v[148:151], v[198:201], v[106:109]
	v_mfma_f32_16x16x32_bf16 v[94:97], v[140:143], v[206:209], v[94:97]
	v_mfma_f32_16x16x32_bf16 v[90:93], v[148:151], v[206:209], v[90:93]
	v_mfma_f32_16x16x32_bf16 v[78:81], v[140:143], v[214:217], v[78:81]
	v_mfma_f32_16x16x32_bf16 v[74:77], v[148:151], v[214:217], v[74:77]
	v_mfma_f32_16x16x32_bf16 v[126:129], v[144:147], v[194:197], v[126:129]
	v_mfma_f32_16x16x32_bf16 v[122:125], v[152:155], v[194:197], v[122:125]
	v_mfma_f32_16x16x32_bf16 v[110:113], v[144:147], v[202:205], v[110:113]
	v_mfma_f32_16x16x32_bf16 v[106:109], v[152:155], v[202:205], v[106:109]
	v_mfma_f32_16x16x32_bf16 v[94:97], v[144:147], v[210:213], v[94:97]
	v_mfma_f32_16x16x32_bf16 v[90:93], v[152:155], v[210:213], v[90:93]
	v_mfma_f32_16x16x32_bf16 v[78:81], v[144:147], v[218:221], v[78:81]
	v_mfma_f32_16x16x32_bf16 v[74:77], v[152:155], v[218:221], v[74:77]
	s_setprio 0
	s_setprio 1
	v_mfma_f32_16x16x32_bf16 v[118:121], v[174:177], v[190:193], v[118:121]
	v_mfma_f32_16x16x32_bf16 v[114:117], v[182:185], v[190:193], v[114:117]
	v_mfma_f32_16x16x32_bf16 v[102:105], v[174:177], v[198:201], v[102:105]
	v_mfma_f32_16x16x32_bf16 v[98:101], v[182:185], v[198:201], v[98:101]
	v_mfma_f32_16x16x32_bf16 v[86:89], v[174:177], v[206:209], v[86:89]
	v_mfma_f32_16x16x32_bf16 v[82:85], v[182:185], v[206:209], v[82:85]
	v_mfma_f32_16x16x32_bf16 v[70:73], v[174:177], v[214:217], v[70:73]
	v_mfma_f32_16x16x32_bf16 v[66:69], v[182:185], v[214:217], v[66:69]
	v_mfma_f32_16x16x32_bf16 v[118:121], v[178:181], v[194:197], v[118:121]
	v_mfma_f32_16x16x32_bf16 v[114:117], v[186:189], v[194:197], v[114:117]
	v_mfma_f32_16x16x32_bf16 v[102:105], v[178:181], v[202:205], v[102:105]
	v_mfma_f32_16x16x32_bf16 v[98:101], v[186:189], v[202:205], v[98:101]
	s_setprio 0
	v_mfma_f32_16x16x32_bf16 v[86:89], v[178:181], v[210:213], v[86:89]
	v_mfma_f32_16x16x32_bf16 v[82:85], v[186:189], v[210:213], v[82:85]
	v_mfma_f32_16x16x32_bf16 v[70:73], v[178:181], v[218:221], v[70:73]
	v_mfma_f32_16x16x32_bf16 v[66:69], v[186:189], v[218:221], v[66:69]
	s_barrier
; #define PG8_STAGE(bufoff, gbase, voff) do { _Pragma("unroll") for (int _i = 0; _i < 2; ++_i) \
;         __builtin_amdgcn_global_load_lds((const unsigned*)((const char*)(gbase) + (voff)[_i]), (PG8_LAS unsigned*)(lds + (bufoff) + ldsw + _i * 8192), 16, 0, 0); } while (0)
; #define PG8_WAIT_V(n) asm volatile("s_waitcnt vmcnt(" #n ")" ::: "memory")
; #define PG8_WAIT_L(n) asm volatile("s_waitcnt lgkmcnt(" #n ")" ::: "memory")
; #define PG8_BAR __builtin_amdgcn_s_barrier()
; #define PG8_SCHED __builtin_amdgcn_sched_barrier(0)
; template <class Epi, class Sched, bool ALIGN_EPI, bool F8 = false>
; __device__ __forceinline__ void gemm_phase(PG8_LAS unsigned char* lds, const Gemm g, const Sched& S, const Epi& E, int tid) {
;     ...
;         for (int t = 0; t < nt; t += 2) {
;             const bool last = (t == nt - 2);
;             const char* a1 = cA + (size_t)(t + 1) * kstep;
;             const char* a2 = last ? nA : cA + (size_t)(t + 2) * kstep; const char* b2 = last ? nB : cB + (size_t)(t + 2) * kstep;
;             const char* a3 = a2 + kstep; const char* b3 = b2 + kstep;
;     ...
;             PG8_LDA(At, 1, 1); PG8_STAGE(PG8_SB(1, 0), b3, voffB); PG8_STAGE(PG8_SB(1, 1), b3 + hstepB, voffB); PG8_STAGE(PG8_SA(1, 0), a3, voffA);
;             PG8_WAIT_V(8); PG8_WAIT_L(0); PG8_BAR; PG8_MMA(1, 0, At, B0); PG8_MMA(1, 1, At, B1); PG8_BAR; PG8_SCHED;
	s_add_i32 s8, s18, s69
	v_lshl_add_u64 v[156:157], v[156:157], 0, s[60:61]
	s_mov_b32 m0, s8
	ds_read_b128 v[190:193], v173 offset:49152
	ds_read_b128 v[194:197], v173 offset:50176
	ds_read_b128 v[198:201], v173 offset:51200
	ds_read_b128 v[202:205], v173 offset:52224
	ds_read_b128 v[206:209], v173 offset:53248
	ds_read_b128 v[210:213], v173 offset:54272
	ds_read_b128 v[214:217], v173 offset:55296
	ds_read_b128 v[218:221], v173 offset:56320
	global_load_lds_dwordx4 v[156:157], off
	s_add_i32 m0, s8, 0x2000
	s_add_u32 s8, s38, 0x80080
	v_lshl_add_u64 v[156:157], v[226:227], 0, s[60:61]
	s_addc_u32 s9, s39, 0
	s_add_i32 s18, s19, s69
	global_load_lds_dwordx4 v[156:157], off
	v_lshl_add_u64 v[156:157], s[8:9], 0, v[0:1]
	s_mov_b32 m0, s18
	s_nop 0
	global_load_lds_dwordx4 v[156:157], off
	v_lshl_add_u64 v[156:157], s[8:9], 0, v[130:131]
	s_add_i32 m0, s18, 0x2000
	s_nop 0
	global_load_lds_dwordx4 v[156:157], off
	v_lshl_add_u64 v[156:157], v[228:229], 0, s[60:61]
	s_mov_b32 m0, s86
	s_nop 0
	global_load_lds_dwordx4 v[156:157], off
	v_lshl_add_u64 v[156:157], v[236:237], 0, s[60:61]
	s_mov_b32 m0, s87
	s_nop 0
	global_load_lds_dwordx4 v[156:157], off
	s_waitcnt vmcnt(8)
	s_waitcnt lgkmcnt(0)
	s_barrier
	s_setprio 1
	s_waitcnt lgkmcnt(0)
	v_mfma_f32_16x16x32_bf16 v[62:65], v[140:143], v[190:193], v[62:65]
	v_mfma_f32_16x16x32_bf16 v[58:61], v[148:151], v[190:193], v[58:61]
	v_mfma_f32_16x16x32_bf16 v[46:49], v[140:143], v[198:201], v[46:49]
	v_mfma_f32_16x16x32_bf16 v[42:45], v[148:151], v[198:201], v[42:45]
	v_mfma_f32_16x16x32_bf16 v[30:33], v[140:143], v[206:209], v[30:33]
	v_mfma_f32_16x16x32_bf16 v[26:29], v[148:151], v[206:209], v[26:29]
	v_mfma_f32_16x16x32_bf16 v[14:17], v[140:143], v[214:217], v[14:17]
	v_mfma_f32_16x16x32_bf16 v[10:13], v[148:151], v[214:217], v[10:13]
	v_mfma_f32_16x16x32_bf16 v[62:65], v[144:147], v[194:197], v[62:65]
	v_mfma_f32_16x16x32_bf16 v[58:61], v[152:155], v[194:197], v[58:61]
	v_mfma_f32_16x16x32_bf16 v[46:49], v[144:147], v[202:205], v[46:49]
	v_mfma_f32_16x16x32_bf16 v[42:45], v[152:155], v[202:205], v[42:45]
	v_mfma_f32_16x16x32_bf16 v[30:33], v[144:147], v[210:213], v[30:33]
	v_mfma_f32_16x16x32_bf16 v[26:29], v[152:155], v[210:213], v[26:29]
	v_mfma_f32_16x16x32_bf16 v[14:17], v[144:147], v[218:221], v[14:17]
	v_mfma_f32_16x16x32_bf16 v[10:13], v[152:155], v[218:221], v[10:13]
	s_setprio 0
	s_setprio 1
	v_mfma_f32_16x16x32_bf16 v[54:57], v[174:177], v[190:193], v[54:57]
	v_mfma_f32_16x16x32_bf16 v[50:53], v[182:185], v[190:193], v[50:53]
	v_mfma_f32_16x16x32_bf16 v[38:41], v[174:177], v[198:201], v[38:41]
	v_mfma_f32_16x16x32_bf16 v[34:37], v[182:185], v[198:201], v[34:37]
	v_mfma_f32_16x16x32_bf16 v[22:25], v[174:177], v[206:209], v[22:25]
	v_mfma_f32_16x16x32_bf16 v[18:21], v[182:185], v[206:209], v[18:21]
	v_mfma_f32_16x16x32_bf16 v[6:9], v[174:177], v[214:217], v[6:9]
	v_mfma_f32_16x16x32_bf16 v[2:5], v[182:185], v[214:217], v[2:5]
	v_mfma_f32_16x16x32_bf16 v[54:57], v[178:181], v[194:197], v[54:57]
	v_mfma_f32_16x16x32_bf16 v[50:53], v[186:189], v[194:197], v[50:53]
	v_mfma_f32_16x16x32_bf16 v[38:41], v[178:181], v[202:205], v[38:41]
	v_mfma_f32_16x16x32_bf16 v[34:37], v[186:189], v[202:205], v[34:37]
	s_setprio 0
	v_mfma_f32_16x16x32_bf16 v[22:25], v[178:181], v[210:213], v[22:25]
	v_mfma_f32_16x16x32_bf16 v[18:21], v[186:189], v[210:213], v[18:21]
	v_mfma_f32_16x16x32_bf16 v[6:9], v[178:181], v[218:221], v[6:9]
	v_mfma_f32_16x16x32_bf16 v[2:5], v[186:189], v[218:221], v[2:5]
	s_barrier
	s_add_i32 s7, s7, 2
	s_add_u32 s14, s14, 0x100
	s_addc_u32 s15, s15, 0
	s_add_u32 s50, s50, 0x100
	s_addc_u32 s6, s6, 0
	s_cmp_gt_u32 s7, 29
	s_cbranch_scc0 .LBB0_1454
	s_and_b64 vcc, exec, s[22:23]
	s_cbranch_vccz .LBB0_1457
	s_barrier

; #define PG8_STAGE(bufoff, gbase, voff) do { _Pragma("unroll") for (int _i = 0; _i < 2; ++_i) \
;         __builtin_amdgcn_global_load_lds((const unsigned*)((const char*)(gbase) + (voff)[_i]), (PG8_LAS unsigned*)(lds + (bufoff) + ldsw + _i * 8192), 16, 0, 0); } while (0)
; #define PG8_WAIT_V(n) asm volatile("s_waitcnt vmcnt(" #n ")" ::: "memory")
; #define PG8_WAIT_L(n) asm volatile("s_waitcnt lgkmcnt(" #n ")" ::: "memory")
; #define PG8_BAR __builtin_amdgcn_s_barrier()
; #define PG8_SCHED __builtin_amdgcn_sched_barrier(0)
; template <class Epi, class Sched, bool ALIGN_EPI, bool F8 = false>
; __device__ __forceinline__ void gemm_phase(PG8_LAS unsigned char* lds, const Gemm g, const Sched& S, const Epi& E, int tid) {
;     ...
;             PG8_LDB(B0, 0, 0); PG8_LDB(B1, 0, 1); PG8_SCHED; PG8_LDA(At, 0, 0); PG8_STAGE(PG8_SA(1, 1), a1 + hstepA, voffA);
;             PG8_WAIT_V(8); PG8_WAIT_L(0); PG8_BAR; PG8_MMA(0, 0, At, B0); PG8_MMA(0, 1, At, B1); PG8_BAR; PG8_SCHED;
;             PG8_LDA(At, 0, 1); PG8_STAGE(PG8_SB(0, 0), b2, voffB); PG8_STAGE(PG8_SB(0, 1), b2 + hstepB, voffB); PG8_STAGE(PG8_SA(0, 0), a2, voffA);
;             PG8_WAIT_V(8); PG8_WAIT_L(0); PG8_BAR; PG8_MMA(1, 0, At, B0); PG8_MMA(1, 1, At, B1); PG8_BAR; PG8_SCHED;
.LBB0_1508:
	s_add_u32 s7, s28, 0xfff80080
	s_addc_u32 s30, s29, -1
	s_add_i32 s94, 0, 0x10000
	s_cmp_eq_u32 s6, 28
	s_cselect_b32 s35, s21, s30
	s_cselect_b32 s34, s87, s7
	s_cselect_b32 s31, s19, s50
	s_cselect_b32 s30, s88, s89
	s_add_i32 s7, 0, 0x14000
	v_add_u32_e32 v152, s94, v215
	v_add_u32_e32 v168, s7, v215
	ds_read_b128 v[140:143], v152
	ds_read_b128 v[144:147], v152 offset:1024
	ds_read_b128 v[148:151], v152 offset:2048
	ds_read_b128 v[152:155], v152 offset:3072
	ds_read_b128 v[156:159], v168
	ds_read_b128 v[160:163], v168 offset:1024
	ds_read_b128 v[164:167], v168 offset:2048
	ds_read_b128 v[168:171], v168 offset:3072
	v_lshl_add_u64 v[204:205], s[28:29], 0, v[136:137]
	s_add_i32 m0, s39, 0xc000
	ds_read_b128 v[172:175], v244
	ds_read_b128 v[176:179], v244 offset:1024
	ds_read_b128 v[180:183], v244 offset:2048
	ds_read_b128 v[184:187], v244 offset:3072
	ds_read_b128 v[188:191], v244 offset:4096
	ds_read_b128 v[192:195], v244 offset:5120
	ds_read_b128 v[196:199], v244 offset:6144
	ds_read_b128 v[200:203], v244 offset:7168
	global_load_lds_dwordx4 v[204:205], off
	v_lshl_add_u64 v[204:205], s[28:29], 0, v[138:139]
	s_add_i32 m0, s39, 0xe000
	s_nop 0
	global_load_lds_dwordx4 v[204:205], off
	s_waitcnt vmcnt(8)
	s_waitcnt lgkmcnt(0)
	s_barrier
	s_setprio 1
	s_waitcnt lgkmcnt(0)
	v_mfma_f32_16x16x32_bf16 v[126:129], v[140:143], v[172:175], v[126:129]
	v_mfma_f32_16x16x32_bf16 v[122:125], v[148:151], v[172:175], v[122:125]
	v_mfma_f32_16x16x32_bf16 v[110:113], v[140:143], v[180:183], v[110:113]
	v_mfma_f32_16x16x32_bf16 v[106:109], v[148:151], v[180:183], v[106:109]
	v_mfma_f32_16x16x32_bf16 v[94:97], v[140:143], v[188:191], v[94:97]
	v_mfma_f32_16x16x32_bf16 v[90:93], v[148:151], v[188:191], v[90:93]
	v_mfma_f32_16x16x32_bf16 v[78:81], v[140:143], v[196:199], v[78:81]
	v_mfma_f32_16x16x32_bf16 v[74:77], v[148:151], v[196:199], v[74:77]
	v_mfma_f32_16x16x32_bf16 v[126:129], v[144:147], v[176:179], v[126:129]
	v_mfma_f32_16x16x32_bf16 v[122:125], v[152:155], v[176:179], v[122:125]
	v_mfma_f32_16x16x32_bf16 v[110:113], v[144:147], v[184:187], v[110:113]
	v_mfma_f32_16x16x32_bf16 v[106:109], v[152:155], v[184:187], v[106:109]
	v_mfma_f32_16x16x32_bf16 v[94:97], v[144:147], v[192:195], v[94:97]
	v_mfma_f32_16x16x32_bf16 v[90:93], v[152:155], v[192:195], v[90:93]
	v_mfma_f32_16x16x32_bf16 v[78:81], v[144:147], v[200:203], v[78:81]
	v_mfma_f32_16x16x32_bf16 v[74:77], v[152:155], v[200:203], v[74:77]
	s_setprio 0
	s_setprio 1
	v_mfma_f32_16x16x32_bf16 v[118:121], v[156:159], v[172:175], v[118:121]
	v_mfma_f32_16x16x32_bf16 v[114:117], v[164:167], v[172:175], v[114:117]
	v_mfma_f32_16x16x32_bf16 v[102:105], v[156:159], v[180:183], v[102:105]
	v_mfma_f32_16x16x32_bf16 v[98:101], v[164:167], v[180:183], v[98:101]
	v_mfma_f32_16x16x32_bf16 v[86:89], v[156:159], v[188:191], v[86:89]
	v_mfma_f32_16x16x32_bf16 v[82:85], v[164:167], v[188:191], v[82:85]
	v_mfma_f32_16x16x32_bf16 v[70:73], v[156:159], v[196:199], v[70:73]
	v_mfma_f32_16x16x32_bf16 v[66:69], v[164:167], v[196:199], v[66:69]
	v_mfma_f32_16x16x32_bf16 v[118:121], v[160:163], v[176:179], v[118:121]
	v_mfma_f32_16x16x32_bf16 v[114:117], v[168:171], v[176:179], v[114:117]
	v_mfma_f32_16x16x32_bf16 v[102:105], v[160:163], v[184:187], v[102:105]
	v_mfma_f32_16x16x32_bf16 v[98:101], v[168:171], v[184:187], v[98:101]
	s_setprio 0
	v_mfma_f32_16x16x32_bf16 v[86:89], v[160:163], v[192:195], v[86:89]
	v_mfma_f32_16x16x32_bf16 v[82:85], v[168:171], v[192:195], v[82:85]
	v_mfma_f32_16x16x32_bf16 v[70:73], v[160:163], v[200:203], v[70:73]
	v_mfma_f32_16x16x32_bf16 v[66:69], v[168:171], v[200:203], v[66:69]
	s_barrier
	s_add_i32 s94, s94, s38
	v_lshl_add_u64 v[204:205], s[30:31], 0, v[0:1]
	s_mov_b32 m0, s94
	ds_read_b128 v[172:175], v244 offset:16384
	ds_read_b128 v[176:179], v244 offset:17408
	ds_read_b128 v[180:183], v244 offset:18432
	ds_read_b128 v[184:187], v244 offset:19456
	ds_read_b128 v[188:191], v244 offset:20480
	ds_read_b128 v[192:195], v244 offset:21504
	ds_read_b128 v[196:199], v244 offset:22528
	ds_read_b128 v[200:203], v244 offset:23552
	global_load_lds_dwordx4 v[204:205], off
	s_add_i32 m0, s94, 0x2000
	s_add_u32 vcc_lo, s30, 0x80000
	v_lshl_add_u64 v[206:207], s[30:31], 0, v[130:131]
	s_addc_u32 vcc_hi, s31, 0
	s_add_i32 s7, s7, s38
	global_load_lds_dwordx4 v[206:207], off
	v_lshl_add_u64 v[208:209], vcc, 0, v[0:1]
	s_mov_b32 m0, s7
	v_lshl_add_u64 v[210:211], s[34:35], 0, v[132:133]
	global_load_lds_dwordx4 v[208:209], off
	v_lshl_add_u64 v[208:209], vcc, 0, v[130:131]
	s_add_i32 m0, s7, 0x2000
	s_nop 0
	global_load_lds_dwordx4 v[208:209], off
	v_lshl_add_u64 v[208:209], s[34:35], 0, v[134:135]
	s_mov_b32 m0, s39
	s_nop 0
	global_load_lds_dwordx4 v[208:209], off
	s_mov_b32 m0, s44
	s_nop 0
	global_load_lds_dwordx4 v[210:211], off
	s_waitcnt vmcnt(8)
	s_waitcnt lgkmcnt(0)
	s_barrier
; #define PG8_STAGE(bufoff, gbase, voff) do { _Pragma("unroll") for (int _i = 0; _i < 2; ++_i) \
;         __builtin_amdgcn_global_load_lds((const unsigned*)((const char*)(gbase) + (voff)[_i]), (PG8_LAS unsigned*)(lds + (bufoff) + ldsw + _i * 8192), 16, 0, 0); } while (0)
; #define PG8_WAIT_V(n) asm volatile("s_waitcnt vmcnt(" #n ")" ::: "memory")
; #define PG8_WAIT_L(n) asm volatile("s_waitcnt lgkmcnt(" #n ")" ::: "memory")
; #define PG8_BAR __builtin_amdgcn_s_barrier()
; #define PG8_SCHED __builtin_amdgcn_sched_barrier(0)
; template <class Epi, class Sched, bool ALIGN_EPI, bool F8 = false>
; __device__ __forceinline__ void gemm_phase(PG8_LAS unsigned char* lds, const Gemm g, const Sched& S, const Epi& E, int tid) {
;     ...
;             PG8_WAIT_V(8); PG8_WAIT_L(0); PG8_BAR; PG8_MMA(1, 0, At, B0); PG8_MMA(1, 1, At, B1); PG8_BAR; PG8_SCHED;
;             PG8_LDB(B0, 1, 0); PG8_LDB(B1, 1, 1); PG8_SCHED; PG8_LDA(At, 1, 0); PG8_STAGE(PG8_SA(0, 1), a2 + hstepA, voffA);
;             PG8_WAIT_V(8); PG8_WAIT_L(0); PG8_BAR; PG8_MMA(0, 0, At, B0); PG8_MMA(0, 1, At, B1); PG8_BAR; PG8_SCHED;
;             PG8_LDA(At, 1, 1); PG8_STAGE(PG8_SB(1, 0), b3, voffB); PG8_STAGE(PG8_SB(1, 1), b3 + hstepB, voffB); PG8_STAGE(PG8_SA(1, 0), a3, voffA);
	s_setprio 1
	s_waitcnt lgkmcnt(0)
	v_mfma_f32_16x16x32_bf16 v[62:65], v[140:143], v[172:175], v[62:65]
	v_mfma_f32_16x16x32_bf16 v[58:61], v[148:151], v[172:175], v[58:61]
	v_mfma_f32_16x16x32_bf16 v[46:49], v[140:143], v[180:183], v[46:49]
	v_mfma_f32_16x16x32_bf16 v[42:45], v[148:151], v[180:183], v[42:45]
	v_mfma_f32_16x16x32_bf16 v[30:33], v[140:143], v[188:191], v[30:33]
	v_mfma_f32_16x16x32_bf16 v[26:29], v[148:151], v[188:191], v[26:29]
	v_mfma_f32_16x16x32_bf16 v[14:17], v[140:143], v[196:199], v[14:17]
	v_mfma_f32_16x16x32_bf16 v[10:13], v[148:151], v[196:199], v[10:13]
	v_mfma_f32_16x16x32_bf16 v[62:65], v[144:147], v[176:179], v[62:65]
	v_mfma_f32_16x16x32_bf16 v[58:61], v[152:155], v[176:179], v[58:61]
	v_mfma_f32_16x16x32_bf16 v[46:49], v[144:147], v[184:187], v[46:49]
	v_mfma_f32_16x16x32_bf16 v[42:45], v[152:155], v[184:187], v[42:45]
	v_mfma_f32_16x16x32_bf16 v[30:33], v[144:147], v[192:195], v[30:33]
	v_mfma_f32_16x16x32_bf16 v[26:29], v[152:155], v[192:195], v[26:29]
	v_mfma_f32_16x16x32_bf16 v[14:17], v[144:147], v[200:203], v[14:17]
	v_mfma_f32_16x16x32_bf16 v[10:13], v[152:155], v[200:203], v[10:13]
	s_setprio 0
	s_setprio 1
	v_mfma_f32_16x16x32_bf16 v[54:57], v[156:159], v[172:175], v[54:57]
	v_mfma_f32_16x16x32_bf16 v[50:53], v[164:167], v[172:175], v[50:53]
	v_mfma_f32_16x16x32_bf16 v[38:41], v[156:159], v[180:183], v[38:41]
	v_mfma_f32_16x16x32_bf16 v[34:37], v[164:167], v[180:183], v[34:37]
	v_mfma_f32_16x16x32_bf16 v[22:25], v[156:159], v[188:191], v[22:25]
	v_mfma_f32_16x16x32_bf16 v[18:21], v[164:167], v[188:191], v[18:21]
	v_mfma_f32_16x16x32_bf16 v[6:9], v[156:159], v[196:199], v[6:9]
	v_mfma_f32_16x16x32_bf16 v[2:5], v[164:167], v[196:199], v[2:5]
	v_mfma_f32_16x16x32_bf16 v[54:57], v[160:163], v[176:179], v[54:57]
	v_mfma_f32_16x16x32_bf16 v[50:53], v[168:171], v[176:179], v[50:53]
	v_mfma_f32_16x16x32_bf16 v[38:41], v[160:163], v[184:187], v[38:41]
	v_mfma_f32_16x16x32_bf16 v[34:37], v[168:171], v[184:187], v[34:37]
	s_setprio 0
	v_mfma_f32_16x16x32_bf16 v[22:25], v[160:163], v[192:195], v[22:25]
	v_mfma_f32_16x16x32_bf16 v[18:21], v[168:171], v[192:195], v[18:21]
	v_mfma_f32_16x16x32_bf16 v[6:9], v[160:163], v[200:203], v[6:9]
	v_mfma_f32_16x16x32_bf16 v[2:5], v[168:171], v[200:203], v[2:5]
	s_barrier
	s_add_i32 s7, 0, 0x18000
	s_add_i32 s94, 0, 0x1c000
	v_add_u32_e32 v152, s7, v215
	v_add_u32_e32 v168, s94, v215
	ds_read_b128 v[140:143], v152
	ds_read_b128 v[144:147], v152 offset:1024
	ds_read_b128 v[148:151], v152 offset:2048
	ds_read_b128 v[152:155], v152 offset:3072
	ds_read_b128 v[156:159], v168
	ds_read_b128 v[160:163], v168 offset:1024
	ds_read_b128 v[164:167], v168 offset:2048
	ds_read_b128 v[168:171], v168 offset:3072
	s_add_u32 s34, s34, 0x80000
	s_addc_u32 s35, s35, 0
	s_mov_b32 m0, s45
	v_lshl_add_u64 v[212:213], s[34:35], 0, v[134:135]
	ds_read_b128 v[172:175], v244 offset:32768
	ds_read_b128 v[176:179], v244 offset:33792
	ds_read_b128 v[180:183], v244 offset:34816
	ds_read_b128 v[184:187], v244 offset:35840
	ds_read_b128 v[188:191], v244 offset:36864
	ds_read_b128 v[192:195], v244 offset:37888
	ds_read_b128 v[196:199], v244 offset:38912
	ds_read_b128 v[200:203], v244 offset:39936
	global_load_lds_dwordx4 v[212:213], off
	v_lshl_add_u64 v[212:213], s[34:35], 0, v[132:133]
	s_mov_b32 m0, s69
	s_nop 0
	global_load_lds_dwordx4 v[212:213], off
	s_waitcnt vmcnt(8)
	s_waitcnt lgkmcnt(0)
	s_barrier
	s_setprio 1
	s_waitcnt lgkmcnt(0)
	v_mfma_f32_16x16x32_bf16 v[126:129], v[140:143], v[172:175], v[126:129]
	v_mfma_f32_16x16x32_bf16 v[122:125], v[148:151], v[172:175], v[122:125]
	v_mfma_f32_16x16x32_bf16 v[110:113], v[140:143], v[180:183], v[110:113]
	v_mfma_f32_16x16x32_bf16 v[106:109], v[148:151], v[180:183], v[106:109]
	v_mfma_f32_16x16x32_bf16 v[94:97], v[140:143], v[188:191], v[94:97]
	v_mfma_f32_16x16x32_bf16 v[90:93], v[148:151], v[188:191], v[90:93]
	v_mfma_f32_16x16x32_bf16 v[78:81], v[140:143], v[196:199], v[78:81]
	v_mfma_f32_16x16x32_bf16 v[74:77], v[148:151], v[196:199], v[74:77]
	v_mfma_f32_16x16x32_bf16 v[126:129], v[144:147], v[176:179], v[126:129]
	v_mfma_f32_16x16x32_bf16 v[122:125], v[152:155], v[176:179], v[122:125]
	v_mfma_f32_16x16x32_bf16 v[110:113], v[144:147], v[184:187], v[110:113]
	v_mfma_f32_16x16x32_bf16 v[106:109], v[152:155], v[184:187], v[106:109]
	v_mfma_f32_16x16x32_bf16 v[94:97], v[144:147], v[192:195], v[94:97]
	v_mfma_f32_16x16x32_bf16 v[90:93], v[152:155], v[192:195], v[90:93]
	v_mfma_f32_16x16x32_bf16 v[78:81], v[144:147], v[200:203], v[78:81]
	v_mfma_f32_16x16x32_bf16 v[74:77], v[152:155], v[200:203], v[74:77]
	s_setprio 0
	s_setprio 1
	v_mfma_f32_16x16x32_bf16 v[118:121], v[156:159], v[172:175], v[118:121]
	v_mfma_f32_16x16x32_bf16 v[114:117], v[164:167], v[172:175], v[114:117]
	v_mfma_f32_16x16x32_bf16 v[102:105], v[156:159], v[180:183], v[102:105]
	v_mfma_f32_16x16x32_bf16 v[98:101], v[164:167], v[180:183], v[98:101]
	v_mfma_f32_16x16x32_bf16 v[86:89], v[156:159], v[188:191], v[86:89]
	v_mfma_f32_16x16x32_bf16 v[82:85], v[164:167], v[188:191], v[82:85]
	v_mfma_f32_16x16x32_bf16 v[70:73], v[156:159], v[196:199], v[70:73]
	v_mfma_f32_16x16x32_bf16 v[66:69], v[164:167], v[196:199], v[66:69]
	v_mfma_f32_16x16x32_bf16 v[118:121], v[160:163], v[176:179], v[118:121]
	v_mfma_f32_16x16x32_bf16 v[114:117], v[168:171], v[176:179], v[114:117]
	v_mfma_f32_16x16x32_bf16 v[102:105], v[160:163], v[184:187], v[102:105]
	v_mfma_f32_16x16x32_bf16 v[98:101], v[168:171], v[184:187], v[98:101]
	s_setprio 0
	v_mfma_f32_16x16x32_bf16 v[86:89], v[160:163], v[192:195], v[86:89]
	v_mfma_f32_16x16x32_bf16 v[82:85], v[168:171], v[192:195], v[82:85]
	v_mfma_f32_16x16x32_bf16 v[70:73], v[160:163], v[200:203], v[70:73]
	v_mfma_f32_16x16x32_bf16 v[66:69], v[168:171], v[200:203], v[66:69]
	s_barrier
; #define PG8_STAGE(bufoff, gbase, voff) do { _Pragma("unroll") for (int _i = 0; _i < 2; ++_i) \
;         __builtin_amdgcn_global_load_lds((const unsigned*)((const char*)(gbase) + (voff)[_i]), (PG8_LAS unsigned*)(lds + (bufoff) + ldsw + _i * 8192), 16, 0, 0); } while (0)
; #define PG8_WAIT_V(n) asm volatile("s_waitcnt vmcnt(" #n ")" ::: "memory")
; #define PG8_WAIT_L(n) asm volatile("s_waitcnt lgkmcnt(" #n ")" ::: "memory")
; #define PG8_BAR __builtin_amdgcn_s_barrier()
; #define PG8_SCHED __builtin_amdgcn_sched_barrier(0)
; template <class Epi, class Sched, bool ALIGN_EPI, bool F8 = false>
; __device__ __forceinline__ void gemm_phase(PG8_LAS unsigned char* lds, const Gemm g, const Sched& S, const Epi& E, int tid) {
;     ...
;         for (int t = 0; t < nt; t += 2) {
;             const bool last = (t == nt - 2);
;             const char* a1 = cA + (size_t)(t + 1) * kstep;
;             const char* a2 = last ? nA : cA + (size_t)(t + 2) * kstep; const char* b2 = last ? nB : cB + (size_t)(t + 2) * kstep;
;             const char* a3 = a2 + kstep; const char* b3 = b2 + kstep;
;     ...
;             PG8_LDA(At, 1, 1); PG8_STAGE(PG8_SB(1, 0), b3, voffB); PG8_STAGE(PG8_SB(1, 1), b3 + hstepB, voffB); PG8_STAGE(PG8_SA(1, 0), a3, voffA);
;             PG8_WAIT_V(8); PG8_WAIT_L(0); PG8_BAR; PG8_MMA(1, 0, At, B0); PG8_MMA(1, 1, At, B1); PG8_BAR; PG8_SCHED;
	s_add_i32 s7, s7, s38
	v_lshl_add_u64 v[204:205], v[204:205], 0, s[60:61]
	s_mov_b32 m0, s7
	ds_read_b128 v[172:175], v244 offset:49152
	ds_read_b128 v[176:179], v244 offset:50176
	ds_read_b128 v[180:183], v244 offset:51200
	ds_read_b128 v[184:187], v244 offset:52224
	ds_read_b128 v[188:191], v244 offset:53248
	ds_read_b128 v[192:195], v244 offset:54272
	ds_read_b128 v[196:199], v244 offset:55296
	ds_read_b128 v[200:203], v244 offset:56320
	global_load_lds_dwordx4 v[204:205], off
	s_add_i32 m0, s7, 0x2000
	s_add_u32 s30, s30, 0x80080
	v_lshl_add_u64 v[204:205], v[206:207], 0, s[60:61]
	s_addc_u32 s31, s31, 0
	s_add_i32 s7, s94, s38
	global_load_lds_dwordx4 v[204:205], off
	v_lshl_add_u64 v[204:205], s[30:31], 0, v[0:1]
	s_mov_b32 m0, s7
	s_nop 0
	global_load_lds_dwordx4 v[204:205], off
	v_lshl_add_u64 v[204:205], s[30:31], 0, v[130:131]
	s_add_i32 m0, s7, 0x2000
	s_nop 0
	global_load_lds_dwordx4 v[204:205], off
	v_lshl_add_u64 v[204:205], v[208:209], 0, s[60:61]
	s_mov_b32 m0, s82
	s_nop 0
	global_load_lds_dwordx4 v[204:205], off
	v_lshl_add_u64 v[204:205], v[210:211], 0, s[60:61]
	s_mov_b32 m0, s83
	s_nop 0
	global_load_lds_dwordx4 v[204:205], off
	s_waitcnt vmcnt(8)
	s_waitcnt lgkmcnt(0)
	s_barrier
	s_setprio 1
	s_waitcnt lgkmcnt(0)
	v_mfma_f32_16x16x32_bf16 v[62:65], v[140:143], v[172:175], v[62:65]
	v_mfma_f32_16x16x32_bf16 v[58:61], v[148:151], v[172:175], v[58:61]
	v_mfma_f32_16x16x32_bf16 v[46:49], v[140:143], v[180:183], v[46:49]
	v_mfma_f32_16x16x32_bf16 v[42:45], v[148:151], v[180:183], v[42:45]
	v_mfma_f32_16x16x32_bf16 v[30:33], v[140:143], v[188:191], v[30:33]
	v_mfma_f32_16x16x32_bf16 v[26:29], v[148:151], v[188:191], v[26:29]
	v_mfma_f32_16x16x32_bf16 v[14:17], v[140:143], v[196:199], v[14:17]
	v_mfma_f32_16x16x32_bf16 v[10:13], v[148:151], v[196:199], v[10:13]
	v_mfma_f32_16x16x32_bf16 v[62:65], v[144:147], v[176:179], v[62:65]
	v_mfma_f32_16x16x32_bf16 v[58:61], v[152:155], v[176:179], v[58:61]
	v_mfma_f32_16x16x32_bf16 v[46:49], v[144:147], v[184:187], v[46:49]
	v_mfma_f32_16x16x32_bf16 v[42:45], v[152:155], v[184:187], v[42:45]
	v_mfma_f32_16x16x32_bf16 v[30:33], v[144:147], v[192:195], v[30:33]
	v_mfma_f32_16x16x32_bf16 v[26:29], v[152:155], v[192:195], v[26:29]
	v_mfma_f32_16x16x32_bf16 v[14:17], v[144:147], v[200:203], v[14:17]
	v_mfma_f32_16x16x32_bf16 v[10:13], v[152:155], v[200:203], v[10:13]
	s_setprio 0
	s_setprio 1
	v_mfma_f32_16x16x32_bf16 v[54:57], v[156:159], v[172:175], v[54:57]
	v_mfma_f32_16x16x32_bf16 v[50:53], v[164:167], v[172:175], v[50:53]
	v_mfma_f32_16x16x32_bf16 v[38:41], v[156:159], v[180:183], v[38:41]
	v_mfma_f32_16x16x32_bf16 v[34:37], v[164:167], v[180:183], v[34:37]
	v_mfma_f32_16x16x32_bf16 v[22:25], v[156:159], v[188:191], v[22:25]
	v_mfma_f32_16x16x32_bf16 v[18:21], v[164:167], v[188:191], v[18:21]
	v_mfma_f32_16x16x32_bf16 v[6:9], v[156:159], v[196:199], v[6:9]
	v_mfma_f32_16x16x32_bf16 v[2:5], v[164:167], v[196:199], v[2:5]
	v_mfma_f32_16x16x32_bf16 v[54:57], v[160:163], v[176:179], v[54:57]
	v_mfma_f32_16x16x32_bf16 v[50:53], v[168:171], v[176:179], v[50:53]
	v_mfma_f32_16x16x32_bf16 v[38:41], v[160:163], v[184:187], v[38:41]
	v_mfma_f32_16x16x32_bf16 v[34:37], v[168:171], v[184:187], v[34:37]
	s_setprio 0
	v_mfma_f32_16x16x32_bf16 v[22:25], v[160:163], v[192:195], v[22:25]
	v_mfma_f32_16x16x32_bf16 v[18:21], v[168:171], v[192:195], v[18:21]
	v_mfma_f32_16x16x32_bf16 v[6:9], v[160:163], v[200:203], v[6:9]
	v_mfma_f32_16x16x32_bf16 v[2:5], v[168:171], v[200:203], v[2:5]
	s_barrier
	s_add_i32 s6, s6, 2
	s_add_u32 s28, s28, 0x100
	s_addc_u32 s29, s29, 0
	s_add_u32 s89, s89, 0x100
	s_addc_u32 s50, s50, 0
	s_cmp_gt_u32 s6, 29
	s_cbranch_scc0 .LBB0_1508
	s_and_b64 vcc, exec, s[14:15]
	s_cbranch_vccz .LBB0_1511
	s_barrier

; #define PG8_STAGE(bufoff, gbase, voff) do { _Pragma("unroll") for (int _i = 0; _i < 2; ++_i) \
;         __builtin_amdgcn_global_load_lds((const unsigned*)((const char*)(gbase) + (voff)[_i]), (PG8_LAS unsigned*)(lds + (bufoff) + ldsw + _i * 8192), 16, 0, 0); } while (0)
; #define PG8_WAIT_V(n) asm volatile("s_waitcnt vmcnt(" #n ")" ::: "memory")
; #define PG8_WAIT_L(n) asm volatile("s_waitcnt lgkmcnt(" #n ")" ::: "memory")
; #define PG8_BAR __builtin_amdgcn_s_barrier()
; #define PG8_SCHED __builtin_amdgcn_sched_barrier(0)
; template <class Epi, class Sched, bool ALIGN_EPI, bool F8 = false>
; __device__ __forceinline__ void gemm_phase(PG8_LAS unsigned char* lds, const Gemm g, const Sched& S, const Epi& E, int tid) {
;     ...
;             PG8_LDB(B0, 0, 0); PG8_LDB(B1, 0, 1); PG8_SCHED; PG8_LDA(At, 0, 0); PG8_STAGE(PG8_SA(1, 1), a1 + hstepA, voffA);
;             PG8_WAIT_V(8); PG8_WAIT_L(0); PG8_BAR; PG8_MMA(0, 0, At, B0); PG8_MMA(0, 1, At, B1); PG8_BAR; PG8_SCHED;
;             PG8_LDA(At, 0, 1); PG8_STAGE(PG8_SB(0, 0), b2, voffB); PG8_STAGE(PG8_SB(0, 1), b2 + hstepB, voffB); PG8_STAGE(PG8_SA(0, 0), a2, voffA);
;             PG8_WAIT_V(8); PG8_WAIT_L(0); PG8_BAR; PG8_MMA(1, 0, At, B0); PG8_MMA(1, 1, At, B1); PG8_BAR; PG8_SCHED;
.LBB0_1568:
	s_add_u32 s28, s26, 0xfffc0080
	s_addc_u32 s29, s27, -1
	s_add_i32 s89, 0, 0x10000
	s_cmp_eq_u32 s7, 12
	s_cselect_b32 s31, s19, s29
	s_cselect_b32 s30, s87, s28
	s_cselect_b32 s29, s17, s6
	s_cselect_b32 s28, s88, s50
	s_add_i32 s94, 0, 0x14000
	v_add_u32_e32 v142, s89, v201
	v_add_u32_e32 v168, s94, v201
	ds_read_b128 v[130:133], v142
	ds_read_b128 v[134:137], v142 offset:1024
	ds_read_b128 v[138:141], v142 offset:2048
	ds_read_b128 v[142:145], v142 offset:3072
	ds_read_b128 v[146:149], v168
	ds_read_b128 v[150:153], v168 offset:1024
	ds_read_b128 v[154:157], v168 offset:2048
	ds_read_b128 v[168:171], v168 offset:3072
	v_lshl_add_u64 v[208:209], s[26:27], 0, v[164:165]
	s_add_i32 m0, s44, 0xc000
	ds_read_b128 v[172:175], v203
	ds_read_b128 v[176:179], v203 offset:1024
	ds_read_b128 v[180:183], v203 offset:2048
	ds_read_b128 v[184:187], v203 offset:3072
	ds_read_b128 v[188:191], v203 offset:4096
	ds_read_b128 v[192:195], v203 offset:5120
	ds_read_b128 v[196:199], v203 offset:6144
	ds_read_b128 v[204:207], v203 offset:7168
	global_load_lds_dwordx4 v[208:209], off
	v_lshl_add_u64 v[208:209], s[26:27], 0, v[166:167]
	s_add_i32 m0, s44, 0xe000
	s_nop 0
	global_load_lds_dwordx4 v[208:209], off
	s_waitcnt vmcnt(8)
	s_waitcnt lgkmcnt(0)
	s_barrier
	s_setprio 1
	s_waitcnt lgkmcnt(0)
	v_mfma_f32_16x16x32_bf16 v[126:129], v[130:133], v[172:175], v[126:129]
	v_mfma_f32_16x16x32_bf16 v[122:125], v[138:141], v[172:175], v[122:125]
	v_mfma_f32_16x16x32_bf16 v[110:113], v[130:133], v[180:183], v[110:113]
	v_mfma_f32_16x16x32_bf16 v[106:109], v[138:141], v[180:183], v[106:109]
	v_mfma_f32_16x16x32_bf16 v[94:97], v[130:133], v[188:191], v[94:97]
	v_mfma_f32_16x16x32_bf16 v[90:93], v[138:141], v[188:191], v[90:93]
	v_mfma_f32_16x16x32_bf16 v[78:81], v[130:133], v[196:199], v[78:81]
	v_mfma_f32_16x16x32_bf16 v[74:77], v[138:141], v[196:199], v[74:77]
	v_mfma_f32_16x16x32_bf16 v[126:129], v[134:137], v[176:179], v[126:129]
	v_mfma_f32_16x16x32_bf16 v[122:125], v[142:145], v[176:179], v[122:125]
	v_mfma_f32_16x16x32_bf16 v[110:113], v[134:137], v[184:187], v[110:113]
	v_mfma_f32_16x16x32_bf16 v[106:109], v[142:145], v[184:187], v[106:109]
	v_mfma_f32_16x16x32_bf16 v[94:97], v[134:137], v[192:195], v[94:97]
	v_mfma_f32_16x16x32_bf16 v[90:93], v[142:145], v[192:195], v[90:93]
	v_mfma_f32_16x16x32_bf16 v[78:81], v[134:137], v[204:207], v[78:81]
	v_mfma_f32_16x16x32_bf16 v[74:77], v[142:145], v[204:207], v[74:77]
	s_setprio 0
	s_setprio 1
	v_mfma_f32_16x16x32_bf16 v[118:121], v[146:149], v[172:175], v[118:121]
	v_mfma_f32_16x16x32_bf16 v[114:117], v[154:157], v[172:175], v[114:117]
	v_mfma_f32_16x16x32_bf16 v[102:105], v[146:149], v[180:183], v[102:105]
	v_mfma_f32_16x16x32_bf16 v[98:101], v[154:157], v[180:183], v[98:101]
	v_mfma_f32_16x16x32_bf16 v[86:89], v[146:149], v[188:191], v[86:89]
	v_mfma_f32_16x16x32_bf16 v[82:85], v[154:157], v[188:191], v[82:85]
	v_mfma_f32_16x16x32_bf16 v[70:73], v[146:149], v[196:199], v[70:73]
	v_mfma_f32_16x16x32_bf16 v[66:69], v[154:157], v[196:199], v[66:69]
	v_mfma_f32_16x16x32_bf16 v[118:121], v[150:153], v[176:179], v[118:121]
	v_mfma_f32_16x16x32_bf16 v[114:117], v[168:171], v[176:179], v[114:117]
	v_mfma_f32_16x16x32_bf16 v[102:105], v[150:153], v[184:187], v[102:105]
	v_mfma_f32_16x16x32_bf16 v[98:101], v[168:171], v[184:187], v[98:101]
	s_setprio 0
	v_mfma_f32_16x16x32_bf16 v[86:89], v[150:153], v[192:195], v[86:89]
	v_mfma_f32_16x16x32_bf16 v[82:85], v[168:171], v[192:195], v[82:85]
	v_mfma_f32_16x16x32_bf16 v[70:73], v[150:153], v[204:207], v[70:73]
	v_mfma_f32_16x16x32_bf16 v[66:69], v[168:171], v[204:207], v[66:69]
	s_barrier
	s_add_i32 s89, s89, s39
	v_lshl_add_u64 v[208:209], s[28:29], 0, v[0:1]
	s_mov_b32 m0, s89
	ds_read_b128 v[172:175], v203 offset:16384
	ds_read_b128 v[176:179], v203 offset:17408
	ds_read_b128 v[180:183], v203 offset:18432
	ds_read_b128 v[184:187], v203 offset:19456
	ds_read_b128 v[188:191], v203 offset:20480
	ds_read_b128 v[192:195], v203 offset:21504
	ds_read_b128 v[196:199], v203 offset:22528
	ds_read_b128 v[204:207], v203 offset:23552
	global_load_lds_dwordx4 v[208:209], off
	s_add_i32 m0, s89, 0x2000
	s_add_u32 vcc_lo, s28, 0x40000
	v_lshl_add_u64 v[210:211], s[28:29], 0, v[158:159]
	s_addc_u32 vcc_hi, s29, 0
	s_add_i32 s89, s94, s39
	global_load_lds_dwordx4 v[210:211], off
	v_lshl_add_u64 v[212:213], vcc, 0, v[0:1]
	s_mov_b32 m0, s89
	v_lshl_add_u64 v[214:215], s[30:31], 0, v[160:161]
	global_load_lds_dwordx4 v[212:213], off
	v_lshl_add_u64 v[212:213], vcc, 0, v[158:159]
	s_add_i32 m0, s89, 0x2000
	s_nop 0
	global_load_lds_dwordx4 v[212:213], off
	v_lshl_add_u64 v[212:213], s[30:31], 0, v[162:163]
	s_mov_b32 m0, s44
	s_nop 0
	global_load_lds_dwordx4 v[212:213], off
	s_mov_b32 m0, s45
	s_nop 0
	global_load_lds_dwordx4 v[214:215], off
	s_waitcnt vmcnt(8)
	s_waitcnt lgkmcnt(0)
	s_barrier
; #define PG8_STAGE(bufoff, gbase, voff) do { _Pragma("unroll") for (int _i = 0; _i < 2; ++_i) \
;         __builtin_amdgcn_global_load_lds((const unsigned*)((const char*)(gbase) + (voff)[_i]), (PG8_LAS unsigned*)(lds + (bufoff) + ldsw + _i * 8192), 16, 0, 0); } while (0)
; #define PG8_WAIT_V(n) asm volatile("s_waitcnt vmcnt(" #n ")" ::: "memory")
; #define PG8_WAIT_L(n) asm volatile("s_waitcnt lgkmcnt(" #n ")" ::: "memory")
; #define PG8_BAR __builtin_amdgcn_s_barrier()
; #define PG8_SCHED __builtin_amdgcn_sched_barrier(0)
; template <class Epi, class Sched, bool ALIGN_EPI, bool F8 = false>
; __device__ __forceinline__ void gemm_phase(PG8_LAS unsigned char* lds, const Gemm g, const Sched& S, const Epi& E, int tid) {
;     ...
;             PG8_WAIT_V(8); PG8_WAIT_L(0); PG8_BAR; PG8_MMA(1, 0, At, B0); PG8_MMA(1, 1, At, B1); PG8_BAR; PG8_SCHED;
;             PG8_LDB(B0, 1, 0); PG8_LDB(B1, 1, 1); PG8_SCHED; PG8_LDA(At, 1, 0); PG8_STAGE(PG8_SA(0, 1), a2 + hstepA, voffA);
;             PG8_WAIT_V(8); PG8_WAIT_L(0); PG8_BAR; PG8_MMA(0, 0, At, B0); PG8_MMA(0, 1, At, B1); PG8_BAR; PG8_SCHED;
;             PG8_LDA(At, 1, 1); PG8_STAGE(PG8_SB(1, 0), b3, voffB); PG8_STAGE(PG8_SB(1, 1), b3 + hstepB, voffB); PG8_STAGE(PG8_SA(1, 0), a3, voffA);
	s_setprio 1
	s_waitcnt lgkmcnt(0)
	v_mfma_f32_16x16x32_bf16 v[62:65], v[130:133], v[172:175], v[62:65]
	v_mfma_f32_16x16x32_bf16 v[58:61], v[138:141], v[172:175], v[58:61]
	v_mfma_f32_16x16x32_bf16 v[46:49], v[130:133], v[180:183], v[46:49]
	v_mfma_f32_16x16x32_bf16 v[42:45], v[138:141], v[180:183], v[42:45]
	v_mfma_f32_16x16x32_bf16 v[30:33], v[130:133], v[188:191], v[30:33]
	v_mfma_f32_16x16x32_bf16 v[26:29], v[138:141], v[188:191], v[26:29]
	v_mfma_f32_16x16x32_bf16 v[14:17], v[130:133], v[196:199], v[14:17]
	v_mfma_f32_16x16x32_bf16 v[10:13], v[138:141], v[196:199], v[10:13]
	v_mfma_f32_16x16x32_bf16 v[62:65], v[134:137], v[176:179], v[62:65]
	v_mfma_f32_16x16x32_bf16 v[58:61], v[142:145], v[176:179], v[58:61]
	v_mfma_f32_16x16x32_bf16 v[46:49], v[134:137], v[184:187], v[46:49]
	v_mfma_f32_16x16x32_bf16 v[42:45], v[142:145], v[184:187], v[42:45]
	v_mfma_f32_16x16x32_bf16 v[30:33], v[134:137], v[192:195], v[30:33]
	v_mfma_f32_16x16x32_bf16 v[26:29], v[142:145], v[192:195], v[26:29]
	v_mfma_f32_16x16x32_bf16 v[14:17], v[134:137], v[204:207], v[14:17]
	v_mfma_f32_16x16x32_bf16 v[10:13], v[142:145], v[204:207], v[10:13]
	s_setprio 0
	s_setprio 1
	v_mfma_f32_16x16x32_bf16 v[54:57], v[146:149], v[172:175], v[54:57]
	v_mfma_f32_16x16x32_bf16 v[50:53], v[154:157], v[172:175], v[50:53]
	v_mfma_f32_16x16x32_bf16 v[38:41], v[146:149], v[180:183], v[38:41]
	v_mfma_f32_16x16x32_bf16 v[34:37], v[154:157], v[180:183], v[34:37]
	v_mfma_f32_16x16x32_bf16 v[22:25], v[146:149], v[188:191], v[22:25]
	v_mfma_f32_16x16x32_bf16 v[18:21], v[154:157], v[188:191], v[18:21]
	v_mfma_f32_16x16x32_bf16 v[6:9], v[146:149], v[196:199], v[6:9]
	v_mfma_f32_16x16x32_bf16 v[2:5], v[154:157], v[196:199], v[2:5]
	v_mfma_f32_16x16x32_bf16 v[54:57], v[150:153], v[176:179], v[54:57]
	v_mfma_f32_16x16x32_bf16 v[50:53], v[168:171], v[176:179], v[50:53]
	v_mfma_f32_16x16x32_bf16 v[38:41], v[150:153], v[184:187], v[38:41]
	v_mfma_f32_16x16x32_bf16 v[34:37], v[168:171], v[184:187], v[34:37]
	s_setprio 0
	v_mfma_f32_16x16x32_bf16 v[22:25], v[150:153], v[192:195], v[22:25]
	v_mfma_f32_16x16x32_bf16 v[18:21], v[168:171], v[192:195], v[18:21]
	v_mfma_f32_16x16x32_bf16 v[6:9], v[150:153], v[204:207], v[6:9]
	v_mfma_f32_16x16x32_bf16 v[2:5], v[168:171], v[204:207], v[2:5]
	s_barrier
	s_add_i32 s89, 0, 0x18000
	s_add_i32 s94, 0, 0x1c000
	v_add_u32_e32 v142, s89, v201
	v_add_u32_e32 v168, s94, v201
	ds_read_b128 v[130:133], v142
	ds_read_b128 v[134:137], v142 offset:1024
	ds_read_b128 v[138:141], v142 offset:2048
	ds_read_b128 v[142:145], v142 offset:3072
	ds_read_b128 v[146:149], v168
	ds_read_b128 v[150:153], v168 offset:1024
	ds_read_b128 v[154:157], v168 offset:2048
	ds_read_b128 v[168:171], v168 offset:3072
	s_add_u32 s30, s30, 0x40000
	s_addc_u32 s31, s31, 0
	s_mov_b32 m0, s51
	v_lshl_add_u64 v[216:217], s[30:31], 0, v[162:163]
	ds_read_b128 v[172:175], v203 offset:32768
	ds_read_b128 v[176:179], v203 offset:33792
	ds_read_b128 v[180:183], v203 offset:34816
	ds_read_b128 v[184:187], v203 offset:35840
	ds_read_b128 v[188:191], v203 offset:36864
	ds_read_b128 v[192:195], v203 offset:37888
	ds_read_b128 v[196:199], v203 offset:38912
	ds_read_b128 v[204:207], v203 offset:39936
	global_load_lds_dwordx4 v[216:217], off
	v_lshl_add_u64 v[216:217], s[30:31], 0, v[160:161]
	s_mov_b32 m0, s68
	s_nop 0
	global_load_lds_dwordx4 v[216:217], off
	s_waitcnt vmcnt(8)
	s_waitcnt lgkmcnt(0)
	s_barrier
	s_setprio 1
	s_waitcnt lgkmcnt(0)
	v_mfma_f32_16x16x32_bf16 v[126:129], v[130:133], v[172:175], v[126:129]
	v_mfma_f32_16x16x32_bf16 v[122:125], v[138:141], v[172:175], v[122:125]
	v_mfma_f32_16x16x32_bf16 v[110:113], v[130:133], v[180:183], v[110:113]
	v_mfma_f32_16x16x32_bf16 v[106:109], v[138:141], v[180:183], v[106:109]
	v_mfma_f32_16x16x32_bf16 v[94:97], v[130:133], v[188:191], v[94:97]
	v_mfma_f32_16x16x32_bf16 v[90:93], v[138:141], v[188:191], v[90:93]
	v_mfma_f32_16x16x32_bf16 v[78:81], v[130:133], v[196:199], v[78:81]
	v_mfma_f32_16x16x32_bf16 v[74:77], v[138:141], v[196:199], v[74:77]
	v_mfma_f32_16x16x32_bf16 v[126:129], v[134:137], v[176:179], v[126:129]
	v_mfma_f32_16x16x32_bf16 v[122:125], v[142:145], v[176:179], v[122:125]
	v_mfma_f32_16x16x32_bf16 v[110:113], v[134:137], v[184:187], v[110:113]
	v_mfma_f32_16x16x32_bf16 v[106:109], v[142:145], v[184:187], v[106:109]
	v_mfma_f32_16x16x32_bf16 v[94:97], v[134:137], v[192:195], v[94:97]
	v_mfma_f32_16x16x32_bf16 v[90:93], v[142:145], v[192:195], v[90:93]
	v_mfma_f32_16x16x32_bf16 v[78:81], v[134:137], v[204:207], v[78:81]
	v_mfma_f32_16x16x32_bf16 v[74:77], v[142:145], v[204:207], v[74:77]
	s_setprio 0
	s_setprio 1
	v_mfma_f32_16x16x32_bf16 v[118:121], v[146:149], v[172:175], v[118:121]
	v_mfma_f32_16x16x32_bf16 v[114:117], v[154:157], v[172:175], v[114:117]
	v_mfma_f32_16x16x32_bf16 v[102:105], v[146:149], v[180:183], v[102:105]
	v_mfma_f32_16x16x32_bf16 v[98:101], v[154:157], v[180:183], v[98:101]
	v_mfma_f32_16x16x32_bf16 v[86:89], v[146:149], v[188:191], v[86:89]
	v_mfma_f32_16x16x32_bf16 v[82:85], v[154:157], v[188:191], v[82:85]
	v_mfma_f32_16x16x32_bf16 v[70:73], v[146:149], v[196:199], v[70:73]
	v_mfma_f32_16x16x32_bf16 v[66:69], v[154:157], v[196:199], v[66:69]
	v_mfma_f32_16x16x32_bf16 v[118:121], v[150:153], v[176:179], v[118:121]
	v_mfma_f32_16x16x32_bf16 v[114:117], v[168:171], v[176:179], v[114:117]
	v_mfma_f32_16x16x32_bf16 v[102:105], v[150:153], v[184:187], v[102:105]
	v_mfma_f32_16x16x32_bf16 v[98:101], v[168:171], v[184:187], v[98:101]
	s_setprio 0
	v_mfma_f32_16x16x32_bf16 v[86:89], v[150:153], v[192:195], v[86:89]
	v_mfma_f32_16x16x32_bf16 v[82:85], v[168:171], v[192:195], v[82:85]
	v_mfma_f32_16x16x32_bf16 v[70:73], v[150:153], v[204:207], v[70:73]
	v_mfma_f32_16x16x32_bf16 v[66:69], v[168:171], v[204:207], v[66:69]
	s_barrier
; #define PG8_STAGE(bufoff, gbase, voff) do { _Pragma("unroll") for (int _i = 0; _i < 2; ++_i) \
;         __builtin_amdgcn_global_load_lds((const unsigned*)((const char*)(gbase) + (voff)[_i]), (PG8_LAS unsigned*)(lds + (bufoff) + ldsw + _i * 8192), 16, 0, 0); } while (0)
; #define PG8_WAIT_V(n) asm volatile("s_waitcnt vmcnt(" #n ")" ::: "memory")
; #define PG8_WAIT_L(n) asm volatile("s_waitcnt lgkmcnt(" #n ")" ::: "memory")
; #define PG8_BAR __builtin_amdgcn_s_barrier()
; #define PG8_SCHED __builtin_amdgcn_sched_barrier(0)
; template <class Epi, class Sched, bool ALIGN_EPI, bool F8 = false>
; __device__ __forceinline__ void gemm_phase(PG8_LAS unsigned char* lds, const Gemm g, const Sched& S, const Epi& E, int tid) {
;     ...
;         for (int t = 0; t < nt; t += 2) {
;             const bool last = (t == nt - 2);
;             const char* a1 = cA + (size_t)(t + 1) * kstep;
;             const char* a2 = last ? nA : cA + (size_t)(t + 2) * kstep; const char* b2 = last ? nB : cB + (size_t)(t + 2) * kstep;
;             const char* a3 = a2 + kstep; const char* b3 = b2 + kstep;
;     ...
;             PG8_LDA(At, 1, 1); PG8_STAGE(PG8_SB(1, 0), b3, voffB); PG8_STAGE(PG8_SB(1, 1), b3 + hstepB, voffB); PG8_STAGE(PG8_SA(1, 0), a3, voffA);
;             PG8_WAIT_V(8); PG8_WAIT_L(0); PG8_BAR; PG8_MMA(1, 0, At, B0); PG8_MMA(1, 1, At, B1); PG8_BAR; PG8_SCHED;
	s_add_i32 s30, s89, s39
	v_lshl_add_u64 v[208:209], v[208:209], 0, s[60:61]
	s_mov_b32 m0, s30
	ds_read_b128 v[172:175], v203 offset:49152
	ds_read_b128 v[176:179], v203 offset:50176
	ds_read_b128 v[180:183], v203 offset:51200
	ds_read_b128 v[184:187], v203 offset:52224
	ds_read_b128 v[188:191], v203 offset:53248
	ds_read_b128 v[192:195], v203 offset:54272
	ds_read_b128 v[196:199], v203 offset:55296
	ds_read_b128 v[204:207], v203 offset:56320
	global_load_lds_dwordx4 v[208:209], off
	s_add_i32 m0, s30, 0x2000
	s_add_u32 s28, s28, 0x40080
	v_lshl_add_u64 v[208:209], v[210:211], 0, s[60:61]
	s_addc_u32 s29, s29, 0
	s_add_i32 s30, s94, s39
	global_load_lds_dwordx4 v[208:209], off
	v_lshl_add_u64 v[208:209], s[28:29], 0, v[0:1]
	s_mov_b32 m0, s30
	s_nop 0
	global_load_lds_dwordx4 v[208:209], off
	v_lshl_add_u64 v[208:209], s[28:29], 0, v[158:159]
	s_add_i32 m0, s30, 0x2000
	s_nop 0
	global_load_lds_dwordx4 v[208:209], off
	v_lshl_add_u64 v[208:209], v[212:213], 0, s[60:61]
	s_mov_b32 m0, s82
	s_nop 0
	global_load_lds_dwordx4 v[208:209], off
	v_lshl_add_u64 v[208:209], v[214:215], 0, s[60:61]
	s_mov_b32 m0, s83
	s_nop 0
	global_load_lds_dwordx4 v[208:209], off
	s_waitcnt vmcnt(8)
	s_waitcnt lgkmcnt(0)
	s_barrier
	s_setprio 1
	s_waitcnt lgkmcnt(0)
	v_mfma_f32_16x16x32_bf16 v[62:65], v[130:133], v[172:175], v[62:65]
	v_mfma_f32_16x16x32_bf16 v[58:61], v[138:141], v[172:175], v[58:61]
	v_mfma_f32_16x16x32_bf16 v[46:49], v[130:133], v[180:183], v[46:49]
	v_mfma_f32_16x16x32_bf16 v[42:45], v[138:141], v[180:183], v[42:45]
	v_mfma_f32_16x16x32_bf16 v[30:33], v[130:133], v[188:191], v[30:33]
	v_mfma_f32_16x16x32_bf16 v[26:29], v[138:141], v[188:191], v[26:29]
	v_mfma_f32_16x16x32_bf16 v[14:17], v[130:133], v[196:199], v[14:17]
	v_mfma_f32_16x16x32_bf16 v[10:13], v[138:141], v[196:199], v[10:13]
	v_mfma_f32_16x16x32_bf16 v[62:65], v[134:137], v[176:179], v[62:65]
	v_mfma_f32_16x16x32_bf16 v[58:61], v[142:145], v[176:179], v[58:61]
	v_mfma_f32_16x16x32_bf16 v[46:49], v[134:137], v[184:187], v[46:49]
	v_mfma_f32_16x16x32_bf16 v[42:45], v[142:145], v[184:187], v[42:45]
	v_mfma_f32_16x16x32_bf16 v[30:33], v[134:137], v[192:195], v[30:33]
	v_mfma_f32_16x16x32_bf16 v[26:29], v[142:145], v[192:195], v[26:29]
	v_mfma_f32_16x16x32_bf16 v[14:17], v[134:137], v[204:207], v[14:17]
	v_mfma_f32_16x16x32_bf16 v[10:13], v[142:145], v[204:207], v[10:13]
	s_setprio 0
	s_setprio 1
	v_mfma_f32_16x16x32_bf16 v[54:57], v[146:149], v[172:175], v[54:57]
	v_mfma_f32_16x16x32_bf16 v[50:53], v[154:157], v[172:175], v[50:53]
	v_mfma_f32_16x16x32_bf16 v[38:41], v[146:149], v[180:183], v[38:41]
	v_mfma_f32_16x16x32_bf16 v[34:37], v[154:157], v[180:183], v[34:37]
	v_mfma_f32_16x16x32_bf16 v[22:25], v[146:149], v[188:191], v[22:25]
	v_mfma_f32_16x16x32_bf16 v[18:21], v[154:157], v[188:191], v[18:21]
	v_mfma_f32_16x16x32_bf16 v[6:9], v[146:149], v[196:199], v[6:9]
	v_mfma_f32_16x16x32_bf16 v[2:5], v[154:157], v[196:199], v[2:5]
	v_mfma_f32_16x16x32_bf16 v[54:57], v[150:153], v[176:179], v[54:57]
	v_mfma_f32_16x16x32_bf16 v[50:53], v[168:171], v[176:179], v[50:53]
	v_mfma_f32_16x16x32_bf16 v[38:41], v[150:153], v[184:187], v[38:41]
	v_mfma_f32_16x16x32_bf16 v[34:37], v[168:171], v[184:187], v[34:37]
	s_setprio 0
	v_mfma_f32_16x16x32_bf16 v[22:25], v[150:153], v[192:195], v[22:25]
	v_mfma_f32_16x16x32_bf16 v[18:21], v[168:171], v[192:195], v[18:21]
	v_mfma_f32_16x16x32_bf16 v[6:9], v[150:153], v[204:207], v[6:9]
	v_mfma_f32_16x16x32_bf16 v[2:5], v[168:171], v[204:207], v[2:5]
	s_barrier
	s_add_i32 s7, s7, 2
	s_add_u32 s26, s26, 0x100
	s_addc_u32 s27, s27, 0
	s_add_u32 s50, s50, 0x100
	s_addc_u32 s6, s6, 0
	s_cmp_gt_u32 s7, 13
	s_cbranch_scc0 .LBB0_1568
; __device__ __forceinline__ float sum_xor16(float v) { auto r = __builtin_amdgcn_permlane16_swap(__float_as_uint(v), __float_as_uint(v), false, false); return __uint_as_float(r[0]) + __uint_as_float(r[1]); }
; __device__ __forceinline__ float sum_xor32(float v) { auto r = __builtin_amdgcn_permlane32_swap(__float_as_uint(v), __float_as_uint(v), false, false); return __uint_as_float(r[0]) + __uint_as_float(r[1]); }
; __device__ __forceinline__ float bf_lo(unsigned w) { return __uint_as_float(w << 16); }
;     __device__ __forceinline__ void operator()(const f32x4 (&acc)[2][2][4][2], const Unit& u, int wr, int wc, int fr, int fq) const {
;         const int row0 = u.pm * BM + wr * 64 + fr, col0 = u.pn * BM + wc * 32 + 8 * fq;
; #pragma unroll
;         for (int ai = 0; ai < 2; ++ai) {
;             u32x4 old[4][2];
; #pragma unroll
;             for (int m = 0; m < 4; ++m)
; #pragma unroll
;                 for (int bj = 0; bj < 2; ++bj) old[m][bj] = *(const u32x4*)(xb + (size_t)(row0 + ai * HALF + m * 16) * 2048 + col0 + bj * HALF);
; #pragma unroll
;             for (int m = 0; m < 4; ++m) { const size_t row = (size_t)(row0 + ai * HALF + m * 16); bf16_t* rowp = xb + row * 2048 + col0; float ss = 0.f;
; #pragma unroll
;                 for (int bj = 0; bj < 2; ++bj) { const u32x4 oo = old[m][bj]; const f32x4 a0 = acc[ai][bj][m][0], a1 = acc[ai][bj][m][1];
;                     const float x0 = a0[0] + bf_lo(oo.x), x1 = a0[1] + bf_hi(oo.x), x2 = a0[2] + bf_lo(oo.y), x3 = a0[3] + bf_hi(oo.y), x4 = a1[0] + bf_lo(oo.z), x5 = a1[1] + bf_hi(oo.z), x6 = a1[2] + bf_lo(oo.w), x7 = a1[3] + bf_hi(oo.w);
;                     ss += (x0 * x0 + x1 * x1) + (x2 * x2 + x3 * x3) + (x4 * x4 + x5 * x5) + (x6 * x6 + x7 * x7);
;                     u32x4 w; w.x = cvt_pk_bf16(x0, x1); w.y = cvt_pk_bf16(x2, x3); w.z = cvt_pk_bf16(x4, x5); w.w = cvt_pk_bf16(x6, x7);
;                     *(u32x4*)(rowp + bj * HALF) = w;
;                     if (h8) { u32x2 q; q.x = pk4_fp8_(x0 * F8_SA_, x1 * F8_SA_, x2 * F8_SA_, x3 * F8_SA_); q.y = pk4_fp8_(x4 * F8_SA_, x5 * F8_SA_, x6 * F8_SA_, x7 * F8_SA_);
;                         *(u32x2*)(h8 + row * 2048 + col0 + bj * HALF) = q; } }
;                 ss = sum_xor32(sum_xor16(ss));
;                 if (fq == 0) SS[row * 32 + u.pn * 4 + wc] = ss; }
;             asm volatile("" ::: "memory"); }
	v_lshl_or_b32 v168, s85, 8, v202
	v_lshl_add_u32 v172, s86, 8, v200
	v_ashrrev_i32_e32 v169, 31, v168
	v_lshlrev_b64 v[182:183], 1, v[168:169]
	v_ashrrev_i32_e32 v173, 31, v172
	v_lshl_add_u64 v[170:171], s[12:13], 0, v[182:183]
	v_lshlrev_b64 v[184:185], 12, v[172:173]
	v_lshl_add_u64 v[130:131], v[170:171], 0, v[184:185]
	global_load_dwordx4 v[178:181], v[130:131], off
	global_load_dwordx4 v[154:157], v[130:131], off offset:256
	v_or_b32_e32 v192, 16, v172
	v_ashrrev_i32_e32 v193, 31, v192
	v_or_b32_e32 v176, 32, v172
	v_lshlrev_b64 v[196:197], 12, v[192:193]
	v_ashrrev_i32_e32 v177, 31, v176
	v_or_b32_e32 v174, 48, v172
	v_lshl_add_u64 v[130:131], v[170:171], 0, v[196:197]
	v_lshlrev_b64 v[194:195], 12, v[176:177]
	v_ashrrev_i32_e32 v175, 31, v174
	global_load_dwordx4 v[150:153], v[130:131], off
	global_load_dwordx4 v[146:149], v[130:131], off offset:256
	v_lshl_add_u64 v[130:131], v[170:171], 0, v[194:195]
	v_lshlrev_b64 v[190:191], 12, v[174:175]
	global_load_dwordx4 v[142:145], v[130:131], off
	global_load_dwordx4 v[138:141], v[130:131], off offset:256
	v_lshl_add_u64 v[130:131], v[170:171], 0, v[190:191]
	global_load_dwordx4 v[134:137], v[130:131], off
	s_nop 0
	global_load_dwordx4 v[130:133], v[130:131], off offset:256
	v_lshl_add_u64 v[184:185], s[12:13], 0, v[184:185]
	v_lshl_add_u64 v[198:199], v[184:185], 0, v[182:183]
	s_waitcnt vmcnt(0)
	v_lshlrev_b32_e32 v182, 16, v178
	v_and_b32_e32 v178, 0xffff0000, v178
	v_add_f32_e32 v127, v127, v178
	v_lshlrev_b32_e32 v178, 16, v179
	v_add_f32_e32 v128, v128, v178
	v_and_b32_e32 v178, 0xffff0000, v179
	v_add_f32_e32 v129, v129, v178
	v_lshlrev_b32_e32 v178, 16, v180
	v_add_f32_e32 v178, v122, v178
	v_and_b32_e32 v122, 0xffff0000, v180
	v_add_f32_e32 v179, v123, v122
	v_lshlrev_b32_e32 v122, 16, v181
	v_add_f32_e32 v180, v124, v122
	v_and_b32_e32 v122, 0xffff0000, v181
	v_add_f32_e32 v126, v126, v182
	v_add_f32_e32 v125, v125, v122
	v_mul_f32_e32 v122, v127, v127
	v_mul_f32_e32 v123, v129, v129
	v_fmac_f32_e32 v122, v126, v126
	v_fmac_f32_e32 v123, v128, v128
	v_add_f32_e32 v122, v122, v123
	v_mul_f32_e32 v123, v179, v179
	v_fmac_f32_e32 v123, v178, v178
	v_add_f32_e32 v122, v123, v122
	v_mul_f32_e32 v123, v125, v125
	v_fmac_f32_e32 v123, v180, v180
	v_add_f32_e32 v181, v123, v122
	v_cvt_pk_bf16_f32 v122, v126, v127
	v_cvt_pk_bf16_f32 v123, v128, v129
	v_cvt_pk_bf16_f32 v124, v178, v179
	v_cvt_pk_bf16_f32 v125, v180, v125
	global_store_dwordx4 v[198:199], v[122:125], off
	s_nop 1
	v_lshlrev_b32_e32 v122, 16, v154
	v_add_f32_e32 v118, v118, v122
	v_and_b32_e32 v122, 0xffff0000, v154
	v_add_f32_e32 v119, v119, v122
	v_lshlrev_b32_e32 v122, 16, v155
	v_add_f32_e32 v120, v120, v122
	v_and_b32_e32 v122, 0xffff0000, v155
	v_add_f32_e32 v121, v121, v122
	v_lshlrev_b32_e32 v122, 16, v156
	v_add_f32_e32 v122, v114, v122
	v_and_b32_e32 v114, 0xffff0000, v156
	v_add_f32_e32 v123, v115, v114
	v_lshlrev_b32_e32 v114, 16, v157
	v_add_f32_e32 v124, v116, v114
	v_and_b32_e32 v114, 0xffff0000, v157
	v_add_f32_e32 v117, v117, v114
	v_mul_f32_e32 v114, v119, v119
	v_mul_f32_e32 v115, v121, v121
	v_fmac_f32_e32 v114, v118, v118
	v_fmac_f32_e32 v115, v120, v120
	v_add_f32_e32 v114, v114, v115
	v_mul_f32_e32 v115, v123, v123
	v_fmac_f32_e32 v115, v122, v122
	v_add_f32_e32 v114, v115, v114
	v_mul_f32_e32 v115, v117, v117
	v_fmac_f32_e32 v115, v124, v124
	v_add_f32_e32 v114, v115, v114
	v_add_f32_e32 v125, v181, v114
	v_cvt_pk_bf16_f32 v114, v118, v119
	v_cvt_pk_bf16_f32 v115, v120, v121
	v_cvt_pk_bf16_f32 v116, v122, v123
	v_cvt_pk_bf16_f32 v117, v124, v117
	global_store_dwordx4 v[198:199], v[114:117], off offset:256
	s_nop 1
	v_mov_b32_e32 v114, v125
	s_nop 1
	v_permlane16_swap_b32_e32 v125, v114
	v_add_f32_e32 v114, v125, v114
	v_mov_b32_e32 v115, v114
	s_nop 1
	v_permlane32_swap_b32_e32 v114, v115
	s_and_saveexec_b64 s[26:27], s[8:9]
	s_cbranch_execz .LBB0_1571
	v_add_f32_e32 v116, v114, v115
	s_lshl_b32 s6, s85, 2
	v_lshlrev_b64 v[114:115], 7, v[172:173]
	s_ashr_i32 s7, s6, 31
	v_lshl_add_u64 v[114:115], s[14:15], 0, v[114:115]
	v_lshl_add_u64 v[114:115], s[6:7], 2, v[114:115]
	s_lshl_b32 s94, s69, 2
	v_lshl_add_u64 v[114:115], v[114:115], 0, s[94:95]
	global_store_dword v[114:115], v116, off

; #define PG8_STAGE(bufoff, gbase, voff) do { _Pragma("unroll") for (int _i = 0; _i < 2; ++_i) \
;         __builtin_amdgcn_global_load_lds((const unsigned*)((const char*)(gbase) + (voff)[_i]), (PG8_LAS unsigned*)(lds + (bufoff) + ldsw + _i * 8192), 16, 0, 0); } while (0)
; #define PG8_WAIT_V(n) asm volatile("s_waitcnt vmcnt(" #n ")" ::: "memory")
; #define PG8_WAIT_L(n) asm volatile("s_waitcnt lgkmcnt(" #n ")" ::: "memory")
; #define PG8_BAR __builtin_amdgcn_s_barrier()
; #define PG8_SCHED __builtin_amdgcn_sched_barrier(0)
; template <class Epi, class Sched, bool ALIGN_EPI, bool F8 = false>
; __device__ __forceinline__ void gemm_phase(PG8_LAS unsigned char* lds, const Gemm g, const Sched& S, const Epi& E, int tid) {
;     ...
;             PG8_LDB(B0, 0, 0); PG8_LDB(B1, 0, 1); PG8_SCHED; PG8_LDA(At, 0, 0); PG8_STAGE(PG8_SA(1, 1), a1 + hstepA, voffA);
;             PG8_WAIT_V(8); PG8_WAIT_L(0); PG8_BAR; PG8_MMA(0, 0, At, B0); PG8_MMA(0, 1, At, B1); PG8_BAR; PG8_SCHED;
;             PG8_LDA(At, 0, 1); PG8_STAGE(PG8_SB(0, 0), b2, voffB); PG8_STAGE(PG8_SB(0, 1), b2 + hstepB, voffB); PG8_STAGE(PG8_SA(0, 0), a2, voffA);
;             PG8_WAIT_V(8); PG8_WAIT_L(0); PG8_BAR; PG8_MMA(1, 0, At, B0); PG8_MMA(1, 1, At, B1); PG8_BAR; PG8_SCHED;
.LBB0_1619:
	s_add_u32 s28, s12, 0xfff80080
	s_addc_u32 s29, s13, -1
	s_add_i32 s88, 0, 0x10000
	s_cmp_eq_u32 s7, 28
	s_cselect_b32 s31, s23, s29
	s_cselect_b32 s30, s87, s28
	s_cselect_b32 s29, s25, s6
	s_cselect_b32 s28, s24, s50
	s_add_i32 s94, 0, 0x14000
	v_add_u32_e32 v154, s88, v169
	v_add_u32_e32 v158, s94, v169
	ds_read_b128 v[130:133], v154
	ds_read_b128 v[134:137], v154 offset:1024
	ds_read_b128 v[138:141], v154 offset:2048
	ds_read_b128 v[154:157], v154 offset:3072
	ds_read_b128 v[160:163], v158
	ds_read_b128 v[164:167], v158 offset:1024
	ds_read_b128 v[174:177], v158 offset:2048
	ds_read_b128 v[178:181], v158 offset:3072
	v_lshl_add_u64 v[214:215], s[12:13], 0, v[150:151]
	s_add_i32 m0, s39, 0xc000
	ds_read_b128 v[182:185], v172
	ds_read_b128 v[186:189], v172 offset:1024
	ds_read_b128 v[190:193], v172 offset:2048
	ds_read_b128 v[194:197], v172 offset:3072
	ds_read_b128 v[198:201], v172 offset:4096
	ds_read_b128 v[202:205], v172 offset:5120
	ds_read_b128 v[206:209], v172 offset:6144
	ds_read_b128 v[210:213], v172 offset:7168
	global_load_lds_dwordx4 v[214:215], off
	v_lshl_add_u64 v[214:215], s[12:13], 0, v[152:153]
	s_add_i32 m0, s39, 0xe000
	s_nop 0
	global_load_lds_dwordx4 v[214:215], off
	s_waitcnt vmcnt(8)
	s_waitcnt lgkmcnt(0)
	s_barrier
	s_setprio 1
	s_waitcnt lgkmcnt(0)
	v_mfma_f32_16x16x32_bf16 v[126:129], v[130:133], v[182:185], v[126:129]
	v_mfma_f32_16x16x32_bf16 v[122:125], v[138:141], v[182:185], v[122:125]
	v_mfma_f32_16x16x32_bf16 v[118:121], v[130:133], v[190:193], v[118:121]
	v_mfma_f32_16x16x32_bf16 v[114:117], v[138:141], v[190:193], v[114:117]
	v_mfma_f32_16x16x32_bf16 v[94:97], v[130:133], v[198:201], v[94:97]
	v_mfma_f32_16x16x32_bf16 v[90:93], v[138:141], v[198:201], v[90:93]
	v_mfma_f32_16x16x32_bf16 v[86:89], v[130:133], v[206:209], v[86:89]
	v_mfma_f32_16x16x32_bf16 v[82:85], v[138:141], v[206:209], v[82:85]
	v_mfma_f32_16x16x32_bf16 v[126:129], v[134:137], v[186:189], v[126:129]
	v_mfma_f32_16x16x32_bf16 v[122:125], v[154:157], v[186:189], v[122:125]
	v_mfma_f32_16x16x32_bf16 v[118:121], v[134:137], v[194:197], v[118:121]
	v_mfma_f32_16x16x32_bf16 v[114:117], v[154:157], v[194:197], v[114:117]
	v_mfma_f32_16x16x32_bf16 v[94:97], v[134:137], v[202:205], v[94:97]
	v_mfma_f32_16x16x32_bf16 v[90:93], v[154:157], v[202:205], v[90:93]
	v_mfma_f32_16x16x32_bf16 v[86:89], v[134:137], v[210:213], v[86:89]
	v_mfma_f32_16x16x32_bf16 v[82:85], v[154:157], v[210:213], v[82:85]
	s_setprio 0
	s_setprio 1
	v_mfma_f32_16x16x32_bf16 v[110:113], v[160:163], v[182:185], v[110:113]
	v_mfma_f32_16x16x32_bf16 v[106:109], v[174:177], v[182:185], v[106:109]
	v_mfma_f32_16x16x32_bf16 v[102:105], v[160:163], v[190:193], v[102:105]
	v_mfma_f32_16x16x32_bf16 v[98:101], v[174:177], v[190:193], v[98:101]
	v_mfma_f32_16x16x32_bf16 v[78:81], v[160:163], v[198:201], v[78:81]
	v_mfma_f32_16x16x32_bf16 v[74:77], v[174:177], v[198:201], v[74:77]
	v_mfma_f32_16x16x32_bf16 v[70:73], v[160:163], v[206:209], v[70:73]
	v_mfma_f32_16x16x32_bf16 v[66:69], v[174:177], v[206:209], v[66:69]
	v_mfma_f32_16x16x32_bf16 v[110:113], v[164:167], v[186:189], v[110:113]
	v_mfma_f32_16x16x32_bf16 v[106:109], v[178:181], v[186:189], v[106:109]
	v_mfma_f32_16x16x32_bf16 v[102:105], v[164:167], v[194:197], v[102:105]
	v_mfma_f32_16x16x32_bf16 v[98:101], v[178:181], v[194:197], v[98:101]
	s_setprio 0
	v_mfma_f32_16x16x32_bf16 v[78:81], v[164:167], v[202:205], v[78:81]
	v_mfma_f32_16x16x32_bf16 v[74:77], v[178:181], v[202:205], v[74:77]
	v_mfma_f32_16x16x32_bf16 v[70:73], v[164:167], v[210:213], v[70:73]
	v_mfma_f32_16x16x32_bf16 v[66:69], v[178:181], v[210:213], v[66:69]
	s_barrier
	s_add_i32 s88, s88, s38
	v_lshl_add_u64 v[214:215], s[28:29], 0, v[0:1]
	s_mov_b32 m0, s88
	ds_read_b128 v[182:185], v172 offset:16384
	ds_read_b128 v[186:189], v172 offset:17408
	ds_read_b128 v[190:193], v172 offset:18432
	ds_read_b128 v[194:197], v172 offset:19456
	ds_read_b128 v[198:201], v172 offset:20480
	ds_read_b128 v[202:205], v172 offset:21504
	ds_read_b128 v[206:209], v172 offset:22528
	ds_read_b128 v[210:213], v172 offset:23552
	global_load_lds_dwordx4 v[214:215], off
	s_add_i32 m0, s88, 0x2000
	s_add_u32 s88, s28, 0x84000
	v_lshl_add_u64 v[216:217], s[28:29], 0, v[142:143]
	s_addc_u32 s89, s29, 0
	s_add_i32 s94, s94, s38
	global_load_lds_dwordx4 v[216:217], off
	v_lshl_add_u64 v[218:219], s[88:89], 0, v[0:1]
	s_mov_b32 m0, s94
	v_lshl_add_u64 v[220:221], s[30:31], 0, v[144:145]
	global_load_lds_dwordx4 v[218:219], off
	v_lshl_add_u64 v[218:219], s[88:89], 0, v[142:143]
	s_add_i32 m0, s94, 0x2000
	s_nop 0
	global_load_lds_dwordx4 v[218:219], off
	v_lshl_add_u64 v[218:219], s[30:31], 0, v[146:147]
	s_mov_b32 m0, s39
	s_nop 0
	global_load_lds_dwordx4 v[218:219], off
	s_mov_b32 m0, s44
	s_nop 0
	global_load_lds_dwordx4 v[220:221], off
	s_waitcnt vmcnt(8)
	s_waitcnt lgkmcnt(0)
	s_barrier
; #define PG8_STAGE(bufoff, gbase, voff) do { _Pragma("unroll") for (int _i = 0; _i < 2; ++_i) \
;         __builtin_amdgcn_global_load_lds((const unsigned*)((const char*)(gbase) + (voff)[_i]), (PG8_LAS unsigned*)(lds + (bufoff) + ldsw + _i * 8192), 16, 0, 0); } while (0)
; #define PG8_WAIT_V(n) asm volatile("s_waitcnt vmcnt(" #n ")" ::: "memory")
; #define PG8_WAIT_L(n) asm volatile("s_waitcnt lgkmcnt(" #n ")" ::: "memory")
; #define PG8_BAR __builtin_amdgcn_s_barrier()
; #define PG8_SCHED __builtin_amdgcn_sched_barrier(0)
; template <class Epi, class Sched, bool ALIGN_EPI, bool F8 = false>
; __device__ __forceinline__ void gemm_phase(PG8_LAS unsigned char* lds, const Gemm g, const Sched& S, const Epi& E, int tid) {
;     ...
;             PG8_WAIT_V(8); PG8_WAIT_L(0); PG8_BAR; PG8_MMA(1, 0, At, B0); PG8_MMA(1, 1, At, B1); PG8_BAR; PG8_SCHED;
;             PG8_LDB(B0, 1, 0); PG8_LDB(B1, 1, 1); PG8_SCHED; PG8_LDA(At, 1, 0); PG8_STAGE(PG8_SA(0, 1), a2 + hstepA, voffA);
;             PG8_WAIT_V(8); PG8_WAIT_L(0); PG8_BAR; PG8_MMA(0, 0, At, B0); PG8_MMA(0, 1, At, B1); PG8_BAR; PG8_SCHED;
;             PG8_LDA(At, 1, 1); PG8_STAGE(PG8_SB(1, 0), b3, voffB); PG8_STAGE(PG8_SB(1, 1), b3 + hstepB, voffB); PG8_STAGE(PG8_SA(1, 0), a3, voffA);
	s_setprio 1
	s_waitcnt lgkmcnt(0)
	v_mfma_f32_16x16x32_bf16 v[62:65], v[130:133], v[182:185], v[62:65]
	v_mfma_f32_16x16x32_bf16 v[58:61], v[138:141], v[182:185], v[58:61]
	v_mfma_f32_16x16x32_bf16 v[54:57], v[130:133], v[190:193], v[54:57]
	v_mfma_f32_16x16x32_bf16 v[50:53], v[138:141], v[190:193], v[50:53]
	v_mfma_f32_16x16x32_bf16 v[30:33], v[130:133], v[198:201], v[30:33]
	v_mfma_f32_16x16x32_bf16 v[26:29], v[138:141], v[198:201], v[26:29]
	v_mfma_f32_16x16x32_bf16 v[22:25], v[130:133], v[206:209], v[22:25]
	v_mfma_f32_16x16x32_bf16 v[18:21], v[138:141], v[206:209], v[18:21]
	v_mfma_f32_16x16x32_bf16 v[62:65], v[134:137], v[186:189], v[62:65]
	v_mfma_f32_16x16x32_bf16 v[58:61], v[154:157], v[186:189], v[58:61]
	v_mfma_f32_16x16x32_bf16 v[54:57], v[134:137], v[194:197], v[54:57]
	v_mfma_f32_16x16x32_bf16 v[50:53], v[154:157], v[194:197], v[50:53]
	v_mfma_f32_16x16x32_bf16 v[30:33], v[134:137], v[202:205], v[30:33]
	v_mfma_f32_16x16x32_bf16 v[26:29], v[154:157], v[202:205], v[26:29]
	v_mfma_f32_16x16x32_bf16 v[22:25], v[134:137], v[210:213], v[22:25]
	v_mfma_f32_16x16x32_bf16 v[18:21], v[154:157], v[210:213], v[18:21]
	s_setprio 0
	s_setprio 1
	v_mfma_f32_16x16x32_bf16 v[46:49], v[160:163], v[182:185], v[46:49]
	v_mfma_f32_16x16x32_bf16 v[42:45], v[174:177], v[182:185], v[42:45]
	v_mfma_f32_16x16x32_bf16 v[38:41], v[160:163], v[190:193], v[38:41]
	v_mfma_f32_16x16x32_bf16 v[34:37], v[174:177], v[190:193], v[34:37]
	v_mfma_f32_16x16x32_bf16 v[14:17], v[160:163], v[198:201], v[14:17]
	v_mfma_f32_16x16x32_bf16 v[10:13], v[174:177], v[198:201], v[10:13]
	v_mfma_f32_16x16x32_bf16 v[6:9], v[160:163], v[206:209], v[6:9]
	v_mfma_f32_16x16x32_bf16 v[2:5], v[174:177], v[206:209], v[2:5]
	v_mfma_f32_16x16x32_bf16 v[46:49], v[164:167], v[186:189], v[46:49]
	v_mfma_f32_16x16x32_bf16 v[42:45], v[178:181], v[186:189], v[42:45]
	v_mfma_f32_16x16x32_bf16 v[38:41], v[164:167], v[194:197], v[38:41]
	v_mfma_f32_16x16x32_bf16 v[34:37], v[178:181], v[194:197], v[34:37]
	s_setprio 0
	v_mfma_f32_16x16x32_bf16 v[14:17], v[164:167], v[202:205], v[14:17]
	v_mfma_f32_16x16x32_bf16 v[10:13], v[178:181], v[202:205], v[10:13]
	v_mfma_f32_16x16x32_bf16 v[6:9], v[164:167], v[210:213], v[6:9]
	v_mfma_f32_16x16x32_bf16 v[2:5], v[178:181], v[210:213], v[2:5]
	s_barrier
	s_add_i32 s88, 0, 0x18000
	s_add_i32 s89, 0, 0x1c000
	v_add_u32_e32 v154, s88, v169
	v_add_u32_e32 v158, s89, v169
	ds_read_b128 v[130:133], v154
	ds_read_b128 v[134:137], v154 offset:1024
	ds_read_b128 v[138:141], v154 offset:2048
	ds_read_b128 v[154:157], v154 offset:3072
	ds_read_b128 v[160:163], v158
	ds_read_b128 v[164:167], v158 offset:1024
	ds_read_b128 v[174:177], v158 offset:2048
	ds_read_b128 v[178:181], v158 offset:3072
	s_add_u32 s30, s30, 0x80000
	s_addc_u32 s31, s31, 0
	s_mov_b32 m0, s45
	v_lshl_add_u64 v[226:227], s[30:31], 0, v[146:147]
	ds_read_b128 v[182:185], v172 offset:32768
	ds_read_b128 v[186:189], v172 offset:33792
	ds_read_b128 v[190:193], v172 offset:34816
	ds_read_b128 v[194:197], v172 offset:35840
	ds_read_b128 v[198:201], v172 offset:36864
	ds_read_b128 v[202:205], v172 offset:37888
	ds_read_b128 v[206:209], v172 offset:38912
	ds_read_b128 v[210:213], v172 offset:39936
	global_load_lds_dwordx4 v[226:227], off
	v_lshl_add_u64 v[226:227], s[30:31], 0, v[144:145]
	s_mov_b32 m0, s51
	s_nop 0
	global_load_lds_dwordx4 v[226:227], off
	s_waitcnt vmcnt(8)
	s_waitcnt lgkmcnt(0)
	s_barrier
	s_setprio 1
	s_waitcnt lgkmcnt(0)
	v_mfma_f32_16x16x32_bf16 v[126:129], v[130:133], v[182:185], v[126:129]
	v_mfma_f32_16x16x32_bf16 v[122:125], v[138:141], v[182:185], v[122:125]
	v_mfma_f32_16x16x32_bf16 v[118:121], v[130:133], v[190:193], v[118:121]
	v_mfma_f32_16x16x32_bf16 v[114:117], v[138:141], v[190:193], v[114:117]
	v_mfma_f32_16x16x32_bf16 v[94:97], v[130:133], v[198:201], v[94:97]
	v_mfma_f32_16x16x32_bf16 v[90:93], v[138:141], v[198:201], v[90:93]
	v_mfma_f32_16x16x32_bf16 v[86:89], v[130:133], v[206:209], v[86:89]
	v_mfma_f32_16x16x32_bf16 v[82:85], v[138:141], v[206:209], v[82:85]
	v_mfma_f32_16x16x32_bf16 v[126:129], v[134:137], v[186:189], v[126:129]
	v_mfma_f32_16x16x32_bf16 v[122:125], v[154:157], v[186:189], v[122:125]
	v_mfma_f32_16x16x32_bf16 v[118:121], v[134:137], v[194:197], v[118:121]
	v_mfma_f32_16x16x32_bf16 v[114:117], v[154:157], v[194:197], v[114:117]
	v_mfma_f32_16x16x32_bf16 v[94:97], v[134:137], v[202:205], v[94:97]
	v_mfma_f32_16x16x32_bf16 v[90:93], v[154:157], v[202:205], v[90:93]
	v_mfma_f32_16x16x32_bf16 v[86:89], v[134:137], v[210:213], v[86:89]
	v_mfma_f32_16x16x32_bf16 v[82:85], v[154:157], v[210:213], v[82:85]
	s_setprio 0
	s_setprio 1
	v_mfma_f32_16x16x32_bf16 v[110:113], v[160:163], v[182:185], v[110:113]
	v_mfma_f32_16x16x32_bf16 v[106:109], v[174:177], v[182:185], v[106:109]
	v_mfma_f32_16x16x32_bf16 v[102:105], v[160:163], v[190:193], v[102:105]
	v_mfma_f32_16x16x32_bf16 v[98:101], v[174:177], v[190:193], v[98:101]
	v_mfma_f32_16x16x32_bf16 v[78:81], v[160:163], v[198:201], v[78:81]
	v_mfma_f32_16x16x32_bf16 v[74:77], v[174:177], v[198:201], v[74:77]
	v_mfma_f32_16x16x32_bf16 v[70:73], v[160:163], v[206:209], v[70:73]
	v_mfma_f32_16x16x32_bf16 v[66:69], v[174:177], v[206:209], v[66:69]
	v_mfma_f32_16x16x32_bf16 v[110:113], v[164:167], v[186:189], v[110:113]
	v_mfma_f32_16x16x32_bf16 v[106:109], v[178:181], v[186:189], v[106:109]
	v_mfma_f32_16x16x32_bf16 v[102:105], v[164:167], v[194:197], v[102:105]
	v_mfma_f32_16x16x32_bf16 v[98:101], v[178:181], v[194:197], v[98:101]
	s_setprio 0
	v_mfma_f32_16x16x32_bf16 v[78:81], v[164:167], v[202:205], v[78:81]
	v_mfma_f32_16x16x32_bf16 v[74:77], v[178:181], v[202:205], v[74:77]
	v_mfma_f32_16x16x32_bf16 v[70:73], v[164:167], v[210:213], v[70:73]
	v_mfma_f32_16x16x32_bf16 v[66:69], v[178:181], v[210:213], v[66:69]
	s_barrier
; #define PG8_STAGE(bufoff, gbase, voff) do { _Pragma("unroll") for (int _i = 0; _i < 2; ++_i) \
;         __builtin_amdgcn_global_load_lds((const unsigned*)((const char*)(gbase) + (voff)[_i]), (PG8_LAS unsigned*)(lds + (bufoff) + ldsw + _i * 8192), 16, 0, 0); } while (0)
; #define PG8_WAIT_V(n) asm volatile("s_waitcnt vmcnt(" #n ")" ::: "memory")
; #define PG8_WAIT_L(n) asm volatile("s_waitcnt lgkmcnt(" #n ")" ::: "memory")
; #define PG8_BAR __builtin_amdgcn_s_barrier()
; #define PG8_SCHED __builtin_amdgcn_sched_barrier(0)
; template <class Epi, class Sched, bool ALIGN_EPI, bool F8 = false>
; __device__ __forceinline__ void gemm_phase(PG8_LAS unsigned char* lds, const Gemm g, const Sched& S, const Epi& E, int tid) {
;     ...
;         for (int t = 0; t < nt; t += 2) {
;             const bool last = (t == nt - 2);
;             const char* a1 = cA + (size_t)(t + 1) * kstep;
;             const char* a2 = last ? nA : cA + (size_t)(t + 2) * kstep; const char* b2 = last ? nB : cB + (size_t)(t + 2) * kstep;
;             const char* a3 = a2 + kstep; const char* b3 = b2 + kstep;
;     ...
;             PG8_LDA(At, 1, 1); PG8_STAGE(PG8_SB(1, 0), b3, voffB); PG8_STAGE(PG8_SB(1, 1), b3 + hstepB, voffB); PG8_STAGE(PG8_SA(1, 0), a3, voffA);
;             PG8_WAIT_V(8); PG8_WAIT_L(0); PG8_BAR; PG8_MMA(1, 0, At, B0); PG8_MMA(1, 1, At, B1); PG8_BAR; PG8_SCHED;
	s_add_i32 s30, s88, s38
	v_lshl_add_u64 v[214:215], v[214:215], 0, s[60:61]
	s_mov_b32 m0, s30
	ds_read_b128 v[182:185], v172 offset:49152
	ds_read_b128 v[186:189], v172 offset:50176
	ds_read_b128 v[190:193], v172 offset:51200
	ds_read_b128 v[194:197], v172 offset:52224
	ds_read_b128 v[198:201], v172 offset:53248
	ds_read_b128 v[202:205], v172 offset:54272
	ds_read_b128 v[206:209], v172 offset:55296
	ds_read_b128 v[210:213], v172 offset:56320
	global_load_lds_dwordx4 v[214:215], off
	s_add_i32 m0, s30, 0x2000
	s_add_u32 s28, s28, 0x84080
	v_lshl_add_u64 v[214:215], v[216:217], 0, s[60:61]
	s_addc_u32 s29, s29, 0
	s_add_i32 s30, s89, s38
	global_load_lds_dwordx4 v[214:215], off
	v_lshl_add_u64 v[214:215], s[28:29], 0, v[0:1]
	s_mov_b32 m0, s30
	s_nop 0
	global_load_lds_dwordx4 v[214:215], off
	v_lshl_add_u64 v[214:215], s[28:29], 0, v[142:143]
	s_add_i32 m0, s30, 0x2000
	s_nop 0
	global_load_lds_dwordx4 v[214:215], off
	v_lshl_add_u64 v[214:215], v[218:219], 0, s[60:61]
	s_mov_b32 m0, s68
	s_nop 0
	global_load_lds_dwordx4 v[214:215], off
	v_lshl_add_u64 v[214:215], v[220:221], 0, s[60:61]
	s_mov_b32 m0, s69
	s_nop 0
	global_load_lds_dwordx4 v[214:215], off
	s_waitcnt vmcnt(8)
	s_waitcnt lgkmcnt(0)
	s_barrier
	s_setprio 1
	s_waitcnt lgkmcnt(0)
	v_mfma_f32_16x16x32_bf16 v[62:65], v[130:133], v[182:185], v[62:65]
	v_mfma_f32_16x16x32_bf16 v[58:61], v[138:141], v[182:185], v[58:61]
	v_mfma_f32_16x16x32_bf16 v[54:57], v[130:133], v[190:193], v[54:57]
	v_mfma_f32_16x16x32_bf16 v[50:53], v[138:141], v[190:193], v[50:53]
	v_mfma_f32_16x16x32_bf16 v[30:33], v[130:133], v[198:201], v[30:33]
	v_mfma_f32_16x16x32_bf16 v[26:29], v[138:141], v[198:201], v[26:29]
	v_mfma_f32_16x16x32_bf16 v[22:25], v[130:133], v[206:209], v[22:25]
	v_mfma_f32_16x16x32_bf16 v[18:21], v[138:141], v[206:209], v[18:21]
	v_mfma_f32_16x16x32_bf16 v[62:65], v[134:137], v[186:189], v[62:65]
	v_mfma_f32_16x16x32_bf16 v[58:61], v[154:157], v[186:189], v[58:61]
	v_mfma_f32_16x16x32_bf16 v[54:57], v[134:137], v[194:197], v[54:57]
	v_mfma_f32_16x16x32_bf16 v[50:53], v[154:157], v[194:197], v[50:53]
	v_mfma_f32_16x16x32_bf16 v[30:33], v[134:137], v[202:205], v[30:33]
	v_mfma_f32_16x16x32_bf16 v[26:29], v[154:157], v[202:205], v[26:29]
	v_mfma_f32_16x16x32_bf16 v[22:25], v[134:137], v[210:213], v[22:25]
	v_mfma_f32_16x16x32_bf16 v[18:21], v[154:157], v[210:213], v[18:21]
	s_setprio 0
	s_setprio 1
	v_mfma_f32_16x16x32_bf16 v[46:49], v[160:163], v[182:185], v[46:49]
	v_mfma_f32_16x16x32_bf16 v[42:45], v[174:177], v[182:185], v[42:45]
	v_mfma_f32_16x16x32_bf16 v[38:41], v[160:163], v[190:193], v[38:41]
	v_mfma_f32_16x16x32_bf16 v[34:37], v[174:177], v[190:193], v[34:37]
	v_mfma_f32_16x16x32_bf16 v[14:17], v[160:163], v[198:201], v[14:17]
	v_mfma_f32_16x16x32_bf16 v[10:13], v[174:177], v[198:201], v[10:13]
	v_mfma_f32_16x16x32_bf16 v[6:9], v[160:163], v[206:209], v[6:9]
	v_mfma_f32_16x16x32_bf16 v[2:5], v[174:177], v[206:209], v[2:5]
	v_mfma_f32_16x16x32_bf16 v[46:49], v[164:167], v[186:189], v[46:49]
	v_mfma_f32_16x16x32_bf16 v[42:45], v[178:181], v[186:189], v[42:45]
	v_mfma_f32_16x16x32_bf16 v[38:41], v[164:167], v[194:197], v[38:41]
	v_mfma_f32_16x16x32_bf16 v[34:37], v[178:181], v[194:197], v[34:37]
	s_setprio 0
	v_mfma_f32_16x16x32_bf16 v[14:17], v[164:167], v[202:205], v[14:17]
	v_mfma_f32_16x16x32_bf16 v[10:13], v[178:181], v[202:205], v[10:13]
	v_mfma_f32_16x16x32_bf16 v[6:9], v[164:167], v[210:213], v[6:9]
	v_mfma_f32_16x16x32_bf16 v[2:5], v[178:181], v[210:213], v[2:5]
	s_barrier
	s_add_i32 s7, s7, 2
	s_add_u32 s12, s12, 0x100
	s_addc_u32 s13, s13, 0
	s_add_u32 s50, s50, 0x100
	s_addc_u32 s6, s6, 0
	s_cmp_gt_u32 s7, 29
	s_cbranch_scc0 .LBB0_1619
	s_and_b64 vcc, exec, s[20:21]
	s_cbranch_vccz .LBB0_1622
	s_barrier

; #define PG8_STAGE(bufoff, gbase, voff) do { _Pragma("unroll") for (int _i = 0; _i < 2; ++_i) \
;         __builtin_amdgcn_global_load_lds((const unsigned*)((const char*)(gbase) + (voff)[_i]), (PG8_LAS unsigned*)(lds + (bufoff) + ldsw + _i * 8192), 16, 0, 0); } while (0)
; #define PG8_WAIT_V(n) asm volatile("s_waitcnt vmcnt(" #n ")" ::: "memory")
; #define PG8_WAIT_L(n) asm volatile("s_waitcnt lgkmcnt(" #n ")" ::: "memory")
; #define PG8_BAR __builtin_amdgcn_s_barrier()
; #define PG8_SCHED __builtin_amdgcn_sched_barrier(0)
; template <class Epi, class Sched, bool ALIGN_EPI, bool F8 = false>
; __device__ __forceinline__ void gemm_phase(PG8_LAS unsigned char* lds, const Gemm g, const Sched& S, const Epi& E, int tid) {
;     ...
;             PG8_LDB(B0, 0, 0); PG8_LDB(B1, 0, 1); PG8_SCHED; PG8_LDA(At, 0, 0); PG8_STAGE(PG8_SA(1, 1), a1 + hstepA, voffA);
;             PG8_WAIT_V(8); PG8_WAIT_L(0); PG8_BAR; PG8_MMA(0, 0, At, B0); PG8_MMA(0, 1, At, B1); PG8_BAR; PG8_SCHED;
;             PG8_LDA(At, 0, 1); PG8_STAGE(PG8_SB(0, 0), b2, voffB); PG8_STAGE(PG8_SB(0, 1), b2 + hstepB, voffB); PG8_STAGE(PG8_SA(0, 0), a2, voffA);
;             PG8_WAIT_V(8); PG8_WAIT_L(0); PG8_BAR; PG8_MMA(1, 0, At, B0); PG8_MMA(1, 1, At, B1); PG8_BAR; PG8_SCHED;
.LBB0_1639:
	s_add_u32 s22, s10, 0xfff80080
	s_addc_u32 s23, s11, -1
	s_add_i32 s82, 0, 0x10000
	s_cmp_eq_u32 s7, 28
	s_cselect_b32 s25, s15, s23
	s_cselect_b32 s24, s69, s22
	s_cselect_b32 s23, s19, s6
	s_cselect_b32 s22, s18, s50
	s_add_i32 s84, 0, 0x14000
	v_add_u32_e32 v160, s82, v147
	v_add_u32_e32 v176, s84, v147
	ds_read_b128 v[142:145], v160
	ds_read_b128 v[152:155], v160 offset:1024
	ds_read_b128 v[156:159], v160 offset:2048
	ds_read_b128 v[160:163], v160 offset:3072
	ds_read_b128 v[164:167], v176
	ds_read_b128 v[168:171], v176 offset:1024
	ds_read_b128 v[172:175], v176 offset:2048
	ds_read_b128 v[176:179], v176 offset:3072
	v_lshl_add_u64 v[212:213], s[10:11], 0, v[138:139]
	s_add_i32 m0, s27, 0xc000
	ds_read_b128 v[180:183], v151
	ds_read_b128 v[184:187], v151 offset:1024
	ds_read_b128 v[188:191], v151 offset:2048
	ds_read_b128 v[192:195], v151 offset:3072
	ds_read_b128 v[196:199], v151 offset:4096
	ds_read_b128 v[200:203], v151 offset:5120
	ds_read_b128 v[204:207], v151 offset:6144
	ds_read_b128 v[208:211], v151 offset:7168
	global_load_lds_dwordx4 v[212:213], off
	v_lshl_add_u64 v[212:213], s[10:11], 0, v[140:141]
	s_add_i32 m0, s27, 0xe000
	s_nop 0
	global_load_lds_dwordx4 v[212:213], off
	s_waitcnt vmcnt(8)
	s_waitcnt lgkmcnt(0)
	s_barrier
	s_setprio 1
	s_waitcnt lgkmcnt(0)
	v_mfma_f32_16x16x32_bf16 v[126:129], v[142:145], v[180:183], v[126:129]
	v_mfma_f32_16x16x32_bf16 v[122:125], v[156:159], v[180:183], v[122:125]
	v_mfma_f32_16x16x32_bf16 v[118:121], v[142:145], v[188:191], v[118:121]
	v_mfma_f32_16x16x32_bf16 v[114:117], v[156:159], v[188:191], v[114:117]
	v_mfma_f32_16x16x32_bf16 v[94:97], v[142:145], v[196:199], v[94:97]
	v_mfma_f32_16x16x32_bf16 v[90:93], v[156:159], v[196:199], v[90:93]
	v_mfma_f32_16x16x32_bf16 v[86:89], v[142:145], v[204:207], v[86:89]
	v_mfma_f32_16x16x32_bf16 v[82:85], v[156:159], v[204:207], v[82:85]
	v_mfma_f32_16x16x32_bf16 v[126:129], v[152:155], v[184:187], v[126:129]
	v_mfma_f32_16x16x32_bf16 v[122:125], v[160:163], v[184:187], v[122:125]
	v_mfma_f32_16x16x32_bf16 v[118:121], v[152:155], v[192:195], v[118:121]
	v_mfma_f32_16x16x32_bf16 v[114:117], v[160:163], v[192:195], v[114:117]
	v_mfma_f32_16x16x32_bf16 v[94:97], v[152:155], v[200:203], v[94:97]
	v_mfma_f32_16x16x32_bf16 v[90:93], v[160:163], v[200:203], v[90:93]
	v_mfma_f32_16x16x32_bf16 v[86:89], v[152:155], v[208:211], v[86:89]
	v_mfma_f32_16x16x32_bf16 v[82:85], v[160:163], v[208:211], v[82:85]
	s_setprio 0
	s_setprio 1
	v_mfma_f32_16x16x32_bf16 v[110:113], v[164:167], v[180:183], v[110:113]
	v_mfma_f32_16x16x32_bf16 v[106:109], v[172:175], v[180:183], v[106:109]
	v_mfma_f32_16x16x32_bf16 v[102:105], v[164:167], v[188:191], v[102:105]
	v_mfma_f32_16x16x32_bf16 v[98:101], v[172:175], v[188:191], v[98:101]
	v_mfma_f32_16x16x32_bf16 v[78:81], v[164:167], v[196:199], v[78:81]
	v_mfma_f32_16x16x32_bf16 v[74:77], v[172:175], v[196:199], v[74:77]
	v_mfma_f32_16x16x32_bf16 v[70:73], v[164:167], v[204:207], v[70:73]
	v_mfma_f32_16x16x32_bf16 v[66:69], v[172:175], v[204:207], v[66:69]
	v_mfma_f32_16x16x32_bf16 v[110:113], v[168:171], v[184:187], v[110:113]
	v_mfma_f32_16x16x32_bf16 v[106:109], v[176:179], v[184:187], v[106:109]
	v_mfma_f32_16x16x32_bf16 v[102:105], v[168:171], v[192:195], v[102:105]
	v_mfma_f32_16x16x32_bf16 v[98:101], v[176:179], v[192:195], v[98:101]
	s_setprio 0
	v_mfma_f32_16x16x32_bf16 v[78:81], v[168:171], v[200:203], v[78:81]
	v_mfma_f32_16x16x32_bf16 v[74:77], v[176:179], v[200:203], v[74:77]
	v_mfma_f32_16x16x32_bf16 v[70:73], v[168:171], v[208:211], v[70:73]
	v_mfma_f32_16x16x32_bf16 v[66:69], v[176:179], v[208:211], v[66:69]
	s_barrier
	s_add_i32 s82, s82, s26
	v_lshl_add_u64 v[212:213], s[22:23], 0, v[0:1]
	s_mov_b32 m0, s82
	ds_read_b128 v[180:183], v151 offset:16384
	ds_read_b128 v[184:187], v151 offset:17408
	ds_read_b128 v[188:191], v151 offset:18432
	ds_read_b128 v[192:195], v151 offset:19456
	ds_read_b128 v[196:199], v151 offset:20480
	ds_read_b128 v[200:203], v151 offset:21504
	ds_read_b128 v[204:207], v151 offset:22528
	ds_read_b128 v[208:211], v151 offset:23552
	global_load_lds_dwordx4 v[212:213], off
	s_add_i32 m0, s82, 0x2000
	s_add_u32 s82, s22, 0x84000
	v_lshl_add_u64 v[214:215], s[22:23], 0, v[130:131]
	s_addc_u32 s83, s23, 0
	s_add_i32 s84, s84, s26
	global_load_lds_dwordx4 v[214:215], off
	v_lshl_add_u64 v[216:217], s[82:83], 0, v[0:1]
	s_mov_b32 m0, s84
	v_lshl_add_u64 v[218:219], s[24:25], 0, v[132:133]
	global_load_lds_dwordx4 v[216:217], off
	v_lshl_add_u64 v[216:217], s[82:83], 0, v[130:131]
	s_add_i32 m0, s84, 0x2000
	s_nop 0
	global_load_lds_dwordx4 v[216:217], off
	v_lshl_add_u64 v[216:217], s[24:25], 0, v[134:135]
	s_mov_b32 m0, s27
	s_nop 0
	global_load_lds_dwordx4 v[216:217], off
	s_mov_b32 m0, s28
	s_nop 0
	global_load_lds_dwordx4 v[218:219], off
	s_waitcnt vmcnt(8)
	s_waitcnt lgkmcnt(0)
	s_barrier
; #define PG8_STAGE(bufoff, gbase, voff) do { _Pragma("unroll") for (int _i = 0; _i < 2; ++_i) \
;         __builtin_amdgcn_global_load_lds((const unsigned*)((const char*)(gbase) + (voff)[_i]), (PG8_LAS unsigned*)(lds + (bufoff) + ldsw + _i * 8192), 16, 0, 0); } while (0)
; #define PG8_WAIT_V(n) asm volatile("s_waitcnt vmcnt(" #n ")" ::: "memory")
; #define PG8_WAIT_L(n) asm volatile("s_waitcnt lgkmcnt(" #n ")" ::: "memory")
; #define PG8_BAR __builtin_amdgcn_s_barrier()
; #define PG8_SCHED __builtin_amdgcn_sched_barrier(0)
; template <class Epi, class Sched, bool ALIGN_EPI, bool F8 = false>
; __device__ __forceinline__ void gemm_phase(PG8_LAS unsigned char* lds, const Gemm g, const Sched& S, const Epi& E, int tid) {
;     ...
;             PG8_WAIT_V(8); PG8_WAIT_L(0); PG8_BAR; PG8_MMA(1, 0, At, B0); PG8_MMA(1, 1, At, B1); PG8_BAR; PG8_SCHED;
;             PG8_LDB(B0, 1, 0); PG8_LDB(B1, 1, 1); PG8_SCHED; PG8_LDA(At, 1, 0); PG8_STAGE(PG8_SA(0, 1), a2 + hstepA, voffA);
;             PG8_WAIT_V(8); PG8_WAIT_L(0); PG8_BAR; PG8_MMA(0, 0, At, B0); PG8_MMA(0, 1, At, B1); PG8_BAR; PG8_SCHED;
;             PG8_LDA(At, 1, 1); PG8_STAGE(PG8_SB(1, 0), b3, voffB); PG8_STAGE(PG8_SB(1, 1), b3 + hstepB, voffB); PG8_STAGE(PG8_SA(1, 0), a3, voffA);
	s_setprio 1
	s_waitcnt lgkmcnt(0)
	v_mfma_f32_16x16x32_bf16 v[62:65], v[142:145], v[180:183], v[62:65]
	v_mfma_f32_16x16x32_bf16 v[58:61], v[156:159], v[180:183], v[58:61]
	v_mfma_f32_16x16x32_bf16 v[54:57], v[142:145], v[188:191], v[54:57]
	v_mfma_f32_16x16x32_bf16 v[50:53], v[156:159], v[188:191], v[50:53]
	v_mfma_f32_16x16x32_bf16 v[30:33], v[142:145], v[196:199], v[30:33]
	v_mfma_f32_16x16x32_bf16 v[26:29], v[156:159], v[196:199], v[26:29]
	v_mfma_f32_16x16x32_bf16 v[22:25], v[142:145], v[204:207], v[22:25]
	v_mfma_f32_16x16x32_bf16 v[18:21], v[156:159], v[204:207], v[18:21]
	v_mfma_f32_16x16x32_bf16 v[62:65], v[152:155], v[184:187], v[62:65]
	v_mfma_f32_16x16x32_bf16 v[58:61], v[160:163], v[184:187], v[58:61]
	v_mfma_f32_16x16x32_bf16 v[54:57], v[152:155], v[192:195], v[54:57]
	v_mfma_f32_16x16x32_bf16 v[50:53], v[160:163], v[192:195], v[50:53]
	v_mfma_f32_16x16x32_bf16 v[30:33], v[152:155], v[200:203], v[30:33]
	v_mfma_f32_16x16x32_bf16 v[26:29], v[160:163], v[200:203], v[26:29]
	v_mfma_f32_16x16x32_bf16 v[22:25], v[152:155], v[208:211], v[22:25]
	v_mfma_f32_16x16x32_bf16 v[18:21], v[160:163], v[208:211], v[18:21]
	s_setprio 0
	s_setprio 1
	v_mfma_f32_16x16x32_bf16 v[46:49], v[164:167], v[180:183], v[46:49]
	v_mfma_f32_16x16x32_bf16 v[42:45], v[172:175], v[180:183], v[42:45]
	v_mfma_f32_16x16x32_bf16 v[38:41], v[164:167], v[188:191], v[38:41]
	v_mfma_f32_16x16x32_bf16 v[34:37], v[172:175], v[188:191], v[34:37]
	v_mfma_f32_16x16x32_bf16 v[14:17], v[164:167], v[196:199], v[14:17]
	v_mfma_f32_16x16x32_bf16 v[10:13], v[172:175], v[196:199], v[10:13]
	v_mfma_f32_16x16x32_bf16 v[6:9], v[164:167], v[204:207], v[6:9]
	v_mfma_f32_16x16x32_bf16 v[2:5], v[172:175], v[204:207], v[2:5]
	v_mfma_f32_16x16x32_bf16 v[46:49], v[168:171], v[184:187], v[46:49]
	v_mfma_f32_16x16x32_bf16 v[42:45], v[176:179], v[184:187], v[42:45]
	v_mfma_f32_16x16x32_bf16 v[38:41], v[168:171], v[192:195], v[38:41]
	v_mfma_f32_16x16x32_bf16 v[34:37], v[176:179], v[192:195], v[34:37]
	s_setprio 0
	v_mfma_f32_16x16x32_bf16 v[14:17], v[168:171], v[200:203], v[14:17]
	v_mfma_f32_16x16x32_bf16 v[10:13], v[176:179], v[200:203], v[10:13]
	v_mfma_f32_16x16x32_bf16 v[6:9], v[168:171], v[208:211], v[6:9]
	v_mfma_f32_16x16x32_bf16 v[2:5], v[176:179], v[208:211], v[2:5]
	s_barrier
	s_add_i32 s82, 0, 0x18000
	s_add_i32 s83, 0, 0x1c000
	v_add_u32_e32 v160, s82, v147
	v_add_u32_e32 v176, s83, v147
	ds_read_b128 v[142:145], v160
	ds_read_b128 v[152:155], v160 offset:1024
	ds_read_b128 v[156:159], v160 offset:2048
	ds_read_b128 v[160:163], v160 offset:3072
	ds_read_b128 v[164:167], v176
	ds_read_b128 v[168:171], v176 offset:1024
	ds_read_b128 v[172:175], v176 offset:2048
	ds_read_b128 v[176:179], v176 offset:3072
	s_add_u32 s24, s24, 0x80000
	s_addc_u32 s25, s25, 0
	s_mov_b32 m0, s29
	v_lshl_add_u64 v[220:221], s[24:25], 0, v[134:135]
	ds_read_b128 v[180:183], v151 offset:32768
	ds_read_b128 v[184:187], v151 offset:33792
	ds_read_b128 v[188:191], v151 offset:34816
	ds_read_b128 v[192:195], v151 offset:35840
	ds_read_b128 v[196:199], v151 offset:36864
	ds_read_b128 v[200:203], v151 offset:37888
	ds_read_b128 v[204:207], v151 offset:38912
	ds_read_b128 v[208:211], v151 offset:39936
	global_load_lds_dwordx4 v[220:221], off
	v_lshl_add_u64 v[220:221], s[24:25], 0, v[132:133]
	s_mov_b32 m0, s30
	s_nop 0
	global_load_lds_dwordx4 v[220:221], off
	s_waitcnt vmcnt(8)
	s_waitcnt lgkmcnt(0)
	s_barrier
	s_setprio 1
	s_waitcnt lgkmcnt(0)
	v_mfma_f32_16x16x32_bf16 v[126:129], v[142:145], v[180:183], v[126:129]
	v_mfma_f32_16x16x32_bf16 v[122:125], v[156:159], v[180:183], v[122:125]
	v_mfma_f32_16x16x32_bf16 v[118:121], v[142:145], v[188:191], v[118:121]
	v_mfma_f32_16x16x32_bf16 v[114:117], v[156:159], v[188:191], v[114:117]
	v_mfma_f32_16x16x32_bf16 v[94:97], v[142:145], v[196:199], v[94:97]
	v_mfma_f32_16x16x32_bf16 v[90:93], v[156:159], v[196:199], v[90:93]
	v_mfma_f32_16x16x32_bf16 v[86:89], v[142:145], v[204:207], v[86:89]
	v_mfma_f32_16x16x32_bf16 v[82:85], v[156:159], v[204:207], v[82:85]
	v_mfma_f32_16x16x32_bf16 v[126:129], v[152:155], v[184:187], v[126:129]
	v_mfma_f32_16x16x32_bf16 v[122:125], v[160:163], v[184:187], v[122:125]
	v_mfma_f32_16x16x32_bf16 v[118:121], v[152:155], v[192:195], v[118:121]
	v_mfma_f32_16x16x32_bf16 v[114:117], v[160:163], v[192:195], v[114:117]
	v_mfma_f32_16x16x32_bf16 v[94:97], v[152:155], v[200:203], v[94:97]
	v_mfma_f32_16x16x32_bf16 v[90:93], v[160:163], v[200:203], v[90:93]
	v_mfma_f32_16x16x32_bf16 v[86:89], v[152:155], v[208:211], v[86:89]
	v_mfma_f32_16x16x32_bf16 v[82:85], v[160:163], v[208:211], v[82:85]
	s_setprio 0
	s_setprio 1
	v_mfma_f32_16x16x32_bf16 v[110:113], v[164:167], v[180:183], v[110:113]
	v_mfma_f32_16x16x32_bf16 v[106:109], v[172:175], v[180:183], v[106:109]
	v_mfma_f32_16x16x32_bf16 v[102:105], v[164:167], v[188:191], v[102:105]
	v_mfma_f32_16x16x32_bf16 v[98:101], v[172:175], v[188:191], v[98:101]
	v_mfma_f32_16x16x32_bf16 v[78:81], v[164:167], v[196:199], v[78:81]
	v_mfma_f32_16x16x32_bf16 v[74:77], v[172:175], v[196:199], v[74:77]
	v_mfma_f32_16x16x32_bf16 v[70:73], v[164:167], v[204:207], v[70:73]
	v_mfma_f32_16x16x32_bf16 v[66:69], v[172:175], v[204:207], v[66:69]
	v_mfma_f32_16x16x32_bf16 v[110:113], v[168:171], v[184:187], v[110:113]
	v_mfma_f32_16x16x32_bf16 v[106:109], v[176:179], v[184:187], v[106:109]
	v_mfma_f32_16x16x32_bf16 v[102:105], v[168:171], v[192:195], v[102:105]
	v_mfma_f32_16x16x32_bf16 v[98:101], v[176:179], v[192:195], v[98:101]
	s_setprio 0
	v_mfma_f32_16x16x32_bf16 v[78:81], v[168:171], v[200:203], v[78:81]
	v_mfma_f32_16x16x32_bf16 v[74:77], v[176:179], v[200:203], v[74:77]
	v_mfma_f32_16x16x32_bf16 v[70:73], v[168:171], v[208:211], v[70:73]
	v_mfma_f32_16x16x32_bf16 v[66:69], v[176:179], v[208:211], v[66:69]
	s_barrier
; #define PG8_STAGE(bufoff, gbase, voff) do { _Pragma("unroll") for (int _i = 0; _i < 2; ++_i) \
;         __builtin_amdgcn_global_load_lds((const unsigned*)((const char*)(gbase) + (voff)[_i]), (PG8_LAS unsigned*)(lds + (bufoff) + ldsw + _i * 8192), 16, 0, 0); } while (0)
; #define PG8_WAIT_V(n) asm volatile("s_waitcnt vmcnt(" #n ")" ::: "memory")
; #define PG8_WAIT_L(n) asm volatile("s_waitcnt lgkmcnt(" #n ")" ::: "memory")
; #define PG8_BAR __builtin_amdgcn_s_barrier()
; #define PG8_SCHED __builtin_amdgcn_sched_barrier(0)
; template <class Epi, class Sched, bool ALIGN_EPI, bool F8 = false>
; __device__ __forceinline__ void gemm_phase(PG8_LAS unsigned char* lds, const Gemm g, const Sched& S, const Epi& E, int tid) {
;     ...
;         for (int t = 0; t < nt; t += 2) {
;             const bool last = (t == nt - 2);
;             const char* a1 = cA + (size_t)(t + 1) * kstep;
;             const char* a2 = last ? nA : cA + (size_t)(t + 2) * kstep; const char* b2 = last ? nB : cB + (size_t)(t + 2) * kstep;
;             const char* a3 = a2 + kstep; const char* b3 = b2 + kstep;
;     ...
;             PG8_LDA(At, 1, 1); PG8_STAGE(PG8_SB(1, 0), b3, voffB); PG8_STAGE(PG8_SB(1, 1), b3 + hstepB, voffB); PG8_STAGE(PG8_SA(1, 0), a3, voffA);
;             PG8_WAIT_V(8); PG8_WAIT_L(0); PG8_BAR; PG8_MMA(1, 0, At, B0); PG8_MMA(1, 1, At, B1); PG8_BAR; PG8_SCHED;
	s_add_i32 s24, s82, s26
	v_lshl_add_u64 v[212:213], v[212:213], 0, s[60:61]
	s_mov_b32 m0, s24
	ds_read_b128 v[180:183], v151 offset:49152
	ds_read_b128 v[184:187], v151 offset:50176
	ds_read_b128 v[188:191], v151 offset:51200
	ds_read_b128 v[192:195], v151 offset:52224
	ds_read_b128 v[196:199], v151 offset:53248
	ds_read_b128 v[200:203], v151 offset:54272
	ds_read_b128 v[204:207], v151 offset:55296
	ds_read_b128 v[208:211], v151 offset:56320
	global_load_lds_dwordx4 v[212:213], off
	s_add_i32 m0, s24, 0x2000
	s_add_u32 s22, s22, 0x84080
	v_lshl_add_u64 v[212:213], v[214:215], 0, s[60:61]
	s_addc_u32 s23, s23, 0
	s_add_i32 s24, s83, s26
	global_load_lds_dwordx4 v[212:213], off
	v_lshl_add_u64 v[212:213], s[22:23], 0, v[0:1]
	s_mov_b32 m0, s24
	s_nop 0
	global_load_lds_dwordx4 v[212:213], off
	v_lshl_add_u64 v[212:213], s[22:23], 0, v[130:131]
	s_add_i32 m0, s24, 0x2000
	s_nop 0
	global_load_lds_dwordx4 v[212:213], off
	v_lshl_add_u64 v[212:213], v[216:217], 0, s[60:61]
	s_mov_b32 m0, s31
	s_nop 0
	global_load_lds_dwordx4 v[212:213], off
	v_lshl_add_u64 v[212:213], v[218:219], 0, s[60:61]
	s_mov_b32 m0, s38
	s_nop 0
	global_load_lds_dwordx4 v[212:213], off
	s_waitcnt vmcnt(8)
	s_waitcnt lgkmcnt(0)
	s_barrier
	s_setprio 1
	s_waitcnt lgkmcnt(0)
	v_mfma_f32_16x16x32_bf16 v[62:65], v[142:145], v[180:183], v[62:65]
	v_mfma_f32_16x16x32_bf16 v[58:61], v[156:159], v[180:183], v[58:61]
	v_mfma_f32_16x16x32_bf16 v[54:57], v[142:145], v[188:191], v[54:57]
	v_mfma_f32_16x16x32_bf16 v[50:53], v[156:159], v[188:191], v[50:53]
	v_mfma_f32_16x16x32_bf16 v[30:33], v[142:145], v[196:199], v[30:33]
	v_mfma_f32_16x16x32_bf16 v[26:29], v[156:159], v[196:199], v[26:29]
	v_mfma_f32_16x16x32_bf16 v[22:25], v[142:145], v[204:207], v[22:25]
	v_mfma_f32_16x16x32_bf16 v[18:21], v[156:159], v[204:207], v[18:21]
	v_mfma_f32_16x16x32_bf16 v[62:65], v[152:155], v[184:187], v[62:65]
	v_mfma_f32_16x16x32_bf16 v[58:61], v[160:163], v[184:187], v[58:61]
	v_mfma_f32_16x16x32_bf16 v[54:57], v[152:155], v[192:195], v[54:57]
	v_mfma_f32_16x16x32_bf16 v[50:53], v[160:163], v[192:195], v[50:53]
	v_mfma_f32_16x16x32_bf16 v[30:33], v[152:155], v[200:203], v[30:33]
	v_mfma_f32_16x16x32_bf16 v[26:29], v[160:163], v[200:203], v[26:29]
	v_mfma_f32_16x16x32_bf16 v[22:25], v[152:155], v[208:211], v[22:25]
	v_mfma_f32_16x16x32_bf16 v[18:21], v[160:163], v[208:211], v[18:21]
	s_setprio 0
	s_setprio 1
	v_mfma_f32_16x16x32_bf16 v[46:49], v[164:167], v[180:183], v[46:49]
	v_mfma_f32_16x16x32_bf16 v[42:45], v[172:175], v[180:183], v[42:45]
	v_mfma_f32_16x16x32_bf16 v[38:41], v[164:167], v[188:191], v[38:41]
	v_mfma_f32_16x16x32_bf16 v[34:37], v[172:175], v[188:191], v[34:37]
	v_mfma_f32_16x16x32_bf16 v[14:17], v[164:167], v[196:199], v[14:17]
	v_mfma_f32_16x16x32_bf16 v[10:13], v[172:175], v[196:199], v[10:13]
	v_mfma_f32_16x16x32_bf16 v[6:9], v[164:167], v[204:207], v[6:9]
	v_mfma_f32_16x16x32_bf16 v[2:5], v[172:175], v[204:207], v[2:5]
	v_mfma_f32_16x16x32_bf16 v[46:49], v[168:171], v[184:187], v[46:49]
	v_mfma_f32_16x16x32_bf16 v[42:45], v[176:179], v[184:187], v[42:45]
	v_mfma_f32_16x16x32_bf16 v[38:41], v[168:171], v[192:195], v[38:41]
	v_mfma_f32_16x16x32_bf16 v[34:37], v[176:179], v[192:195], v[34:37]
	s_setprio 0
	v_mfma_f32_16x16x32_bf16 v[14:17], v[168:171], v[200:203], v[14:17]
	v_mfma_f32_16x16x32_bf16 v[10:13], v[176:179], v[200:203], v[10:13]
	v_mfma_f32_16x16x32_bf16 v[6:9], v[168:171], v[208:211], v[6:9]
	v_mfma_f32_16x16x32_bf16 v[2:5], v[176:179], v[208:211], v[2:5]
	s_barrier
	s_add_i32 s7, s7, 2
	s_add_u32 s10, s10, 0x100
	s_addc_u32 s11, s11, 0
	s_add_u32 s50, s50, 0x100
	s_addc_u32 s6, s6, 0
	s_cmp_gt_u32 s7, 29
	s_cbranch_scc0 .LBB0_1639
	s_and_b64 vcc, exec, s[16:17]
	s_cbranch_vccz .LBB0_1642
	s_barrier

; #define PG8_STAGE(bufoff, gbase, voff) do { _Pragma("unroll") for (int _i = 0; _i < 2; ++_i) \
;         __builtin_amdgcn_global_load_lds((const unsigned*)((const char*)(gbase) + (voff)[_i]), (PG8_LAS unsigned*)(lds + (bufoff) + ldsw + _i * 8192), 16, 0, 0); } while (0)
; #define PG8_WAIT_V(n) asm volatile("s_waitcnt vmcnt(" #n ")" ::: "memory")
; #define PG8_WAIT_L(n) asm volatile("s_waitcnt lgkmcnt(" #n ")" ::: "memory")
; #define PG8_BAR __builtin_amdgcn_s_barrier()
; #define PG8_SCHED __builtin_amdgcn_sched_barrier(0)
; template <class Epi, class Sched, bool ALIGN_EPI, bool F8 = false>
; __device__ __forceinline__ void gemm_phase(PG8_LAS unsigned char* lds, const Gemm g, const Sched& S, const Epi& E, int tid) {
;     ...
;             PG8_LDB(B0, 0, 0); PG8_LDB(B1, 0, 1); PG8_SCHED; PG8_LDA(At, 0, 0); PG8_STAGE(PG8_SA(1, 1), a1 + hstepA, voffA);
;             PG8_WAIT_V(8); PG8_WAIT_L(0); PG8_BAR; PG8_MMA(0, 0, At, B0); PG8_MMA(0, 1, At, B1); PG8_BAR; PG8_SCHED;
;             PG8_LDA(At, 0, 1); PG8_STAGE(PG8_SB(0, 0), b2, voffB); PG8_STAGE(PG8_SB(0, 1), b2 + hstepB, voffB); PG8_STAGE(PG8_SA(0, 0), a2, voffA);
;             PG8_WAIT_V(8); PG8_WAIT_L(0); PG8_BAR; PG8_MMA(1, 0, At, B0); PG8_MMA(1, 1, At, B1); PG8_BAR; PG8_SCHED;
.LBB0_1671:
	s_add_u32 s22, s20, 0x100
	s_addc_u32 s23, s21, 0
	s_add_i32 s87, 0, 0x10000
	s_cmpk_eq_i32 s86, 0x54
	s_cselect_b32 s27, s11, s23
	s_cselect_b32 s26, s10, s22
	s_cselect_b32 s25, s13, s85
	s_cselect_b32 s24, s12, s50
	s_add_i32 s88, 0, 0x14000
	v_add_u32_e32 v142, s87, v201
	v_add_u32_e32 v168, s88, v201
	ds_read_b128 v[130:133], v142
	ds_read_b128 v[134:137], v142 offset:1024
	ds_read_b128 v[138:141], v142 offset:2048
	ds_read_b128 v[142:145], v142 offset:3072
	ds_read_b128 v[146:149], v168
	ds_read_b128 v[150:153], v168 offset:1024
	ds_read_b128 v[154:157], v168 offset:2048
	ds_read_b128 v[168:171], v168 offset:3072
	v_lshl_add_u64 v[208:209], s[20:21], 0, v[164:165]
	s_add_i32 m0, s34, 0xc000
	ds_read_b128 v[172:175], v203
	ds_read_b128 v[176:179], v203 offset:1024
	ds_read_b128 v[180:183], v203 offset:2048
	ds_read_b128 v[184:187], v203 offset:3072
	ds_read_b128 v[188:191], v203 offset:4096
	ds_read_b128 v[192:195], v203 offset:5120
	ds_read_b128 v[196:199], v203 offset:6144
	ds_read_b128 v[204:207], v203 offset:7168
	global_load_lds_dwordx4 v[208:209], off
	v_lshl_add_u64 v[208:209], s[20:21], 0, v[166:167]
	s_add_i32 m0, s34, 0xe000
	s_nop 0
	global_load_lds_dwordx4 v[208:209], off
	s_waitcnt vmcnt(8)
	s_waitcnt lgkmcnt(0)
	s_barrier
	s_setprio 1
	s_waitcnt lgkmcnt(0)
	v_mfma_f32_16x16x32_bf16 v[126:129], v[130:133], v[172:175], v[126:129]
	v_mfma_f32_16x16x32_bf16 v[122:125], v[138:141], v[172:175], v[122:125]
	v_mfma_f32_16x16x32_bf16 v[110:113], v[130:133], v[180:183], v[110:113]
	v_mfma_f32_16x16x32_bf16 v[106:109], v[138:141], v[180:183], v[106:109]
	v_mfma_f32_16x16x32_bf16 v[94:97], v[130:133], v[188:191], v[94:97]
	v_mfma_f32_16x16x32_bf16 v[90:93], v[138:141], v[188:191], v[90:93]
	v_mfma_f32_16x16x32_bf16 v[78:81], v[130:133], v[196:199], v[78:81]
	v_mfma_f32_16x16x32_bf16 v[74:77], v[138:141], v[196:199], v[74:77]
	v_mfma_f32_16x16x32_bf16 v[126:129], v[134:137], v[176:179], v[126:129]
	v_mfma_f32_16x16x32_bf16 v[122:125], v[142:145], v[176:179], v[122:125]
	v_mfma_f32_16x16x32_bf16 v[110:113], v[134:137], v[184:187], v[110:113]
	v_mfma_f32_16x16x32_bf16 v[106:109], v[142:145], v[184:187], v[106:109]
	v_mfma_f32_16x16x32_bf16 v[94:97], v[134:137], v[192:195], v[94:97]
	v_mfma_f32_16x16x32_bf16 v[90:93], v[142:145], v[192:195], v[90:93]
	v_mfma_f32_16x16x32_bf16 v[78:81], v[134:137], v[204:207], v[78:81]
	v_mfma_f32_16x16x32_bf16 v[74:77], v[142:145], v[204:207], v[74:77]
	s_setprio 0
	s_setprio 1
	v_mfma_f32_16x16x32_bf16 v[118:121], v[146:149], v[172:175], v[118:121]
	v_mfma_f32_16x16x32_bf16 v[114:117], v[154:157], v[172:175], v[114:117]
	v_mfma_f32_16x16x32_bf16 v[102:105], v[146:149], v[180:183], v[102:105]
	v_mfma_f32_16x16x32_bf16 v[98:101], v[154:157], v[180:183], v[98:101]
	v_mfma_f32_16x16x32_bf16 v[86:89], v[146:149], v[188:191], v[86:89]
	v_mfma_f32_16x16x32_bf16 v[82:85], v[154:157], v[188:191], v[82:85]
	v_mfma_f32_16x16x32_bf16 v[70:73], v[146:149], v[196:199], v[70:73]
	v_mfma_f32_16x16x32_bf16 v[66:69], v[154:157], v[196:199], v[66:69]
	v_mfma_f32_16x16x32_bf16 v[118:121], v[150:153], v[176:179], v[118:121]
	v_mfma_f32_16x16x32_bf16 v[114:117], v[168:171], v[176:179], v[114:117]
	v_mfma_f32_16x16x32_bf16 v[102:105], v[150:153], v[184:187], v[102:105]
	v_mfma_f32_16x16x32_bf16 v[98:101], v[168:171], v[184:187], v[98:101]
	s_setprio 0
	v_mfma_f32_16x16x32_bf16 v[86:89], v[150:153], v[192:195], v[86:89]
	v_mfma_f32_16x16x32_bf16 v[82:85], v[168:171], v[192:195], v[82:85]
	v_mfma_f32_16x16x32_bf16 v[70:73], v[150:153], v[204:207], v[70:73]
	v_mfma_f32_16x16x32_bf16 v[66:69], v[168:171], v[204:207], v[66:69]
	s_barrier
	s_add_i32 s20, s87, s31
	v_lshl_add_u64 v[208:209], s[24:25], 0, v[0:1]
	s_mov_b32 m0, s20
	ds_read_b128 v[172:175], v203 offset:16384
	ds_read_b128 v[176:179], v203 offset:17408
	ds_read_b128 v[180:183], v203 offset:18432
	ds_read_b128 v[184:187], v203 offset:19456
	ds_read_b128 v[188:191], v203 offset:20480
	ds_read_b128 v[192:195], v203 offset:21504
	ds_read_b128 v[196:199], v203 offset:22528
	ds_read_b128 v[204:207], v203 offset:23552
	global_load_lds_dwordx4 v[208:209], off
	s_add_i32 m0, s20, 0x2000
	s_add_u32 s20, s24, 0x164000
	v_lshl_add_u64 v[210:211], s[24:25], 0, v[158:159]
	s_addc_u32 s21, s25, 0
	s_add_i32 s87, s88, s31
	global_load_lds_dwordx4 v[210:211], off
	v_lshl_add_u64 v[212:213], s[20:21], 0, v[0:1]
	s_mov_b32 m0, s87
	v_lshl_add_u64 v[214:215], s[26:27], 0, v[160:161]
	global_load_lds_dwordx4 v[212:213], off
	v_lshl_add_u64 v[212:213], s[20:21], 0, v[158:159]
	s_add_i32 m0, s87, 0x2000
	s_nop 0
	global_load_lds_dwordx4 v[212:213], off
	v_lshl_add_u64 v[212:213], s[26:27], 0, v[162:163]
	s_mov_b32 m0, s34
	s_nop 0
	global_load_lds_dwordx4 v[212:213], off
	s_mov_b32 m0, s35
	s_nop 0
	global_load_lds_dwordx4 v[214:215], off
	s_waitcnt vmcnt(8)
	s_waitcnt lgkmcnt(0)
	s_barrier
; #define PG8_STAGE(bufoff, gbase, voff) do { _Pragma("unroll") for (int _i = 0; _i < 2; ++_i) \
;         __builtin_amdgcn_global_load_lds((const unsigned*)((const char*)(gbase) + (voff)[_i]), (PG8_LAS unsigned*)(lds + (bufoff) + ldsw + _i * 8192), 16, 0, 0); } while (0)
; #define PG8_WAIT_V(n) asm volatile("s_waitcnt vmcnt(" #n ")" ::: "memory")
; #define PG8_WAIT_L(n) asm volatile("s_waitcnt lgkmcnt(" #n ")" ::: "memory")
; #define PG8_BAR __builtin_amdgcn_s_barrier()
; #define PG8_SCHED __builtin_amdgcn_sched_barrier(0)
; template <class Epi, class Sched, bool ALIGN_EPI, bool F8 = false>
; __device__ __forceinline__ void gemm_phase(PG8_LAS unsigned char* lds, const Gemm g, const Sched& S, const Epi& E, int tid) {
;     ...
;             PG8_WAIT_V(8); PG8_WAIT_L(0); PG8_BAR; PG8_MMA(1, 0, At, B0); PG8_MMA(1, 1, At, B1); PG8_BAR; PG8_SCHED;
;             PG8_LDB(B0, 1, 0); PG8_LDB(B1, 1, 1); PG8_SCHED; PG8_LDA(At, 1, 0); PG8_STAGE(PG8_SA(0, 1), a2 + hstepA, voffA);
;             PG8_WAIT_V(8); PG8_WAIT_L(0); PG8_BAR; PG8_MMA(0, 0, At, B0); PG8_MMA(0, 1, At, B1); PG8_BAR; PG8_SCHED;
;             PG8_LDA(At, 1, 1); PG8_STAGE(PG8_SB(1, 0), b3, voffB); PG8_STAGE(PG8_SB(1, 1), b3 + hstepB, voffB); PG8_STAGE(PG8_SA(1, 0), a3, voffA);
	s_setprio 1
	s_waitcnt lgkmcnt(0)
	v_mfma_f32_16x16x32_bf16 v[62:65], v[130:133], v[172:175], v[62:65]
	v_mfma_f32_16x16x32_bf16 v[58:61], v[138:141], v[172:175], v[58:61]
	v_mfma_f32_16x16x32_bf16 v[46:49], v[130:133], v[180:183], v[46:49]
	v_mfma_f32_16x16x32_bf16 v[42:45], v[138:141], v[180:183], v[42:45]
	v_mfma_f32_16x16x32_bf16 v[30:33], v[130:133], v[188:191], v[30:33]
	v_mfma_f32_16x16x32_bf16 v[26:29], v[138:141], v[188:191], v[26:29]
	v_mfma_f32_16x16x32_bf16 v[14:17], v[130:133], v[196:199], v[14:17]
	v_mfma_f32_16x16x32_bf16 v[10:13], v[138:141], v[196:199], v[10:13]
	v_mfma_f32_16x16x32_bf16 v[62:65], v[134:137], v[176:179], v[62:65]
	v_mfma_f32_16x16x32_bf16 v[58:61], v[142:145], v[176:179], v[58:61]
	v_mfma_f32_16x16x32_bf16 v[46:49], v[134:137], v[184:187], v[46:49]
	v_mfma_f32_16x16x32_bf16 v[42:45], v[142:145], v[184:187], v[42:45]
	v_mfma_f32_16x16x32_bf16 v[30:33], v[134:137], v[192:195], v[30:33]
	v_mfma_f32_16x16x32_bf16 v[26:29], v[142:145], v[192:195], v[26:29]
	v_mfma_f32_16x16x32_bf16 v[14:17], v[134:137], v[204:207], v[14:17]
	v_mfma_f32_16x16x32_bf16 v[10:13], v[142:145], v[204:207], v[10:13]
	s_setprio 0
	s_setprio 1
	v_mfma_f32_16x16x32_bf16 v[54:57], v[146:149], v[172:175], v[54:57]
	v_mfma_f32_16x16x32_bf16 v[50:53], v[154:157], v[172:175], v[50:53]
	v_mfma_f32_16x16x32_bf16 v[38:41], v[146:149], v[180:183], v[38:41]
	v_mfma_f32_16x16x32_bf16 v[34:37], v[154:157], v[180:183], v[34:37]
	v_mfma_f32_16x16x32_bf16 v[22:25], v[146:149], v[188:191], v[22:25]
	v_mfma_f32_16x16x32_bf16 v[18:21], v[154:157], v[188:191], v[18:21]
	v_mfma_f32_16x16x32_bf16 v[6:9], v[146:149], v[196:199], v[6:9]
	v_mfma_f32_16x16x32_bf16 v[2:5], v[154:157], v[196:199], v[2:5]
	v_mfma_f32_16x16x32_bf16 v[54:57], v[150:153], v[176:179], v[54:57]
	v_mfma_f32_16x16x32_bf16 v[50:53], v[168:171], v[176:179], v[50:53]
	v_mfma_f32_16x16x32_bf16 v[38:41], v[150:153], v[184:187], v[38:41]
	v_mfma_f32_16x16x32_bf16 v[34:37], v[168:171], v[184:187], v[34:37]
	s_setprio 0
	v_mfma_f32_16x16x32_bf16 v[22:25], v[150:153], v[192:195], v[22:25]
	v_mfma_f32_16x16x32_bf16 v[18:21], v[168:171], v[192:195], v[18:21]
	v_mfma_f32_16x16x32_bf16 v[6:9], v[150:153], v[204:207], v[6:9]
	v_mfma_f32_16x16x32_bf16 v[2:5], v[168:171], v[204:207], v[2:5]
	s_barrier
	s_add_i32 s87, 0, 0x18000
	s_add_i32 s88, 0, 0x1c000
	v_add_u32_e32 v142, s87, v201
	v_add_u32_e32 v168, s88, v201
	ds_read_b128 v[130:133], v142
	ds_read_b128 v[134:137], v142 offset:1024
	ds_read_b128 v[138:141], v142 offset:2048
	ds_read_b128 v[142:145], v142 offset:3072
	ds_read_b128 v[146:149], v168
	ds_read_b128 v[150:153], v168 offset:1024
	ds_read_b128 v[154:157], v168 offset:2048
	ds_read_b128 v[168:171], v168 offset:3072
	s_add_u32 s20, s26, 0x180000
	s_addc_u32 s21, s27, 0
	s_mov_b32 m0, s38
	v_lshl_add_u64 v[216:217], s[20:21], 0, v[162:163]
	ds_read_b128 v[172:175], v203 offset:32768
	ds_read_b128 v[176:179], v203 offset:33792
	ds_read_b128 v[180:183], v203 offset:34816
	ds_read_b128 v[184:187], v203 offset:35840
	ds_read_b128 v[188:191], v203 offset:36864
	ds_read_b128 v[192:195], v203 offset:37888
	ds_read_b128 v[196:199], v203 offset:38912
	ds_read_b128 v[204:207], v203 offset:39936
	global_load_lds_dwordx4 v[216:217], off
	v_lshl_add_u64 v[216:217], s[20:21], 0, v[160:161]
	s_mov_b32 m0, s39
	s_nop 0
	global_load_lds_dwordx4 v[216:217], off
	s_waitcnt vmcnt(8)
	s_waitcnt lgkmcnt(0)
	s_barrier
	s_setprio 1
	s_waitcnt lgkmcnt(0)
	v_mfma_f32_16x16x32_bf16 v[126:129], v[130:133], v[172:175], v[126:129]
	v_mfma_f32_16x16x32_bf16 v[122:125], v[138:141], v[172:175], v[122:125]
	v_mfma_f32_16x16x32_bf16 v[110:113], v[130:133], v[180:183], v[110:113]
	v_mfma_f32_16x16x32_bf16 v[106:109], v[138:141], v[180:183], v[106:109]
	v_mfma_f32_16x16x32_bf16 v[94:97], v[130:133], v[188:191], v[94:97]
	v_mfma_f32_16x16x32_bf16 v[90:93], v[138:141], v[188:191], v[90:93]
	v_mfma_f32_16x16x32_bf16 v[78:81], v[130:133], v[196:199], v[78:81]
	v_mfma_f32_16x16x32_bf16 v[74:77], v[138:141], v[196:199], v[74:77]
	v_mfma_f32_16x16x32_bf16 v[126:129], v[134:137], v[176:179], v[126:129]
	v_mfma_f32_16x16x32_bf16 v[122:125], v[142:145], v[176:179], v[122:125]
	v_mfma_f32_16x16x32_bf16 v[110:113], v[134:137], v[184:187], v[110:113]
	v_mfma_f32_16x16x32_bf16 v[106:109], v[142:145], v[184:187], v[106:109]
	v_mfma_f32_16x16x32_bf16 v[94:97], v[134:137], v[192:195], v[94:97]
	v_mfma_f32_16x16x32_bf16 v[90:93], v[142:145], v[192:195], v[90:93]
	v_mfma_f32_16x16x32_bf16 v[78:81], v[134:137], v[204:207], v[78:81]
	v_mfma_f32_16x16x32_bf16 v[74:77], v[142:145], v[204:207], v[74:77]
	s_setprio 0
	s_setprio 1
	v_mfma_f32_16x16x32_bf16 v[118:121], v[146:149], v[172:175], v[118:121]
	v_mfma_f32_16x16x32_bf16 v[114:117], v[154:157], v[172:175], v[114:117]
	v_mfma_f32_16x16x32_bf16 v[102:105], v[146:149], v[180:183], v[102:105]
	v_mfma_f32_16x16x32_bf16 v[98:101], v[154:157], v[180:183], v[98:101]
	v_mfma_f32_16x16x32_bf16 v[86:89], v[146:149], v[188:191], v[86:89]
	v_mfma_f32_16x16x32_bf16 v[82:85], v[154:157], v[188:191], v[82:85]
	v_mfma_f32_16x16x32_bf16 v[70:73], v[146:149], v[196:199], v[70:73]
	v_mfma_f32_16x16x32_bf16 v[66:69], v[154:157], v[196:199], v[66:69]
	v_mfma_f32_16x16x32_bf16 v[118:121], v[150:153], v[176:179], v[118:121]
	v_mfma_f32_16x16x32_bf16 v[114:117], v[168:171], v[176:179], v[114:117]
	v_mfma_f32_16x16x32_bf16 v[102:105], v[150:153], v[184:187], v[102:105]
	v_mfma_f32_16x16x32_bf16 v[98:101], v[168:171], v[184:187], v[98:101]
	s_setprio 0
	v_mfma_f32_16x16x32_bf16 v[86:89], v[150:153], v[192:195], v[86:89]
	v_mfma_f32_16x16x32_bf16 v[82:85], v[168:171], v[192:195], v[82:85]
	v_mfma_f32_16x16x32_bf16 v[70:73], v[150:153], v[204:207], v[70:73]
	v_mfma_f32_16x16x32_bf16 v[66:69], v[168:171], v[204:207], v[66:69]
	s_barrier
; #define PG8_BAR __builtin_amdgcn_s_barrier()
;     __device__ __forceinline__ void operator()(const f32x4 (&acc)[2][2][4][2], const Unit& u, int wr, int wc, int fr, int fq) const {
;         const int row0 = u.pm * BM + wr * 64 + fr, col0 = u.pn * BM + wc * 32 + 8 * fq;
; #pragma unroll
;         for (int ai = 0; ai < 2; ++ai) {
;             u32x4 old[4][2];
; #pragma unroll
;             for (int m = 0; m < 4; ++m)
; #pragma unroll
;                 for (int bj = 0; bj < 2; ++bj) old[m][bj] = *(const u32x4*)(xb + (size_t)(row0 + ai * HALF + m * 16) * 2048 + col0 + bj * HALF);
; #pragma unroll
;             for (int m = 0; m < 4; ++m) { const size_t row = (size_t)(row0 + ai * HALF + m * 16); bf16_t* rowp = xb + row * 2048 + col0; float ss = 0.f;
; #pragma unroll
;                 for (int bj = 0; bj < 2; ++bj) { const u32x4 oo = old[m][bj]; const f32x4 a0 = acc[ai][bj][m][0], a1 = acc[ai][bj][m][1];
;                     const float x0 = a0[0] + bf_lo(oo.x), x1 = a0[1] + bf_hi(oo.x), x2 = a0[2] + bf_lo(oo.y), x3 = a0[3] + bf_hi(oo.y), x4 = a1[0] + bf_lo(oo.z), x5 = a1[1] + bf_hi(oo.z), x6 = a1[2] + bf_lo(oo.w), x7 = a1[3] + bf_hi(oo.w);
;                     ss += (x0 * x0 + x1 * x1) + (x2 * x2 + x3 * x3) + (x4 * x4 + x5 * x5) + (x6 * x6 + x7 * x7);
;                     u32x4 w; w.x = cvt_pk_bf16(x0, x1); w.y = cvt_pk_bf16(x2, x3); w.z = cvt_pk_bf16(x4, x5); w.w = cvt_pk_bf16(x6, x7);
;                     *(u32x4*)(rowp + bj * HALF) = w;
;                     if (h8) { u32x2 q; q.x = pk4_fp8_(x0 * F8_SA_, x1 * F8_SA_, x2 * F8_SA_, x3 * F8_SA_); q.y = pk4_fp8_(x4 * F8_SA_, x5 * F8_SA_, x6 * F8_SA_, x7 * F8_SA_);
;                         *(u32x2*)(h8 + row * 2048 + col0 + bj * HALF) = q; } }
; template <class Epi, class Sched, bool ALIGN_EPI, bool F8 = false>
; __device__ __forceinline__ void gemm_phase(PG8_LAS unsigned char* lds, const Gemm g, const Sched& S, const Epi& E, int tid) {
;     ...
;             PG8_LDA(At, 1, 1); PG8_STAGE(PG8_SB(1, 0), b3, voffB); PG8_STAGE(PG8_SB(1, 1), b3 + hstepB, voffB); PG8_STAGE(PG8_SA(1, 0), a3, voffA);
;             PG8_WAIT_V(8); PG8_WAIT_L(0); PG8_BAR; PG8_MMA(1, 0, At, B0); PG8_MMA(1, 1, At, B1); PG8_BAR; PG8_SCHED;
;         }
;         if constexpr (ALIGN_EPI) { if (wr == 0) PG8_BAR; }
;         if constexpr (F8) asm volatile("s_nop 15\n\ts_nop 15" ::: "memory");
;         E(acc, cur, wr, wc, fr, fq); S.done(cur);
	s_add_i32 s20, s87, s31
	v_lshl_add_u64 v[208:209], v[208:209], 0, s[60:61]
	s_mov_b32 m0, s20
	ds_read_b128 v[172:175], v203 offset:49152
	ds_read_b128 v[176:179], v203 offset:50176
	ds_read_b128 v[180:183], v203 offset:51200
	ds_read_b128 v[184:187], v203 offset:52224
	ds_read_b128 v[188:191], v203 offset:53248
	ds_read_b128 v[192:195], v203 offset:54272
	ds_read_b128 v[196:199], v203 offset:55296
	ds_read_b128 v[204:207], v203 offset:56320
	global_load_lds_dwordx4 v[208:209], off
	s_add_i32 m0, s20, 0x2000
	s_add_u32 s20, s24, 0x164080
	v_lshl_add_u64 v[208:209], v[210:211], 0, s[60:61]
	s_addc_u32 s21, s25, 0
	s_add_i32 s24, s88, s31
	global_load_lds_dwordx4 v[208:209], off
	v_lshl_add_u64 v[208:209], s[20:21], 0, v[0:1]
	s_mov_b32 m0, s24
	s_nop 0
	global_load_lds_dwordx4 v[208:209], off
	v_lshl_add_u64 v[208:209], s[20:21], 0, v[158:159]
	s_add_i32 m0, s24, 0x2000
	s_nop 0
	global_load_lds_dwordx4 v[208:209], off
	v_lshl_add_u64 v[208:209], v[212:213], 0, s[60:61]
	s_mov_b32 m0, s45
	s_nop 0
	global_load_lds_dwordx4 v[208:209], off
	v_lshl_add_u64 v[208:209], v[214:215], 0, s[60:61]
	s_mov_b32 m0, s51
	s_nop 0
	global_load_lds_dwordx4 v[208:209], off
	s_waitcnt vmcnt(8)
	s_waitcnt lgkmcnt(0)
	s_barrier
	s_setprio 1
	s_waitcnt lgkmcnt(0)
	v_mfma_f32_16x16x32_bf16 v[62:65], v[130:133], v[172:175], v[62:65]
	v_mfma_f32_16x16x32_bf16 v[58:61], v[138:141], v[172:175], v[58:61]
	v_mfma_f32_16x16x32_bf16 v[46:49], v[130:133], v[180:183], v[46:49]
	v_mfma_f32_16x16x32_bf16 v[42:45], v[138:141], v[180:183], v[42:45]
	v_mfma_f32_16x16x32_bf16 v[30:33], v[130:133], v[188:191], v[30:33]
	v_mfma_f32_16x16x32_bf16 v[26:29], v[138:141], v[188:191], v[26:29]
	v_mfma_f32_16x16x32_bf16 v[14:17], v[130:133], v[196:199], v[14:17]
	v_mfma_f32_16x16x32_bf16 v[10:13], v[138:141], v[196:199], v[10:13]
	v_mfma_f32_16x16x32_bf16 v[62:65], v[134:137], v[176:179], v[62:65]
	v_mfma_f32_16x16x32_bf16 v[58:61], v[142:145], v[176:179], v[58:61]
	v_mfma_f32_16x16x32_bf16 v[46:49], v[134:137], v[184:187], v[46:49]
	v_mfma_f32_16x16x32_bf16 v[42:45], v[142:145], v[184:187], v[42:45]
	v_mfma_f32_16x16x32_bf16 v[30:33], v[134:137], v[192:195], v[30:33]
	v_mfma_f32_16x16x32_bf16 v[26:29], v[142:145], v[192:195], v[26:29]
	v_mfma_f32_16x16x32_bf16 v[14:17], v[134:137], v[204:207], v[14:17]
	v_mfma_f32_16x16x32_bf16 v[10:13], v[142:145], v[204:207], v[10:13]
	s_setprio 0
	s_setprio 1
	v_mfma_f32_16x16x32_bf16 v[54:57], v[146:149], v[172:175], v[54:57]
	v_mfma_f32_16x16x32_bf16 v[50:53], v[154:157], v[172:175], v[50:53]
	v_mfma_f32_16x16x32_bf16 v[38:41], v[146:149], v[180:183], v[38:41]
	v_mfma_f32_16x16x32_bf16 v[34:37], v[154:157], v[180:183], v[34:37]
	v_mfma_f32_16x16x32_bf16 v[22:25], v[146:149], v[188:191], v[22:25]
	v_mfma_f32_16x16x32_bf16 v[18:21], v[154:157], v[188:191], v[18:21]
	v_mfma_f32_16x16x32_bf16 v[6:9], v[146:149], v[196:199], v[6:9]
	v_mfma_f32_16x16x32_bf16 v[2:5], v[154:157], v[196:199], v[2:5]
	v_mfma_f32_16x16x32_bf16 v[54:57], v[150:153], v[176:179], v[54:57]
	v_mfma_f32_16x16x32_bf16 v[50:53], v[168:171], v[176:179], v[50:53]
	v_mfma_f32_16x16x32_bf16 v[38:41], v[150:153], v[184:187], v[38:41]
	v_mfma_f32_16x16x32_bf16 v[34:37], v[168:171], v[184:187], v[34:37]
	s_setprio 0
	v_mfma_f32_16x16x32_bf16 v[22:25], v[150:153], v[192:195], v[22:25]
	v_mfma_f32_16x16x32_bf16 v[18:21], v[168:171], v[192:195], v[18:21]
	v_mfma_f32_16x16x32_bf16 v[6:9], v[150:153], v[204:207], v[6:9]
	v_mfma_f32_16x16x32_bf16 v[2:5], v[168:171], v[204:207], v[2:5]
	s_barrier
	s_add_i32 s86, s86, 2
	s_add_u32 s50, s50, 0x100
	s_addc_u32 s85, s85, 0
	s_cmpk_gt_u32 s86, 0x55
	s_mov_b64 s[20:21], s[22:23]
	s_cbranch_scc0 .LBB0_1671
	v_lshl_or_b32 v168, s69, 8, v202
	v_lshl_add_u32 v172, s84, 8, v200
	v_ashrrev_i32_e32 v169, 31, v168
	v_lshlrev_b64 v[182:183], 1, v[168:169]
	v_ashrrev_i32_e32 v173, 31, v172
	v_lshl_add_u64 v[170:171], s[14:15], 0, v[182:183]
	v_lshlrev_b64 v[184:185], 12, v[172:173]
	v_lshl_add_u64 v[130:131], v[170:171], 0, v[184:185]
	global_load_dwordx4 v[178:181], v[130:131], off
	global_load_dwordx4 v[154:157], v[130:131], off offset:256
	v_or_b32_e32 v192, 16, v172
	v_ashrrev_i32_e32 v193, 31, v192
	v_or_b32_e32 v176, 32, v172
	v_lshlrev_b64 v[196:197], 12, v[192:193]
	v_ashrrev_i32_e32 v177, 31, v176
	v_or_b32_e32 v174, 48, v172
	v_lshl_add_u64 v[130:131], v[170:171], 0, v[196:197]
	v_lshlrev_b64 v[194:195], 12, v[176:177]
	v_ashrrev_i32_e32 v175, 31, v174
	global_load_dwordx4 v[150:153], v[130:131], off
	global_load_dwordx4 v[146:149], v[130:131], off offset:256
	v_lshl_add_u64 v[130:131], v[170:171], 0, v[194:195]
	v_lshlrev_b64 v[190:191], 12, v[174:175]
	global_load_dwordx4 v[142:145], v[130:131], off
	global_load_dwordx4 v[138:141], v[130:131], off offset:256
	v_lshl_add_u64 v[130:131], v[170:171], 0, v[190:191]
	global_load_dwordx4 v[134:137], v[130:131], off
	s_nop 0
	global_load_dwordx4 v[130:133], v[130:131], off offset:256
	v_lshl_add_u64 v[184:185], s[14:15], 0, v[184:185]
	v_lshl_add_u64 v[198:199], v[184:185], 0, v[182:183]
	v_lshlrev_b64 v[186:187], 11, v[172:173]
	s_and_b64 vcc, exec, s[4:5]
	s_waitcnt vmcnt(0)
	v_lshlrev_b32_e32 v182, 16, v178
	v_and_b32_e32 v178, 0xffff0000, v178
	v_add_f32_e32 v204, v127, v178
	v_lshlrev_b32_e32 v127, 16, v179
	v_add_f32_e32 v127, v128, v127
	v_and_b32_e32 v128, 0xffff0000, v179
	v_add_f32_e32 v129, v129, v128
	v_lshlrev_b32_e32 v128, 16, v180
	v_add_f32_e32 v128, v122, v128
	v_and_b32_e32 v122, 0xffff0000, v180
	v_add_f32_e32 v205, v123, v122
	v_lshlrev_b32_e32 v122, 16, v181
	v_add_f32_e32 v124, v124, v122
	v_and_b32_e32 v122, 0xffff0000, v181
	v_add_f32_e32 v125, v125, v122
	v_lshl_add_u64 v[122:123], s[18:19], 0, v[186:187]
	v_add_f32_e32 v126, v126, v182
	v_lshl_add_u64 v[122:123], v[122:123], 0, v[168:169]
	v_cvt_pk_bf16_f32 v178, v126, v204
	v_cvt_pk_bf16_f32 v179, v127, v129
	v_cvt_pk_bf16_f32 v180, v128, v205
	v_cvt_pk_bf16_f32 v181, v124, v125
	global_store_dwordx4 v[198:199], v[178:181], off
	s_cbranch_vccnz .LBB0_1674
	s_nop 0
	v_add_f32_e32 v179, v126, v126
	v_add_f32_e32 v180, v204, v204
	v_mov_b32_e32 v178, v1
	v_cvt_pk_fp8_f32 v178, v179, v180
	v_add_f32_e32 v180, v128, v128
	v_add_f32_e32 v183, v205, v205
	v_mov_b32_e32 v179, v1
	v_cvt_pk_fp8_f32 v179, v180, v183
	v_add_f32_e32 v181, v127, v127
	v_add_f32_e32 v182, v129, v129
	v_cvt_pk_fp8_f32 v178, v181, v182 op_sel:[0,0,1]
	v_add_f32_e32 v180, v124, v124
	v_add_f32_e32 v181, v125, v125
	v_cvt_pk_fp8_f32 v179, v180, v181 op_sel:[0,0,1]
	global_store_dwordx2 v[122:123], v[178:179], off
